# v79 + back-to-back s_setprio 0 / s_setprio 1|2 pairs between the two MFMA blocks of each compute segment removed
# speedup vs baseline: 1.0013x; 1.0013x over previous
; #define PG8_STAGE(bufoff, gbase, voff) do { _Pragma("unroll") for (int _i = 0; _i < 2; ++_i) \
;         __builtin_amdgcn_global_load_lds((const unsigned*)((const char*)(gbase) + (voff)[_i]), (PG8_LAS unsigned*)(lds + (bufoff) + ldsw + _i * 8192), 16, 0, 0); } while (0)
; template <class Epi, class Sched, bool ALIGN_EPI = true, bool F8 = false>
; __device__ __forceinline__ void gemm_phase(PG8_LAS unsigned char* lds, const Sched& S, const Epi& E) {
;     ...
;         const bool has_next = S.next(ui + 1, nxt);
;         const char* nA = has_next ? nxt.A : cA; const char* nB = has_next ? nxt.B : cB;
;         const int nt = cur.nt;
; #pragma unroll 1
;         for (int t = 0; t < nt; t += 2) {
;             const bool last = (t == nt - 2);
;             if constexpr (Sched::GATHER) { if (last && has_next) S.a_off(nxt, Rs, Cs, voffAn); }
;             const char* a1 = cA + (size_t)(t + 1) * kstep;
;             const char* a2 = last ? nA : cA + (size_t)(t + 2) * kstep; const char* b2 = last ? nB : cB + (size_t)(t + 2) * kstepB;
;             const char* a3 = a2 + kstep; const char* b3 = b2 + kstepB;
;             unsigned vA2[2][2];
; #pragma unroll
;             for (int h = 0; h < 2; ++h)
; #pragma unroll
;                 for (int i = 0; i < 2; ++i) { if constexpr (Sched::GATHER) vA2[h][i] = (last && has_next) ? voffAn[h][i] : voffA[h][i]; else vA2[h][i] = voffA[h][i]; }
;             PG8_LDB(B0, 0, 0); PG8_LDB(B1, 0, 1); PG8_SCHED; PG8_LDA(At, 0, 0); PG8_STAGE(PG8_SA(1, 1), a1, voffA[1]);
;             PG8_WAIT_V(8); PG8_WAIT_L(0); PG8_BAR; PG8_MMA(0, 0, At, B0); PG8_MMA(0, 1, At, B1); PG8_BAR; PG8_SCHED;
;             PG8_LDA(At, 0, 1); PG8_STAGE(PG8_SB(0, 0), b2, voffB[0]); PG8_STAGE(PG8_SB(0, 1), b2, voffB[1]); PG8_STAGE(PG8_SA(0, 0), a2, vA2[0]);
;             PG8_WAIT_V(8); PG8_WAIT_L(0); PG8_BAR; PG8_MMA(1, 0, At, B0); PG8_MMA(1, 1, At, B1); PG8_BAR; PG8_SCHED;
;             PG8_LDB(B0, 1, 0); PG8_LDB(B1, 1, 1); PG8_SCHED; PG8_LDA(At, 1, 0); PG8_STAGE(PG8_SA(0, 1), a2, vA2[1]);
;             PG8_WAIT_V(8); PG8_WAIT_L(0); PG8_BAR; PG8_MMA(0, 0, At, B0); PG8_MMA(0, 1, At, B1); PG8_BAR; PG8_SCHED;
;             PG8_LDA(At, 1, 1); PG8_STAGE(PG8_SB(1, 0), b3, voffB[0]); PG8_STAGE(PG8_SB(1, 1), b3, voffB[1]); PG8_STAGE(PG8_SA(1, 0), a3, vA2[0]);
;             PG8_WAIT_V(8); PG8_WAIT_L(0); PG8_BAR; PG8_MMA(1, 0, At, B0); PG8_MMA(1, 1, At, B1); PG8_BAR; PG8_SCHED;
.Lpk0_372:
	ds_read_b128 v[18:21], v207
	ds_read_b128 v[22:25], v207 offset:1024
	ds_read_b128 v[26:29], v207 offset:2048
	ds_read_b128 v[30:33], v207 offset:3072
	ds_read_b128 v[2:5], v208
	ds_read_b128 v[6:9], v208 offset:1024
	ds_read_b128 v[10:13], v208 offset:2048
	ds_read_b128 v[14:17], v208 offset:3072
	s_add_u32 s28, s26, 0x8000
	s_addc_u32 s29, s27, 0
	s_cmp_eq_u32 s21, 12
	s_cselect_b32 s40, s22, s28
	s_cselect_b32 s41, s23, s29
	s_cselect_b32 s30, s24, s5
	s_cselect_b32 s31, s25, s19
	s_add_u32 s28, s40, 0x8000
	s_addc_u32 s29, s41, 0
	s_add_i32 m0, s46, 0xc000
	ds_read_b128 v[212:215], v209
	ds_read_b128 v[216:219], v209 offset:1024
	ds_read_b128 v[220:223], v209 offset:2048
	ds_read_b128 v[224:227], v209 offset:3072
	ds_read_b128 v[228:231], v209 offset:4096
	ds_read_b128 v[232:235], v209 offset:5120
	ds_read_b128 v[236:239], v209 offset:6144
	ds_read_b128 v[240:243], v209 offset:7168
	global_load_lds_dwordx4 v190, s[26:27]
	s_add_i32 m0, s46, 0xe000
	s_nop 0
	global_load_lds_dwordx4 v188, s[26:27]
	s_waitcnt vmcnt(8)
	s_waitcnt lgkmcnt(0)
	s_setprio 1
	v_mfma_f32_16x16x128_f8f6f4 v[158:161], v[18:25], v[212:219], 0
	v_mfma_f32_16x16x128_f8f6f4 v[154:157], v[26:33], v[212:219], 0
	v_mfma_f32_16x16x128_f8f6f4 v[142:145], v[18:25], v[220:227], 0
	v_mfma_f32_16x16x128_f8f6f4 v[138:141], v[26:33], v[220:227], 0
	v_mfma_f32_16x16x128_f8f6f4 v[126:129], v[18:25], v[228:235], 0
	v_mfma_f32_16x16x128_f8f6f4 v[122:125], v[26:33], v[228:235], 0
	v_mfma_f32_16x16x128_f8f6f4 v[110:113], v[18:25], v[236:243], 0
	v_mfma_f32_16x16x128_f8f6f4 v[106:109], v[26:33], v[236:243], 0
	s_nop 3
	v_mfma_f32_16x16x128_f8f6f4 v[150:153], v[2:9], v[212:219], 0
	v_mfma_f32_16x16x128_f8f6f4 v[146:149], v[10:17], v[212:219], 0
	v_mfma_f32_16x16x128_f8f6f4 v[134:137], v[2:9], v[220:227], 0
	v_mfma_f32_16x16x128_f8f6f4 v[130:133], v[10:17], v[220:227], 0
	v_mfma_f32_16x16x128_f8f6f4 v[118:121], v[2:9], v[228:235], 0
	v_mfma_f32_16x16x128_f8f6f4 v[114:117], v[10:17], v[228:235], 0
	v_mfma_f32_16x16x128_f8f6f4 v[102:105], v[2:9], v[236:243], 0
	v_mfma_f32_16x16x128_f8f6f4 v[98:101], v[10:17], v[236:243], 0
	s_setprio 0
	s_barrier
	s_add_i32 s67, s62, s45
	s_mov_b32 m0, s67
	ds_read_b128 v[212:215], v209 offset:16384
	ds_read_b128 v[216:219], v209 offset:17408
	ds_read_b128 v[220:223], v209 offset:18432
	ds_read_b128 v[224:227], v209 offset:19456
	ds_read_b128 v[228:231], v209 offset:20480
	ds_read_b128 v[232:235], v209 offset:21504
	ds_read_b128 v[236:239], v209 offset:22528
	ds_read_b128 v[240:243], v209 offset:23552
	global_load_lds_dwordx4 v164, s[30:31]
	s_add_i32 m0, s67, 0x2000
	s_add_i32 s67, s63, s45
	global_load_lds_dwordx4 v166, s[30:31]
	s_add_u32 s98, s30, s8
	s_addc_u32 s99, s31, s9
	s_mov_b32 m0, s67
	s_nop 0
	global_load_lds_dwordx4 v164, s[98:99]
	s_add_u32 s100, s30, s8
	s_addc_u32 s101, s31, s9
	s_add_i32 m0, s67, 0x2000
	s_nop 0
	global_load_lds_dwordx4 v166, s[100:101]
	s_mov_b32 m0, s46
	s_nop 0
	global_load_lds_dwordx4 v174, s[40:41]
	s_mov_b32 m0, s47
	s_nop 0
	global_load_lds_dwordx4 v176, s[40:41]
	s_waitcnt vmcnt(8)
	s_waitcnt lgkmcnt(0)
	s_setprio 1
	v_mfma_f32_16x16x128_f8f6f4 v[94:97], v[18:25], v[212:219], 0
	v_mfma_f32_16x16x128_f8f6f4 v[90:93], v[26:33], v[212:219], 0
	v_mfma_f32_16x16x128_f8f6f4 v[78:81], v[18:25], v[220:227], 0
	v_mfma_f32_16x16x128_f8f6f4 v[74:77], v[26:33], v[220:227], 0
	v_mfma_f32_16x16x128_f8f6f4 v[62:65], v[18:25], v[228:235], 0
	v_mfma_f32_16x16x128_f8f6f4 v[58:61], v[26:33], v[228:235], 0
	v_mfma_f32_16x16x128_f8f6f4 v[46:49], v[18:25], v[236:243], 0
	v_mfma_f32_16x16x128_f8f6f4 v[42:45], v[26:33], v[236:243], 0
	s_nop 3
	v_mfma_f32_16x16x128_f8f6f4 v[86:89], v[2:9], v[212:219], 0
	v_mfma_f32_16x16x128_f8f6f4 v[82:85], v[10:17], v[212:219], 0
	v_mfma_f32_16x16x128_f8f6f4 v[70:73], v[2:9], v[220:227], 0
	v_mfma_f32_16x16x128_f8f6f4 v[66:69], v[10:17], v[220:227], 0
	v_mfma_f32_16x16x128_f8f6f4 v[54:57], v[2:9], v[228:235], 0
	v_mfma_f32_16x16x128_f8f6f4 v[50:53], v[10:17], v[228:235], 0
	v_mfma_f32_16x16x128_f8f6f4 v[38:41], v[2:9], v[236:243], 0
	v_mfma_f32_16x16x128_f8f6f4 v[34:37], v[10:17], v[236:243], 0
	s_setprio 0
	s_barrier
	s_add_i32 s67, 0, 0x18000
	s_add_i32 s68, 0, 0x1c000
	v_add_u32_e32 v14, s67, v202
	v_add_u32_e32 v30, s68, v202
	ds_read_b128 v[2:5], v14
	ds_read_b128 v[6:9], v14 offset:1024
	ds_read_b128 v[10:13], v14 offset:2048
	ds_read_b128 v[14:17], v14 offset:3072
	ds_read_b128 v[18:21], v30
	ds_read_b128 v[22:25], v30 offset:1024
	ds_read_b128 v[26:29], v30 offset:2048
	ds_read_b128 v[30:33], v30 offset:3072
	s_mov_b32 m0, s48
	ds_read_b128 v[212:215], v209 offset:32768
	ds_read_b128 v[216:219], v209 offset:33792
	ds_read_b128 v[220:223], v209 offset:34816
	ds_read_b128 v[224:227], v209 offset:35840
	ds_read_b128 v[228:231], v209 offset:36864
	ds_read_b128 v[232:235], v209 offset:37888
	ds_read_b128 v[236:239], v209 offset:38912
	ds_read_b128 v[240:243], v209 offset:39936
	global_load_lds_dwordx4 v178, s[40:41]
	s_mov_b32 m0, s49
	s_nop 0
	global_load_lds_dwordx4 v180, s[40:41]
	s_waitcnt vmcnt(8)
	s_waitcnt lgkmcnt(0)
	s_setprio 1
	v_mfma_f32_16x16x128_f8f6f4 v[158:161], v[2:9], v[212:219], v[158:161]
	v_mfma_f32_16x16x128_f8f6f4 v[154:157], v[10:17], v[212:219], v[154:157]
	v_mfma_f32_16x16x128_f8f6f4 v[142:145], v[2:9], v[220:227], v[142:145]
	v_mfma_f32_16x16x128_f8f6f4 v[138:141], v[10:17], v[220:227], v[138:141]
	v_mfma_f32_16x16x128_f8f6f4 v[126:129], v[2:9], v[228:235], v[126:129]
	v_mfma_f32_16x16x128_f8f6f4 v[122:125], v[10:17], v[228:235], v[122:125]
	v_mfma_f32_16x16x128_f8f6f4 v[110:113], v[2:9], v[236:243], v[110:113]
	v_mfma_f32_16x16x128_f8f6f4 v[106:109], v[10:17], v[236:243], v[106:109]
	s_nop 3
	v_mfma_f32_16x16x128_f8f6f4 v[150:153], v[18:25], v[212:219], v[150:153]
	v_mfma_f32_16x16x128_f8f6f4 v[146:149], v[26:33], v[212:219], v[146:149]
	v_mfma_f32_16x16x128_f8f6f4 v[134:137], v[18:25], v[220:227], v[134:137]
	v_mfma_f32_16x16x128_f8f6f4 v[130:133], v[26:33], v[220:227], v[130:133]
	v_mfma_f32_16x16x128_f8f6f4 v[118:121], v[18:25], v[228:235], v[118:121]
	v_mfma_f32_16x16x128_f8f6f4 v[114:117], v[26:33], v[228:235], v[114:117]
	v_mfma_f32_16x16x128_f8f6f4 v[102:105], v[18:25], v[236:243], v[102:105]
	v_mfma_f32_16x16x128_f8f6f4 v[98:101], v[26:33], v[236:243], v[98:101]
	s_setprio 0
	s_barrier
; #define PG8_STAGE(bufoff, gbase, voff) do { _Pragma("unroll") for (int _i = 0; _i < 2; ++_i) \
;         __builtin_amdgcn_global_load_lds((const unsigned*)((const char*)(gbase) + (voff)[_i]), (PG8_LAS unsigned*)(lds + (bufoff) + ldsw + _i * 8192), 16, 0, 0); } while (0)
; #define PG8_WAIT_V(n) asm volatile("s_waitcnt vmcnt(" #n ")" ::: "memory")
; #define PG8_WAIT_L(n) asm volatile("s_waitcnt lgkmcnt(" #n ")" ::: "memory")
; #define PG8_BAR __builtin_amdgcn_s_barrier()
; #define PG8_SCHED __builtin_amdgcn_sched_barrier(0)
; template <class Epi, class Sched, bool ALIGN_EPI = true, bool F8 = false>
; __device__ __forceinline__ void gemm_phase(PG8_LAS unsigned char* lds, const Sched& S, const Epi& E) {
;     ...
;             const char* a1 = cA + (size_t)(t + 1) * kstep;
;             const char* a2 = last ? nA : cA + (size_t)(t + 2) * kstep; const char* b2 = last ? nB : cB + (size_t)(t + 2) * kstepB;
;             const char* a3 = a2 + kstep; const char* b3 = b2 + kstepB;
;             unsigned vA2[2][2];
; #pragma unroll
;             for (int h = 0; h < 2; ++h)
; #pragma unroll
;                 for (int i = 0; i < 2; ++i) { if constexpr (Sched::GATHER) vA2[h][i] = (last && has_next) ? voffAn[h][i] : voffA[h][i]; else vA2[h][i] = voffA[h][i]; }
;             PG8_LDB(B0, 0, 0); PG8_LDB(B1, 0, 1); PG8_SCHED; PG8_LDA(At, 0, 0); PG8_STAGE(PG8_SA(1, 1), a1, voffA[1]);
;             PG8_WAIT_V(8); PG8_WAIT_L(0); PG8_BAR; PG8_MMA(0, 0, At, B0); PG8_MMA(0, 1, At, B1); PG8_BAR; PG8_SCHED;
;             PG8_LDA(At, 0, 1); PG8_STAGE(PG8_SB(0, 0), b2, voffB[0]); PG8_STAGE(PG8_SB(0, 1), b2, voffB[1]); PG8_STAGE(PG8_SA(0, 0), a2, vA2[0]);
;             PG8_WAIT_V(8); PG8_WAIT_L(0); PG8_BAR; PG8_MMA(1, 0, At, B0); PG8_MMA(1, 1, At, B1); PG8_BAR; PG8_SCHED;
;             PG8_LDB(B0, 1, 0); PG8_LDB(B1, 1, 1); PG8_SCHED; PG8_LDA(At, 1, 0); PG8_STAGE(PG8_SA(0, 1), a2, vA2[1]);
;             PG8_WAIT_V(8); PG8_WAIT_L(0); PG8_BAR; PG8_MMA(0, 0, At, B0); PG8_MMA(0, 1, At, B1); PG8_BAR; PG8_SCHED;
;             PG8_LDA(At, 1, 1); PG8_STAGE(PG8_SB(1, 0), b3, voffB[0]); PG8_STAGE(PG8_SB(1, 1), b3, voffB[1]); PG8_STAGE(PG8_SA(1, 0), a3, vA2[0]);
;             PG8_WAIT_V(8); PG8_WAIT_L(0); PG8_BAR; PG8_MMA(1, 0, At, B0); PG8_MMA(1, 1, At, B1); PG8_BAR; PG8_SCHED;
	s_add_u32 s30, s30, 0x8000
	s_addc_u32 s31, s31, 0
	s_add_i32 s40, s67, s45
	s_mov_b32 m0, s40
	ds_read_b128 v[212:215], v209 offset:49152
	ds_read_b128 v[216:219], v209 offset:50176
	ds_read_b128 v[220:223], v209 offset:51200
	ds_read_b128 v[224:227], v209 offset:52224
	ds_read_b128 v[228:231], v209 offset:53248
	ds_read_b128 v[232:235], v209 offset:54272
	ds_read_b128 v[236:239], v209 offset:55296
	ds_read_b128 v[240:243], v209 offset:56320
	global_load_lds_dwordx4 v164, s[30:31]
	s_add_i32 m0, s40, 0x2000
	s_add_i32 s40, s68, s45
	global_load_lds_dwordx4 v166, s[30:31]
	s_mov_b32 m0, s40
	s_nop 0
	global_load_lds_dwordx4 v168, s[30:31]
	s_add_i32 m0, s40, 0x2000
	s_nop 0
	global_load_lds_dwordx4 v172, s[30:31]
	s_mov_b32 m0, s52
	s_nop 0
	global_load_lds_dwordx4 v174, s[28:29]
	s_mov_b32 m0, s53
	s_nop 0
	global_load_lds_dwordx4 v176, s[28:29]
	s_waitcnt vmcnt(8)
	s_waitcnt lgkmcnt(0)
	s_setprio 1
	v_mfma_f32_16x16x128_f8f6f4 v[94:97], v[2:9], v[212:219], v[94:97]
	v_mfma_f32_16x16x128_f8f6f4 v[90:93], v[10:17], v[212:219], v[90:93]
	v_mfma_f32_16x16x128_f8f6f4 v[78:81], v[2:9], v[220:227], v[78:81]
	v_mfma_f32_16x16x128_f8f6f4 v[74:77], v[10:17], v[220:227], v[74:77]
	v_mfma_f32_16x16x128_f8f6f4 v[62:65], v[2:9], v[228:235], v[62:65]
	v_mfma_f32_16x16x128_f8f6f4 v[58:61], v[10:17], v[228:235], v[58:61]
	v_mfma_f32_16x16x128_f8f6f4 v[46:49], v[2:9], v[236:243], v[46:49]
	v_mfma_f32_16x16x128_f8f6f4 v[42:45], v[10:17], v[236:243], v[42:45]
	s_nop 3
	v_mfma_f32_16x16x128_f8f6f4 v[86:89], v[18:25], v[212:219], v[86:89]
	v_mfma_f32_16x16x128_f8f6f4 v[82:85], v[26:33], v[212:219], v[82:85]
	v_mfma_f32_16x16x128_f8f6f4 v[70:73], v[18:25], v[220:227], v[70:73]
	v_mfma_f32_16x16x128_f8f6f4 v[66:69], v[26:33], v[220:227], v[66:69]
	v_mfma_f32_16x16x128_f8f6f4 v[54:57], v[18:25], v[228:235], v[54:57]
	v_mfma_f32_16x16x128_f8f6f4 v[50:53], v[26:33], v[228:235], v[50:53]
	v_mfma_f32_16x16x128_f8f6f4 v[38:41], v[18:25], v[236:243], v[38:41]
	v_mfma_f32_16x16x128_f8f6f4 v[34:37], v[26:33], v[236:243], v[34:37]
	s_setprio 0
	s_barrier
	s_add_i32 s21, s21, 2
	s_add_u32 s5, s5, 0x10000
	s_addc_u32 s19, s19, 0
	s_add_u32 s26, s26, 0x10000
	s_addc_u32 s27, s27, 0
	s_cmp_gt_u32 s21, 13
	s_cbranch_scc0 .LBB0_372
	s_branch .Lfx_9967
.LBB0_372:
	ds_read_b128 v[18:21], v207
	ds_read_b128 v[22:25], v207 offset:1024
	ds_read_b128 v[26:29], v207 offset:2048
	ds_read_b128 v[30:33], v207 offset:3072
	ds_read_b128 v[2:5], v208
	ds_read_b128 v[6:9], v208 offset:1024
	ds_read_b128 v[10:13], v208 offset:2048
	ds_read_b128 v[14:17], v208 offset:3072
	s_add_u32 s28, s26, 0x8000
	s_addc_u32 s29, s27, 0
	s_cmp_eq_u32 s21, 12
	s_cselect_b32 s40, s22, s28
	s_cselect_b32 s41, s23, s29
	s_cselect_b32 s30, s24, s5
	s_cselect_b32 s31, s25, s19
	s_add_u32 s28, s40, 0x8000
	s_addc_u32 s29, s41, 0
	s_add_i32 m0, s46, 0xc000
	ds_read_b128 v[212:215], v209
	ds_read_b128 v[216:219], v209 offset:1024
	ds_read_b128 v[220:223], v209 offset:2048
	ds_read_b128 v[224:227], v209 offset:3072
	ds_read_b128 v[228:231], v209 offset:4096
	ds_read_b128 v[232:235], v209 offset:5120
	ds_read_b128 v[236:239], v209 offset:6144
	ds_read_b128 v[240:243], v209 offset:7168
	global_load_lds_dwordx4 v190, s[26:27]
	s_add_i32 m0, s46, 0xe000
	s_nop 0
	global_load_lds_dwordx4 v188, s[26:27]
	s_waitcnt vmcnt(8)
	s_waitcnt lgkmcnt(0)
	s_setprio 1
	v_mfma_f32_16x16x128_f8f6f4 v[158:161], v[18:25], v[212:219], v[158:161]
	v_mfma_f32_16x16x128_f8f6f4 v[154:157], v[26:33], v[212:219], v[154:157]
	v_mfma_f32_16x16x128_f8f6f4 v[142:145], v[18:25], v[220:227], v[142:145]
	v_mfma_f32_16x16x128_f8f6f4 v[138:141], v[26:33], v[220:227], v[138:141]
	v_mfma_f32_16x16x128_f8f6f4 v[126:129], v[18:25], v[228:235], v[126:129]
	v_mfma_f32_16x16x128_f8f6f4 v[122:125], v[26:33], v[228:235], v[122:125]
	v_mfma_f32_16x16x128_f8f6f4 v[110:113], v[18:25], v[236:243], v[110:113]
	v_mfma_f32_16x16x128_f8f6f4 v[106:109], v[26:33], v[236:243], v[106:109]
	s_nop 3
	v_mfma_f32_16x16x128_f8f6f4 v[150:153], v[2:9], v[212:219], v[150:153]
	v_mfma_f32_16x16x128_f8f6f4 v[146:149], v[10:17], v[212:219], v[146:149]
	v_mfma_f32_16x16x128_f8f6f4 v[134:137], v[2:9], v[220:227], v[134:137]
	v_mfma_f32_16x16x128_f8f6f4 v[130:133], v[10:17], v[220:227], v[130:133]
	v_mfma_f32_16x16x128_f8f6f4 v[118:121], v[2:9], v[228:235], v[118:121]
	v_mfma_f32_16x16x128_f8f6f4 v[114:117], v[10:17], v[228:235], v[114:117]
	v_mfma_f32_16x16x128_f8f6f4 v[102:105], v[2:9], v[236:243], v[102:105]
	v_mfma_f32_16x16x128_f8f6f4 v[98:101], v[10:17], v[236:243], v[98:101]
	s_setprio 0
	s_barrier
	s_add_i32 s67, s62, s45
	s_mov_b32 m0, s67
	ds_read_b128 v[212:215], v209 offset:16384
	ds_read_b128 v[216:219], v209 offset:17408
	ds_read_b128 v[220:223], v209 offset:18432
	ds_read_b128 v[224:227], v209 offset:19456
	ds_read_b128 v[228:231], v209 offset:20480
	ds_read_b128 v[232:235], v209 offset:21504
	ds_read_b128 v[236:239], v209 offset:22528
	ds_read_b128 v[240:243], v209 offset:23552
	global_load_lds_dwordx4 v164, s[30:31]
	s_add_i32 m0, s67, 0x2000
	s_add_i32 s67, s63, s45
	global_load_lds_dwordx4 v166, s[30:31]
	s_add_u32 s98, s30, s8
	s_addc_u32 s99, s31, s9
	s_mov_b32 m0, s67
	s_nop 0
	global_load_lds_dwordx4 v164, s[98:99]
	s_add_u32 s100, s30, s8
	s_addc_u32 s101, s31, s9
	s_add_i32 m0, s67, 0x2000
	s_nop 0
	global_load_lds_dwordx4 v166, s[100:101]
	s_mov_b32 m0, s46
	s_nop 0
	global_load_lds_dwordx4 v174, s[40:41]
	s_mov_b32 m0, s47
	s_nop 0
	global_load_lds_dwordx4 v176, s[40:41]
	s_waitcnt vmcnt(8)
	s_waitcnt lgkmcnt(0)
	s_setprio 1
	v_mfma_f32_16x16x128_f8f6f4 v[94:97], v[18:25], v[212:219], v[94:97]
	v_mfma_f32_16x16x128_f8f6f4 v[90:93], v[26:33], v[212:219], v[90:93]
	v_mfma_f32_16x16x128_f8f6f4 v[78:81], v[18:25], v[220:227], v[78:81]
	v_mfma_f32_16x16x128_f8f6f4 v[74:77], v[26:33], v[220:227], v[74:77]
	v_mfma_f32_16x16x128_f8f6f4 v[62:65], v[18:25], v[228:235], v[62:65]
	v_mfma_f32_16x16x128_f8f6f4 v[58:61], v[26:33], v[228:235], v[58:61]
	v_mfma_f32_16x16x128_f8f6f4 v[46:49], v[18:25], v[236:243], v[46:49]
	v_mfma_f32_16x16x128_f8f6f4 v[42:45], v[26:33], v[236:243], v[42:45]
	s_nop 3
	v_mfma_f32_16x16x128_f8f6f4 v[86:89], v[2:9], v[212:219], v[86:89]
	v_mfma_f32_16x16x128_f8f6f4 v[82:85], v[10:17], v[212:219], v[82:85]
	v_mfma_f32_16x16x128_f8f6f4 v[70:73], v[2:9], v[220:227], v[70:73]
	v_mfma_f32_16x16x128_f8f6f4 v[66:69], v[10:17], v[220:227], v[66:69]
	v_mfma_f32_16x16x128_f8f6f4 v[54:57], v[2:9], v[228:235], v[54:57]
	v_mfma_f32_16x16x128_f8f6f4 v[50:53], v[10:17], v[228:235], v[50:53]
	v_mfma_f32_16x16x128_f8f6f4 v[38:41], v[2:9], v[236:243], v[38:41]
	v_mfma_f32_16x16x128_f8f6f4 v[34:37], v[10:17], v[236:243], v[34:37]
	s_setprio 0
	s_barrier
; #define PG8_STAGE(bufoff, gbase, voff) do { _Pragma("unroll") for (int _i = 0; _i < 2; ++_i) \
;         __builtin_amdgcn_global_load_lds((const unsigned*)((const char*)(gbase) + (voff)[_i]), (PG8_LAS unsigned*)(lds + (bufoff) + ldsw + _i * 8192), 16, 0, 0); } while (0)
; #define PG8_WAIT_V(n) asm volatile("s_waitcnt vmcnt(" #n ")" ::: "memory")
; #define PG8_WAIT_L(n) asm volatile("s_waitcnt lgkmcnt(" #n ")" ::: "memory")
; #define PG8_BAR __builtin_amdgcn_s_barrier()
; #define PG8_SCHED __builtin_amdgcn_sched_barrier(0)
; template <class Epi, class Sched, bool ALIGN_EPI = true, bool F8 = false>
; __device__ __forceinline__ void gemm_phase(PG8_LAS unsigned char* lds, const Sched& S, const Epi& E) {
;     ...
;             const char* a1 = cA + (size_t)(t + 1) * kstep;
;             const char* a2 = last ? nA : cA + (size_t)(t + 2) * kstep; const char* b2 = last ? nB : cB + (size_t)(t + 2) * kstepB;
;             const char* a3 = a2 + kstep; const char* b3 = b2 + kstepB;
;             unsigned vA2[2][2];
; #pragma unroll
;             for (int h = 0; h < 2; ++h)
; #pragma unroll
;                 for (int i = 0; i < 2; ++i) { if constexpr (Sched::GATHER) vA2[h][i] = (last && has_next) ? voffAn[h][i] : voffA[h][i]; else vA2[h][i] = voffA[h][i]; }
;             PG8_LDB(B0, 0, 0); PG8_LDB(B1, 0, 1); PG8_SCHED; PG8_LDA(At, 0, 0); PG8_STAGE(PG8_SA(1, 1), a1, voffA[1]);
;             PG8_WAIT_V(8); PG8_WAIT_L(0); PG8_BAR; PG8_MMA(0, 0, At, B0); PG8_MMA(0, 1, At, B1); PG8_BAR; PG8_SCHED;
;             PG8_LDA(At, 0, 1); PG8_STAGE(PG8_SB(0, 0), b2, voffB[0]); PG8_STAGE(PG8_SB(0, 1), b2, voffB[1]); PG8_STAGE(PG8_SA(0, 0), a2, vA2[0]);
;             PG8_WAIT_V(8); PG8_WAIT_L(0); PG8_BAR; PG8_MMA(1, 0, At, B0); PG8_MMA(1, 1, At, B1); PG8_BAR; PG8_SCHED;
;             PG8_LDB(B0, 1, 0); PG8_LDB(B1, 1, 1); PG8_SCHED; PG8_LDA(At, 1, 0); PG8_STAGE(PG8_SA(0, 1), a2, vA2[1]);
;             PG8_WAIT_V(8); PG8_WAIT_L(0); PG8_BAR; PG8_MMA(0, 0, At, B0); PG8_MMA(0, 1, At, B1); PG8_BAR; PG8_SCHED;
;             PG8_LDA(At, 1, 1); PG8_STAGE(PG8_SB(1, 0), b3, voffB[0]); PG8_STAGE(PG8_SB(1, 1), b3, voffB[1]); PG8_STAGE(PG8_SA(1, 0), a3, vA2[0]);
;             PG8_WAIT_V(8); PG8_WAIT_L(0); PG8_BAR; PG8_MMA(1, 0, At, B0); PG8_MMA(1, 1, At, B1); PG8_BAR; PG8_SCHED;
	s_add_i32 s67, 0, 0x18000
	s_add_i32 s68, 0, 0x1c000
	v_add_u32_e32 v14, s67, v202
	v_add_u32_e32 v30, s68, v202
	ds_read_b128 v[2:5], v14
	ds_read_b128 v[6:9], v14 offset:1024
	ds_read_b128 v[10:13], v14 offset:2048
	ds_read_b128 v[14:17], v14 offset:3072
	ds_read_b128 v[18:21], v30
	ds_read_b128 v[22:25], v30 offset:1024
	ds_read_b128 v[26:29], v30 offset:2048
	ds_read_b128 v[30:33], v30 offset:3072
	s_mov_b32 m0, s48
	ds_read_b128 v[212:215], v209 offset:32768
	ds_read_b128 v[216:219], v209 offset:33792
	ds_read_b128 v[220:223], v209 offset:34816
	ds_read_b128 v[224:227], v209 offset:35840
	ds_read_b128 v[228:231], v209 offset:36864
	ds_read_b128 v[232:235], v209 offset:37888
	ds_read_b128 v[236:239], v209 offset:38912
	ds_read_b128 v[240:243], v209 offset:39936
	global_load_lds_dwordx4 v178, s[40:41]
	s_mov_b32 m0, s49
	s_nop 0
	global_load_lds_dwordx4 v180, s[40:41]
	s_waitcnt vmcnt(8)
	s_waitcnt lgkmcnt(0)
	s_setprio 1
	v_mfma_f32_16x16x128_f8f6f4 v[158:161], v[2:9], v[212:219], v[158:161]
	v_mfma_f32_16x16x128_f8f6f4 v[154:157], v[10:17], v[212:219], v[154:157]
	v_mfma_f32_16x16x128_f8f6f4 v[142:145], v[2:9], v[220:227], v[142:145]
	v_mfma_f32_16x16x128_f8f6f4 v[138:141], v[10:17], v[220:227], v[138:141]
	v_mfma_f32_16x16x128_f8f6f4 v[126:129], v[2:9], v[228:235], v[126:129]
	v_mfma_f32_16x16x128_f8f6f4 v[122:125], v[10:17], v[228:235], v[122:125]
	v_mfma_f32_16x16x128_f8f6f4 v[110:113], v[2:9], v[236:243], v[110:113]
	v_mfma_f32_16x16x128_f8f6f4 v[106:109], v[10:17], v[236:243], v[106:109]
	s_nop 3
	v_mfma_f32_16x16x128_f8f6f4 v[150:153], v[18:25], v[212:219], v[150:153]
	v_mfma_f32_16x16x128_f8f6f4 v[146:149], v[26:33], v[212:219], v[146:149]
	v_mfma_f32_16x16x128_f8f6f4 v[134:137], v[18:25], v[220:227], v[134:137]
	v_mfma_f32_16x16x128_f8f6f4 v[130:133], v[26:33], v[220:227], v[130:133]
	v_mfma_f32_16x16x128_f8f6f4 v[118:121], v[18:25], v[228:235], v[118:121]
	v_mfma_f32_16x16x128_f8f6f4 v[114:117], v[26:33], v[228:235], v[114:117]
	v_mfma_f32_16x16x128_f8f6f4 v[102:105], v[18:25], v[236:243], v[102:105]
	v_mfma_f32_16x16x128_f8f6f4 v[98:101], v[26:33], v[236:243], v[98:101]
	s_setprio 0
	s_barrier
	s_add_u32 s30, s30, 0x8000
	s_addc_u32 s31, s31, 0
	s_add_i32 s40, s67, s45
	s_mov_b32 m0, s40
	ds_read_b128 v[212:215], v209 offset:49152
	ds_read_b128 v[216:219], v209 offset:50176
	ds_read_b128 v[220:223], v209 offset:51200
	ds_read_b128 v[224:227], v209 offset:52224
	ds_read_b128 v[228:231], v209 offset:53248
	ds_read_b128 v[232:235], v209 offset:54272
	ds_read_b128 v[236:239], v209 offset:55296
	ds_read_b128 v[240:243], v209 offset:56320
	global_load_lds_dwordx4 v164, s[30:31]
	s_add_i32 m0, s40, 0x2000
	s_add_i32 s40, s68, s45
	global_load_lds_dwordx4 v166, s[30:31]
	s_mov_b32 m0, s40
	s_nop 0
	global_load_lds_dwordx4 v168, s[30:31]
	s_add_i32 m0, s40, 0x2000
	s_nop 0
	global_load_lds_dwordx4 v172, s[30:31]
	s_mov_b32 m0, s52
	s_nop 0
	global_load_lds_dwordx4 v174, s[28:29]
	s_mov_b32 m0, s53
	s_nop 0
	global_load_lds_dwordx4 v176, s[28:29]
	s_waitcnt vmcnt(8)
	s_waitcnt lgkmcnt(0)
	s_setprio 1
	v_mfma_f32_16x16x128_f8f6f4 v[94:97], v[2:9], v[212:219], v[94:97]
	v_mfma_f32_16x16x128_f8f6f4 v[90:93], v[10:17], v[212:219], v[90:93]
	v_mfma_f32_16x16x128_f8f6f4 v[78:81], v[2:9], v[220:227], v[78:81]
	v_mfma_f32_16x16x128_f8f6f4 v[74:77], v[10:17], v[220:227], v[74:77]
	v_mfma_f32_16x16x128_f8f6f4 v[62:65], v[2:9], v[228:235], v[62:65]
	v_mfma_f32_16x16x128_f8f6f4 v[58:61], v[10:17], v[228:235], v[58:61]
	v_mfma_f32_16x16x128_f8f6f4 v[46:49], v[2:9], v[236:243], v[46:49]
	v_mfma_f32_16x16x128_f8f6f4 v[42:45], v[10:17], v[236:243], v[42:45]
	s_nop 3
	v_mfma_f32_16x16x128_f8f6f4 v[86:89], v[18:25], v[212:219], v[86:89]
	v_mfma_f32_16x16x128_f8f6f4 v[82:85], v[26:33], v[212:219], v[82:85]
	v_mfma_f32_16x16x128_f8f6f4 v[70:73], v[18:25], v[220:227], v[70:73]
	v_mfma_f32_16x16x128_f8f6f4 v[66:69], v[26:33], v[220:227], v[66:69]
	v_mfma_f32_16x16x128_f8f6f4 v[54:57], v[18:25], v[228:235], v[54:57]
	v_mfma_f32_16x16x128_f8f6f4 v[50:53], v[26:33], v[228:235], v[50:53]
	v_mfma_f32_16x16x128_f8f6f4 v[38:41], v[18:25], v[236:243], v[38:41]
	v_mfma_f32_16x16x128_f8f6f4 v[34:37], v[26:33], v[236:243], v[34:37]
	s_setprio 0
	s_barrier
	s_add_i32 s21, s21, 2
	s_add_u32 s5, s5, 0x10000
	s_addc_u32 s19, s19, 0
	s_add_u32 s26, s26, 0x10000
	s_addc_u32 s27, s27, 0
	s_cmp_gt_u32 s21, 13
	s_cbranch_scc0 .LBB0_372
	s_branch .Lfx_9967
; #define PG8_STAGE(bufoff, gbase, voff) do { _Pragma("unroll") for (int _i = 0; _i < 2; ++_i) \
;         __builtin_amdgcn_global_load_lds((const unsigned*)((const char*)(gbase) + (voff)[_i]), (PG8_LAS unsigned*)(lds + (bufoff) + ldsw + _i * 8192), 16, 0, 0); } while (0)
; template <class Epi, class Sched, bool ALIGN_EPI = true, bool F8 = false>
; __device__ __forceinline__ void gemm_phase(PG8_LAS unsigned char* lds, const Sched& S, const Epi& E) {
;     ...
;         const bool has_next = S.next(ui + 1, nxt);
;         const char* nA = has_next ? nxt.A : cA; const char* nB = has_next ? nxt.B : cB;
;         const int nt = cur.nt;
; #pragma unroll 1
;         for (int t = 0; t < nt; t += 2) {
;             const bool last = (t == nt - 2);
;             if constexpr (Sched::GATHER) { if (last && has_next) S.a_off(nxt, Rs, Cs, voffAn); }
;             const char* a1 = cA + (size_t)(t + 1) * kstep;
;             const char* a2 = last ? nA : cA + (size_t)(t + 2) * kstep; const char* b2 = last ? nB : cB + (size_t)(t + 2) * kstepB;
;             const char* a3 = a2 + kstep; const char* b3 = b2 + kstepB;
;             unsigned vA2[2][2];
; #pragma unroll
;             for (int h = 0; h < 2; ++h)
; #pragma unroll
;                 for (int i = 0; i < 2; ++i) { if constexpr (Sched::GATHER) vA2[h][i] = (last && has_next) ? voffAn[h][i] : voffA[h][i]; else vA2[h][i] = voffA[h][i]; }
;             PG8_LDB(B0, 0, 0); PG8_LDB(B1, 0, 1); PG8_SCHED; PG8_LDA(At, 0, 0); PG8_STAGE(PG8_SA(1, 1), a1, voffA[1]);
;             PG8_WAIT_V(8); PG8_WAIT_L(0); PG8_BAR; PG8_MMA(0, 0, At, B0); PG8_MMA(0, 1, At, B1); PG8_BAR; PG8_SCHED;
;             PG8_LDA(At, 0, 1); PG8_STAGE(PG8_SB(0, 0), b2, voffB[0]); PG8_STAGE(PG8_SB(0, 1), b2, voffB[1]); PG8_STAGE(PG8_SA(0, 0), a2, vA2[0]);
;             PG8_WAIT_V(8); PG8_WAIT_L(0); PG8_BAR; PG8_MMA(1, 0, At, B0); PG8_MMA(1, 1, At, B1); PG8_BAR; PG8_SCHED;
;             PG8_LDB(B0, 1, 0); PG8_LDB(B1, 1, 1); PG8_SCHED; PG8_LDA(At, 1, 0); PG8_STAGE(PG8_SA(0, 1), a2, vA2[1]);
;             PG8_WAIT_V(8); PG8_WAIT_L(0); PG8_BAR; PG8_MMA(0, 0, At, B0); PG8_MMA(0, 1, At, B1); PG8_BAR; PG8_SCHED;
;             PG8_LDA(At, 1, 1); PG8_STAGE(PG8_SB(1, 0), b3, voffB[0]); PG8_STAGE(PG8_SB(1, 1), b3, voffB[1]); PG8_STAGE(PG8_SA(1, 0), a3, vA2[0]);
;             PG8_WAIT_V(8); PG8_WAIT_L(0); PG8_BAR; PG8_MMA(1, 0, At, B0); PG8_MMA(1, 1, At, B1); PG8_BAR; PG8_SCHED;
.Lh1e_9967:
.Lpk1_372:
	ds_read_b128 v[18:21], v207
	ds_read_b128 v[22:25], v207 offset:1024
	ds_read_b128 v[26:29], v207 offset:2048
	ds_read_b128 v[30:33], v207 offset:3072
	ds_read_b128 v[2:5], v208
	ds_read_b128 v[6:9], v208 offset:1024
	ds_read_b128 v[10:13], v208 offset:2048
	ds_read_b128 v[14:17], v208 offset:3072
	s_add_u32 s28, s26, 0x8000
	s_addc_u32 s29, s27, 0
	s_cmp_eq_u32 s21, 12
	s_cselect_b32 s40, s22, s28
	s_cselect_b32 s41, s23, s29
	s_cselect_b32 s30, s24, s5
	s_cselect_b32 s31, s25, s19
	s_add_u32 s28, s40, 0x8000
	s_addc_u32 s29, s41, 0
	s_add_i32 m0, s46, 0xc000
	ds_read_b128 v[212:215], v209
	ds_read_b128 v[216:219], v209 offset:1024
	ds_read_b128 v[220:223], v209 offset:2048
	ds_read_b128 v[224:227], v209 offset:3072
	ds_read_b128 v[228:231], v209 offset:4096
	ds_read_b128 v[232:235], v209 offset:5120
	ds_read_b128 v[236:239], v209 offset:6144
	ds_read_b128 v[240:243], v209 offset:7168
	global_load_lds_dwordx4 v190, s[26:27]
	s_add_i32 m0, s46, 0xe000
	s_nop 0
	global_load_lds_dwordx4 v188, s[26:27]
	s_waitcnt vmcnt(8)
	s_waitcnt lgkmcnt(0)
	s_barrier
	s_setprio 2
	v_mfma_f32_16x16x128_f8f6f4 v[158:161], v[18:25], v[212:219], 0
	v_mfma_f32_16x16x128_f8f6f4 v[154:157], v[26:33], v[212:219], 0
	v_mfma_f32_16x16x128_f8f6f4 v[142:145], v[18:25], v[220:227], 0
	v_mfma_f32_16x16x128_f8f6f4 v[138:141], v[26:33], v[220:227], 0
	v_mfma_f32_16x16x128_f8f6f4 v[126:129], v[18:25], v[228:235], 0
	v_mfma_f32_16x16x128_f8f6f4 v[122:125], v[26:33], v[228:235], 0
	v_mfma_f32_16x16x128_f8f6f4 v[110:113], v[18:25], v[236:243], 0
	v_mfma_f32_16x16x128_f8f6f4 v[106:109], v[26:33], v[236:243], 0
	s_nop 3
	v_mfma_f32_16x16x128_f8f6f4 v[150:153], v[2:9], v[212:219], 0
	v_mfma_f32_16x16x128_f8f6f4 v[146:149], v[10:17], v[212:219], 0
	v_mfma_f32_16x16x128_f8f6f4 v[134:137], v[2:9], v[220:227], 0
	v_mfma_f32_16x16x128_f8f6f4 v[130:133], v[10:17], v[220:227], 0
	v_mfma_f32_16x16x128_f8f6f4 v[118:121], v[2:9], v[228:235], 0
	v_mfma_f32_16x16x128_f8f6f4 v[114:117], v[10:17], v[228:235], 0
	v_mfma_f32_16x16x128_f8f6f4 v[102:105], v[2:9], v[236:243], 0
	v_mfma_f32_16x16x128_f8f6f4 v[98:101], v[10:17], v[236:243], 0
	s_setprio 0
	s_add_i32 s67, s62, s45
	s_mov_b32 m0, s67
	ds_read_b128 v[212:215], v209 offset:16384
	ds_read_b128 v[216:219], v209 offset:17408
	ds_read_b128 v[220:223], v209 offset:18432
	ds_read_b128 v[224:227], v209 offset:19456
	ds_read_b128 v[228:231], v209 offset:20480
	ds_read_b128 v[232:235], v209 offset:21504
	ds_read_b128 v[236:239], v209 offset:22528
	ds_read_b128 v[240:243], v209 offset:23552
	global_load_lds_dwordx4 v164, s[30:31]
	s_add_i32 m0, s67, 0x2000
	s_add_i32 s67, s63, s45
	global_load_lds_dwordx4 v166, s[30:31]
	s_add_u32 s98, s30, s8
	s_addc_u32 s99, s31, s9
	s_mov_b32 m0, s67
	s_nop 0
	global_load_lds_dwordx4 v164, s[98:99]
	s_add_u32 s100, s30, s8
	s_addc_u32 s101, s31, s9
	s_add_i32 m0, s67, 0x2000
	s_nop 0
	global_load_lds_dwordx4 v166, s[100:101]
	s_mov_b32 m0, s46
	s_nop 0
	global_load_lds_dwordx4 v174, s[40:41]
	s_mov_b32 m0, s47
	s_nop 0
	global_load_lds_dwordx4 v176, s[40:41]
	s_waitcnt vmcnt(8)
	s_waitcnt lgkmcnt(0)
	s_barrier
	s_setprio 2
	v_mfma_f32_16x16x128_f8f6f4 v[94:97], v[18:25], v[212:219], 0
	v_mfma_f32_16x16x128_f8f6f4 v[90:93], v[26:33], v[212:219], 0
	v_mfma_f32_16x16x128_f8f6f4 v[78:81], v[18:25], v[220:227], 0
	v_mfma_f32_16x16x128_f8f6f4 v[74:77], v[26:33], v[220:227], 0
	v_mfma_f32_16x16x128_f8f6f4 v[62:65], v[18:25], v[228:235], 0
	v_mfma_f32_16x16x128_f8f6f4 v[58:61], v[26:33], v[228:235], 0
	v_mfma_f32_16x16x128_f8f6f4 v[46:49], v[18:25], v[236:243], 0
	v_mfma_f32_16x16x128_f8f6f4 v[42:45], v[26:33], v[236:243], 0
	s_nop 3
	v_mfma_f32_16x16x128_f8f6f4 v[86:89], v[2:9], v[212:219], 0
	v_mfma_f32_16x16x128_f8f6f4 v[82:85], v[10:17], v[212:219], 0
	v_mfma_f32_16x16x128_f8f6f4 v[70:73], v[2:9], v[220:227], 0
	v_mfma_f32_16x16x128_f8f6f4 v[66:69], v[10:17], v[220:227], 0
	v_mfma_f32_16x16x128_f8f6f4 v[54:57], v[2:9], v[228:235], 0
	v_mfma_f32_16x16x128_f8f6f4 v[50:53], v[10:17], v[228:235], 0
	v_mfma_f32_16x16x128_f8f6f4 v[38:41], v[2:9], v[236:243], 0
	v_mfma_f32_16x16x128_f8f6f4 v[34:37], v[10:17], v[236:243], 0
	s_setprio 0
	s_add_i32 s67, 0, 0x18000
	s_add_i32 s68, 0, 0x1c000
	v_add_u32_e32 v14, s67, v202
	v_add_u32_e32 v30, s68, v202
	ds_read_b128 v[2:5], v14
	ds_read_b128 v[6:9], v14 offset:1024
	ds_read_b128 v[10:13], v14 offset:2048
	ds_read_b128 v[14:17], v14 offset:3072
	ds_read_b128 v[18:21], v30
	ds_read_b128 v[22:25], v30 offset:1024
	ds_read_b128 v[26:29], v30 offset:2048
	ds_read_b128 v[30:33], v30 offset:3072
	s_mov_b32 m0, s48
	ds_read_b128 v[212:215], v209 offset:32768
	ds_read_b128 v[216:219], v209 offset:33792
	ds_read_b128 v[220:223], v209 offset:34816
	ds_read_b128 v[224:227], v209 offset:35840
	ds_read_b128 v[228:231], v209 offset:36864
	ds_read_b128 v[232:235], v209 offset:37888
	ds_read_b128 v[236:239], v209 offset:38912
	ds_read_b128 v[240:243], v209 offset:39936
	global_load_lds_dwordx4 v178, s[40:41]
	s_mov_b32 m0, s49
	s_nop 0
	global_load_lds_dwordx4 v180, s[40:41]
	s_waitcnt vmcnt(8)
	s_waitcnt lgkmcnt(0)
	s_barrier
; #define PG8_STAGE(bufoff, gbase, voff) do { _Pragma("unroll") for (int _i = 0; _i < 2; ++_i) \
;         __builtin_amdgcn_global_load_lds((const unsigned*)((const char*)(gbase) + (voff)[_i]), (PG8_LAS unsigned*)(lds + (bufoff) + ldsw + _i * 8192), 16, 0, 0); } while (0)
; #define PG8_WAIT_V(n) asm volatile("s_waitcnt vmcnt(" #n ")" ::: "memory")
; #define PG8_WAIT_L(n) asm volatile("s_waitcnt lgkmcnt(" #n ")" ::: "memory")
; #define PG8_BAR __builtin_amdgcn_s_barrier()
; #define PG8_SCHED __builtin_amdgcn_sched_barrier(0)
; template <class Epi, class Sched, bool ALIGN_EPI = true, bool F8 = false>
; __device__ __forceinline__ void gemm_phase(PG8_LAS unsigned char* lds, const Sched& S, const Epi& E) {
;     ...
;             const char* a1 = cA + (size_t)(t + 1) * kstep;
;             const char* a2 = last ? nA : cA + (size_t)(t + 2) * kstep; const char* b2 = last ? nB : cB + (size_t)(t + 2) * kstepB;
;             const char* a3 = a2 + kstep; const char* b3 = b2 + kstepB;
;             unsigned vA2[2][2];
; #pragma unroll
;             for (int h = 0; h < 2; ++h)
; #pragma unroll
;                 for (int i = 0; i < 2; ++i) { if constexpr (Sched::GATHER) vA2[h][i] = (last && has_next) ? voffAn[h][i] : voffA[h][i]; else vA2[h][i] = voffA[h][i]; }
;             PG8_LDB(B0, 0, 0); PG8_LDB(B1, 0, 1); PG8_SCHED; PG8_LDA(At, 0, 0); PG8_STAGE(PG8_SA(1, 1), a1, voffA[1]);
;             PG8_WAIT_V(8); PG8_WAIT_L(0); PG8_BAR; PG8_MMA(0, 0, At, B0); PG8_MMA(0, 1, At, B1); PG8_BAR; PG8_SCHED;
;             PG8_LDA(At, 0, 1); PG8_STAGE(PG8_SB(0, 0), b2, voffB[0]); PG8_STAGE(PG8_SB(0, 1), b2, voffB[1]); PG8_STAGE(PG8_SA(0, 0), a2, vA2[0]);
;             PG8_WAIT_V(8); PG8_WAIT_L(0); PG8_BAR; PG8_MMA(1, 0, At, B0); PG8_MMA(1, 1, At, B1); PG8_BAR; PG8_SCHED;
;             PG8_LDB(B0, 1, 0); PG8_LDB(B1, 1, 1); PG8_SCHED; PG8_LDA(At, 1, 0); PG8_STAGE(PG8_SA(0, 1), a2, vA2[1]);
;             PG8_WAIT_V(8); PG8_WAIT_L(0); PG8_BAR; PG8_MMA(0, 0, At, B0); PG8_MMA(0, 1, At, B1); PG8_BAR; PG8_SCHED;
;             PG8_LDA(At, 1, 1); PG8_STAGE(PG8_SB(1, 0), b3, voffB[0]); PG8_STAGE(PG8_SB(1, 1), b3, voffB[1]); PG8_STAGE(PG8_SA(1, 0), a3, vA2[0]);
;             PG8_WAIT_V(8); PG8_WAIT_L(0); PG8_BAR; PG8_MMA(1, 0, At, B0); PG8_MMA(1, 1, At, B1); PG8_BAR; PG8_SCHED;
	s_setprio 2
	v_mfma_f32_16x16x128_f8f6f4 v[158:161], v[2:9], v[212:219], v[158:161]
	v_mfma_f32_16x16x128_f8f6f4 v[154:157], v[10:17], v[212:219], v[154:157]
	v_mfma_f32_16x16x128_f8f6f4 v[142:145], v[2:9], v[220:227], v[142:145]
	v_mfma_f32_16x16x128_f8f6f4 v[138:141], v[10:17], v[220:227], v[138:141]
	v_mfma_f32_16x16x128_f8f6f4 v[126:129], v[2:9], v[228:235], v[126:129]
	v_mfma_f32_16x16x128_f8f6f4 v[122:125], v[10:17], v[228:235], v[122:125]
	v_mfma_f32_16x16x128_f8f6f4 v[110:113], v[2:9], v[236:243], v[110:113]
	v_mfma_f32_16x16x128_f8f6f4 v[106:109], v[10:17], v[236:243], v[106:109]
	s_nop 3
	v_mfma_f32_16x16x128_f8f6f4 v[150:153], v[18:25], v[212:219], v[150:153]
	v_mfma_f32_16x16x128_f8f6f4 v[146:149], v[26:33], v[212:219], v[146:149]
	v_mfma_f32_16x16x128_f8f6f4 v[134:137], v[18:25], v[220:227], v[134:137]
	v_mfma_f32_16x16x128_f8f6f4 v[130:133], v[26:33], v[220:227], v[130:133]
	v_mfma_f32_16x16x128_f8f6f4 v[118:121], v[18:25], v[228:235], v[118:121]
	v_mfma_f32_16x16x128_f8f6f4 v[114:117], v[26:33], v[228:235], v[114:117]
	v_mfma_f32_16x16x128_f8f6f4 v[102:105], v[18:25], v[236:243], v[102:105]
	v_mfma_f32_16x16x128_f8f6f4 v[98:101], v[26:33], v[236:243], v[98:101]
	s_setprio 0
	s_add_u32 s30, s30, 0x8000
	s_addc_u32 s31, s31, 0
	s_add_i32 s40, s67, s45
	s_mov_b32 m0, s40
	ds_read_b128 v[212:215], v209 offset:49152
	ds_read_b128 v[216:219], v209 offset:50176
	ds_read_b128 v[220:223], v209 offset:51200
	ds_read_b128 v[224:227], v209 offset:52224
	ds_read_b128 v[228:231], v209 offset:53248
	ds_read_b128 v[232:235], v209 offset:54272
	ds_read_b128 v[236:239], v209 offset:55296
	ds_read_b128 v[240:243], v209 offset:56320
	global_load_lds_dwordx4 v164, s[30:31]
	s_add_i32 m0, s40, 0x2000
	s_add_i32 s40, s68, s45
	global_load_lds_dwordx4 v166, s[30:31]
	s_mov_b32 m0, s40
	s_nop 0
	global_load_lds_dwordx4 v168, s[30:31]
	s_add_i32 m0, s40, 0x2000
	s_nop 0
	global_load_lds_dwordx4 v172, s[30:31]
	s_mov_b32 m0, s52
	s_nop 0
	global_load_lds_dwordx4 v174, s[28:29]
	s_mov_b32 m0, s53
	s_nop 0
	global_load_lds_dwordx4 v176, s[28:29]
	s_waitcnt vmcnt(8)
	s_waitcnt lgkmcnt(0)
	s_barrier
	s_setprio 2
	v_mfma_f32_16x16x128_f8f6f4 v[94:97], v[2:9], v[212:219], v[94:97]
	v_mfma_f32_16x16x128_f8f6f4 v[90:93], v[10:17], v[212:219], v[90:93]
	v_mfma_f32_16x16x128_f8f6f4 v[78:81], v[2:9], v[220:227], v[78:81]
	v_mfma_f32_16x16x128_f8f6f4 v[74:77], v[10:17], v[220:227], v[74:77]
	v_mfma_f32_16x16x128_f8f6f4 v[62:65], v[2:9], v[228:235], v[62:65]
	v_mfma_f32_16x16x128_f8f6f4 v[58:61], v[10:17], v[228:235], v[58:61]
	v_mfma_f32_16x16x128_f8f6f4 v[46:49], v[2:9], v[236:243], v[46:49]
	v_mfma_f32_16x16x128_f8f6f4 v[42:45], v[10:17], v[236:243], v[42:45]
	s_nop 3
	v_mfma_f32_16x16x128_f8f6f4 v[86:89], v[18:25], v[212:219], v[86:89]
	v_mfma_f32_16x16x128_f8f6f4 v[82:85], v[26:33], v[212:219], v[82:85]
	v_mfma_f32_16x16x128_f8f6f4 v[70:73], v[18:25], v[220:227], v[70:73]
	v_mfma_f32_16x16x128_f8f6f4 v[66:69], v[26:33], v[220:227], v[66:69]
	v_mfma_f32_16x16x128_f8f6f4 v[54:57], v[18:25], v[228:235], v[54:57]
	v_mfma_f32_16x16x128_f8f6f4 v[50:53], v[26:33], v[228:235], v[50:53]
	v_mfma_f32_16x16x128_f8f6f4 v[38:41], v[18:25], v[236:243], v[38:41]
	v_mfma_f32_16x16x128_f8f6f4 v[34:37], v[26:33], v[236:243], v[34:37]
	s_setprio 0
	s_add_i32 s21, s21, 2
	s_add_u32 s5, s5, 0x10000
	s_addc_u32 s19, s19, 0
	s_add_u32 s26, s26, 0x10000
	s_addc_u32 s27, s27, 0
	s_cmp_gt_u32 s21, 13
	s_cbranch_scc0 .Lh1_372
	s_branch .Lfx_9967
.Lh1_372:
	ds_read_b128 v[18:21], v207
	ds_read_b128 v[22:25], v207 offset:1024
	ds_read_b128 v[26:29], v207 offset:2048
	ds_read_b128 v[30:33], v207 offset:3072
	ds_read_b128 v[2:5], v208
	ds_read_b128 v[6:9], v208 offset:1024
	ds_read_b128 v[10:13], v208 offset:2048
	ds_read_b128 v[14:17], v208 offset:3072
	s_add_u32 s28, s26, 0x8000
	s_addc_u32 s29, s27, 0
	s_cmp_eq_u32 s21, 12
	s_cselect_b32 s40, s22, s28
	s_cselect_b32 s41, s23, s29
	s_cselect_b32 s30, s24, s5
	s_cselect_b32 s31, s25, s19
	s_add_u32 s28, s40, 0x8000
	s_addc_u32 s29, s41, 0
	s_add_i32 m0, s46, 0xc000
	ds_read_b128 v[212:215], v209
	ds_read_b128 v[216:219], v209 offset:1024
	ds_read_b128 v[220:223], v209 offset:2048
	ds_read_b128 v[224:227], v209 offset:3072
	ds_read_b128 v[228:231], v209 offset:4096
	ds_read_b128 v[232:235], v209 offset:5120
	ds_read_b128 v[236:239], v209 offset:6144
	ds_read_b128 v[240:243], v209 offset:7168
	global_load_lds_dwordx4 v190, s[26:27]
	s_add_i32 m0, s46, 0xe000
	s_nop 0
	global_load_lds_dwordx4 v188, s[26:27]
	s_waitcnt vmcnt(8)
	s_waitcnt lgkmcnt(0)
	s_barrier
	s_setprio 2
	v_mfma_f32_16x16x128_f8f6f4 v[158:161], v[18:25], v[212:219], v[158:161]
	v_mfma_f32_16x16x128_f8f6f4 v[154:157], v[26:33], v[212:219], v[154:157]
	v_mfma_f32_16x16x128_f8f6f4 v[142:145], v[18:25], v[220:227], v[142:145]
	v_mfma_f32_16x16x128_f8f6f4 v[138:141], v[26:33], v[220:227], v[138:141]
	v_mfma_f32_16x16x128_f8f6f4 v[126:129], v[18:25], v[228:235], v[126:129]
	v_mfma_f32_16x16x128_f8f6f4 v[122:125], v[26:33], v[228:235], v[122:125]
	v_mfma_f32_16x16x128_f8f6f4 v[110:113], v[18:25], v[236:243], v[110:113]
	v_mfma_f32_16x16x128_f8f6f4 v[106:109], v[26:33], v[236:243], v[106:109]
	s_nop 3
	v_mfma_f32_16x16x128_f8f6f4 v[150:153], v[2:9], v[212:219], v[150:153]
	v_mfma_f32_16x16x128_f8f6f4 v[146:149], v[10:17], v[212:219], v[146:149]
	v_mfma_f32_16x16x128_f8f6f4 v[134:137], v[2:9], v[220:227], v[134:137]
	v_mfma_f32_16x16x128_f8f6f4 v[130:133], v[10:17], v[220:227], v[130:133]
	v_mfma_f32_16x16x128_f8f6f4 v[118:121], v[2:9], v[228:235], v[118:121]
	v_mfma_f32_16x16x128_f8f6f4 v[114:117], v[10:17], v[228:235], v[114:117]
	v_mfma_f32_16x16x128_f8f6f4 v[102:105], v[2:9], v[236:243], v[102:105]
	v_mfma_f32_16x16x128_f8f6f4 v[98:101], v[10:17], v[236:243], v[98:101]
	s_setprio 0
	s_add_i32 s67, s62, s45
	s_mov_b32 m0, s67
	ds_read_b128 v[212:215], v209 offset:16384
	ds_read_b128 v[216:219], v209 offset:17408
	ds_read_b128 v[220:223], v209 offset:18432
	ds_read_b128 v[224:227], v209 offset:19456
	ds_read_b128 v[228:231], v209 offset:20480
	ds_read_b128 v[232:235], v209 offset:21504
	ds_read_b128 v[236:239], v209 offset:22528
	ds_read_b128 v[240:243], v209 offset:23552
	global_load_lds_dwordx4 v164, s[30:31]
	s_add_i32 m0, s67, 0x2000
	s_add_i32 s67, s63, s45
	global_load_lds_dwordx4 v166, s[30:31]
	s_add_u32 s98, s30, s8
	s_addc_u32 s99, s31, s9
	s_mov_b32 m0, s67
	s_nop 0
	global_load_lds_dwordx4 v164, s[98:99]
	s_add_u32 s100, s30, s8
	s_addc_u32 s101, s31, s9
	s_add_i32 m0, s67, 0x2000
	s_nop 0
	global_load_lds_dwordx4 v166, s[100:101]
	s_mov_b32 m0, s46
	s_nop 0
	global_load_lds_dwordx4 v174, s[40:41]
	s_mov_b32 m0, s47
	s_nop 0
	global_load_lds_dwordx4 v176, s[40:41]
	s_waitcnt vmcnt(8)
	s_waitcnt lgkmcnt(0)
	s_barrier
; #define PG8_STAGE(bufoff, gbase, voff) do { _Pragma("unroll") for (int _i = 0; _i < 2; ++_i) \
;         __builtin_amdgcn_global_load_lds((const unsigned*)((const char*)(gbase) + (voff)[_i]), (PG8_LAS unsigned*)(lds + (bufoff) + ldsw + _i * 8192), 16, 0, 0); } while (0)
; #define PG8_WAIT_V(n) asm volatile("s_waitcnt vmcnt(" #n ")" ::: "memory")
; #define PG8_WAIT_L(n) asm volatile("s_waitcnt lgkmcnt(" #n ")" ::: "memory")
; #define PG8_BAR __builtin_amdgcn_s_barrier()
; #define PG8_SCHED __builtin_amdgcn_sched_barrier(0)
; template <class Epi, class Sched, bool ALIGN_EPI = true, bool F8 = false>
; __device__ __forceinline__ void gemm_phase(PG8_LAS unsigned char* lds, const Sched& S, const Epi& E) {
;     ...
;             const char* a1 = cA + (size_t)(t + 1) * kstep;
;             const char* a2 = last ? nA : cA + (size_t)(t + 2) * kstep; const char* b2 = last ? nB : cB + (size_t)(t + 2) * kstepB;
;             const char* a3 = a2 + kstep; const char* b3 = b2 + kstepB;
;             unsigned vA2[2][2];
; #pragma unroll
;             for (int h = 0; h < 2; ++h)
; #pragma unroll
;                 for (int i = 0; i < 2; ++i) { if constexpr (Sched::GATHER) vA2[h][i] = (last && has_next) ? voffAn[h][i] : voffA[h][i]; else vA2[h][i] = voffA[h][i]; }
;             PG8_LDB(B0, 0, 0); PG8_LDB(B1, 0, 1); PG8_SCHED; PG8_LDA(At, 0, 0); PG8_STAGE(PG8_SA(1, 1), a1, voffA[1]);
;             PG8_WAIT_V(8); PG8_WAIT_L(0); PG8_BAR; PG8_MMA(0, 0, At, B0); PG8_MMA(0, 1, At, B1); PG8_BAR; PG8_SCHED;
;             PG8_LDA(At, 0, 1); PG8_STAGE(PG8_SB(0, 0), b2, voffB[0]); PG8_STAGE(PG8_SB(0, 1), b2, voffB[1]); PG8_STAGE(PG8_SA(0, 0), a2, vA2[0]);
;             PG8_WAIT_V(8); PG8_WAIT_L(0); PG8_BAR; PG8_MMA(1, 0, At, B0); PG8_MMA(1, 1, At, B1); PG8_BAR; PG8_SCHED;
;             PG8_LDB(B0, 1, 0); PG8_LDB(B1, 1, 1); PG8_SCHED; PG8_LDA(At, 1, 0); PG8_STAGE(PG8_SA(0, 1), a2, vA2[1]);
;             PG8_WAIT_V(8); PG8_WAIT_L(0); PG8_BAR; PG8_MMA(0, 0, At, B0); PG8_MMA(0, 1, At, B1); PG8_BAR; PG8_SCHED;
;             PG8_LDA(At, 1, 1); PG8_STAGE(PG8_SB(1, 0), b3, voffB[0]); PG8_STAGE(PG8_SB(1, 1), b3, voffB[1]); PG8_STAGE(PG8_SA(1, 0), a3, vA2[0]);
;             PG8_WAIT_V(8); PG8_WAIT_L(0); PG8_BAR; PG8_MMA(1, 0, At, B0); PG8_MMA(1, 1, At, B1); PG8_BAR; PG8_SCHED;
	s_setprio 2
	v_mfma_f32_16x16x128_f8f6f4 v[94:97], v[18:25], v[212:219], v[94:97]
	v_mfma_f32_16x16x128_f8f6f4 v[90:93], v[26:33], v[212:219], v[90:93]
	v_mfma_f32_16x16x128_f8f6f4 v[78:81], v[18:25], v[220:227], v[78:81]
	v_mfma_f32_16x16x128_f8f6f4 v[74:77], v[26:33], v[220:227], v[74:77]
	v_mfma_f32_16x16x128_f8f6f4 v[62:65], v[18:25], v[228:235], v[62:65]
	v_mfma_f32_16x16x128_f8f6f4 v[58:61], v[26:33], v[228:235], v[58:61]
	v_mfma_f32_16x16x128_f8f6f4 v[46:49], v[18:25], v[236:243], v[46:49]
	v_mfma_f32_16x16x128_f8f6f4 v[42:45], v[26:33], v[236:243], v[42:45]
	s_nop 3
	v_mfma_f32_16x16x128_f8f6f4 v[86:89], v[2:9], v[212:219], v[86:89]
	v_mfma_f32_16x16x128_f8f6f4 v[82:85], v[10:17], v[212:219], v[82:85]
	v_mfma_f32_16x16x128_f8f6f4 v[70:73], v[2:9], v[220:227], v[70:73]
	v_mfma_f32_16x16x128_f8f6f4 v[66:69], v[10:17], v[220:227], v[66:69]
	v_mfma_f32_16x16x128_f8f6f4 v[54:57], v[2:9], v[228:235], v[54:57]
	v_mfma_f32_16x16x128_f8f6f4 v[50:53], v[10:17], v[228:235], v[50:53]
	v_mfma_f32_16x16x128_f8f6f4 v[38:41], v[2:9], v[236:243], v[38:41]
	v_mfma_f32_16x16x128_f8f6f4 v[34:37], v[10:17], v[236:243], v[34:37]
	s_setprio 0
	s_add_i32 s67, 0, 0x18000
	s_add_i32 s68, 0, 0x1c000
	v_add_u32_e32 v14, s67, v202
	v_add_u32_e32 v30, s68, v202
	ds_read_b128 v[2:5], v14
	ds_read_b128 v[6:9], v14 offset:1024
	ds_read_b128 v[10:13], v14 offset:2048
	ds_read_b128 v[14:17], v14 offset:3072
	ds_read_b128 v[18:21], v30
	ds_read_b128 v[22:25], v30 offset:1024
	ds_read_b128 v[26:29], v30 offset:2048
	ds_read_b128 v[30:33], v30 offset:3072
	s_mov_b32 m0, s48
	ds_read_b128 v[212:215], v209 offset:32768
	ds_read_b128 v[216:219], v209 offset:33792
	ds_read_b128 v[220:223], v209 offset:34816
	ds_read_b128 v[224:227], v209 offset:35840
	ds_read_b128 v[228:231], v209 offset:36864
	ds_read_b128 v[232:235], v209 offset:37888
	ds_read_b128 v[236:239], v209 offset:38912
	ds_read_b128 v[240:243], v209 offset:39936
	global_load_lds_dwordx4 v178, s[40:41]
	s_mov_b32 m0, s49
	s_nop 0
	global_load_lds_dwordx4 v180, s[40:41]
	s_waitcnt vmcnt(8)
	s_waitcnt lgkmcnt(0)
	s_barrier
	s_setprio 2
	v_mfma_f32_16x16x128_f8f6f4 v[158:161], v[2:9], v[212:219], v[158:161]
	v_mfma_f32_16x16x128_f8f6f4 v[154:157], v[10:17], v[212:219], v[154:157]
	v_mfma_f32_16x16x128_f8f6f4 v[142:145], v[2:9], v[220:227], v[142:145]
	v_mfma_f32_16x16x128_f8f6f4 v[138:141], v[10:17], v[220:227], v[138:141]
	v_mfma_f32_16x16x128_f8f6f4 v[126:129], v[2:9], v[228:235], v[126:129]
	v_mfma_f32_16x16x128_f8f6f4 v[122:125], v[10:17], v[228:235], v[122:125]
	v_mfma_f32_16x16x128_f8f6f4 v[110:113], v[2:9], v[236:243], v[110:113]
	v_mfma_f32_16x16x128_f8f6f4 v[106:109], v[10:17], v[236:243], v[106:109]
	s_nop 3
	v_mfma_f32_16x16x128_f8f6f4 v[150:153], v[18:25], v[212:219], v[150:153]
	v_mfma_f32_16x16x128_f8f6f4 v[146:149], v[26:33], v[212:219], v[146:149]
	v_mfma_f32_16x16x128_f8f6f4 v[134:137], v[18:25], v[220:227], v[134:137]
	v_mfma_f32_16x16x128_f8f6f4 v[130:133], v[26:33], v[220:227], v[130:133]
	v_mfma_f32_16x16x128_f8f6f4 v[118:121], v[18:25], v[228:235], v[118:121]
	v_mfma_f32_16x16x128_f8f6f4 v[114:117], v[26:33], v[228:235], v[114:117]
	v_mfma_f32_16x16x128_f8f6f4 v[102:105], v[18:25], v[236:243], v[102:105]
	v_mfma_f32_16x16x128_f8f6f4 v[98:101], v[26:33], v[236:243], v[98:101]
	s_setprio 0
	s_add_u32 s30, s30, 0x8000
	s_addc_u32 s31, s31, 0
	s_add_i32 s40, s67, s45
	s_mov_b32 m0, s40
	ds_read_b128 v[212:215], v209 offset:49152
	ds_read_b128 v[216:219], v209 offset:50176
	ds_read_b128 v[220:223], v209 offset:51200
	ds_read_b128 v[224:227], v209 offset:52224
	ds_read_b128 v[228:231], v209 offset:53248
	ds_read_b128 v[232:235], v209 offset:54272
	ds_read_b128 v[236:239], v209 offset:55296
	ds_read_b128 v[240:243], v209 offset:56320
	global_load_lds_dwordx4 v164, s[30:31]
	s_add_i32 m0, s40, 0x2000
	s_add_i32 s40, s68, s45
	global_load_lds_dwordx4 v166, s[30:31]
	s_mov_b32 m0, s40
	s_nop 0
	global_load_lds_dwordx4 v168, s[30:31]
	s_add_i32 m0, s40, 0x2000
	s_nop 0
	global_load_lds_dwordx4 v172, s[30:31]
	s_mov_b32 m0, s52
	s_nop 0
	global_load_lds_dwordx4 v174, s[28:29]
	s_mov_b32 m0, s53
	s_nop 0
	global_load_lds_dwordx4 v176, s[28:29]
	s_waitcnt vmcnt(8)
	s_waitcnt lgkmcnt(0)
	s_barrier
	s_setprio 2
	v_mfma_f32_16x16x128_f8f6f4 v[94:97], v[2:9], v[212:219], v[94:97]
	v_mfma_f32_16x16x128_f8f6f4 v[90:93], v[10:17], v[212:219], v[90:93]
	v_mfma_f32_16x16x128_f8f6f4 v[78:81], v[2:9], v[220:227], v[78:81]
	v_mfma_f32_16x16x128_f8f6f4 v[74:77], v[10:17], v[220:227], v[74:77]
	v_mfma_f32_16x16x128_f8f6f4 v[62:65], v[2:9], v[228:235], v[62:65]
	v_mfma_f32_16x16x128_f8f6f4 v[58:61], v[10:17], v[228:235], v[58:61]
	v_mfma_f32_16x16x128_f8f6f4 v[46:49], v[2:9], v[236:243], v[46:49]
	v_mfma_f32_16x16x128_f8f6f4 v[42:45], v[10:17], v[236:243], v[42:45]
	s_nop 3
	v_mfma_f32_16x16x128_f8f6f4 v[86:89], v[18:25], v[212:219], v[86:89]
	v_mfma_f32_16x16x128_f8f6f4 v[82:85], v[26:33], v[212:219], v[82:85]
	v_mfma_f32_16x16x128_f8f6f4 v[70:73], v[18:25], v[220:227], v[70:73]
	v_mfma_f32_16x16x128_f8f6f4 v[66:69], v[26:33], v[220:227], v[66:69]
	v_mfma_f32_16x16x128_f8f6f4 v[54:57], v[18:25], v[228:235], v[54:57]
	v_mfma_f32_16x16x128_f8f6f4 v[50:53], v[26:33], v[228:235], v[50:53]
	v_mfma_f32_16x16x128_f8f6f4 v[38:41], v[18:25], v[236:243], v[38:41]
	v_mfma_f32_16x16x128_f8f6f4 v[34:37], v[26:33], v[236:243], v[34:37]
	s_setprio 0
	s_add_i32 s21, s21, 2
	s_add_u32 s5, s5, 0x10000
	s_addc_u32 s19, s19, 0
	s_add_u32 s26, s26, 0x10000
	s_addc_u32 s27, s27, 0
	s_cmp_gt_u32 s21, 13
	s_cbranch_scc0 .Lh1_372

; #define PG8_STAGE(bufoff, gbase, voff) do { _Pragma("unroll") for (int _i = 0; _i < 2; ++_i) \
;         __builtin_amdgcn_global_load_lds((const unsigned*)((const char*)(gbase) + (voff)[_i]), (PG8_LAS unsigned*)(lds + (bufoff) + ldsw + _i * 8192), 16, 0, 0); } while (0)
; template <class Epi, class Sched, bool ALIGN_EPI = true, bool F8 = false>
; __device__ __forceinline__ void gemm_phase(PG8_LAS unsigned char* lds, const Sched& S, const Epi& E) {
;     ...
;         const bool has_next = S.next(ui + 1, nxt);
;         const char* nA = has_next ? nxt.A : cA; const char* nB = has_next ? nxt.B : cB;
;         const int nt = cur.nt;
; #pragma unroll 1
;         for (int t = 0; t < nt; t += 2) {
;             const bool last = (t == nt - 2);
;             if constexpr (Sched::GATHER) { if (last && has_next) S.a_off(nxt, Rs, Cs, voffAn); }
;             const char* a1 = cA + (size_t)(t + 1) * kstep;
;             const char* a2 = last ? nA : cA + (size_t)(t + 2) * kstep; const char* b2 = last ? nB : cB + (size_t)(t + 2) * kstepB;
;             const char* a3 = a2 + kstep; const char* b3 = b2 + kstepB;
;             unsigned vA2[2][2];
; #pragma unroll
;             for (int h = 0; h < 2; ++h)
; #pragma unroll
;                 for (int i = 0; i < 2; ++i) { if constexpr (Sched::GATHER) vA2[h][i] = (last && has_next) ? voffAn[h][i] : voffA[h][i]; else vA2[h][i] = voffA[h][i]; }
;             PG8_LDB(B0, 0, 0); PG8_LDB(B1, 0, 1); PG8_SCHED; PG8_LDA(At, 0, 0); PG8_STAGE(PG8_SA(1, 1), a1, voffA[1]);
;             PG8_WAIT_V(8); PG8_WAIT_L(0); PG8_BAR; PG8_MMA(0, 0, At, B0); PG8_MMA(0, 1, At, B1); PG8_BAR; PG8_SCHED;
;             PG8_LDA(At, 0, 1); PG8_STAGE(PG8_SB(0, 0), b2, voffB[0]); PG8_STAGE(PG8_SB(0, 1), b2, voffB[1]); PG8_STAGE(PG8_SA(0, 0), a2, vA2[0]);
;             PG8_WAIT_V(8); PG8_WAIT_L(0); PG8_BAR; PG8_MMA(1, 0, At, B0); PG8_MMA(1, 1, At, B1); PG8_BAR; PG8_SCHED;
;             PG8_LDB(B0, 1, 0); PG8_LDB(B1, 1, 1); PG8_SCHED; PG8_LDA(At, 1, 0); PG8_STAGE(PG8_SA(0, 1), a2, vA2[1]);
;             PG8_WAIT_V(8); PG8_WAIT_L(0); PG8_BAR; PG8_MMA(0, 0, At, B0); PG8_MMA(0, 1, At, B1); PG8_BAR; PG8_SCHED;
;             PG8_LDA(At, 1, 1); PG8_STAGE(PG8_SB(1, 0), b3, voffB[0]); PG8_STAGE(PG8_SB(1, 1), b3, voffB[1]); PG8_STAGE(PG8_SA(1, 0), a3, vA2[0]);
;             PG8_WAIT_V(8); PG8_WAIT_L(0); PG8_BAR; PG8_MMA(1, 0, At, B0); PG8_MMA(1, 1, At, B1); PG8_BAR; PG8_SCHED;
.Lpk0_428:
	ds_read_b128 v[18:21], v192
	ds_read_b128 v[22:25], v192 offset:1024
	ds_read_b128 v[26:29], v192 offset:2048
	ds_read_b128 v[30:33], v192 offset:3072
	ds_read_b128 v[2:5], v193
	ds_read_b128 v[6:9], v193 offset:1024
	ds_read_b128 v[10:13], v193 offset:2048
	ds_read_b128 v[14:17], v193 offset:3072
	s_add_u32 s26, s24, 0x8000
	s_addc_u32 s27, s25, 0
	s_cmp_eq_u32 s74, 12
	s_cselect_b32 s30, s20, s26
	s_cselect_b32 s31, s21, s27
	s_cselect_b32 s28, s22, s17
	s_cselect_b32 s29, s23, s19
	s_add_u32 s26, s30, 0x8000
	s_addc_u32 s27, s31, 0
	s_add_i32 m0, s48, 0xc000
	ds_read_b128 v[198:201], v194
	ds_read_b128 v[202:205], v194 offset:1024
	ds_read_b128 v[206:209], v194 offset:2048
	ds_read_b128 v[210:213], v194 offset:3072
	ds_read_b128 v[214:217], v194 offset:4096
	ds_read_b128 v[218:221], v194 offset:5120
	ds_read_b128 v[222:225], v194 offset:6144
	ds_read_b128 v[226:229], v194 offset:7168
	global_load_lds_dwordx4 v184, s[24:25]
	s_add_i32 m0, s48, 0xe000
	s_nop 0
	global_load_lds_dwordx4 v182, s[24:25]
	s_waitcnt vmcnt(8)
	s_waitcnt lgkmcnt(0)
	s_setprio 1
	v_mfma_f32_16x16x128_f8f6f4 v[158:161], v[18:25], v[198:205], 0
	v_mfma_f32_16x16x128_f8f6f4 v[154:157], v[26:33], v[198:205], 0
	v_mfma_f32_16x16x128_f8f6f4 v[142:145], v[18:25], v[206:213], 0
	v_mfma_f32_16x16x128_f8f6f4 v[138:141], v[26:33], v[206:213], 0
	v_mfma_f32_16x16x128_f8f6f4 v[126:129], v[18:25], v[214:221], 0
	v_mfma_f32_16x16x128_f8f6f4 v[122:125], v[26:33], v[214:221], 0
	v_mfma_f32_16x16x128_f8f6f4 v[110:113], v[18:25], v[222:229], 0
	v_mfma_f32_16x16x128_f8f6f4 v[106:109], v[26:33], v[222:229], 0
	s_nop 3
	v_mfma_f32_16x16x128_f8f6f4 v[150:153], v[2:9], v[198:205], 0
	v_mfma_f32_16x16x128_f8f6f4 v[146:149], v[10:17], v[198:205], 0
	v_mfma_f32_16x16x128_f8f6f4 v[134:137], v[2:9], v[206:213], 0
	v_mfma_f32_16x16x128_f8f6f4 v[130:133], v[10:17], v[206:213], 0
	v_mfma_f32_16x16x128_f8f6f4 v[118:121], v[2:9], v[214:221], 0
	v_mfma_f32_16x16x128_f8f6f4 v[114:117], v[10:17], v[214:221], 0
	v_mfma_f32_16x16x128_f8f6f4 v[102:105], v[2:9], v[222:229], 0
	v_mfma_f32_16x16x128_f8f6f4 v[98:101], v[10:17], v[222:229], 0
	s_setprio 0
	s_barrier
	s_add_i32 s75, s65, s47
	s_mov_b32 m0, s75
	ds_read_b128 v[198:201], v194 offset:16384
	ds_read_b128 v[202:205], v194 offset:17408
	ds_read_b128 v[206:209], v194 offset:18432
	ds_read_b128 v[210:213], v194 offset:19456
	ds_read_b128 v[214:217], v194 offset:20480
	ds_read_b128 v[218:221], v194 offset:21504
	ds_read_b128 v[222:225], v194 offset:22528
	ds_read_b128 v[226:229], v194 offset:23552
	global_load_lds_dwordx4 v164, s[28:29]
	s_add_i32 m0, s75, 0x2000
	s_add_i32 s75, s66, s47
	global_load_lds_dwordx4 v166, s[28:29]
	s_add_u32 s98, s28, s4
	s_addc_u32 s99, s29, s5
	s_mov_b32 m0, s75
	s_nop 0
	global_load_lds_dwordx4 v164, s[98:99]
	s_add_u32 s100, s28, s4
	s_addc_u32 s101, s29, s5
	s_add_i32 m0, s75, 0x2000
	s_nop 0
	global_load_lds_dwordx4 v166, s[100:101]
	s_mov_b32 m0, s48
	s_nop 0
	global_load_lds_dwordx4 v174, s[30:31]
	s_mov_b32 m0, s49
	s_nop 0
	global_load_lds_dwordx4 v176, s[30:31]
	s_waitcnt vmcnt(8)
	s_waitcnt lgkmcnt(0)
	s_setprio 1
	v_mfma_f32_16x16x128_f8f6f4 v[94:97], v[18:25], v[198:205], 0
	v_mfma_f32_16x16x128_f8f6f4 v[90:93], v[26:33], v[198:205], 0
	v_mfma_f32_16x16x128_f8f6f4 v[78:81], v[18:25], v[206:213], 0
	v_mfma_f32_16x16x128_f8f6f4 v[74:77], v[26:33], v[206:213], 0
	v_mfma_f32_16x16x128_f8f6f4 v[62:65], v[18:25], v[214:221], 0
	v_mfma_f32_16x16x128_f8f6f4 v[58:61], v[26:33], v[214:221], 0
	v_mfma_f32_16x16x128_f8f6f4 v[46:49], v[18:25], v[222:229], 0
	v_mfma_f32_16x16x128_f8f6f4 v[42:45], v[26:33], v[222:229], 0
	s_nop 3
	v_mfma_f32_16x16x128_f8f6f4 v[86:89], v[2:9], v[198:205], 0
	v_mfma_f32_16x16x128_f8f6f4 v[82:85], v[10:17], v[198:205], 0
	v_mfma_f32_16x16x128_f8f6f4 v[70:73], v[2:9], v[206:213], 0
	v_mfma_f32_16x16x128_f8f6f4 v[66:69], v[10:17], v[206:213], 0
	v_mfma_f32_16x16x128_f8f6f4 v[54:57], v[2:9], v[214:221], 0
	v_mfma_f32_16x16x128_f8f6f4 v[50:53], v[10:17], v[214:221], 0
	v_mfma_f32_16x16x128_f8f6f4 v[38:41], v[2:9], v[222:229], 0
	v_mfma_f32_16x16x128_f8f6f4 v[34:37], v[10:17], v[222:229], 0
	s_setprio 0
	s_barrier
	s_add_i32 s75, 0, 0x18000
	s_add_i32 s76, 0, 0x1c000
	v_add_u32_e32 v14, s75, v191
	v_add_u32_e32 v30, s76, v191
	ds_read_b128 v[2:5], v14
	ds_read_b128 v[6:9], v14 offset:1024
	ds_read_b128 v[10:13], v14 offset:2048
	ds_read_b128 v[14:17], v14 offset:3072
	ds_read_b128 v[18:21], v30
	ds_read_b128 v[22:25], v30 offset:1024
	ds_read_b128 v[26:29], v30 offset:2048
	ds_read_b128 v[30:33], v30 offset:3072
	s_mov_b32 m0, s50
	ds_read_b128 v[198:201], v194 offset:32768
	ds_read_b128 v[202:205], v194 offset:33792
	ds_read_b128 v[206:209], v194 offset:34816
	ds_read_b128 v[210:213], v194 offset:35840
	ds_read_b128 v[214:217], v194 offset:36864
	ds_read_b128 v[218:221], v194 offset:37888
	ds_read_b128 v[222:225], v194 offset:38912
	ds_read_b128 v[226:229], v194 offset:39936
	global_load_lds_dwordx4 v178, s[30:31]
	s_mov_b32 m0, s51
	s_nop 0
	global_load_lds_dwordx4 v180, s[30:31]
	s_waitcnt vmcnt(8)
	s_waitcnt lgkmcnt(0)
	s_setprio 1
	v_mfma_f32_16x16x128_f8f6f4 v[158:161], v[2:9], v[198:205], v[158:161]
	v_mfma_f32_16x16x128_f8f6f4 v[154:157], v[10:17], v[198:205], v[154:157]
	v_mfma_f32_16x16x128_f8f6f4 v[142:145], v[2:9], v[206:213], v[142:145]
	v_mfma_f32_16x16x128_f8f6f4 v[138:141], v[10:17], v[206:213], v[138:141]
	v_mfma_f32_16x16x128_f8f6f4 v[126:129], v[2:9], v[214:221], v[126:129]
	v_mfma_f32_16x16x128_f8f6f4 v[122:125], v[10:17], v[214:221], v[122:125]
	v_mfma_f32_16x16x128_f8f6f4 v[110:113], v[2:9], v[222:229], v[110:113]
	v_mfma_f32_16x16x128_f8f6f4 v[106:109], v[10:17], v[222:229], v[106:109]
	s_nop 3
	v_mfma_f32_16x16x128_f8f6f4 v[150:153], v[18:25], v[198:205], v[150:153]
	v_mfma_f32_16x16x128_f8f6f4 v[146:149], v[26:33], v[198:205], v[146:149]
	v_mfma_f32_16x16x128_f8f6f4 v[134:137], v[18:25], v[206:213], v[134:137]
	v_mfma_f32_16x16x128_f8f6f4 v[130:133], v[26:33], v[206:213], v[130:133]
	v_mfma_f32_16x16x128_f8f6f4 v[118:121], v[18:25], v[214:221], v[118:121]
	v_mfma_f32_16x16x128_f8f6f4 v[114:117], v[26:33], v[214:221], v[114:117]
	v_mfma_f32_16x16x128_f8f6f4 v[102:105], v[18:25], v[222:229], v[102:105]
	v_mfma_f32_16x16x128_f8f6f4 v[98:101], v[26:33], v[222:229], v[98:101]
	s_setprio 0
	s_barrier
; #define PG8_STAGE(bufoff, gbase, voff) do { _Pragma("unroll") for (int _i = 0; _i < 2; ++_i) \
;         __builtin_amdgcn_global_load_lds((const unsigned*)((const char*)(gbase) + (voff)[_i]), (PG8_LAS unsigned*)(lds + (bufoff) + ldsw + _i * 8192), 16, 0, 0); } while (0)
; #define PG8_WAIT_V(n) asm volatile("s_waitcnt vmcnt(" #n ")" ::: "memory")
; #define PG8_WAIT_L(n) asm volatile("s_waitcnt lgkmcnt(" #n ")" ::: "memory")
; #define PG8_BAR __builtin_amdgcn_s_barrier()
; #define PG8_SCHED __builtin_amdgcn_sched_barrier(0)
; template <class Epi, class Sched, bool ALIGN_EPI = true, bool F8 = false>
; __device__ __forceinline__ void gemm_phase(PG8_LAS unsigned char* lds, const Sched& S, const Epi& E) {
;     ...
;             PG8_LDB(B0, 0, 0); PG8_LDB(B1, 0, 1); PG8_SCHED; PG8_LDA(At, 0, 0); PG8_STAGE(PG8_SA(1, 1), a1, voffA[1]);
;             PG8_WAIT_V(8); PG8_WAIT_L(0); PG8_BAR; PG8_MMA(0, 0, At, B0); PG8_MMA(0, 1, At, B1); PG8_BAR; PG8_SCHED;
;             PG8_LDA(At, 0, 1); PG8_STAGE(PG8_SB(0, 0), b2, voffB[0]); PG8_STAGE(PG8_SB(0, 1), b2, voffB[1]); PG8_STAGE(PG8_SA(0, 0), a2, vA2[0]);
;             PG8_WAIT_V(8); PG8_WAIT_L(0); PG8_BAR; PG8_MMA(1, 0, At, B0); PG8_MMA(1, 1, At, B1); PG8_BAR; PG8_SCHED;
;             PG8_LDB(B0, 1, 0); PG8_LDB(B1, 1, 1); PG8_SCHED; PG8_LDA(At, 1, 0); PG8_STAGE(PG8_SA(0, 1), a2, vA2[1]);
;             PG8_WAIT_V(8); PG8_WAIT_L(0); PG8_BAR; PG8_MMA(0, 0, At, B0); PG8_MMA(0, 1, At, B1); PG8_BAR; PG8_SCHED;
;             PG8_LDA(At, 1, 1); PG8_STAGE(PG8_SB(1, 0), b3, voffB[0]); PG8_STAGE(PG8_SB(1, 1), b3, voffB[1]); PG8_STAGE(PG8_SA(1, 0), a3, vA2[0]);
;             PG8_WAIT_V(8); PG8_WAIT_L(0); PG8_BAR; PG8_MMA(1, 0, At, B0); PG8_MMA(1, 1, At, B1); PG8_BAR; PG8_SCHED;
	s_add_u32 s28, s28, 0x8000
	s_addc_u32 s29, s29, 0
	s_add_i32 s30, s75, s47
	s_mov_b32 m0, s30
	ds_read_b128 v[198:201], v194 offset:49152
	ds_read_b128 v[202:205], v194 offset:50176
	ds_read_b128 v[206:209], v194 offset:51200
	ds_read_b128 v[210:213], v194 offset:52224
	ds_read_b128 v[214:217], v194 offset:53248
	ds_read_b128 v[218:221], v194 offset:54272
	ds_read_b128 v[222:225], v194 offset:55296
	ds_read_b128 v[226:229], v194 offset:56320
	global_load_lds_dwordx4 v164, s[28:29]
	s_add_i32 m0, s30, 0x2000
	s_add_i32 s30, s76, s47
	global_load_lds_dwordx4 v166, s[28:29]
	s_mov_b32 m0, s30
	s_nop 0
	global_load_lds_dwordx4 v168, s[28:29]
	s_add_i32 m0, s30, 0x2000
	s_nop 0
	global_load_lds_dwordx4 v172, s[28:29]
	s_mov_b32 m0, s60
	s_nop 0
	global_load_lds_dwordx4 v174, s[26:27]
	s_mov_b32 m0, s61
	s_nop 0
	global_load_lds_dwordx4 v176, s[26:27]
	s_waitcnt vmcnt(8)
	s_waitcnt lgkmcnt(0)
	s_setprio 1
	v_mfma_f32_16x16x128_f8f6f4 v[94:97], v[2:9], v[198:205], v[94:97]
	v_mfma_f32_16x16x128_f8f6f4 v[90:93], v[10:17], v[198:205], v[90:93]
	v_mfma_f32_16x16x128_f8f6f4 v[78:81], v[2:9], v[206:213], v[78:81]
	v_mfma_f32_16x16x128_f8f6f4 v[74:77], v[10:17], v[206:213], v[74:77]
	v_mfma_f32_16x16x128_f8f6f4 v[62:65], v[2:9], v[214:221], v[62:65]
	v_mfma_f32_16x16x128_f8f6f4 v[58:61], v[10:17], v[214:221], v[58:61]
	v_mfma_f32_16x16x128_f8f6f4 v[46:49], v[2:9], v[222:229], v[46:49]
	v_mfma_f32_16x16x128_f8f6f4 v[42:45], v[10:17], v[222:229], v[42:45]
	s_nop 3
	v_mfma_f32_16x16x128_f8f6f4 v[86:89], v[18:25], v[198:205], v[86:89]
	v_mfma_f32_16x16x128_f8f6f4 v[82:85], v[26:33], v[198:205], v[82:85]
	v_mfma_f32_16x16x128_f8f6f4 v[70:73], v[18:25], v[206:213], v[70:73]
	v_mfma_f32_16x16x128_f8f6f4 v[66:69], v[26:33], v[206:213], v[66:69]
	v_mfma_f32_16x16x128_f8f6f4 v[54:57], v[18:25], v[214:221], v[54:57]
	v_mfma_f32_16x16x128_f8f6f4 v[50:53], v[26:33], v[214:221], v[50:53]
	v_mfma_f32_16x16x128_f8f6f4 v[38:41], v[18:25], v[222:229], v[38:41]
	v_mfma_f32_16x16x128_f8f6f4 v[34:37], v[26:33], v[222:229], v[34:37]
	s_setprio 0
	s_barrier
	s_add_i32 s74, s74, 2
	s_add_u32 s17, s17, 0x10000
	s_addc_u32 s19, s19, 0
	s_add_u32 s24, s24, 0x10000
	s_addc_u32 s25, s25, 0
	s_cmp_gt_u32 s74, 13
	s_cbranch_scc0 .LBB0_428
	s_branch .Lfx_11141
.LBB0_428:
	ds_read_b128 v[18:21], v192
	ds_read_b128 v[22:25], v192 offset:1024
	ds_read_b128 v[26:29], v192 offset:2048
	ds_read_b128 v[30:33], v192 offset:3072
	ds_read_b128 v[2:5], v193
	ds_read_b128 v[6:9], v193 offset:1024
	ds_read_b128 v[10:13], v193 offset:2048
	ds_read_b128 v[14:17], v193 offset:3072
	s_add_u32 s26, s24, 0x8000
	s_addc_u32 s27, s25, 0
	s_cmp_eq_u32 s74, 12
	s_cselect_b32 s30, s20, s26
	s_cselect_b32 s31, s21, s27
	s_cselect_b32 s28, s22, s17
	s_cselect_b32 s29, s23, s19
	s_add_u32 s26, s30, 0x8000
	s_addc_u32 s27, s31, 0
	s_add_i32 m0, s48, 0xc000
	ds_read_b128 v[198:201], v194
	ds_read_b128 v[202:205], v194 offset:1024
	ds_read_b128 v[206:209], v194 offset:2048
	ds_read_b128 v[210:213], v194 offset:3072
	ds_read_b128 v[214:217], v194 offset:4096
	ds_read_b128 v[218:221], v194 offset:5120
	ds_read_b128 v[222:225], v194 offset:6144
	ds_read_b128 v[226:229], v194 offset:7168
	global_load_lds_dwordx4 v184, s[24:25]
	s_add_i32 m0, s48, 0xe000
	s_nop 0
	global_load_lds_dwordx4 v182, s[24:25]
	s_waitcnt vmcnt(8)
	s_waitcnt lgkmcnt(0)
	s_setprio 1
	v_mfma_f32_16x16x128_f8f6f4 v[158:161], v[18:25], v[198:205], v[158:161]
	v_mfma_f32_16x16x128_f8f6f4 v[154:157], v[26:33], v[198:205], v[154:157]
	v_mfma_f32_16x16x128_f8f6f4 v[142:145], v[18:25], v[206:213], v[142:145]
	v_mfma_f32_16x16x128_f8f6f4 v[138:141], v[26:33], v[206:213], v[138:141]
	v_mfma_f32_16x16x128_f8f6f4 v[126:129], v[18:25], v[214:221], v[126:129]
	v_mfma_f32_16x16x128_f8f6f4 v[122:125], v[26:33], v[214:221], v[122:125]
	v_mfma_f32_16x16x128_f8f6f4 v[110:113], v[18:25], v[222:229], v[110:113]
	v_mfma_f32_16x16x128_f8f6f4 v[106:109], v[26:33], v[222:229], v[106:109]
	s_nop 3
	v_mfma_f32_16x16x128_f8f6f4 v[150:153], v[2:9], v[198:205], v[150:153]
	v_mfma_f32_16x16x128_f8f6f4 v[146:149], v[10:17], v[198:205], v[146:149]
	v_mfma_f32_16x16x128_f8f6f4 v[134:137], v[2:9], v[206:213], v[134:137]
	v_mfma_f32_16x16x128_f8f6f4 v[130:133], v[10:17], v[206:213], v[130:133]
	v_mfma_f32_16x16x128_f8f6f4 v[118:121], v[2:9], v[214:221], v[118:121]
	v_mfma_f32_16x16x128_f8f6f4 v[114:117], v[10:17], v[214:221], v[114:117]
	v_mfma_f32_16x16x128_f8f6f4 v[102:105], v[2:9], v[222:229], v[102:105]
	v_mfma_f32_16x16x128_f8f6f4 v[98:101], v[10:17], v[222:229], v[98:101]
	s_setprio 0
	s_barrier
	s_add_i32 s75, s65, s47
	s_mov_b32 m0, s75
	ds_read_b128 v[198:201], v194 offset:16384
	ds_read_b128 v[202:205], v194 offset:17408
	ds_read_b128 v[206:209], v194 offset:18432
	ds_read_b128 v[210:213], v194 offset:19456
	ds_read_b128 v[214:217], v194 offset:20480
	ds_read_b128 v[218:221], v194 offset:21504
	ds_read_b128 v[222:225], v194 offset:22528
	ds_read_b128 v[226:229], v194 offset:23552
	global_load_lds_dwordx4 v164, s[28:29]
	s_add_i32 m0, s75, 0x2000
	s_add_i32 s75, s66, s47
	global_load_lds_dwordx4 v166, s[28:29]
	s_add_u32 s98, s28, s4
	s_addc_u32 s99, s29, s5
	s_mov_b32 m0, s75
	s_nop 0
	global_load_lds_dwordx4 v164, s[98:99]
	s_add_u32 s100, s28, s4
	s_addc_u32 s101, s29, s5
	s_add_i32 m0, s75, 0x2000
	s_nop 0
	global_load_lds_dwordx4 v166, s[100:101]
	s_mov_b32 m0, s48
	s_nop 0
	global_load_lds_dwordx4 v174, s[30:31]
	s_mov_b32 m0, s49
	s_nop 0
	global_load_lds_dwordx4 v176, s[30:31]
	s_waitcnt vmcnt(8)
	s_waitcnt lgkmcnt(0)
	s_setprio 1
	v_mfma_f32_16x16x128_f8f6f4 v[94:97], v[18:25], v[198:205], v[94:97]
	v_mfma_f32_16x16x128_f8f6f4 v[90:93], v[26:33], v[198:205], v[90:93]
	v_mfma_f32_16x16x128_f8f6f4 v[78:81], v[18:25], v[206:213], v[78:81]
	v_mfma_f32_16x16x128_f8f6f4 v[74:77], v[26:33], v[206:213], v[74:77]
	v_mfma_f32_16x16x128_f8f6f4 v[62:65], v[18:25], v[214:221], v[62:65]
	v_mfma_f32_16x16x128_f8f6f4 v[58:61], v[26:33], v[214:221], v[58:61]
	v_mfma_f32_16x16x128_f8f6f4 v[46:49], v[18:25], v[222:229], v[46:49]
	v_mfma_f32_16x16x128_f8f6f4 v[42:45], v[26:33], v[222:229], v[42:45]
	s_nop 3
	v_mfma_f32_16x16x128_f8f6f4 v[86:89], v[2:9], v[198:205], v[86:89]
	v_mfma_f32_16x16x128_f8f6f4 v[82:85], v[10:17], v[198:205], v[82:85]
	v_mfma_f32_16x16x128_f8f6f4 v[70:73], v[2:9], v[206:213], v[70:73]
	v_mfma_f32_16x16x128_f8f6f4 v[66:69], v[10:17], v[206:213], v[66:69]
	v_mfma_f32_16x16x128_f8f6f4 v[54:57], v[2:9], v[214:221], v[54:57]
	v_mfma_f32_16x16x128_f8f6f4 v[50:53], v[10:17], v[214:221], v[50:53]
	v_mfma_f32_16x16x128_f8f6f4 v[38:41], v[2:9], v[222:229], v[38:41]
	v_mfma_f32_16x16x128_f8f6f4 v[34:37], v[10:17], v[222:229], v[34:37]
	s_setprio 0
	s_barrier
; #define PG8_STAGE(bufoff, gbase, voff) do { _Pragma("unroll") for (int _i = 0; _i < 2; ++_i) \
;         __builtin_amdgcn_global_load_lds((const unsigned*)((const char*)(gbase) + (voff)[_i]), (PG8_LAS unsigned*)(lds + (bufoff) + ldsw + _i * 8192), 16, 0, 0); } while (0)
; #define PG8_WAIT_V(n) asm volatile("s_waitcnt vmcnt(" #n ")" ::: "memory")
; #define PG8_WAIT_L(n) asm volatile("s_waitcnt lgkmcnt(" #n ")" ::: "memory")
; #define PG8_BAR __builtin_amdgcn_s_barrier()
; #define PG8_SCHED __builtin_amdgcn_sched_barrier(0)
; template <class Epi, class Sched, bool ALIGN_EPI = true, bool F8 = false>
; __device__ __forceinline__ void gemm_phase(PG8_LAS unsigned char* lds, const Sched& S, const Epi& E) {
;     ...
;             PG8_LDB(B0, 1, 0); PG8_LDB(B1, 1, 1); PG8_SCHED; PG8_LDA(At, 1, 0); PG8_STAGE(PG8_SA(0, 1), a2, vA2[1]);
;             PG8_WAIT_V(8); PG8_WAIT_L(0); PG8_BAR; PG8_MMA(0, 0, At, B0); PG8_MMA(0, 1, At, B1); PG8_BAR; PG8_SCHED;
;             PG8_LDA(At, 1, 1); PG8_STAGE(PG8_SB(1, 0), b3, voffB[0]); PG8_STAGE(PG8_SB(1, 1), b3, voffB[1]); PG8_STAGE(PG8_SA(1, 0), a3, vA2[0]);
;             PG8_WAIT_V(8); PG8_WAIT_L(0); PG8_BAR; PG8_MMA(1, 0, At, B0); PG8_MMA(1, 1, At, B1); PG8_BAR; PG8_SCHED;
	s_add_i32 s75, 0, 0x18000
	s_add_i32 s76, 0, 0x1c000
	v_add_u32_e32 v14, s75, v191
	v_add_u32_e32 v30, s76, v191
	ds_read_b128 v[2:5], v14
	ds_read_b128 v[6:9], v14 offset:1024
	ds_read_b128 v[10:13], v14 offset:2048
	ds_read_b128 v[14:17], v14 offset:3072
	ds_read_b128 v[18:21], v30
	ds_read_b128 v[22:25], v30 offset:1024
	ds_read_b128 v[26:29], v30 offset:2048
	ds_read_b128 v[30:33], v30 offset:3072
	s_mov_b32 m0, s50
	ds_read_b128 v[198:201], v194 offset:32768
	ds_read_b128 v[202:205], v194 offset:33792
	ds_read_b128 v[206:209], v194 offset:34816
	ds_read_b128 v[210:213], v194 offset:35840
	ds_read_b128 v[214:217], v194 offset:36864
	ds_read_b128 v[218:221], v194 offset:37888
	ds_read_b128 v[222:225], v194 offset:38912
	ds_read_b128 v[226:229], v194 offset:39936
	global_load_lds_dwordx4 v178, s[30:31]
	s_mov_b32 m0, s51
	s_nop 0
	global_load_lds_dwordx4 v180, s[30:31]
	s_waitcnt vmcnt(8)
	s_waitcnt lgkmcnt(0)
	s_setprio 1
	v_mfma_f32_16x16x128_f8f6f4 v[158:161], v[2:9], v[198:205], v[158:161]
	v_mfma_f32_16x16x128_f8f6f4 v[154:157], v[10:17], v[198:205], v[154:157]
	v_mfma_f32_16x16x128_f8f6f4 v[142:145], v[2:9], v[206:213], v[142:145]
	v_mfma_f32_16x16x128_f8f6f4 v[138:141], v[10:17], v[206:213], v[138:141]
	v_mfma_f32_16x16x128_f8f6f4 v[126:129], v[2:9], v[214:221], v[126:129]
	v_mfma_f32_16x16x128_f8f6f4 v[122:125], v[10:17], v[214:221], v[122:125]
	v_mfma_f32_16x16x128_f8f6f4 v[110:113], v[2:9], v[222:229], v[110:113]
	v_mfma_f32_16x16x128_f8f6f4 v[106:109], v[10:17], v[222:229], v[106:109]
	s_nop 3
	v_mfma_f32_16x16x128_f8f6f4 v[150:153], v[18:25], v[198:205], v[150:153]
	v_mfma_f32_16x16x128_f8f6f4 v[146:149], v[26:33], v[198:205], v[146:149]
	v_mfma_f32_16x16x128_f8f6f4 v[134:137], v[18:25], v[206:213], v[134:137]
	v_mfma_f32_16x16x128_f8f6f4 v[130:133], v[26:33], v[206:213], v[130:133]
	v_mfma_f32_16x16x128_f8f6f4 v[118:121], v[18:25], v[214:221], v[118:121]
	v_mfma_f32_16x16x128_f8f6f4 v[114:117], v[26:33], v[214:221], v[114:117]
	v_mfma_f32_16x16x128_f8f6f4 v[102:105], v[18:25], v[222:229], v[102:105]
	v_mfma_f32_16x16x128_f8f6f4 v[98:101], v[26:33], v[222:229], v[98:101]
	s_setprio 0
	s_barrier
	s_add_u32 s28, s28, 0x8000
	s_addc_u32 s29, s29, 0
	s_add_i32 s30, s75, s47
	s_mov_b32 m0, s30
	ds_read_b128 v[198:201], v194 offset:49152
	ds_read_b128 v[202:205], v194 offset:50176
	ds_read_b128 v[206:209], v194 offset:51200
	ds_read_b128 v[210:213], v194 offset:52224
	ds_read_b128 v[214:217], v194 offset:53248
	ds_read_b128 v[218:221], v194 offset:54272
	ds_read_b128 v[222:225], v194 offset:55296
	ds_read_b128 v[226:229], v194 offset:56320
	global_load_lds_dwordx4 v164, s[28:29]
	s_add_i32 m0, s30, 0x2000
	s_add_i32 s30, s76, s47
	global_load_lds_dwordx4 v166, s[28:29]
	s_mov_b32 m0, s30
	s_nop 0
	global_load_lds_dwordx4 v168, s[28:29]
	s_add_i32 m0, s30, 0x2000
	s_nop 0
	global_load_lds_dwordx4 v172, s[28:29]
	s_mov_b32 m0, s60
	s_nop 0
	global_load_lds_dwordx4 v174, s[26:27]
	s_mov_b32 m0, s61
	s_nop 0
	global_load_lds_dwordx4 v176, s[26:27]
	s_waitcnt vmcnt(8)
	s_waitcnt lgkmcnt(0)
	s_setprio 1
	v_mfma_f32_16x16x128_f8f6f4 v[94:97], v[2:9], v[198:205], v[94:97]
	v_mfma_f32_16x16x128_f8f6f4 v[90:93], v[10:17], v[198:205], v[90:93]
	v_mfma_f32_16x16x128_f8f6f4 v[78:81], v[2:9], v[206:213], v[78:81]
	v_mfma_f32_16x16x128_f8f6f4 v[74:77], v[10:17], v[206:213], v[74:77]
	v_mfma_f32_16x16x128_f8f6f4 v[62:65], v[2:9], v[214:221], v[62:65]
	v_mfma_f32_16x16x128_f8f6f4 v[58:61], v[10:17], v[214:221], v[58:61]
	v_mfma_f32_16x16x128_f8f6f4 v[46:49], v[2:9], v[222:229], v[46:49]
	v_mfma_f32_16x16x128_f8f6f4 v[42:45], v[10:17], v[222:229], v[42:45]
	s_nop 3
	v_mfma_f32_16x16x128_f8f6f4 v[86:89], v[18:25], v[198:205], v[86:89]
	v_mfma_f32_16x16x128_f8f6f4 v[82:85], v[26:33], v[198:205], v[82:85]
	v_mfma_f32_16x16x128_f8f6f4 v[70:73], v[18:25], v[206:213], v[70:73]
	v_mfma_f32_16x16x128_f8f6f4 v[66:69], v[26:33], v[206:213], v[66:69]
	v_mfma_f32_16x16x128_f8f6f4 v[54:57], v[18:25], v[214:221], v[54:57]
	v_mfma_f32_16x16x128_f8f6f4 v[50:53], v[26:33], v[214:221], v[50:53]
	v_mfma_f32_16x16x128_f8f6f4 v[38:41], v[18:25], v[222:229], v[38:41]
	v_mfma_f32_16x16x128_f8f6f4 v[34:37], v[26:33], v[222:229], v[34:37]
	s_setprio 0
	s_barrier
	s_add_i32 s74, s74, 2
	s_add_u32 s17, s17, 0x10000
	s_addc_u32 s19, s19, 0
	s_add_u32 s24, s24, 0x10000
	s_addc_u32 s25, s25, 0
	s_cmp_gt_u32 s74, 13
	s_cbranch_scc0 .LBB0_428
	s_branch .Lfx_11141
; #define PG8_STAGE(bufoff, gbase, voff) do { _Pragma("unroll") for (int _i = 0; _i < 2; ++_i) \
;         __builtin_amdgcn_global_load_lds((const unsigned*)((const char*)(gbase) + (voff)[_i]), (PG8_LAS unsigned*)(lds + (bufoff) + ldsw + _i * 8192), 16, 0, 0); } while (0)
; #define PG8_WAIT_V(n) asm volatile("s_waitcnt vmcnt(" #n ")" ::: "memory")
; #define PG8_WAIT_L(n) asm volatile("s_waitcnt lgkmcnt(" #n ")" ::: "memory")
; #define PG8_BAR __builtin_amdgcn_s_barrier()
; #define PG8_SCHED __builtin_amdgcn_sched_barrier(0)
; template <class Epi, class Sched, bool ALIGN_EPI = true, bool F8 = false>
; __device__ __forceinline__ void gemm_phase(PG8_LAS unsigned char* lds, const Sched& S, const Epi& E) {
;     ...
;             PG8_LDB(B0, 0, 0); PG8_LDB(B1, 0, 1); PG8_SCHED; PG8_LDA(At, 0, 0); PG8_STAGE(PG8_SA(1, 1), a1, voffA[1]);
;             PG8_WAIT_V(8); PG8_WAIT_L(0); PG8_BAR; PG8_MMA(0, 0, At, B0); PG8_MMA(0, 1, At, B1); PG8_BAR; PG8_SCHED;
;             PG8_LDA(At, 0, 1); PG8_STAGE(PG8_SB(0, 0), b2, voffB[0]); PG8_STAGE(PG8_SB(0, 1), b2, voffB[1]); PG8_STAGE(PG8_SA(0, 0), a2, vA2[0]);
;             PG8_WAIT_V(8); PG8_WAIT_L(0); PG8_BAR; PG8_MMA(1, 0, At, B0); PG8_MMA(1, 1, At, B1); PG8_BAR; PG8_SCHED;
;             PG8_LDB(B0, 1, 0); PG8_LDB(B1, 1, 1); PG8_SCHED; PG8_LDA(At, 1, 0); PG8_STAGE(PG8_SA(0, 1), a2, vA2[1]);
;             PG8_WAIT_V(8); PG8_WAIT_L(0); PG8_BAR; PG8_MMA(0, 0, At, B0); PG8_MMA(0, 1, At, B1); PG8_BAR; PG8_SCHED;
.Lh1e_11141:
.Lpk1_428:
	ds_read_b128 v[18:21], v192
	ds_read_b128 v[22:25], v192 offset:1024
	ds_read_b128 v[26:29], v192 offset:2048
	ds_read_b128 v[30:33], v192 offset:3072
	ds_read_b128 v[2:5], v193
	ds_read_b128 v[6:9], v193 offset:1024
	ds_read_b128 v[10:13], v193 offset:2048
	ds_read_b128 v[14:17], v193 offset:3072
	s_add_u32 s26, s24, 0x8000
	s_addc_u32 s27, s25, 0
	s_cmp_eq_u32 s74, 12
	s_cselect_b32 s30, s20, s26
	s_cselect_b32 s31, s21, s27
	s_cselect_b32 s28, s22, s17
	s_cselect_b32 s29, s23, s19
	s_add_u32 s26, s30, 0x8000
	s_addc_u32 s27, s31, 0
	s_add_i32 m0, s48, 0xc000
	ds_read_b128 v[198:201], v194
	ds_read_b128 v[202:205], v194 offset:1024
	ds_read_b128 v[206:209], v194 offset:2048
	ds_read_b128 v[210:213], v194 offset:3072
	ds_read_b128 v[214:217], v194 offset:4096
	ds_read_b128 v[218:221], v194 offset:5120
	ds_read_b128 v[222:225], v194 offset:6144
	ds_read_b128 v[226:229], v194 offset:7168
	global_load_lds_dwordx4 v184, s[24:25]
	s_add_i32 m0, s48, 0xe000
	s_nop 0
	global_load_lds_dwordx4 v182, s[24:25]
	s_waitcnt vmcnt(8)
	s_waitcnt lgkmcnt(0)
	s_barrier
	s_setprio 2
	v_mfma_f32_16x16x128_f8f6f4 v[158:161], v[18:25], v[198:205], 0
	v_mfma_f32_16x16x128_f8f6f4 v[154:157], v[26:33], v[198:205], 0
	v_mfma_f32_16x16x128_f8f6f4 v[142:145], v[18:25], v[206:213], 0
	v_mfma_f32_16x16x128_f8f6f4 v[138:141], v[26:33], v[206:213], 0
	v_mfma_f32_16x16x128_f8f6f4 v[126:129], v[18:25], v[214:221], 0
	v_mfma_f32_16x16x128_f8f6f4 v[122:125], v[26:33], v[214:221], 0
	v_mfma_f32_16x16x128_f8f6f4 v[110:113], v[18:25], v[222:229], 0
	v_mfma_f32_16x16x128_f8f6f4 v[106:109], v[26:33], v[222:229], 0
	s_nop 3
	v_mfma_f32_16x16x128_f8f6f4 v[150:153], v[2:9], v[198:205], 0
	v_mfma_f32_16x16x128_f8f6f4 v[146:149], v[10:17], v[198:205], 0
	v_mfma_f32_16x16x128_f8f6f4 v[134:137], v[2:9], v[206:213], 0
	v_mfma_f32_16x16x128_f8f6f4 v[130:133], v[10:17], v[206:213], 0
	v_mfma_f32_16x16x128_f8f6f4 v[118:121], v[2:9], v[214:221], 0
	v_mfma_f32_16x16x128_f8f6f4 v[114:117], v[10:17], v[214:221], 0
	v_mfma_f32_16x16x128_f8f6f4 v[102:105], v[2:9], v[222:229], 0
	v_mfma_f32_16x16x128_f8f6f4 v[98:101], v[10:17], v[222:229], 0
	s_setprio 0
	s_add_i32 s75, s65, s47
	s_mov_b32 m0, s75
	ds_read_b128 v[198:201], v194 offset:16384
	ds_read_b128 v[202:205], v194 offset:17408
	ds_read_b128 v[206:209], v194 offset:18432
	ds_read_b128 v[210:213], v194 offset:19456
	ds_read_b128 v[214:217], v194 offset:20480
	ds_read_b128 v[218:221], v194 offset:21504
	ds_read_b128 v[222:225], v194 offset:22528
	ds_read_b128 v[226:229], v194 offset:23552
	global_load_lds_dwordx4 v164, s[28:29]
	s_add_i32 m0, s75, 0x2000
	s_add_i32 s75, s66, s47
	global_load_lds_dwordx4 v166, s[28:29]
	s_add_u32 s98, s28, s4
	s_addc_u32 s99, s29, s5
	s_mov_b32 m0, s75
	s_nop 0
	global_load_lds_dwordx4 v164, s[98:99]
	s_add_u32 s100, s28, s4
	s_addc_u32 s101, s29, s5
	s_add_i32 m0, s75, 0x2000
	s_nop 0
	global_load_lds_dwordx4 v166, s[100:101]
	s_mov_b32 m0, s48
	s_nop 0
	global_load_lds_dwordx4 v174, s[30:31]
	s_mov_b32 m0, s49
	s_nop 0
	global_load_lds_dwordx4 v176, s[30:31]
	s_waitcnt vmcnt(8)
	s_waitcnt lgkmcnt(0)
	s_barrier
	s_setprio 2
	v_mfma_f32_16x16x128_f8f6f4 v[94:97], v[18:25], v[198:205], 0
	v_mfma_f32_16x16x128_f8f6f4 v[90:93], v[26:33], v[198:205], 0
	v_mfma_f32_16x16x128_f8f6f4 v[78:81], v[18:25], v[206:213], 0
	v_mfma_f32_16x16x128_f8f6f4 v[74:77], v[26:33], v[206:213], 0
	v_mfma_f32_16x16x128_f8f6f4 v[62:65], v[18:25], v[214:221], 0
	v_mfma_f32_16x16x128_f8f6f4 v[58:61], v[26:33], v[214:221], 0
	v_mfma_f32_16x16x128_f8f6f4 v[46:49], v[18:25], v[222:229], 0
	v_mfma_f32_16x16x128_f8f6f4 v[42:45], v[26:33], v[222:229], 0
	s_nop 3
	v_mfma_f32_16x16x128_f8f6f4 v[86:89], v[2:9], v[198:205], 0
	v_mfma_f32_16x16x128_f8f6f4 v[82:85], v[10:17], v[198:205], 0
	v_mfma_f32_16x16x128_f8f6f4 v[70:73], v[2:9], v[206:213], 0
	v_mfma_f32_16x16x128_f8f6f4 v[66:69], v[10:17], v[206:213], 0
	v_mfma_f32_16x16x128_f8f6f4 v[54:57], v[2:9], v[214:221], 0
	v_mfma_f32_16x16x128_f8f6f4 v[50:53], v[10:17], v[214:221], 0
	v_mfma_f32_16x16x128_f8f6f4 v[38:41], v[2:9], v[222:229], 0
	v_mfma_f32_16x16x128_f8f6f4 v[34:37], v[10:17], v[222:229], 0
	s_setprio 0
	s_add_i32 s75, 0, 0x18000
	s_add_i32 s76, 0, 0x1c000
	v_add_u32_e32 v14, s75, v191
	v_add_u32_e32 v30, s76, v191
	ds_read_b128 v[2:5], v14
	ds_read_b128 v[6:9], v14 offset:1024
	ds_read_b128 v[10:13], v14 offset:2048
	ds_read_b128 v[14:17], v14 offset:3072
	ds_read_b128 v[18:21], v30
	ds_read_b128 v[22:25], v30 offset:1024
	ds_read_b128 v[26:29], v30 offset:2048
	ds_read_b128 v[30:33], v30 offset:3072
	s_mov_b32 m0, s50
	ds_read_b128 v[198:201], v194 offset:32768
	ds_read_b128 v[202:205], v194 offset:33792
	ds_read_b128 v[206:209], v194 offset:34816
	ds_read_b128 v[210:213], v194 offset:35840
	ds_read_b128 v[214:217], v194 offset:36864
	ds_read_b128 v[218:221], v194 offset:37888
	ds_read_b128 v[222:225], v194 offset:38912
	ds_read_b128 v[226:229], v194 offset:39936
	global_load_lds_dwordx4 v178, s[30:31]
	s_mov_b32 m0, s51
	s_nop 0
	global_load_lds_dwordx4 v180, s[30:31]
	s_waitcnt vmcnt(8)
	s_waitcnt lgkmcnt(0)
	s_barrier
; #define PG8_STAGE(bufoff, gbase, voff) do { _Pragma("unroll") for (int _i = 0; _i < 2; ++_i) \
;         __builtin_amdgcn_global_load_lds((const unsigned*)((const char*)(gbase) + (voff)[_i]), (PG8_LAS unsigned*)(lds + (bufoff) + ldsw + _i * 8192), 16, 0, 0); } while (0)
; #define PG8_WAIT_V(n) asm volatile("s_waitcnt vmcnt(" #n ")" ::: "memory")
; #define PG8_WAIT_L(n) asm volatile("s_waitcnt lgkmcnt(" #n ")" ::: "memory")
; #define PG8_BAR __builtin_amdgcn_s_barrier()
; #define PG8_SCHED __builtin_amdgcn_sched_barrier(0)
; template <class Epi, class Sched, bool ALIGN_EPI = true, bool F8 = false>
; __device__ __forceinline__ void gemm_phase(PG8_LAS unsigned char* lds, const Sched& S, const Epi& E) {
;     ...
;             PG8_WAIT_V(8); PG8_WAIT_L(0); PG8_BAR; PG8_MMA(1, 0, At, B0); PG8_MMA(1, 1, At, B1); PG8_BAR; PG8_SCHED;
;             PG8_LDB(B0, 1, 0); PG8_LDB(B1, 1, 1); PG8_SCHED; PG8_LDA(At, 1, 0); PG8_STAGE(PG8_SA(0, 1), a2, vA2[1]);
;             PG8_WAIT_V(8); PG8_WAIT_L(0); PG8_BAR; PG8_MMA(0, 0, At, B0); PG8_MMA(0, 1, At, B1); PG8_BAR; PG8_SCHED;
;             PG8_LDA(At, 1, 1); PG8_STAGE(PG8_SB(1, 0), b3, voffB[0]); PG8_STAGE(PG8_SB(1, 1), b3, voffB[1]); PG8_STAGE(PG8_SA(1, 0), a3, vA2[0]);
;             PG8_WAIT_V(8); PG8_WAIT_L(0); PG8_BAR; PG8_MMA(1, 0, At, B0); PG8_MMA(1, 1, At, B1); PG8_BAR; PG8_SCHED;
	s_setprio 2
	v_mfma_f32_16x16x128_f8f6f4 v[158:161], v[2:9], v[198:205], v[158:161]
	v_mfma_f32_16x16x128_f8f6f4 v[154:157], v[10:17], v[198:205], v[154:157]
	v_mfma_f32_16x16x128_f8f6f4 v[142:145], v[2:9], v[206:213], v[142:145]
	v_mfma_f32_16x16x128_f8f6f4 v[138:141], v[10:17], v[206:213], v[138:141]
	v_mfma_f32_16x16x128_f8f6f4 v[126:129], v[2:9], v[214:221], v[126:129]
	v_mfma_f32_16x16x128_f8f6f4 v[122:125], v[10:17], v[214:221], v[122:125]
	v_mfma_f32_16x16x128_f8f6f4 v[110:113], v[2:9], v[222:229], v[110:113]
	v_mfma_f32_16x16x128_f8f6f4 v[106:109], v[10:17], v[222:229], v[106:109]
	s_nop 3
	v_mfma_f32_16x16x128_f8f6f4 v[150:153], v[18:25], v[198:205], v[150:153]
	v_mfma_f32_16x16x128_f8f6f4 v[146:149], v[26:33], v[198:205], v[146:149]
	v_mfma_f32_16x16x128_f8f6f4 v[134:137], v[18:25], v[206:213], v[134:137]
	v_mfma_f32_16x16x128_f8f6f4 v[130:133], v[26:33], v[206:213], v[130:133]
	v_mfma_f32_16x16x128_f8f6f4 v[118:121], v[18:25], v[214:221], v[118:121]
	v_mfma_f32_16x16x128_f8f6f4 v[114:117], v[26:33], v[214:221], v[114:117]
	v_mfma_f32_16x16x128_f8f6f4 v[102:105], v[18:25], v[222:229], v[102:105]
	v_mfma_f32_16x16x128_f8f6f4 v[98:101], v[26:33], v[222:229], v[98:101]
	s_setprio 0
	s_add_u32 s28, s28, 0x8000
	s_addc_u32 s29, s29, 0
	s_add_i32 s30, s75, s47
	s_mov_b32 m0, s30
	ds_read_b128 v[198:201], v194 offset:49152
	ds_read_b128 v[202:205], v194 offset:50176
	ds_read_b128 v[206:209], v194 offset:51200
	ds_read_b128 v[210:213], v194 offset:52224
	ds_read_b128 v[214:217], v194 offset:53248
	ds_read_b128 v[218:221], v194 offset:54272
	ds_read_b128 v[222:225], v194 offset:55296
	ds_read_b128 v[226:229], v194 offset:56320
	global_load_lds_dwordx4 v164, s[28:29]
	s_add_i32 m0, s30, 0x2000
	s_add_i32 s30, s76, s47
	global_load_lds_dwordx4 v166, s[28:29]
	s_mov_b32 m0, s30
	s_nop 0
	global_load_lds_dwordx4 v168, s[28:29]
	s_add_i32 m0, s30, 0x2000
	s_nop 0
	global_load_lds_dwordx4 v172, s[28:29]
	s_mov_b32 m0, s60
	s_nop 0
	global_load_lds_dwordx4 v174, s[26:27]
	s_mov_b32 m0, s61
	s_nop 0
	global_load_lds_dwordx4 v176, s[26:27]
	s_waitcnt vmcnt(8)
	s_waitcnt lgkmcnt(0)
	s_barrier
	s_setprio 2
	v_mfma_f32_16x16x128_f8f6f4 v[94:97], v[2:9], v[198:205], v[94:97]
	v_mfma_f32_16x16x128_f8f6f4 v[90:93], v[10:17], v[198:205], v[90:93]
	v_mfma_f32_16x16x128_f8f6f4 v[78:81], v[2:9], v[206:213], v[78:81]
	v_mfma_f32_16x16x128_f8f6f4 v[74:77], v[10:17], v[206:213], v[74:77]
	v_mfma_f32_16x16x128_f8f6f4 v[62:65], v[2:9], v[214:221], v[62:65]
	v_mfma_f32_16x16x128_f8f6f4 v[58:61], v[10:17], v[214:221], v[58:61]
	v_mfma_f32_16x16x128_f8f6f4 v[46:49], v[2:9], v[222:229], v[46:49]
	v_mfma_f32_16x16x128_f8f6f4 v[42:45], v[10:17], v[222:229], v[42:45]
	s_nop 3
	v_mfma_f32_16x16x128_f8f6f4 v[86:89], v[18:25], v[198:205], v[86:89]
	v_mfma_f32_16x16x128_f8f6f4 v[82:85], v[26:33], v[198:205], v[82:85]
	v_mfma_f32_16x16x128_f8f6f4 v[70:73], v[18:25], v[206:213], v[70:73]
	v_mfma_f32_16x16x128_f8f6f4 v[66:69], v[26:33], v[206:213], v[66:69]
	v_mfma_f32_16x16x128_f8f6f4 v[54:57], v[18:25], v[214:221], v[54:57]
	v_mfma_f32_16x16x128_f8f6f4 v[50:53], v[26:33], v[214:221], v[50:53]
	v_mfma_f32_16x16x128_f8f6f4 v[38:41], v[18:25], v[222:229], v[38:41]
	v_mfma_f32_16x16x128_f8f6f4 v[34:37], v[26:33], v[222:229], v[34:37]
	s_setprio 0
	s_add_i32 s74, s74, 2
	s_add_u32 s17, s17, 0x10000
	s_addc_u32 s19, s19, 0
	s_add_u32 s24, s24, 0x10000
	s_addc_u32 s25, s25, 0
	s_cmp_gt_u32 s74, 13
	s_cbranch_scc0 .Lh1_428
	s_branch .Lfx_11141
.Lh1_428:
	ds_read_b128 v[18:21], v192
	ds_read_b128 v[22:25], v192 offset:1024
	ds_read_b128 v[26:29], v192 offset:2048
	ds_read_b128 v[30:33], v192 offset:3072
	ds_read_b128 v[2:5], v193
	ds_read_b128 v[6:9], v193 offset:1024
	ds_read_b128 v[10:13], v193 offset:2048
	ds_read_b128 v[14:17], v193 offset:3072
	s_add_u32 s26, s24, 0x8000
	s_addc_u32 s27, s25, 0
	s_cmp_eq_u32 s74, 12
	s_cselect_b32 s30, s20, s26
	s_cselect_b32 s31, s21, s27
	s_cselect_b32 s28, s22, s17
	s_cselect_b32 s29, s23, s19
	s_add_u32 s26, s30, 0x8000
	s_addc_u32 s27, s31, 0
	s_add_i32 m0, s48, 0xc000
	ds_read_b128 v[198:201], v194
	ds_read_b128 v[202:205], v194 offset:1024
	ds_read_b128 v[206:209], v194 offset:2048
	ds_read_b128 v[210:213], v194 offset:3072
	ds_read_b128 v[214:217], v194 offset:4096
	ds_read_b128 v[218:221], v194 offset:5120
	ds_read_b128 v[222:225], v194 offset:6144
	ds_read_b128 v[226:229], v194 offset:7168
	global_load_lds_dwordx4 v184, s[24:25]
	s_add_i32 m0, s48, 0xe000
	s_nop 0
	global_load_lds_dwordx4 v182, s[24:25]
	s_waitcnt vmcnt(8)
	s_waitcnt lgkmcnt(0)
	s_barrier
	s_setprio 2
	v_mfma_f32_16x16x128_f8f6f4 v[158:161], v[18:25], v[198:205], v[158:161]
	v_mfma_f32_16x16x128_f8f6f4 v[154:157], v[26:33], v[198:205], v[154:157]
	v_mfma_f32_16x16x128_f8f6f4 v[142:145], v[18:25], v[206:213], v[142:145]
	v_mfma_f32_16x16x128_f8f6f4 v[138:141], v[26:33], v[206:213], v[138:141]
	v_mfma_f32_16x16x128_f8f6f4 v[126:129], v[18:25], v[214:221], v[126:129]
	v_mfma_f32_16x16x128_f8f6f4 v[122:125], v[26:33], v[214:221], v[122:125]
	v_mfma_f32_16x16x128_f8f6f4 v[110:113], v[18:25], v[222:229], v[110:113]
	v_mfma_f32_16x16x128_f8f6f4 v[106:109], v[26:33], v[222:229], v[106:109]
	s_nop 3
	v_mfma_f32_16x16x128_f8f6f4 v[150:153], v[2:9], v[198:205], v[150:153]
	v_mfma_f32_16x16x128_f8f6f4 v[146:149], v[10:17], v[198:205], v[146:149]
	v_mfma_f32_16x16x128_f8f6f4 v[134:137], v[2:9], v[206:213], v[134:137]
	v_mfma_f32_16x16x128_f8f6f4 v[130:133], v[10:17], v[206:213], v[130:133]
	v_mfma_f32_16x16x128_f8f6f4 v[118:121], v[2:9], v[214:221], v[118:121]
	v_mfma_f32_16x16x128_f8f6f4 v[114:117], v[10:17], v[214:221], v[114:117]
	v_mfma_f32_16x16x128_f8f6f4 v[102:105], v[2:9], v[222:229], v[102:105]
	v_mfma_f32_16x16x128_f8f6f4 v[98:101], v[10:17], v[222:229], v[98:101]
	s_setprio 0
	s_add_i32 s75, s65, s47
	s_mov_b32 m0, s75
	ds_read_b128 v[198:201], v194 offset:16384
	ds_read_b128 v[202:205], v194 offset:17408
	ds_read_b128 v[206:209], v194 offset:18432
	ds_read_b128 v[210:213], v194 offset:19456
	ds_read_b128 v[214:217], v194 offset:20480
	ds_read_b128 v[218:221], v194 offset:21504
	ds_read_b128 v[222:225], v194 offset:22528
	ds_read_b128 v[226:229], v194 offset:23552
	global_load_lds_dwordx4 v164, s[28:29]
	s_add_i32 m0, s75, 0x2000
	s_add_i32 s75, s66, s47
	global_load_lds_dwordx4 v166, s[28:29]
	s_add_u32 s98, s28, s4
	s_addc_u32 s99, s29, s5
	s_mov_b32 m0, s75
	s_nop 0
	global_load_lds_dwordx4 v164, s[98:99]
	s_add_u32 s100, s28, s4
	s_addc_u32 s101, s29, s5
	s_add_i32 m0, s75, 0x2000
	s_nop 0
	global_load_lds_dwordx4 v166, s[100:101]
	s_mov_b32 m0, s48
	s_nop 0
	global_load_lds_dwordx4 v174, s[30:31]
	s_mov_b32 m0, s49
	s_nop 0
	global_load_lds_dwordx4 v176, s[30:31]
	s_waitcnt vmcnt(8)
	s_waitcnt lgkmcnt(0)
	s_barrier
; #define PG8_STAGE(bufoff, gbase, voff) do { _Pragma("unroll") for (int _i = 0; _i < 2; ++_i) \
;         __builtin_amdgcn_global_load_lds((const unsigned*)((const char*)(gbase) + (voff)[_i]), (PG8_LAS unsigned*)(lds + (bufoff) + ldsw + _i * 8192), 16, 0, 0); } while (0)
; #define PG8_WAIT_V(n) asm volatile("s_waitcnt vmcnt(" #n ")" ::: "memory")
; #define PG8_WAIT_L(n) asm volatile("s_waitcnt lgkmcnt(" #n ")" ::: "memory")
; #define PG8_BAR __builtin_amdgcn_s_barrier()
; #define PG8_SCHED __builtin_amdgcn_sched_barrier(0)
; template <class Epi, class Sched, bool ALIGN_EPI = true, bool F8 = false>
; __device__ __forceinline__ void gemm_phase(PG8_LAS unsigned char* lds, const Sched& S, const Epi& E) {
;     ...
;             PG8_WAIT_V(8); PG8_WAIT_L(0); PG8_BAR; PG8_MMA(1, 0, At, B0); PG8_MMA(1, 1, At, B1); PG8_BAR; PG8_SCHED;
;             PG8_LDB(B0, 1, 0); PG8_LDB(B1, 1, 1); PG8_SCHED; PG8_LDA(At, 1, 0); PG8_STAGE(PG8_SA(0, 1), a2, vA2[1]);
;             PG8_WAIT_V(8); PG8_WAIT_L(0); PG8_BAR; PG8_MMA(0, 0, At, B0); PG8_MMA(0, 1, At, B1); PG8_BAR; PG8_SCHED;
;             PG8_LDA(At, 1, 1); PG8_STAGE(PG8_SB(1, 0), b3, voffB[0]); PG8_STAGE(PG8_SB(1, 1), b3, voffB[1]); PG8_STAGE(PG8_SA(1, 0), a3, vA2[0]);
;             PG8_WAIT_V(8); PG8_WAIT_L(0); PG8_BAR; PG8_MMA(1, 0, At, B0); PG8_MMA(1, 1, At, B1); PG8_BAR; PG8_SCHED;
	s_setprio 2
	v_mfma_f32_16x16x128_f8f6f4 v[94:97], v[18:25], v[198:205], v[94:97]
	v_mfma_f32_16x16x128_f8f6f4 v[90:93], v[26:33], v[198:205], v[90:93]
	v_mfma_f32_16x16x128_f8f6f4 v[78:81], v[18:25], v[206:213], v[78:81]
	v_mfma_f32_16x16x128_f8f6f4 v[74:77], v[26:33], v[206:213], v[74:77]
	v_mfma_f32_16x16x128_f8f6f4 v[62:65], v[18:25], v[214:221], v[62:65]
	v_mfma_f32_16x16x128_f8f6f4 v[58:61], v[26:33], v[214:221], v[58:61]
	v_mfma_f32_16x16x128_f8f6f4 v[46:49], v[18:25], v[222:229], v[46:49]
	v_mfma_f32_16x16x128_f8f6f4 v[42:45], v[26:33], v[222:229], v[42:45]
	s_nop 3
	v_mfma_f32_16x16x128_f8f6f4 v[86:89], v[2:9], v[198:205], v[86:89]
	v_mfma_f32_16x16x128_f8f6f4 v[82:85], v[10:17], v[198:205], v[82:85]
	v_mfma_f32_16x16x128_f8f6f4 v[70:73], v[2:9], v[206:213], v[70:73]
	v_mfma_f32_16x16x128_f8f6f4 v[66:69], v[10:17], v[206:213], v[66:69]
	v_mfma_f32_16x16x128_f8f6f4 v[54:57], v[2:9], v[214:221], v[54:57]
	v_mfma_f32_16x16x128_f8f6f4 v[50:53], v[10:17], v[214:221], v[50:53]
	v_mfma_f32_16x16x128_f8f6f4 v[38:41], v[2:9], v[222:229], v[38:41]
	v_mfma_f32_16x16x128_f8f6f4 v[34:37], v[10:17], v[222:229], v[34:37]
	s_setprio 0
	s_add_i32 s75, 0, 0x18000
	s_add_i32 s76, 0, 0x1c000
	v_add_u32_e32 v14, s75, v191
	v_add_u32_e32 v30, s76, v191
	ds_read_b128 v[2:5], v14
	ds_read_b128 v[6:9], v14 offset:1024
	ds_read_b128 v[10:13], v14 offset:2048
	ds_read_b128 v[14:17], v14 offset:3072
	ds_read_b128 v[18:21], v30
	ds_read_b128 v[22:25], v30 offset:1024
	ds_read_b128 v[26:29], v30 offset:2048
	ds_read_b128 v[30:33], v30 offset:3072
	s_mov_b32 m0, s50
	ds_read_b128 v[198:201], v194 offset:32768
	ds_read_b128 v[202:205], v194 offset:33792
	ds_read_b128 v[206:209], v194 offset:34816
	ds_read_b128 v[210:213], v194 offset:35840
	ds_read_b128 v[214:217], v194 offset:36864
	ds_read_b128 v[218:221], v194 offset:37888
	ds_read_b128 v[222:225], v194 offset:38912
	ds_read_b128 v[226:229], v194 offset:39936
	global_load_lds_dwordx4 v178, s[30:31]
	s_mov_b32 m0, s51
	s_nop 0
	global_load_lds_dwordx4 v180, s[30:31]
	s_waitcnt vmcnt(8)
	s_waitcnt lgkmcnt(0)
	s_barrier
	s_setprio 2
	v_mfma_f32_16x16x128_f8f6f4 v[158:161], v[2:9], v[198:205], v[158:161]
	v_mfma_f32_16x16x128_f8f6f4 v[154:157], v[10:17], v[198:205], v[154:157]
	v_mfma_f32_16x16x128_f8f6f4 v[142:145], v[2:9], v[206:213], v[142:145]
	v_mfma_f32_16x16x128_f8f6f4 v[138:141], v[10:17], v[206:213], v[138:141]
	v_mfma_f32_16x16x128_f8f6f4 v[126:129], v[2:9], v[214:221], v[126:129]
	v_mfma_f32_16x16x128_f8f6f4 v[122:125], v[10:17], v[214:221], v[122:125]
	v_mfma_f32_16x16x128_f8f6f4 v[110:113], v[2:9], v[222:229], v[110:113]
	v_mfma_f32_16x16x128_f8f6f4 v[106:109], v[10:17], v[222:229], v[106:109]
	s_nop 3
	v_mfma_f32_16x16x128_f8f6f4 v[150:153], v[18:25], v[198:205], v[150:153]
	v_mfma_f32_16x16x128_f8f6f4 v[146:149], v[26:33], v[198:205], v[146:149]
	v_mfma_f32_16x16x128_f8f6f4 v[134:137], v[18:25], v[206:213], v[134:137]
	v_mfma_f32_16x16x128_f8f6f4 v[130:133], v[26:33], v[206:213], v[130:133]
	v_mfma_f32_16x16x128_f8f6f4 v[118:121], v[18:25], v[214:221], v[118:121]
	v_mfma_f32_16x16x128_f8f6f4 v[114:117], v[26:33], v[214:221], v[114:117]
	v_mfma_f32_16x16x128_f8f6f4 v[102:105], v[18:25], v[222:229], v[102:105]
	v_mfma_f32_16x16x128_f8f6f4 v[98:101], v[26:33], v[222:229], v[98:101]
	s_setprio 0
	s_add_u32 s28, s28, 0x8000
	s_addc_u32 s29, s29, 0
	s_add_i32 s30, s75, s47
	s_mov_b32 m0, s30
	ds_read_b128 v[198:201], v194 offset:49152
	ds_read_b128 v[202:205], v194 offset:50176
	ds_read_b128 v[206:209], v194 offset:51200
	ds_read_b128 v[210:213], v194 offset:52224
	ds_read_b128 v[214:217], v194 offset:53248
	ds_read_b128 v[218:221], v194 offset:54272
	ds_read_b128 v[222:225], v194 offset:55296
	ds_read_b128 v[226:229], v194 offset:56320
	global_load_lds_dwordx4 v164, s[28:29]
	s_add_i32 m0, s30, 0x2000
	s_add_i32 s30, s76, s47
	global_load_lds_dwordx4 v166, s[28:29]
	s_mov_b32 m0, s30
	s_nop 0
	global_load_lds_dwordx4 v168, s[28:29]
	s_add_i32 m0, s30, 0x2000
	s_nop 0
	global_load_lds_dwordx4 v172, s[28:29]
	s_mov_b32 m0, s60
	s_nop 0
	global_load_lds_dwordx4 v174, s[26:27]
	s_mov_b32 m0, s61
	s_nop 0
	global_load_lds_dwordx4 v176, s[26:27]
	s_waitcnt vmcnt(8)
	s_waitcnt lgkmcnt(0)
	s_barrier
	s_setprio 2
	v_mfma_f32_16x16x128_f8f6f4 v[94:97], v[2:9], v[198:205], v[94:97]
	v_mfma_f32_16x16x128_f8f6f4 v[90:93], v[10:17], v[198:205], v[90:93]
	v_mfma_f32_16x16x128_f8f6f4 v[78:81], v[2:9], v[206:213], v[78:81]
	v_mfma_f32_16x16x128_f8f6f4 v[74:77], v[10:17], v[206:213], v[74:77]
	v_mfma_f32_16x16x128_f8f6f4 v[62:65], v[2:9], v[214:221], v[62:65]
	v_mfma_f32_16x16x128_f8f6f4 v[58:61], v[10:17], v[214:221], v[58:61]
	v_mfma_f32_16x16x128_f8f6f4 v[46:49], v[2:9], v[222:229], v[46:49]
	v_mfma_f32_16x16x128_f8f6f4 v[42:45], v[10:17], v[222:229], v[42:45]
	s_nop 3
	v_mfma_f32_16x16x128_f8f6f4 v[86:89], v[18:25], v[198:205], v[86:89]
	v_mfma_f32_16x16x128_f8f6f4 v[82:85], v[26:33], v[198:205], v[82:85]
	v_mfma_f32_16x16x128_f8f6f4 v[70:73], v[18:25], v[206:213], v[70:73]
	v_mfma_f32_16x16x128_f8f6f4 v[66:69], v[26:33], v[206:213], v[66:69]
	v_mfma_f32_16x16x128_f8f6f4 v[54:57], v[18:25], v[214:221], v[54:57]
	v_mfma_f32_16x16x128_f8f6f4 v[50:53], v[26:33], v[214:221], v[50:53]
	v_mfma_f32_16x16x128_f8f6f4 v[38:41], v[18:25], v[222:229], v[38:41]
	v_mfma_f32_16x16x128_f8f6f4 v[34:37], v[26:33], v[222:229], v[34:37]
	s_setprio 0
	s_add_i32 s74, s74, 2
	s_add_u32 s17, s17, 0x10000
	s_addc_u32 s19, s19, 0
	s_add_u32 s24, s24, 0x10000
	s_addc_u32 s25, s25, 0
	s_cmp_gt_u32 s74, 13
	s_cbranch_scc0 .Lh1_428

; #define PG8_STAGE(bufoff, gbase, voff) do { _Pragma("unroll") for (int _i = 0; _i < 2; ++_i) \
;         __builtin_amdgcn_global_load_lds((const unsigned*)((const char*)(gbase) + (voff)[_i]), (PG8_LAS unsigned*)(lds + (bufoff) + ldsw + _i * 8192), 16, 0, 0); } while (0)
; #define PG8_WAIT_V(n) asm volatile("s_waitcnt vmcnt(" #n ")" ::: "memory")
; #define PG8_WAIT_L(n) asm volatile("s_waitcnt lgkmcnt(" #n ")" ::: "memory")
; #define PG8_BAR __builtin_amdgcn_s_barrier()
; #define PG8_SCHED __builtin_amdgcn_sched_barrier(0)
; template <class Epi, class Sched, bool ALIGN_EPI = true, bool F8 = false>
; __device__ __forceinline__ void gemm_phase(PG8_LAS unsigned char* lds, const Sched& S, const Epi& E) {
;     ...
;             PG8_LDB(B0, 0, 0); PG8_LDB(B1, 0, 1); PG8_SCHED; PG8_LDA(At, 0, 0); PG8_STAGE(PG8_SA(1, 1), a1, voffA[1]);
;             PG8_WAIT_V(8); PG8_WAIT_L(0); PG8_BAR; PG8_MMA(0, 0, At, B0); PG8_MMA(0, 1, At, B1); PG8_BAR; PG8_SCHED;
;             PG8_LDA(At, 0, 1); PG8_STAGE(PG8_SB(0, 0), b2, voffB[0]); PG8_STAGE(PG8_SB(0, 1), b2, voffB[1]); PG8_STAGE(PG8_SA(0, 0), a2, vA2[0]);
;             PG8_WAIT_V(8); PG8_WAIT_L(0); PG8_BAR; PG8_MMA(1, 0, At, B0); PG8_MMA(1, 1, At, B1); PG8_BAR; PG8_SCHED;
.Lpkb_491:
	ds_read_b128 v[178:181], v173
	ds_read_b128 v[182:185], v173 offset:1024
	ds_read_b128 v[186:189], v173 offset:2048
	ds_read_b128 v[190:193], v173 offset:3072
	ds_read_b128 v[194:197], v174
	ds_read_b128 v[198:201], v174 offset:1024
	ds_read_b128 v[202:205], v174 offset:2048
	ds_read_b128 v[206:209], v174 offset:3072
	s_add_u32 s24, s22, 0x100
	s_addc_u32 s25, s23, 0
	s_cmp_eq_u32 s66, 4
	s_cselect_b32 s29, s17, s25
	s_cselect_b32 s28, s16, s24
	s_cselect_b32 s27, s19, s65
	s_cselect_b32 s26, s18, s15
	s_mov_b32 m0, s49
	v_lshl_add_u64 v[242:243], s[22:23], 0, v[166:167]
	ds_read_b128 v[210:213], v175
	ds_read_b128 v[214:217], v175 offset:1024
	ds_read_b128 v[218:221], v175 offset:2048
	ds_read_b128 v[222:225], v175 offset:3072
	ds_read_b128 v[226:229], v175 offset:4096
	ds_read_b128 v[230:233], v175 offset:5120
	ds_read_b128 v[234:237], v175 offset:6144
	ds_read_b128 v[238:241], v175 offset:7168
	global_load_lds_dwordx4 v[242:243], off
	v_lshl_add_u64 v[242:243], s[22:23], 0, v[164:165]
	s_mov_b32 m0, s50
	s_nop 0
	global_load_lds_dwordx4 v[242:243], off
	s_waitcnt vmcnt(8)
	s_waitcnt lgkmcnt(0)
	s_barrier
	s_setprio 1
	s_waitcnt lgkmcnt(0)
	v_mfma_f32_16x16x32_bf16 v[126:129], v[178:181], v[210:213], 0
	v_mfma_f32_16x16x32_bf16 v[122:125], v[186:189], v[210:213], 0
	v_mfma_f32_16x16x32_bf16 v[118:121], v[178:181], v[218:221], 0
	v_mfma_f32_16x16x32_bf16 v[114:117], v[186:189], v[218:221], 0
	v_mfma_f32_16x16x32_bf16 v[110:113], v[178:181], v[226:229], 0
	v_mfma_f32_16x16x32_bf16 v[106:109], v[186:189], v[226:229], 0
	v_mfma_f32_16x16x32_bf16 v[98:101], v[178:181], v[234:237], 0
	v_mfma_f32_16x16x32_bf16 v[90:93], v[186:189], v[234:237], 0
	v_mfma_f32_16x16x32_bf16 v[126:129], v[182:185], v[214:217], v[126:129]
	v_mfma_f32_16x16x32_bf16 v[122:125], v[190:193], v[214:217], v[122:125]
	v_mfma_f32_16x16x32_bf16 v[118:121], v[182:185], v[222:225], v[118:121]
	v_mfma_f32_16x16x32_bf16 v[114:117], v[190:193], v[222:225], v[114:117]
	v_mfma_f32_16x16x32_bf16 v[110:113], v[182:185], v[230:233], v[110:113]
	v_mfma_f32_16x16x32_bf16 v[106:109], v[190:193], v[230:233], v[106:109]
	v_mfma_f32_16x16x32_bf16 v[98:101], v[182:185], v[238:241], v[98:101]
	v_mfma_f32_16x16x32_bf16 v[90:93], v[190:193], v[238:241], v[90:93]
	v_mfma_f32_16x16x32_bf16 v[102:105], v[194:197], v[210:213], 0
	v_mfma_f32_16x16x32_bf16 v[94:97], v[202:205], v[210:213], 0
	v_mfma_f32_16x16x32_bf16 v[86:89], v[194:197], v[218:221], 0
	v_mfma_f32_16x16x32_bf16 v[82:85], v[202:205], v[218:221], 0
	v_mfma_f32_16x16x32_bf16 v[78:81], v[194:197], v[226:229], 0
	v_mfma_f32_16x16x32_bf16 v[74:77], v[202:205], v[226:229], 0
	v_mfma_f32_16x16x32_bf16 v[70:73], v[194:197], v[234:237], 0
	v_mfma_f32_16x16x32_bf16 v[66:69], v[202:205], v[234:237], 0
	v_mfma_f32_16x16x32_bf16 v[102:105], v[198:201], v[214:217], v[102:105]
	v_mfma_f32_16x16x32_bf16 v[94:97], v[206:209], v[214:217], v[94:97]
	v_mfma_f32_16x16x32_bf16 v[86:89], v[198:201], v[222:225], v[86:89]
	v_mfma_f32_16x16x32_bf16 v[82:85], v[206:209], v[222:225], v[82:85]
	v_mfma_f32_16x16x32_bf16 v[78:81], v[198:201], v[230:233], v[78:81]
	v_mfma_f32_16x16x32_bf16 v[74:77], v[206:209], v[230:233], v[74:77]
	v_mfma_f32_16x16x32_bf16 v[70:73], v[198:201], v[238:241], v[70:73]
	v_mfma_f32_16x16x32_bf16 v[66:69], v[206:209], v[238:241], v[66:69]
	s_setprio 0
	s_barrier
	s_mov_b32 m0, s51
	v_lshl_add_u64 v[242:243], s[26:27], 0, v[134:135]
	ds_read_b128 v[210:213], v175 offset:16384
	ds_read_b128 v[214:217], v175 offset:17408
	ds_read_b128 v[218:221], v175 offset:18432
	ds_read_b128 v[222:225], v175 offset:19456
	ds_read_b128 v[226:229], v175 offset:20480
	ds_read_b128 v[230:233], v175 offset:21504
	ds_read_b128 v[234:237], v175 offset:22528
	ds_read_b128 v[238:241], v175 offset:23552
	global_load_lds_dwordx4 v[242:243], off
	v_lshl_add_u64 v[244:245], s[26:27], 0, v[130:131]
	s_mov_b32 m0, s52
	v_lshl_add_u64 v[246:247], s[26:27], 0, v[136:137]
	global_load_lds_dwordx4 v[244:245], off
	s_mov_b32 m0, s53
	v_lshl_add_u64 v[248:249], s[28:29], 0, v[140:141]
	global_load_lds_dwordx4 v[246:247], off
	v_lshl_add_u64 v[246:247], s[26:27], 0, v[132:133]
	s_mov_b32 m0, s59
	s_nop 0
	global_load_lds_dwordx4 v[246:247], off
	v_lshl_add_u64 v[246:247], s[28:29], 0, v[138:139]
	s_mov_b32 m0, s42
	s_nop 0
	global_load_lds_dwordx4 v[246:247], off
	s_mov_b32 m0, s43
	s_nop 0
	global_load_lds_dwordx4 v[248:249], off
	s_waitcnt vmcnt(8)
	s_waitcnt lgkmcnt(0)
	s_barrier
	s_setprio 1
	s_waitcnt lgkmcnt(0)
	v_mfma_f32_16x16x32_bf16 v[62:65], v[178:181], v[210:213], 0
	v_mfma_f32_16x16x32_bf16 v[58:61], v[186:189], v[210:213], 0
	v_mfma_f32_16x16x32_bf16 v[54:57], v[178:181], v[218:221], 0
	v_mfma_f32_16x16x32_bf16 v[50:53], v[186:189], v[218:221], 0
	v_mfma_f32_16x16x32_bf16 v[46:49], v[178:181], v[226:229], 0
	v_mfma_f32_16x16x32_bf16 v[42:45], v[186:189], v[226:229], 0
	v_mfma_f32_16x16x32_bf16 v[34:37], v[178:181], v[234:237], 0
	v_mfma_f32_16x16x32_bf16 v[26:29], v[186:189], v[234:237], 0
	v_mfma_f32_16x16x32_bf16 v[62:65], v[182:185], v[214:217], v[62:65]
	v_mfma_f32_16x16x32_bf16 v[58:61], v[190:193], v[214:217], v[58:61]
	v_mfma_f32_16x16x32_bf16 v[54:57], v[182:185], v[222:225], v[54:57]
	v_mfma_f32_16x16x32_bf16 v[50:53], v[190:193], v[222:225], v[50:53]
	v_mfma_f32_16x16x32_bf16 v[46:49], v[182:185], v[230:233], v[46:49]
	v_mfma_f32_16x16x32_bf16 v[42:45], v[190:193], v[230:233], v[42:45]
	v_mfma_f32_16x16x32_bf16 v[34:37], v[182:185], v[238:241], v[34:37]
	v_mfma_f32_16x16x32_bf16 v[26:29], v[190:193], v[238:241], v[26:29]
	v_mfma_f32_16x16x32_bf16 v[38:41], v[194:197], v[210:213], 0
	v_mfma_f32_16x16x32_bf16 v[30:33], v[202:205], v[210:213], 0
	v_mfma_f32_16x16x32_bf16 v[22:25], v[194:197], v[218:221], 0
	v_mfma_f32_16x16x32_bf16 v[18:21], v[202:205], v[218:221], 0
	v_mfma_f32_16x16x32_bf16 v[14:17], v[194:197], v[226:229], 0
	v_mfma_f32_16x16x32_bf16 v[10:13], v[202:205], v[226:229], 0
	v_mfma_f32_16x16x32_bf16 v[6:9], v[194:197], v[234:237], 0
	v_mfma_f32_16x16x32_bf16 v[2:5], v[202:205], v[234:237], 0
	v_mfma_f32_16x16x32_bf16 v[38:41], v[198:201], v[214:217], v[38:41]
	v_mfma_f32_16x16x32_bf16 v[30:33], v[206:209], v[214:217], v[30:33]
	v_mfma_f32_16x16x32_bf16 v[22:25], v[198:201], v[222:225], v[22:25]
	v_mfma_f32_16x16x32_bf16 v[18:21], v[206:209], v[222:225], v[18:21]
	v_mfma_f32_16x16x32_bf16 v[14:17], v[198:201], v[230:233], v[14:17]
	v_mfma_f32_16x16x32_bf16 v[10:13], v[206:209], v[230:233], v[10:13]
	v_mfma_f32_16x16x32_bf16 v[6:9], v[198:201], v[238:241], v[6:9]
	v_mfma_f32_16x16x32_bf16 v[2:5], v[206:209], v[238:241], v[2:5]
	s_setprio 0
	s_barrier
; #define PG8_STAGE(bufoff, gbase, voff) do { _Pragma("unroll") for (int _i = 0; _i < 2; ++_i) \
;         __builtin_amdgcn_global_load_lds((const unsigned*)((const char*)(gbase) + (voff)[_i]), (PG8_LAS unsigned*)(lds + (bufoff) + ldsw + _i * 8192), 16, 0, 0); } while (0)
; #define PG8_WAIT_V(n) asm volatile("s_waitcnt vmcnt(" #n ")" ::: "memory")
; #define PG8_WAIT_L(n) asm volatile("s_waitcnt lgkmcnt(" #n ")" ::: "memory")
; #define PG8_BAR __builtin_amdgcn_s_barrier()
; #define PG8_SCHED __builtin_amdgcn_sched_barrier(0)
; template <class Epi, class Sched, bool ALIGN_EPI = true, bool F8 = false>
; __device__ __forceinline__ void gemm_phase(PG8_LAS unsigned char* lds, const Sched& S, const Epi& E) {
;     ...
;             PG8_LDB(B0, 1, 0); PG8_LDB(B1, 1, 1); PG8_SCHED; PG8_LDA(At, 1, 0); PG8_STAGE(PG8_SA(0, 1), a2, vA2[1]);
;             PG8_WAIT_V(8); PG8_WAIT_L(0); PG8_BAR; PG8_MMA(0, 0, At, B0); PG8_MMA(0, 1, At, B1); PG8_BAR; PG8_SCHED;
;             PG8_LDA(At, 1, 1); PG8_STAGE(PG8_SB(1, 0), b3, voffB[0]); PG8_STAGE(PG8_SB(1, 1), b3, voffB[1]); PG8_STAGE(PG8_SA(1, 0), a3, vA2[0]);
;             PG8_WAIT_V(8); PG8_WAIT_L(0); PG8_BAR; PG8_MMA(1, 0, At, B0); PG8_MMA(1, 1, At, B1); PG8_BAR; PG8_SCHED;
	ds_read_b128 v[178:181], v176
	ds_read_b128 v[182:185], v176 offset:1024
	ds_read_b128 v[186:189], v176 offset:2048
	ds_read_b128 v[190:193], v176 offset:3072
	ds_read_b128 v[194:197], v177
	ds_read_b128 v[198:201], v177 offset:1024
	ds_read_b128 v[202:205], v177 offset:2048
	ds_read_b128 v[206:209], v177 offset:3072
	s_mov_b32 m0, s44
	v_lshl_add_u64 v[250:251], s[28:29], 0, v[142:143]
	ds_read_b128 v[210:213], v175 offset:32768
	ds_read_b128 v[214:217], v175 offset:33792
	ds_read_b128 v[218:221], v175 offset:34816
	ds_read_b128 v[222:225], v175 offset:35840
	ds_read_b128 v[226:229], v175 offset:36864
	ds_read_b128 v[230:233], v175 offset:37888
	ds_read_b128 v[234:237], v175 offset:38912
	ds_read_b128 v[238:241], v175 offset:39936
	global_load_lds_dwordx4 v[250:251], off
	v_lshl_add_u64 v[250:251], s[28:29], 0, v[144:145]
	s_mov_b32 m0, s45
	s_nop 0
	global_load_lds_dwordx4 v[250:251], off
	s_waitcnt vmcnt(8)
	s_waitcnt lgkmcnt(0)
	s_barrier
	s_setprio 1
	s_waitcnt lgkmcnt(0)
	v_mfma_f32_16x16x32_bf16 v[126:129], v[178:181], v[210:213], v[126:129]
	v_mfma_f32_16x16x32_bf16 v[122:125], v[186:189], v[210:213], v[122:125]
	v_mfma_f32_16x16x32_bf16 v[118:121], v[178:181], v[218:221], v[118:121]
	v_mfma_f32_16x16x32_bf16 v[114:117], v[186:189], v[218:221], v[114:117]
	v_mfma_f32_16x16x32_bf16 v[110:113], v[178:181], v[226:229], v[110:113]
	v_mfma_f32_16x16x32_bf16 v[106:109], v[186:189], v[226:229], v[106:109]
	v_mfma_f32_16x16x32_bf16 v[98:101], v[178:181], v[234:237], v[98:101]
	v_mfma_f32_16x16x32_bf16 v[90:93], v[186:189], v[234:237], v[90:93]
	v_mfma_f32_16x16x32_bf16 v[126:129], v[182:185], v[214:217], v[126:129]
	v_mfma_f32_16x16x32_bf16 v[122:125], v[190:193], v[214:217], v[122:125]
	v_mfma_f32_16x16x32_bf16 v[118:121], v[182:185], v[222:225], v[118:121]
	v_mfma_f32_16x16x32_bf16 v[114:117], v[190:193], v[222:225], v[114:117]
	v_mfma_f32_16x16x32_bf16 v[110:113], v[182:185], v[230:233], v[110:113]
	v_mfma_f32_16x16x32_bf16 v[106:109], v[190:193], v[230:233], v[106:109]
	v_mfma_f32_16x16x32_bf16 v[98:101], v[182:185], v[238:241], v[98:101]
	v_mfma_f32_16x16x32_bf16 v[90:93], v[190:193], v[238:241], v[90:93]
	v_mfma_f32_16x16x32_bf16 v[102:105], v[194:197], v[210:213], v[102:105]
	v_mfma_f32_16x16x32_bf16 v[94:97], v[202:205], v[210:213], v[94:97]
	v_mfma_f32_16x16x32_bf16 v[86:89], v[194:197], v[218:221], v[86:89]
	v_mfma_f32_16x16x32_bf16 v[82:85], v[202:205], v[218:221], v[82:85]
	v_mfma_f32_16x16x32_bf16 v[78:81], v[194:197], v[226:229], v[78:81]
	v_mfma_f32_16x16x32_bf16 v[74:77], v[202:205], v[226:229], v[74:77]
	v_mfma_f32_16x16x32_bf16 v[70:73], v[194:197], v[234:237], v[70:73]
	v_mfma_f32_16x16x32_bf16 v[66:69], v[202:205], v[234:237], v[66:69]
	v_mfma_f32_16x16x32_bf16 v[102:105], v[198:201], v[214:217], v[102:105]
	v_mfma_f32_16x16x32_bf16 v[94:97], v[206:209], v[214:217], v[94:97]
	v_mfma_f32_16x16x32_bf16 v[86:89], v[198:201], v[222:225], v[86:89]
	v_mfma_f32_16x16x32_bf16 v[82:85], v[206:209], v[222:225], v[82:85]
	v_mfma_f32_16x16x32_bf16 v[78:81], v[198:201], v[230:233], v[78:81]
	v_mfma_f32_16x16x32_bf16 v[74:77], v[206:209], v[230:233], v[74:77]
	v_mfma_f32_16x16x32_bf16 v[70:73], v[198:201], v[238:241], v[70:73]
	v_mfma_f32_16x16x32_bf16 v[66:69], v[206:209], v[238:241], v[66:69]
	s_setprio 0
	s_barrier
	s_mov_b32 m0, s60
	s_add_u32 s22, s26, 0x80
	v_lshl_add_u64 v[242:243], v[242:243], 0, s[8:9]
	ds_read_b128 v[210:213], v175 offset:49152
	ds_read_b128 v[214:217], v175 offset:50176
	ds_read_b128 v[218:221], v175 offset:51200
	ds_read_b128 v[222:225], v175 offset:52224
	ds_read_b128 v[226:229], v175 offset:53248
	ds_read_b128 v[230:233], v175 offset:54272
	ds_read_b128 v[234:237], v175 offset:55296
	ds_read_b128 v[238:241], v175 offset:56320
	s_addc_u32 s23, s27, 0
	global_load_lds_dwordx4 v[242:243], off
	v_lshl_add_u64 v[242:243], v[244:245], 0, s[8:9]
	s_mov_b32 m0, s61
	s_nop 0
	global_load_lds_dwordx4 v[242:243], off
	v_lshl_add_u64 v[242:243], s[22:23], 0, v[136:137]
	s_mov_b32 m0, s62
	s_nop 0
	global_load_lds_dwordx4 v[242:243], off
	v_lshl_add_u64 v[242:243], s[22:23], 0, v[132:133]
	s_mov_b32 m0, s63
	s_nop 0
	global_load_lds_dwordx4 v[242:243], off
	v_lshl_add_u64 v[242:243], v[246:247], 0, s[8:9]
	s_mov_b32 m0, s47
	s_nop 0
	global_load_lds_dwordx4 v[242:243], off
	v_lshl_add_u64 v[242:243], v[248:249], 0, s[8:9]
	s_mov_b32 m0, s48
	s_nop 0
	global_load_lds_dwordx4 v[242:243], off
	s_waitcnt vmcnt(8)
	s_waitcnt lgkmcnt(0)
	s_barrier
	s_setprio 1
	s_waitcnt lgkmcnt(0)
	v_mfma_f32_16x16x32_bf16 v[62:65], v[178:181], v[210:213], v[62:65]
	v_mfma_f32_16x16x32_bf16 v[58:61], v[186:189], v[210:213], v[58:61]
	v_mfma_f32_16x16x32_bf16 v[54:57], v[178:181], v[218:221], v[54:57]
	v_mfma_f32_16x16x32_bf16 v[50:53], v[186:189], v[218:221], v[50:53]
	v_mfma_f32_16x16x32_bf16 v[46:49], v[178:181], v[226:229], v[46:49]
	v_mfma_f32_16x16x32_bf16 v[42:45], v[186:189], v[226:229], v[42:45]
	v_mfma_f32_16x16x32_bf16 v[34:37], v[178:181], v[234:237], v[34:37]
	v_mfma_f32_16x16x32_bf16 v[26:29], v[186:189], v[234:237], v[26:29]
	v_mfma_f32_16x16x32_bf16 v[62:65], v[182:185], v[214:217], v[62:65]
	v_mfma_f32_16x16x32_bf16 v[58:61], v[190:193], v[214:217], v[58:61]
	v_mfma_f32_16x16x32_bf16 v[54:57], v[182:185], v[222:225], v[54:57]
	v_mfma_f32_16x16x32_bf16 v[50:53], v[190:193], v[222:225], v[50:53]
	v_mfma_f32_16x16x32_bf16 v[46:49], v[182:185], v[230:233], v[46:49]
	v_mfma_f32_16x16x32_bf16 v[42:45], v[190:193], v[230:233], v[42:45]
	v_mfma_f32_16x16x32_bf16 v[34:37], v[182:185], v[238:241], v[34:37]
	v_mfma_f32_16x16x32_bf16 v[26:29], v[190:193], v[238:241], v[26:29]
	v_mfma_f32_16x16x32_bf16 v[38:41], v[194:197], v[210:213], v[38:41]
	v_mfma_f32_16x16x32_bf16 v[30:33], v[202:205], v[210:213], v[30:33]
	v_mfma_f32_16x16x32_bf16 v[22:25], v[194:197], v[218:221], v[22:25]
	v_mfma_f32_16x16x32_bf16 v[18:21], v[202:205], v[218:221], v[18:21]
	v_mfma_f32_16x16x32_bf16 v[14:17], v[194:197], v[226:229], v[14:17]
	v_mfma_f32_16x16x32_bf16 v[10:13], v[202:205], v[226:229], v[10:13]
	v_mfma_f32_16x16x32_bf16 v[6:9], v[194:197], v[234:237], v[6:9]
	v_mfma_f32_16x16x32_bf16 v[2:5], v[202:205], v[234:237], v[2:5]
	v_mfma_f32_16x16x32_bf16 v[38:41], v[198:201], v[214:217], v[38:41]
	v_mfma_f32_16x16x32_bf16 v[30:33], v[206:209], v[214:217], v[30:33]
	v_mfma_f32_16x16x32_bf16 v[22:25], v[198:201], v[222:225], v[22:25]
	v_mfma_f32_16x16x32_bf16 v[18:21], v[206:209], v[222:225], v[18:21]
	v_mfma_f32_16x16x32_bf16 v[14:17], v[198:201], v[230:233], v[14:17]
	v_mfma_f32_16x16x32_bf16 v[10:13], v[206:209], v[230:233], v[10:13]
	v_mfma_f32_16x16x32_bf16 v[6:9], v[198:201], v[238:241], v[6:9]
	v_mfma_f32_16x16x32_bf16 v[2:5], v[206:209], v[238:241], v[2:5]
	s_setprio 0
	s_barrier
	s_add_i32 s66, s66, 2
	s_add_u32 s15, s15, 0x100
	s_addc_u32 s65, s65, 0
	s_cmp_gt_u32 s66, 5
	s_mov_b64 s[22:23], s[24:25]
	s_cbranch_scc0 .LBB0_491
	s_branch .Lpx_13405
; #define PG8_STAGE(bufoff, gbase, voff) do { _Pragma("unroll") for (int _i = 0; _i < 2; ++_i) \
;         __builtin_amdgcn_global_load_lds((const unsigned*)((const char*)(gbase) + (voff)[_i]), (PG8_LAS unsigned*)(lds + (bufoff) + ldsw + _i * 8192), 16, 0, 0); } while (0)
; #define PG8_WAIT_V(n) asm volatile("s_waitcnt vmcnt(" #n ")" ::: "memory")
; #define PG8_WAIT_L(n) asm volatile("s_waitcnt lgkmcnt(" #n ")" ::: "memory")
; #define PG8_BAR __builtin_amdgcn_s_barrier()
; #define PG8_SCHED __builtin_amdgcn_sched_barrier(0)
; template <class Epi, class Sched, bool ALIGN_EPI = true, bool F8 = false>
; __device__ __forceinline__ void gemm_phase(PG8_LAS unsigned char* lds, const Sched& S, const Epi& E) {
;     ...
;             PG8_LDB(B0, 0, 0); PG8_LDB(B1, 0, 1); PG8_SCHED; PG8_LDA(At, 0, 0); PG8_STAGE(PG8_SA(1, 1), a1, voffA[1]);
;             PG8_WAIT_V(8); PG8_WAIT_L(0); PG8_BAR; PG8_MMA(0, 0, At, B0); PG8_MMA(0, 1, At, B1); PG8_BAR; PG8_SCHED;
;             PG8_LDA(At, 0, 1); PG8_STAGE(PG8_SB(0, 0), b2, voffB[0]); PG8_STAGE(PG8_SB(0, 1), b2, voffB[1]); PG8_STAGE(PG8_SA(0, 0), a2, vA2[0]);
.LBB0_491:
	ds_read_b128 v[178:181], v173
	ds_read_b128 v[182:185], v173 offset:1024
	ds_read_b128 v[186:189], v173 offset:2048
	ds_read_b128 v[190:193], v173 offset:3072
	ds_read_b128 v[194:197], v174
	ds_read_b128 v[198:201], v174 offset:1024
	ds_read_b128 v[202:205], v174 offset:2048
	ds_read_b128 v[206:209], v174 offset:3072
	s_add_u32 s24, s22, 0x100
	s_addc_u32 s25, s23, 0
	s_cmp_eq_u32 s66, 4
	s_cselect_b32 s29, s17, s25
	s_cselect_b32 s28, s16, s24
	s_cselect_b32 s27, s19, s65
	s_cselect_b32 s26, s18, s15
	s_mov_b32 m0, s49
	v_lshl_add_u64 v[242:243], s[22:23], 0, v[166:167]
	ds_read_b128 v[210:213], v175
	ds_read_b128 v[214:217], v175 offset:1024
	ds_read_b128 v[218:221], v175 offset:2048
	ds_read_b128 v[222:225], v175 offset:3072
	ds_read_b128 v[226:229], v175 offset:4096
	ds_read_b128 v[230:233], v175 offset:5120
	ds_read_b128 v[234:237], v175 offset:6144
	ds_read_b128 v[238:241], v175 offset:7168
	global_load_lds_dwordx4 v[242:243], off
	v_lshl_add_u64 v[242:243], s[22:23], 0, v[164:165]
	s_mov_b32 m0, s50
	s_nop 0
	global_load_lds_dwordx4 v[242:243], off
	s_waitcnt vmcnt(8)
	s_waitcnt lgkmcnt(0)
	s_barrier
	s_setprio 1
	s_waitcnt lgkmcnt(0)
	v_mfma_f32_16x16x32_bf16 v[126:129], v[178:181], v[210:213], v[126:129]
	v_mfma_f32_16x16x32_bf16 v[122:125], v[186:189], v[210:213], v[122:125]
	v_mfma_f32_16x16x32_bf16 v[118:121], v[178:181], v[218:221], v[118:121]
	v_mfma_f32_16x16x32_bf16 v[114:117], v[186:189], v[218:221], v[114:117]
	v_mfma_f32_16x16x32_bf16 v[110:113], v[178:181], v[226:229], v[110:113]
	v_mfma_f32_16x16x32_bf16 v[106:109], v[186:189], v[226:229], v[106:109]
	v_mfma_f32_16x16x32_bf16 v[98:101], v[178:181], v[234:237], v[98:101]
	v_mfma_f32_16x16x32_bf16 v[90:93], v[186:189], v[234:237], v[90:93]
	v_mfma_f32_16x16x32_bf16 v[126:129], v[182:185], v[214:217], v[126:129]
	v_mfma_f32_16x16x32_bf16 v[122:125], v[190:193], v[214:217], v[122:125]
	v_mfma_f32_16x16x32_bf16 v[118:121], v[182:185], v[222:225], v[118:121]
	v_mfma_f32_16x16x32_bf16 v[114:117], v[190:193], v[222:225], v[114:117]
	v_mfma_f32_16x16x32_bf16 v[110:113], v[182:185], v[230:233], v[110:113]
	v_mfma_f32_16x16x32_bf16 v[106:109], v[190:193], v[230:233], v[106:109]
	v_mfma_f32_16x16x32_bf16 v[98:101], v[182:185], v[238:241], v[98:101]
	v_mfma_f32_16x16x32_bf16 v[90:93], v[190:193], v[238:241], v[90:93]
	v_mfma_f32_16x16x32_bf16 v[102:105], v[194:197], v[210:213], v[102:105]
	v_mfma_f32_16x16x32_bf16 v[94:97], v[202:205], v[210:213], v[94:97]
	v_mfma_f32_16x16x32_bf16 v[86:89], v[194:197], v[218:221], v[86:89]
	v_mfma_f32_16x16x32_bf16 v[82:85], v[202:205], v[218:221], v[82:85]
	v_mfma_f32_16x16x32_bf16 v[78:81], v[194:197], v[226:229], v[78:81]
	v_mfma_f32_16x16x32_bf16 v[74:77], v[202:205], v[226:229], v[74:77]
	v_mfma_f32_16x16x32_bf16 v[70:73], v[194:197], v[234:237], v[70:73]
	v_mfma_f32_16x16x32_bf16 v[66:69], v[202:205], v[234:237], v[66:69]
	v_mfma_f32_16x16x32_bf16 v[102:105], v[198:201], v[214:217], v[102:105]
	v_mfma_f32_16x16x32_bf16 v[94:97], v[206:209], v[214:217], v[94:97]
	v_mfma_f32_16x16x32_bf16 v[86:89], v[198:201], v[222:225], v[86:89]
	v_mfma_f32_16x16x32_bf16 v[82:85], v[206:209], v[222:225], v[82:85]
	v_mfma_f32_16x16x32_bf16 v[78:81], v[198:201], v[230:233], v[78:81]
	v_mfma_f32_16x16x32_bf16 v[74:77], v[206:209], v[230:233], v[74:77]
	v_mfma_f32_16x16x32_bf16 v[70:73], v[198:201], v[238:241], v[70:73]
	v_mfma_f32_16x16x32_bf16 v[66:69], v[206:209], v[238:241], v[66:69]
	s_setprio 0
	s_barrier
	s_mov_b32 m0, s51
	v_lshl_add_u64 v[242:243], s[26:27], 0, v[134:135]
	ds_read_b128 v[210:213], v175 offset:16384
	ds_read_b128 v[214:217], v175 offset:17408
	ds_read_b128 v[218:221], v175 offset:18432
	ds_read_b128 v[222:225], v175 offset:19456
	ds_read_b128 v[226:229], v175 offset:20480
	ds_read_b128 v[230:233], v175 offset:21504
	ds_read_b128 v[234:237], v175 offset:22528
	ds_read_b128 v[238:241], v175 offset:23552
	global_load_lds_dwordx4 v[242:243], off
	v_lshl_add_u64 v[244:245], s[26:27], 0, v[130:131]
	s_mov_b32 m0, s52
	v_lshl_add_u64 v[246:247], s[26:27], 0, v[136:137]
	global_load_lds_dwordx4 v[244:245], off
	s_mov_b32 m0, s53
	v_lshl_add_u64 v[248:249], s[28:29], 0, v[140:141]
	global_load_lds_dwordx4 v[246:247], off
	v_lshl_add_u64 v[246:247], s[26:27], 0, v[132:133]
	s_mov_b32 m0, s59
	s_nop 0
	global_load_lds_dwordx4 v[246:247], off
	v_lshl_add_u64 v[246:247], s[28:29], 0, v[138:139]
	s_mov_b32 m0, s42
	s_nop 0
	global_load_lds_dwordx4 v[246:247], off
	s_mov_b32 m0, s43
	s_nop 0
	global_load_lds_dwordx4 v[248:249], off
	s_waitcnt vmcnt(8)
	s_waitcnt lgkmcnt(0)
	s_barrier
; #define PG8_STAGE(bufoff, gbase, voff) do { _Pragma("unroll") for (int _i = 0; _i < 2; ++_i) \
;         __builtin_amdgcn_global_load_lds((const unsigned*)((const char*)(gbase) + (voff)[_i]), (PG8_LAS unsigned*)(lds + (bufoff) + ldsw + _i * 8192), 16, 0, 0); } while (0)
; #define PG8_WAIT_V(n) asm volatile("s_waitcnt vmcnt(" #n ")" ::: "memory")
; #define PG8_WAIT_L(n) asm volatile("s_waitcnt lgkmcnt(" #n ")" ::: "memory")
; #define PG8_BAR __builtin_amdgcn_s_barrier()
; #define PG8_SCHED __builtin_amdgcn_sched_barrier(0)
; template <class Epi, class Sched, bool ALIGN_EPI = true, bool F8 = false>
; __device__ __forceinline__ void gemm_phase(PG8_LAS unsigned char* lds, const Sched& S, const Epi& E) {
;     ...
;             PG8_WAIT_V(8); PG8_WAIT_L(0); PG8_BAR; PG8_MMA(1, 0, At, B0); PG8_MMA(1, 1, At, B1); PG8_BAR; PG8_SCHED;
;             PG8_LDB(B0, 1, 0); PG8_LDB(B1, 1, 1); PG8_SCHED; PG8_LDA(At, 1, 0); PG8_STAGE(PG8_SA(0, 1), a2, vA2[1]);
;             PG8_WAIT_V(8); PG8_WAIT_L(0); PG8_BAR; PG8_MMA(0, 0, At, B0); PG8_MMA(0, 1, At, B1); PG8_BAR; PG8_SCHED;
	s_setprio 1
	s_waitcnt lgkmcnt(0)
	v_mfma_f32_16x16x32_bf16 v[62:65], v[178:181], v[210:213], v[62:65]
	v_mfma_f32_16x16x32_bf16 v[58:61], v[186:189], v[210:213], v[58:61]
	v_mfma_f32_16x16x32_bf16 v[54:57], v[178:181], v[218:221], v[54:57]
	v_mfma_f32_16x16x32_bf16 v[50:53], v[186:189], v[218:221], v[50:53]
	v_mfma_f32_16x16x32_bf16 v[46:49], v[178:181], v[226:229], v[46:49]
	v_mfma_f32_16x16x32_bf16 v[42:45], v[186:189], v[226:229], v[42:45]
	v_mfma_f32_16x16x32_bf16 v[34:37], v[178:181], v[234:237], v[34:37]
	v_mfma_f32_16x16x32_bf16 v[26:29], v[186:189], v[234:237], v[26:29]
	v_mfma_f32_16x16x32_bf16 v[62:65], v[182:185], v[214:217], v[62:65]
	v_mfma_f32_16x16x32_bf16 v[58:61], v[190:193], v[214:217], v[58:61]
	v_mfma_f32_16x16x32_bf16 v[54:57], v[182:185], v[222:225], v[54:57]
	v_mfma_f32_16x16x32_bf16 v[50:53], v[190:193], v[222:225], v[50:53]
	v_mfma_f32_16x16x32_bf16 v[46:49], v[182:185], v[230:233], v[46:49]
	v_mfma_f32_16x16x32_bf16 v[42:45], v[190:193], v[230:233], v[42:45]
	v_mfma_f32_16x16x32_bf16 v[34:37], v[182:185], v[238:241], v[34:37]
	v_mfma_f32_16x16x32_bf16 v[26:29], v[190:193], v[238:241], v[26:29]
	v_mfma_f32_16x16x32_bf16 v[38:41], v[194:197], v[210:213], v[38:41]
	v_mfma_f32_16x16x32_bf16 v[30:33], v[202:205], v[210:213], v[30:33]
	v_mfma_f32_16x16x32_bf16 v[22:25], v[194:197], v[218:221], v[22:25]
	v_mfma_f32_16x16x32_bf16 v[18:21], v[202:205], v[218:221], v[18:21]
	v_mfma_f32_16x16x32_bf16 v[14:17], v[194:197], v[226:229], v[14:17]
	v_mfma_f32_16x16x32_bf16 v[10:13], v[202:205], v[226:229], v[10:13]
	v_mfma_f32_16x16x32_bf16 v[6:9], v[194:197], v[234:237], v[6:9]
	v_mfma_f32_16x16x32_bf16 v[2:5], v[202:205], v[234:237], v[2:5]
	v_mfma_f32_16x16x32_bf16 v[38:41], v[198:201], v[214:217], v[38:41]
	v_mfma_f32_16x16x32_bf16 v[30:33], v[206:209], v[214:217], v[30:33]
	v_mfma_f32_16x16x32_bf16 v[22:25], v[198:201], v[222:225], v[22:25]
	v_mfma_f32_16x16x32_bf16 v[18:21], v[206:209], v[222:225], v[18:21]
	v_mfma_f32_16x16x32_bf16 v[14:17], v[198:201], v[230:233], v[14:17]
	v_mfma_f32_16x16x32_bf16 v[10:13], v[206:209], v[230:233], v[10:13]
	v_mfma_f32_16x16x32_bf16 v[6:9], v[198:201], v[238:241], v[6:9]
	v_mfma_f32_16x16x32_bf16 v[2:5], v[206:209], v[238:241], v[2:5]
	s_setprio 0
	s_barrier
	ds_read_b128 v[178:181], v176
	ds_read_b128 v[182:185], v176 offset:1024
	ds_read_b128 v[186:189], v176 offset:2048
	ds_read_b128 v[190:193], v176 offset:3072
	ds_read_b128 v[194:197], v177
	ds_read_b128 v[198:201], v177 offset:1024
	ds_read_b128 v[202:205], v177 offset:2048
	ds_read_b128 v[206:209], v177 offset:3072
	s_mov_b32 m0, s44
	v_lshl_add_u64 v[250:251], s[28:29], 0, v[142:143]
	ds_read_b128 v[210:213], v175 offset:32768
	ds_read_b128 v[214:217], v175 offset:33792
	ds_read_b128 v[218:221], v175 offset:34816
	ds_read_b128 v[222:225], v175 offset:35840
	ds_read_b128 v[226:229], v175 offset:36864
	ds_read_b128 v[230:233], v175 offset:37888
	ds_read_b128 v[234:237], v175 offset:38912
	ds_read_b128 v[238:241], v175 offset:39936
	global_load_lds_dwordx4 v[250:251], off
	v_lshl_add_u64 v[250:251], s[28:29], 0, v[144:145]
	s_mov_b32 m0, s45
	s_nop 0
	global_load_lds_dwordx4 v[250:251], off
	s_waitcnt vmcnt(8)
	s_waitcnt lgkmcnt(0)
	s_barrier
	s_setprio 1
	s_waitcnt lgkmcnt(0)
	v_mfma_f32_16x16x32_bf16 v[126:129], v[178:181], v[210:213], v[126:129]
	v_mfma_f32_16x16x32_bf16 v[122:125], v[186:189], v[210:213], v[122:125]
	v_mfma_f32_16x16x32_bf16 v[118:121], v[178:181], v[218:221], v[118:121]
	v_mfma_f32_16x16x32_bf16 v[114:117], v[186:189], v[218:221], v[114:117]
	v_mfma_f32_16x16x32_bf16 v[110:113], v[178:181], v[226:229], v[110:113]
	v_mfma_f32_16x16x32_bf16 v[106:109], v[186:189], v[226:229], v[106:109]
	v_mfma_f32_16x16x32_bf16 v[98:101], v[178:181], v[234:237], v[98:101]
	v_mfma_f32_16x16x32_bf16 v[90:93], v[186:189], v[234:237], v[90:93]
	v_mfma_f32_16x16x32_bf16 v[126:129], v[182:185], v[214:217], v[126:129]
	v_mfma_f32_16x16x32_bf16 v[122:125], v[190:193], v[214:217], v[122:125]
	v_mfma_f32_16x16x32_bf16 v[118:121], v[182:185], v[222:225], v[118:121]
	v_mfma_f32_16x16x32_bf16 v[114:117], v[190:193], v[222:225], v[114:117]
	v_mfma_f32_16x16x32_bf16 v[110:113], v[182:185], v[230:233], v[110:113]
	v_mfma_f32_16x16x32_bf16 v[106:109], v[190:193], v[230:233], v[106:109]
	v_mfma_f32_16x16x32_bf16 v[98:101], v[182:185], v[238:241], v[98:101]
	v_mfma_f32_16x16x32_bf16 v[90:93], v[190:193], v[238:241], v[90:93]
	v_mfma_f32_16x16x32_bf16 v[102:105], v[194:197], v[210:213], v[102:105]
	v_mfma_f32_16x16x32_bf16 v[94:97], v[202:205], v[210:213], v[94:97]
	v_mfma_f32_16x16x32_bf16 v[86:89], v[194:197], v[218:221], v[86:89]
	v_mfma_f32_16x16x32_bf16 v[82:85], v[202:205], v[218:221], v[82:85]
	v_mfma_f32_16x16x32_bf16 v[78:81], v[194:197], v[226:229], v[78:81]
	v_mfma_f32_16x16x32_bf16 v[74:77], v[202:205], v[226:229], v[74:77]
	v_mfma_f32_16x16x32_bf16 v[70:73], v[194:197], v[234:237], v[70:73]
	v_mfma_f32_16x16x32_bf16 v[66:69], v[202:205], v[234:237], v[66:69]
	v_mfma_f32_16x16x32_bf16 v[102:105], v[198:201], v[214:217], v[102:105]
	v_mfma_f32_16x16x32_bf16 v[94:97], v[206:209], v[214:217], v[94:97]
	v_mfma_f32_16x16x32_bf16 v[86:89], v[198:201], v[222:225], v[86:89]
	v_mfma_f32_16x16x32_bf16 v[82:85], v[206:209], v[222:225], v[82:85]
	v_mfma_f32_16x16x32_bf16 v[78:81], v[198:201], v[230:233], v[78:81]
	v_mfma_f32_16x16x32_bf16 v[74:77], v[206:209], v[230:233], v[74:77]
	v_mfma_f32_16x16x32_bf16 v[70:73], v[198:201], v[238:241], v[70:73]
	v_mfma_f32_16x16x32_bf16 v[66:69], v[206:209], v[238:241], v[66:69]
	s_setprio 0
	s_barrier
; #define PG8_STAGE(bufoff, gbase, voff) do { _Pragma("unroll") for (int _i = 0; _i < 2; ++_i) \
;         __builtin_amdgcn_global_load_lds((const unsigned*)((const char*)(gbase) + (voff)[_i]), (PG8_LAS unsigned*)(lds + (bufoff) + ldsw + _i * 8192), 16, 0, 0); } while (0)
; #define PG8_WAIT_V(n) asm volatile("s_waitcnt vmcnt(" #n ")" ::: "memory")
; #define PG8_WAIT_L(n) asm volatile("s_waitcnt lgkmcnt(" #n ")" ::: "memory")
; #define PG8_BAR __builtin_amdgcn_s_barrier()
; #define PG8_SCHED __builtin_amdgcn_sched_barrier(0)
; template <class Epi, class Sched, bool ALIGN_EPI = true, bool F8 = false>
; __device__ __forceinline__ void gemm_phase(PG8_LAS unsigned char* lds, const Sched& S, const Epi& E) {
;     ...
;             PG8_LDA(At, 1, 1); PG8_STAGE(PG8_SB(1, 0), b3, voffB[0]); PG8_STAGE(PG8_SB(1, 1), b3, voffB[1]); PG8_STAGE(PG8_SA(1, 0), a3, vA2[0]);
;             PG8_WAIT_V(8); PG8_WAIT_L(0); PG8_BAR; PG8_MMA(1, 0, At, B0); PG8_MMA(1, 1, At, B1); PG8_BAR; PG8_SCHED;
;         }
	s_mov_b32 m0, s60
	s_add_u32 s22, s26, 0x80
	v_lshl_add_u64 v[242:243], v[242:243], 0, s[8:9]
	ds_read_b128 v[210:213], v175 offset:49152
	ds_read_b128 v[214:217], v175 offset:50176
	ds_read_b128 v[218:221], v175 offset:51200
	ds_read_b128 v[222:225], v175 offset:52224
	ds_read_b128 v[226:229], v175 offset:53248
	ds_read_b128 v[230:233], v175 offset:54272
	ds_read_b128 v[234:237], v175 offset:55296
	ds_read_b128 v[238:241], v175 offset:56320
	s_addc_u32 s23, s27, 0
	global_load_lds_dwordx4 v[242:243], off
	v_lshl_add_u64 v[242:243], v[244:245], 0, s[8:9]
	s_mov_b32 m0, s61
	s_nop 0
	global_load_lds_dwordx4 v[242:243], off
	v_lshl_add_u64 v[242:243], s[22:23], 0, v[136:137]
	s_mov_b32 m0, s62
	s_nop 0
	global_load_lds_dwordx4 v[242:243], off
	v_lshl_add_u64 v[242:243], s[22:23], 0, v[132:133]
	s_mov_b32 m0, s63
	s_nop 0
	global_load_lds_dwordx4 v[242:243], off
	v_lshl_add_u64 v[242:243], v[246:247], 0, s[8:9]
	s_mov_b32 m0, s47
	s_nop 0
	global_load_lds_dwordx4 v[242:243], off
	v_lshl_add_u64 v[242:243], v[248:249], 0, s[8:9]
	s_mov_b32 m0, s48
	s_nop 0
	global_load_lds_dwordx4 v[242:243], off
	s_waitcnt vmcnt(8)
	s_waitcnt lgkmcnt(0)
	s_barrier
	s_setprio 1
	s_waitcnt lgkmcnt(0)
	v_mfma_f32_16x16x32_bf16 v[62:65], v[178:181], v[210:213], v[62:65]
	v_mfma_f32_16x16x32_bf16 v[58:61], v[186:189], v[210:213], v[58:61]
	v_mfma_f32_16x16x32_bf16 v[54:57], v[178:181], v[218:221], v[54:57]
	v_mfma_f32_16x16x32_bf16 v[50:53], v[186:189], v[218:221], v[50:53]
	v_mfma_f32_16x16x32_bf16 v[46:49], v[178:181], v[226:229], v[46:49]
	v_mfma_f32_16x16x32_bf16 v[42:45], v[186:189], v[226:229], v[42:45]
	v_mfma_f32_16x16x32_bf16 v[34:37], v[178:181], v[234:237], v[34:37]
	v_mfma_f32_16x16x32_bf16 v[26:29], v[186:189], v[234:237], v[26:29]
	v_mfma_f32_16x16x32_bf16 v[62:65], v[182:185], v[214:217], v[62:65]
	v_mfma_f32_16x16x32_bf16 v[58:61], v[190:193], v[214:217], v[58:61]
	v_mfma_f32_16x16x32_bf16 v[54:57], v[182:185], v[222:225], v[54:57]
	v_mfma_f32_16x16x32_bf16 v[50:53], v[190:193], v[222:225], v[50:53]
	v_mfma_f32_16x16x32_bf16 v[46:49], v[182:185], v[230:233], v[46:49]
	v_mfma_f32_16x16x32_bf16 v[42:45], v[190:193], v[230:233], v[42:45]
	v_mfma_f32_16x16x32_bf16 v[34:37], v[182:185], v[238:241], v[34:37]
	v_mfma_f32_16x16x32_bf16 v[26:29], v[190:193], v[238:241], v[26:29]
	v_mfma_f32_16x16x32_bf16 v[38:41], v[194:197], v[210:213], v[38:41]
	v_mfma_f32_16x16x32_bf16 v[30:33], v[202:205], v[210:213], v[30:33]
	v_mfma_f32_16x16x32_bf16 v[22:25], v[194:197], v[218:221], v[22:25]
	v_mfma_f32_16x16x32_bf16 v[18:21], v[202:205], v[218:221], v[18:21]
	v_mfma_f32_16x16x32_bf16 v[14:17], v[194:197], v[226:229], v[14:17]
	v_mfma_f32_16x16x32_bf16 v[10:13], v[202:205], v[226:229], v[10:13]
	v_mfma_f32_16x16x32_bf16 v[6:9], v[194:197], v[234:237], v[6:9]
	v_mfma_f32_16x16x32_bf16 v[2:5], v[202:205], v[234:237], v[2:5]
	v_mfma_f32_16x16x32_bf16 v[38:41], v[198:201], v[214:217], v[38:41]
	v_mfma_f32_16x16x32_bf16 v[30:33], v[206:209], v[214:217], v[30:33]
	v_mfma_f32_16x16x32_bf16 v[22:25], v[198:201], v[222:225], v[22:25]
	v_mfma_f32_16x16x32_bf16 v[18:21], v[206:209], v[222:225], v[18:21]
	v_mfma_f32_16x16x32_bf16 v[14:17], v[198:201], v[230:233], v[14:17]
	v_mfma_f32_16x16x32_bf16 v[10:13], v[206:209], v[230:233], v[10:13]
	v_mfma_f32_16x16x32_bf16 v[6:9], v[198:201], v[238:241], v[6:9]
	v_mfma_f32_16x16x32_bf16 v[2:5], v[206:209], v[238:241], v[2:5]
	s_setprio 0
	s_barrier
	s_add_i32 s66, s66, 2
	s_add_u32 s15, s15, 0x100
	s_addc_u32 s65, s65, 0
	s_cmp_gt_u32 s66, 5
	s_mov_b64 s[22:23], s[24:25]
	s_cbranch_scc0 .LBB0_491

; #define PG8_STAGE(bufoff, gbase, voff) do { _Pragma("unroll") for (int _i = 0; _i < 2; ++_i) \
;         __builtin_amdgcn_global_load_lds((const unsigned*)((const char*)(gbase) + (voff)[_i]), (PG8_LAS unsigned*)(lds + (bufoff) + ldsw + _i * 8192), 16, 0, 0); } while (0)
; #define PG8_WAIT_V(n) asm volatile("s_waitcnt vmcnt(" #n ")" ::: "memory")
; #define PG8_WAIT_L(n) asm volatile("s_waitcnt lgkmcnt(" #n ")" ::: "memory")
; #define PG8_BAR __builtin_amdgcn_s_barrier()
; #define PG8_SCHED __builtin_amdgcn_sched_barrier(0)
; template <class Epi, class Sched, bool ALIGN_EPI = true, bool F8 = false>
; __device__ __forceinline__ void gemm_phase(PG8_LAS unsigned char* lds, const Sched& S, const Epi& E) {
;     ...
;             PG8_LDB(B0, 0, 0); PG8_LDB(B1, 0, 1); PG8_SCHED; PG8_LDA(At, 0, 0); PG8_STAGE(PG8_SA(1, 1), a1, voffA[1]);
;             PG8_WAIT_V(8); PG8_WAIT_L(0); PG8_BAR; PG8_MMA(0, 0, At, B0); PG8_MMA(0, 1, At, B1); PG8_BAR; PG8_SCHED;
;             PG8_LDA(At, 0, 1); PG8_STAGE(PG8_SB(0, 0), b2, voffB[0]); PG8_STAGE(PG8_SB(0, 1), b2, voffB[1]); PG8_STAGE(PG8_SA(0, 0), a2, vA2[0]);
;             PG8_WAIT_V(8); PG8_WAIT_L(0); PG8_BAR; PG8_MMA(1, 0, At, B0); PG8_MMA(1, 1, At, B1); PG8_BAR; PG8_SCHED;
.Lpkb_514:
	s_add_u32 s44, s22, s15
	ds_read_b128 v[172:175], v164
	ds_read_b128 v[176:179], v164 offset:1024
	ds_read_b128 v[180:183], v164 offset:2048
	ds_read_b128 v[184:187], v164 offset:3072
	ds_read_b128 v[188:191], v165
	ds_read_b128 v[192:195], v165 offset:1024
	ds_read_b128 v[196:199], v165 offset:2048
	ds_read_b128 v[200:203], v165 offset:3072
	s_addc_u32 s45, s23, 0
	s_add_u32 s17, s44, 0x100
	s_addc_u32 s72, s45, 0
	s_and_b64 s[42:43], s[40:41], exec
	s_cselect_b32 s42, s24, s17
	s_cselect_b32 s43, s25, s72
	s_add_u32 s15, s26, s15
	s_addc_u32 s17, s27, 0
	s_add_u32 s15, s15, 0x100
	s_addc_u32 s17, s17, 0
	s_and_b64 s[40:41], s[40:41], exec
	s_cselect_b32 s40, s20, s15
	s_cselect_b32 s41, s21, s17
	v_lshl_add_u64 v[236:237], s[44:45], 0, v[142:143]
	s_mov_b32 m0, s61
	v_lshl_add_u64 v[236:237], v[236:237], 0, s[10:11]
	ds_read_b128 v[204:207], v166
	ds_read_b128 v[208:211], v166 offset:1024
	ds_read_b128 v[212:215], v166 offset:2048
	ds_read_b128 v[216:219], v166 offset:3072
	ds_read_b128 v[220:223], v166 offset:4096
	ds_read_b128 v[224:227], v166 offset:5120
	ds_read_b128 v[228:231], v166 offset:6144
	ds_read_b128 v[232:235], v166 offset:7168
	global_load_lds_dwordx4 v[236:237], off
	v_lshl_add_u64 v[236:237], s[44:45], 0, v[144:145]
	v_lshl_add_u64 v[236:237], v[236:237], 0, s[10:11]
	s_mov_b32 m0, s62
	s_nop 0
	global_load_lds_dwordx4 v[236:237], off
	s_waitcnt vmcnt(8)
	s_waitcnt lgkmcnt(0)
	s_barrier
	s_setprio 1
	s_waitcnt lgkmcnt(0)
	v_mfma_f32_16x16x32_bf16 v[126:129], v[172:175], v[204:207], 0
	v_mfma_f32_16x16x32_bf16 v[122:125], v[180:183], v[204:207], 0
	v_mfma_f32_16x16x32_bf16 v[118:121], v[172:175], v[212:215], 0
	v_mfma_f32_16x16x32_bf16 v[114:117], v[180:183], v[212:215], 0
	v_mfma_f32_16x16x32_bf16 v[102:105], v[172:175], v[220:223], 0
	v_mfma_f32_16x16x32_bf16 v[98:101], v[180:183], v[220:223], 0
	v_mfma_f32_16x16x32_bf16 v[86:89], v[172:175], v[228:231], 0
	v_mfma_f32_16x16x32_bf16 v[82:85], v[180:183], v[228:231], 0
	v_mfma_f32_16x16x32_bf16 v[126:129], v[176:179], v[208:211], v[126:129]
	v_mfma_f32_16x16x32_bf16 v[122:125], v[184:187], v[208:211], v[122:125]
	v_mfma_f32_16x16x32_bf16 v[118:121], v[176:179], v[216:219], v[118:121]
	v_mfma_f32_16x16x32_bf16 v[114:117], v[184:187], v[216:219], v[114:117]
	v_mfma_f32_16x16x32_bf16 v[102:105], v[176:179], v[224:227], v[102:105]
	v_mfma_f32_16x16x32_bf16 v[98:101], v[184:187], v[224:227], v[98:101]
	v_mfma_f32_16x16x32_bf16 v[86:89], v[176:179], v[232:235], v[86:89]
	v_mfma_f32_16x16x32_bf16 v[82:85], v[184:187], v[232:235], v[82:85]
	v_mfma_f32_16x16x32_bf16 v[110:113], v[188:191], v[204:207], 0
	v_mfma_f32_16x16x32_bf16 v[106:109], v[196:199], v[204:207], 0
	v_mfma_f32_16x16x32_bf16 v[94:97], v[188:191], v[212:215], 0
	v_mfma_f32_16x16x32_bf16 v[90:93], v[196:199], v[212:215], 0
	v_mfma_f32_16x16x32_bf16 v[78:81], v[188:191], v[220:223], 0
	v_mfma_f32_16x16x32_bf16 v[74:77], v[196:199], v[220:223], 0
	v_mfma_f32_16x16x32_bf16 v[70:73], v[188:191], v[228:231], 0
	v_mfma_f32_16x16x32_bf16 v[66:69], v[196:199], v[228:231], 0
	v_mfma_f32_16x16x32_bf16 v[110:113], v[192:195], v[208:211], v[110:113]
	v_mfma_f32_16x16x32_bf16 v[106:109], v[200:203], v[208:211], v[106:109]
	v_mfma_f32_16x16x32_bf16 v[94:97], v[192:195], v[216:219], v[94:97]
	v_mfma_f32_16x16x32_bf16 v[90:93], v[200:203], v[216:219], v[90:93]
	v_mfma_f32_16x16x32_bf16 v[78:81], v[192:195], v[224:227], v[78:81]
	v_mfma_f32_16x16x32_bf16 v[74:77], v[200:203], v[224:227], v[74:77]
	v_mfma_f32_16x16x32_bf16 v[70:73], v[192:195], v[232:235], v[70:73]
	v_mfma_f32_16x16x32_bf16 v[66:69], v[200:203], v[232:235], v[66:69]
	s_setprio 0
	s_barrier
	s_mov_b32 m0, s63
	v_lshl_add_u64 v[236:237], s[40:41], 0, v[136:137]
	ds_read_b128 v[204:207], v166 offset:16384
	ds_read_b128 v[208:211], v166 offset:17408
	ds_read_b128 v[212:215], v166 offset:18432
	ds_read_b128 v[216:219], v166 offset:19456
	ds_read_b128 v[220:223], v166 offset:20480
	ds_read_b128 v[224:227], v166 offset:21504
	ds_read_b128 v[228:231], v166 offset:22528
	ds_read_b128 v[232:235], v166 offset:23552
	global_load_lds_dwordx4 v[236:237], off
	v_lshl_add_u64 v[238:239], s[40:41], 0, v[134:135]
	s_mov_b32 m0, s64
	v_lshl_add_u64 v[240:241], s[40:41], 0, v[132:133]
	global_load_lds_dwordx4 v[238:239], off
	s_mov_b32 m0, s65
	v_lshl_add_u64 v[242:243], s[40:41], 0, v[130:131]
	global_load_lds_dwordx4 v[240:241], off
	s_mov_b32 m0, s66
	v_lshl_add_u64 v[244:245], s[42:43], 0, v[138:139]
	global_load_lds_dwordx4 v[242:243], off
	s_mov_b32 m0, s50
	v_lshl_add_u64 v[246:247], s[42:43], 0, v[140:141]
	global_load_lds_dwordx4 v[244:245], off
	s_mov_b32 m0, s51
	s_nop 0
	global_load_lds_dwordx4 v[246:247], off
	s_waitcnt vmcnt(8)
	s_waitcnt lgkmcnt(0)
	s_barrier
; #define PG8_STAGE(bufoff, gbase, voff) do { _Pragma("unroll") for (int _i = 0; _i < 2; ++_i) \
;         __builtin_amdgcn_global_load_lds((const unsigned*)((const char*)(gbase) + (voff)[_i]), (PG8_LAS unsigned*)(lds + (bufoff) + ldsw + _i * 8192), 16, 0, 0); } while (0)
; #define PG8_WAIT_V(n) asm volatile("s_waitcnt vmcnt(" #n ")" ::: "memory")
; #define PG8_WAIT_L(n) asm volatile("s_waitcnt lgkmcnt(" #n ")" ::: "memory")
; #define PG8_BAR __builtin_amdgcn_s_barrier()
; #define PG8_SCHED __builtin_amdgcn_sched_barrier(0)
; template <class Epi, class Sched, bool ALIGN_EPI = true, bool F8 = false>
; __device__ __forceinline__ void gemm_phase(PG8_LAS unsigned char* lds, const Sched& S, const Epi& E) {
;     ...
;             PG8_WAIT_V(8); PG8_WAIT_L(0); PG8_BAR; PG8_MMA(1, 0, At, B0); PG8_MMA(1, 1, At, B1); PG8_BAR; PG8_SCHED;
;             PG8_LDB(B0, 1, 0); PG8_LDB(B1, 1, 1); PG8_SCHED; PG8_LDA(At, 1, 0); PG8_STAGE(PG8_SA(0, 1), a2, vA2[1]);
;             PG8_WAIT_V(8); PG8_WAIT_L(0); PG8_BAR; PG8_MMA(0, 0, At, B0); PG8_MMA(0, 1, At, B1); PG8_BAR; PG8_SCHED;
	s_setprio 1
	s_waitcnt lgkmcnt(0)
	v_mfma_f32_16x16x32_bf16 v[62:65], v[172:175], v[204:207], 0
	v_mfma_f32_16x16x32_bf16 v[58:61], v[180:183], v[204:207], 0
	v_mfma_f32_16x16x32_bf16 v[54:57], v[172:175], v[212:215], 0
	v_mfma_f32_16x16x32_bf16 v[50:53], v[180:183], v[212:215], 0
	v_mfma_f32_16x16x32_bf16 v[38:41], v[172:175], v[220:223], 0
	v_mfma_f32_16x16x32_bf16 v[34:37], v[180:183], v[220:223], 0
	v_mfma_f32_16x16x32_bf16 v[22:25], v[172:175], v[228:231], 0
	v_mfma_f32_16x16x32_bf16 v[18:21], v[180:183], v[228:231], 0
	v_mfma_f32_16x16x32_bf16 v[62:65], v[176:179], v[208:211], v[62:65]
	v_mfma_f32_16x16x32_bf16 v[58:61], v[184:187], v[208:211], v[58:61]
	v_mfma_f32_16x16x32_bf16 v[54:57], v[176:179], v[216:219], v[54:57]
	v_mfma_f32_16x16x32_bf16 v[50:53], v[184:187], v[216:219], v[50:53]
	v_mfma_f32_16x16x32_bf16 v[38:41], v[176:179], v[224:227], v[38:41]
	v_mfma_f32_16x16x32_bf16 v[34:37], v[184:187], v[224:227], v[34:37]
	v_mfma_f32_16x16x32_bf16 v[22:25], v[176:179], v[232:235], v[22:25]
	v_mfma_f32_16x16x32_bf16 v[18:21], v[184:187], v[232:235], v[18:21]
	v_mfma_f32_16x16x32_bf16 v[46:49], v[188:191], v[204:207], 0
	v_mfma_f32_16x16x32_bf16 v[42:45], v[196:199], v[204:207], 0
	v_mfma_f32_16x16x32_bf16 v[30:33], v[188:191], v[212:215], 0
	v_mfma_f32_16x16x32_bf16 v[26:29], v[196:199], v[212:215], 0
	v_mfma_f32_16x16x32_bf16 v[14:17], v[188:191], v[220:223], 0
	v_mfma_f32_16x16x32_bf16 v[10:13], v[196:199], v[220:223], 0
	v_mfma_f32_16x16x32_bf16 v[6:9], v[188:191], v[228:231], 0
	v_mfma_f32_16x16x32_bf16 v[2:5], v[196:199], v[228:231], 0
	v_mfma_f32_16x16x32_bf16 v[46:49], v[192:195], v[208:211], v[46:49]
	v_mfma_f32_16x16x32_bf16 v[42:45], v[200:203], v[208:211], v[42:45]
	v_mfma_f32_16x16x32_bf16 v[30:33], v[192:195], v[216:219], v[30:33]
	v_mfma_f32_16x16x32_bf16 v[26:29], v[200:203], v[216:219], v[26:29]
	v_mfma_f32_16x16x32_bf16 v[14:17], v[192:195], v[224:227], v[14:17]
	v_mfma_f32_16x16x32_bf16 v[10:13], v[200:203], v[224:227], v[10:13]
	v_mfma_f32_16x16x32_bf16 v[6:9], v[192:195], v[232:235], v[6:9]
	v_mfma_f32_16x16x32_bf16 v[2:5], v[200:203], v[232:235], v[2:5]
	s_setprio 0
	s_barrier
	ds_read_b128 v[172:175], v167
	ds_read_b128 v[176:179], v167 offset:1024
	ds_read_b128 v[180:183], v167 offset:2048
	ds_read_b128 v[184:187], v167 offset:3072
	ds_read_b128 v[188:191], v168
	ds_read_b128 v[192:195], v168 offset:1024
	ds_read_b128 v[196:199], v168 offset:2048
	ds_read_b128 v[200:203], v168 offset:3072
	s_mov_b32 m0, s52
	v_lshl_add_u64 v[248:249], s[42:43], 0, v[142:143]
	ds_read_b128 v[204:207], v166 offset:32768
	ds_read_b128 v[208:211], v166 offset:33792
	ds_read_b128 v[212:215], v166 offset:34816
	ds_read_b128 v[216:219], v166 offset:35840
	ds_read_b128 v[220:223], v166 offset:36864
	ds_read_b128 v[224:227], v166 offset:37888
	ds_read_b128 v[228:231], v166 offset:38912
	ds_read_b128 v[232:235], v166 offset:39936
	global_load_lds_dwordx4 v[248:249], off
	v_lshl_add_u64 v[248:249], s[42:43], 0, v[144:145]
	s_mov_b32 m0, s53
	s_nop 0
	global_load_lds_dwordx4 v[248:249], off
	s_waitcnt vmcnt(8)
	s_waitcnt lgkmcnt(0)
	s_barrier
	s_setprio 1
	s_waitcnt lgkmcnt(0)
	v_mfma_f32_16x16x32_bf16 v[126:129], v[172:175], v[204:207], v[126:129]
	v_mfma_f32_16x16x32_bf16 v[122:125], v[180:183], v[204:207], v[122:125]
	v_mfma_f32_16x16x32_bf16 v[118:121], v[172:175], v[212:215], v[118:121]
	v_mfma_f32_16x16x32_bf16 v[114:117], v[180:183], v[212:215], v[114:117]
	v_mfma_f32_16x16x32_bf16 v[102:105], v[172:175], v[220:223], v[102:105]
	v_mfma_f32_16x16x32_bf16 v[98:101], v[180:183], v[220:223], v[98:101]
	v_mfma_f32_16x16x32_bf16 v[86:89], v[172:175], v[228:231], v[86:89]
	v_mfma_f32_16x16x32_bf16 v[82:85], v[180:183], v[228:231], v[82:85]
	v_mfma_f32_16x16x32_bf16 v[126:129], v[176:179], v[208:211], v[126:129]
	v_mfma_f32_16x16x32_bf16 v[122:125], v[184:187], v[208:211], v[122:125]
	v_mfma_f32_16x16x32_bf16 v[118:121], v[176:179], v[216:219], v[118:121]
	v_mfma_f32_16x16x32_bf16 v[114:117], v[184:187], v[216:219], v[114:117]
	v_mfma_f32_16x16x32_bf16 v[102:105], v[176:179], v[224:227], v[102:105]
	v_mfma_f32_16x16x32_bf16 v[98:101], v[184:187], v[224:227], v[98:101]
	v_mfma_f32_16x16x32_bf16 v[86:89], v[176:179], v[232:235], v[86:89]
	v_mfma_f32_16x16x32_bf16 v[82:85], v[184:187], v[232:235], v[82:85]
	v_mfma_f32_16x16x32_bf16 v[110:113], v[188:191], v[204:207], v[110:113]
	v_mfma_f32_16x16x32_bf16 v[106:109], v[196:199], v[204:207], v[106:109]
	v_mfma_f32_16x16x32_bf16 v[94:97], v[188:191], v[212:215], v[94:97]
	v_mfma_f32_16x16x32_bf16 v[90:93], v[196:199], v[212:215], v[90:93]
	v_mfma_f32_16x16x32_bf16 v[78:81], v[188:191], v[220:223], v[78:81]
	v_mfma_f32_16x16x32_bf16 v[74:77], v[196:199], v[220:223], v[74:77]
	v_mfma_f32_16x16x32_bf16 v[70:73], v[188:191], v[228:231], v[70:73]
	v_mfma_f32_16x16x32_bf16 v[66:69], v[196:199], v[228:231], v[66:69]
	v_mfma_f32_16x16x32_bf16 v[110:113], v[192:195], v[208:211], v[110:113]
	v_mfma_f32_16x16x32_bf16 v[106:109], v[200:203], v[208:211], v[106:109]
	v_mfma_f32_16x16x32_bf16 v[94:97], v[192:195], v[216:219], v[94:97]
	v_mfma_f32_16x16x32_bf16 v[90:93], v[200:203], v[216:219], v[90:93]
	v_mfma_f32_16x16x32_bf16 v[78:81], v[192:195], v[224:227], v[78:81]
	v_mfma_f32_16x16x32_bf16 v[74:77], v[200:203], v[224:227], v[74:77]
	v_mfma_f32_16x16x32_bf16 v[70:73], v[192:195], v[232:235], v[70:73]
	v_mfma_f32_16x16x32_bf16 v[66:69], v[200:203], v[232:235], v[66:69]
	s_setprio 0
	s_barrier
; #define PG8_STAGE(bufoff, gbase, voff) do { _Pragma("unroll") for (int _i = 0; _i < 2; ++_i) \
;         __builtin_amdgcn_global_load_lds((const unsigned*)((const char*)(gbase) + (voff)[_i]), (PG8_LAS unsigned*)(lds + (bufoff) + ldsw + _i * 8192), 16, 0, 0); } while (0)
; #define PG8_WAIT_V(n) asm volatile("s_waitcnt vmcnt(" #n ")" ::: "memory")
; #define PG8_WAIT_L(n) asm volatile("s_waitcnt lgkmcnt(" #n ")" ::: "memory")
; #define PG8_BAR __builtin_amdgcn_s_barrier()
; #define PG8_SCHED __builtin_amdgcn_sched_barrier(0)
; template <class Epi, class Sched, bool ALIGN_EPI = true, bool F8 = false>
; __device__ __forceinline__ void gemm_phase(PG8_LAS unsigned char* lds, const Sched& S, const Epi& E) {
;     ...
;             PG8_LDA(At, 1, 1); PG8_STAGE(PG8_SB(1, 0), b3, voffB[0]); PG8_STAGE(PG8_SB(1, 1), b3, voffB[1]); PG8_STAGE(PG8_SA(1, 0), a3, vA2[0]);
;             PG8_WAIT_V(8); PG8_WAIT_L(0); PG8_BAR; PG8_MMA(1, 0, At, B0); PG8_MMA(1, 1, At, B1); PG8_BAR; PG8_SCHED;
;         }
	s_mov_b32 m0, s67
	v_lshl_add_u64 v[236:237], v[236:237], 0, s[10:11]
	ds_read_b128 v[204:207], v166 offset:49152
	ds_read_b128 v[208:211], v166 offset:50176
	ds_read_b128 v[212:215], v166 offset:51200
	ds_read_b128 v[216:219], v166 offset:52224
	ds_read_b128 v[220:223], v166 offset:53248
	ds_read_b128 v[224:227], v166 offset:54272
	ds_read_b128 v[228:231], v166 offset:55296
	ds_read_b128 v[232:235], v166 offset:56320
	global_load_lds_dwordx4 v[236:237], off
	v_lshl_add_u64 v[236:237], v[238:239], 0, s[10:11]
	s_mov_b32 m0, s68
	s_nop 0
	global_load_lds_dwordx4 v[236:237], off
	v_lshl_add_u64 v[236:237], v[240:241], 0, s[10:11]
	s_mov_b32 m0, s69
	s_nop 0
	global_load_lds_dwordx4 v[236:237], off
	v_lshl_add_u64 v[236:237], v[242:243], 0, s[10:11]
	s_mov_b32 m0, s70
	s_nop 0
	global_load_lds_dwordx4 v[236:237], off
	v_lshl_add_u64 v[236:237], v[244:245], 0, s[10:11]
	s_mov_b32 m0, s59
	s_nop 0
	global_load_lds_dwordx4 v[236:237], off
	v_lshl_add_u64 v[236:237], v[246:247], 0, s[10:11]
	s_mov_b32 m0, s60
	s_nop 0
	global_load_lds_dwordx4 v[236:237], off
	s_waitcnt vmcnt(8)
	s_waitcnt lgkmcnt(0)
	s_barrier
	s_setprio 1
	s_waitcnt lgkmcnt(0)
	v_mfma_f32_16x16x32_bf16 v[62:65], v[172:175], v[204:207], v[62:65]
	v_mfma_f32_16x16x32_bf16 v[58:61], v[180:183], v[204:207], v[58:61]
	v_mfma_f32_16x16x32_bf16 v[54:57], v[172:175], v[212:215], v[54:57]
	v_mfma_f32_16x16x32_bf16 v[50:53], v[180:183], v[212:215], v[50:53]
	v_mfma_f32_16x16x32_bf16 v[38:41], v[172:175], v[220:223], v[38:41]
	v_mfma_f32_16x16x32_bf16 v[34:37], v[180:183], v[220:223], v[34:37]
	v_mfma_f32_16x16x32_bf16 v[22:25], v[172:175], v[228:231], v[22:25]
	v_mfma_f32_16x16x32_bf16 v[18:21], v[180:183], v[228:231], v[18:21]
	v_mfma_f32_16x16x32_bf16 v[62:65], v[176:179], v[208:211], v[62:65]
	v_mfma_f32_16x16x32_bf16 v[58:61], v[184:187], v[208:211], v[58:61]
	v_mfma_f32_16x16x32_bf16 v[54:57], v[176:179], v[216:219], v[54:57]
	v_mfma_f32_16x16x32_bf16 v[50:53], v[184:187], v[216:219], v[50:53]
	v_mfma_f32_16x16x32_bf16 v[38:41], v[176:179], v[224:227], v[38:41]
	v_mfma_f32_16x16x32_bf16 v[34:37], v[184:187], v[224:227], v[34:37]
	v_mfma_f32_16x16x32_bf16 v[22:25], v[176:179], v[232:235], v[22:25]
	v_mfma_f32_16x16x32_bf16 v[18:21], v[184:187], v[232:235], v[18:21]
	v_mfma_f32_16x16x32_bf16 v[46:49], v[188:191], v[204:207], v[46:49]
	v_mfma_f32_16x16x32_bf16 v[42:45], v[196:199], v[204:207], v[42:45]
	v_mfma_f32_16x16x32_bf16 v[30:33], v[188:191], v[212:215], v[30:33]
	v_mfma_f32_16x16x32_bf16 v[26:29], v[196:199], v[212:215], v[26:29]
	v_mfma_f32_16x16x32_bf16 v[14:17], v[188:191], v[220:223], v[14:17]
	v_mfma_f32_16x16x32_bf16 v[10:13], v[196:199], v[220:223], v[10:13]
	v_mfma_f32_16x16x32_bf16 v[6:9], v[188:191], v[228:231], v[6:9]
	v_mfma_f32_16x16x32_bf16 v[2:5], v[196:199], v[228:231], v[2:5]
	v_mfma_f32_16x16x32_bf16 v[46:49], v[192:195], v[208:211], v[46:49]
	v_mfma_f32_16x16x32_bf16 v[42:45], v[200:203], v[208:211], v[42:45]
	v_mfma_f32_16x16x32_bf16 v[30:33], v[192:195], v[216:219], v[30:33]
	v_mfma_f32_16x16x32_bf16 v[26:29], v[200:203], v[216:219], v[26:29]
	v_mfma_f32_16x16x32_bf16 v[14:17], v[192:195], v[224:227], v[14:17]
	v_mfma_f32_16x16x32_bf16 v[10:13], v[200:203], v[224:227], v[10:13]
	v_mfma_f32_16x16x32_bf16 v[6:9], v[192:195], v[232:235], v[6:9]
	v_mfma_f32_16x16x32_bf16 v[2:5], v[200:203], v[232:235], v[2:5]
	s_setprio 0
	s_barrier
	s_movk_i32 s15, 0x100
	s_andn2_b64 vcc, exec, s[30:31]
	s_mov_b64 s[40:41], -1
	s_mov_b64 s[30:31], 0
	s_cbranch_vccz .LBB0_514
	s_branch .Lpx_14299
.LBB0_514:
	s_add_u32 s44, s22, s15
	ds_read_b128 v[172:175], v164
	ds_read_b128 v[176:179], v164 offset:1024
	ds_read_b128 v[180:183], v164 offset:2048
	ds_read_b128 v[184:187], v164 offset:3072
	ds_read_b128 v[188:191], v165
	ds_read_b128 v[192:195], v165 offset:1024
	ds_read_b128 v[196:199], v165 offset:2048
	ds_read_b128 v[200:203], v165 offset:3072
	s_addc_u32 s45, s23, 0
	s_add_u32 s17, s44, 0x100
	s_addc_u32 s72, s45, 0
	s_and_b64 s[42:43], s[40:41], exec
	s_cselect_b32 s42, s24, s17
	s_cselect_b32 s43, s25, s72
	s_add_u32 s15, s26, s15
	s_addc_u32 s17, s27, 0
	s_add_u32 s15, s15, 0x100
	s_addc_u32 s17, s17, 0
	s_and_b64 s[40:41], s[40:41], exec
	s_cselect_b32 s40, s20, s15
	s_cselect_b32 s41, s21, s17
	v_lshl_add_u64 v[236:237], s[44:45], 0, v[142:143]
	s_mov_b32 m0, s61
	v_lshl_add_u64 v[236:237], v[236:237], 0, s[10:11]
	ds_read_b128 v[204:207], v166
	ds_read_b128 v[208:211], v166 offset:1024
	ds_read_b128 v[212:215], v166 offset:2048
	ds_read_b128 v[216:219], v166 offset:3072
	ds_read_b128 v[220:223], v166 offset:4096
	ds_read_b128 v[224:227], v166 offset:5120
	ds_read_b128 v[228:231], v166 offset:6144
	ds_read_b128 v[232:235], v166 offset:7168
	global_load_lds_dwordx4 v[236:237], off
	v_lshl_add_u64 v[236:237], s[44:45], 0, v[144:145]
	v_lshl_add_u64 v[236:237], v[236:237], 0, s[10:11]
	s_mov_b32 m0, s62
	s_nop 0
	global_load_lds_dwordx4 v[236:237], off
	s_waitcnt vmcnt(8)
	s_waitcnt lgkmcnt(0)
	s_barrier
; #define PG8_STAGE(bufoff, gbase, voff) do { _Pragma("unroll") for (int _i = 0; _i < 2; ++_i) \
;         __builtin_amdgcn_global_load_lds((const unsigned*)((const char*)(gbase) + (voff)[_i]), (PG8_LAS unsigned*)(lds + (bufoff) + ldsw + _i * 8192), 16, 0, 0); } while (0)
; #define PG8_WAIT_V(n) asm volatile("s_waitcnt vmcnt(" #n ")" ::: "memory")
; #define PG8_WAIT_L(n) asm volatile("s_waitcnt lgkmcnt(" #n ")" ::: "memory")
; #define PG8_BAR __builtin_amdgcn_s_barrier()
; #define PG8_SCHED __builtin_amdgcn_sched_barrier(0)
; template <class Epi, class Sched, bool ALIGN_EPI = true, bool F8 = false>
; __device__ __forceinline__ void gemm_phase(PG8_LAS unsigned char* lds, const Sched& S, const Epi& E) {
;     ...
;             PG8_LDB(B0, 0, 0); PG8_LDB(B1, 0, 1); PG8_SCHED; PG8_LDA(At, 0, 0); PG8_STAGE(PG8_SA(1, 1), a1, voffA[1]);
;             PG8_WAIT_V(8); PG8_WAIT_L(0); PG8_BAR; PG8_MMA(0, 0, At, B0); PG8_MMA(0, 1, At, B1); PG8_BAR; PG8_SCHED;
;             PG8_LDA(At, 0, 1); PG8_STAGE(PG8_SB(0, 0), b2, voffB[0]); PG8_STAGE(PG8_SB(0, 1), b2, voffB[1]); PG8_STAGE(PG8_SA(0, 0), a2, vA2[0]);
;             PG8_WAIT_V(8); PG8_WAIT_L(0); PG8_BAR; PG8_MMA(1, 0, At, B0); PG8_MMA(1, 1, At, B1); PG8_BAR; PG8_SCHED;
;             PG8_LDB(B0, 1, 0); PG8_LDB(B1, 1, 1); PG8_SCHED; PG8_LDA(At, 1, 0); PG8_STAGE(PG8_SA(0, 1), a2, vA2[1]);
;             PG8_WAIT_V(8); PG8_WAIT_L(0); PG8_BAR; PG8_MMA(0, 0, At, B0); PG8_MMA(0, 1, At, B1); PG8_BAR; PG8_SCHED;
	s_setprio 1
	s_waitcnt lgkmcnt(0)
	v_mfma_f32_16x16x32_bf16 v[126:129], v[172:175], v[204:207], v[126:129]
	v_mfma_f32_16x16x32_bf16 v[122:125], v[180:183], v[204:207], v[122:125]
	v_mfma_f32_16x16x32_bf16 v[118:121], v[172:175], v[212:215], v[118:121]
	v_mfma_f32_16x16x32_bf16 v[114:117], v[180:183], v[212:215], v[114:117]
	v_mfma_f32_16x16x32_bf16 v[102:105], v[172:175], v[220:223], v[102:105]
	v_mfma_f32_16x16x32_bf16 v[98:101], v[180:183], v[220:223], v[98:101]
	v_mfma_f32_16x16x32_bf16 v[86:89], v[172:175], v[228:231], v[86:89]
	v_mfma_f32_16x16x32_bf16 v[82:85], v[180:183], v[228:231], v[82:85]
	v_mfma_f32_16x16x32_bf16 v[126:129], v[176:179], v[208:211], v[126:129]
	v_mfma_f32_16x16x32_bf16 v[122:125], v[184:187], v[208:211], v[122:125]
	v_mfma_f32_16x16x32_bf16 v[118:121], v[176:179], v[216:219], v[118:121]
	v_mfma_f32_16x16x32_bf16 v[114:117], v[184:187], v[216:219], v[114:117]
	v_mfma_f32_16x16x32_bf16 v[102:105], v[176:179], v[224:227], v[102:105]
	v_mfma_f32_16x16x32_bf16 v[98:101], v[184:187], v[224:227], v[98:101]
	v_mfma_f32_16x16x32_bf16 v[86:89], v[176:179], v[232:235], v[86:89]
	v_mfma_f32_16x16x32_bf16 v[82:85], v[184:187], v[232:235], v[82:85]
	v_mfma_f32_16x16x32_bf16 v[110:113], v[188:191], v[204:207], v[110:113]
	v_mfma_f32_16x16x32_bf16 v[106:109], v[196:199], v[204:207], v[106:109]
	v_mfma_f32_16x16x32_bf16 v[94:97], v[188:191], v[212:215], v[94:97]
	v_mfma_f32_16x16x32_bf16 v[90:93], v[196:199], v[212:215], v[90:93]
	v_mfma_f32_16x16x32_bf16 v[78:81], v[188:191], v[220:223], v[78:81]
	v_mfma_f32_16x16x32_bf16 v[74:77], v[196:199], v[220:223], v[74:77]
	v_mfma_f32_16x16x32_bf16 v[70:73], v[188:191], v[228:231], v[70:73]
	v_mfma_f32_16x16x32_bf16 v[66:69], v[196:199], v[228:231], v[66:69]
	v_mfma_f32_16x16x32_bf16 v[110:113], v[192:195], v[208:211], v[110:113]
	v_mfma_f32_16x16x32_bf16 v[106:109], v[200:203], v[208:211], v[106:109]
	v_mfma_f32_16x16x32_bf16 v[94:97], v[192:195], v[216:219], v[94:97]
	v_mfma_f32_16x16x32_bf16 v[90:93], v[200:203], v[216:219], v[90:93]
	v_mfma_f32_16x16x32_bf16 v[78:81], v[192:195], v[224:227], v[78:81]
	v_mfma_f32_16x16x32_bf16 v[74:77], v[200:203], v[224:227], v[74:77]
	v_mfma_f32_16x16x32_bf16 v[70:73], v[192:195], v[232:235], v[70:73]
	v_mfma_f32_16x16x32_bf16 v[66:69], v[200:203], v[232:235], v[66:69]
	s_setprio 0
	s_barrier
	s_mov_b32 m0, s63
	v_lshl_add_u64 v[236:237], s[40:41], 0, v[136:137]
	ds_read_b128 v[204:207], v166 offset:16384
	ds_read_b128 v[208:211], v166 offset:17408
	ds_read_b128 v[212:215], v166 offset:18432
	ds_read_b128 v[216:219], v166 offset:19456
	ds_read_b128 v[220:223], v166 offset:20480
	ds_read_b128 v[224:227], v166 offset:21504
	ds_read_b128 v[228:231], v166 offset:22528
	ds_read_b128 v[232:235], v166 offset:23552
	global_load_lds_dwordx4 v[236:237], off
	v_lshl_add_u64 v[238:239], s[40:41], 0, v[134:135]
	s_mov_b32 m0, s64
	v_lshl_add_u64 v[240:241], s[40:41], 0, v[132:133]
	global_load_lds_dwordx4 v[238:239], off
	s_mov_b32 m0, s65
	v_lshl_add_u64 v[242:243], s[40:41], 0, v[130:131]
	global_load_lds_dwordx4 v[240:241], off
	s_mov_b32 m0, s66
	v_lshl_add_u64 v[244:245], s[42:43], 0, v[138:139]
	global_load_lds_dwordx4 v[242:243], off
	s_mov_b32 m0, s50
	v_lshl_add_u64 v[246:247], s[42:43], 0, v[140:141]
	global_load_lds_dwordx4 v[244:245], off
	s_mov_b32 m0, s51
	s_nop 0
	global_load_lds_dwordx4 v[246:247], off
	s_waitcnt vmcnt(8)
	s_waitcnt lgkmcnt(0)
	s_barrier
	s_setprio 1
	s_waitcnt lgkmcnt(0)
	v_mfma_f32_16x16x32_bf16 v[62:65], v[172:175], v[204:207], v[62:65]
	v_mfma_f32_16x16x32_bf16 v[58:61], v[180:183], v[204:207], v[58:61]
	v_mfma_f32_16x16x32_bf16 v[54:57], v[172:175], v[212:215], v[54:57]
	v_mfma_f32_16x16x32_bf16 v[50:53], v[180:183], v[212:215], v[50:53]
	v_mfma_f32_16x16x32_bf16 v[38:41], v[172:175], v[220:223], v[38:41]
	v_mfma_f32_16x16x32_bf16 v[34:37], v[180:183], v[220:223], v[34:37]
	v_mfma_f32_16x16x32_bf16 v[22:25], v[172:175], v[228:231], v[22:25]
	v_mfma_f32_16x16x32_bf16 v[18:21], v[180:183], v[228:231], v[18:21]
	v_mfma_f32_16x16x32_bf16 v[62:65], v[176:179], v[208:211], v[62:65]
	v_mfma_f32_16x16x32_bf16 v[58:61], v[184:187], v[208:211], v[58:61]
	v_mfma_f32_16x16x32_bf16 v[54:57], v[176:179], v[216:219], v[54:57]
	v_mfma_f32_16x16x32_bf16 v[50:53], v[184:187], v[216:219], v[50:53]
	v_mfma_f32_16x16x32_bf16 v[38:41], v[176:179], v[224:227], v[38:41]
	v_mfma_f32_16x16x32_bf16 v[34:37], v[184:187], v[224:227], v[34:37]
	v_mfma_f32_16x16x32_bf16 v[22:25], v[176:179], v[232:235], v[22:25]
	v_mfma_f32_16x16x32_bf16 v[18:21], v[184:187], v[232:235], v[18:21]
	v_mfma_f32_16x16x32_bf16 v[46:49], v[188:191], v[204:207], v[46:49]
	v_mfma_f32_16x16x32_bf16 v[42:45], v[196:199], v[204:207], v[42:45]
	v_mfma_f32_16x16x32_bf16 v[30:33], v[188:191], v[212:215], v[30:33]
	v_mfma_f32_16x16x32_bf16 v[26:29], v[196:199], v[212:215], v[26:29]
	v_mfma_f32_16x16x32_bf16 v[14:17], v[188:191], v[220:223], v[14:17]
	v_mfma_f32_16x16x32_bf16 v[10:13], v[196:199], v[220:223], v[10:13]
	v_mfma_f32_16x16x32_bf16 v[6:9], v[188:191], v[228:231], v[6:9]
	v_mfma_f32_16x16x32_bf16 v[2:5], v[196:199], v[228:231], v[2:5]
	v_mfma_f32_16x16x32_bf16 v[46:49], v[192:195], v[208:211], v[46:49]
	v_mfma_f32_16x16x32_bf16 v[42:45], v[200:203], v[208:211], v[42:45]
	v_mfma_f32_16x16x32_bf16 v[30:33], v[192:195], v[216:219], v[30:33]
	v_mfma_f32_16x16x32_bf16 v[26:29], v[200:203], v[216:219], v[26:29]
	v_mfma_f32_16x16x32_bf16 v[14:17], v[192:195], v[224:227], v[14:17]
	v_mfma_f32_16x16x32_bf16 v[10:13], v[200:203], v[224:227], v[10:13]
	v_mfma_f32_16x16x32_bf16 v[6:9], v[192:195], v[232:235], v[6:9]
	v_mfma_f32_16x16x32_bf16 v[2:5], v[200:203], v[232:235], v[2:5]
	s_setprio 0
	s_barrier
; #define PG8_STAGE(bufoff, gbase, voff) do { _Pragma("unroll") for (int _i = 0; _i < 2; ++_i) \
;         __builtin_amdgcn_global_load_lds((const unsigned*)((const char*)(gbase) + (voff)[_i]), (PG8_LAS unsigned*)(lds + (bufoff) + ldsw + _i * 8192), 16, 0, 0); } while (0)
; #define PG8_WAIT_V(n) asm volatile("s_waitcnt vmcnt(" #n ")" ::: "memory")
; #define PG8_WAIT_L(n) asm volatile("s_waitcnt lgkmcnt(" #n ")" ::: "memory")
; #define PG8_BAR __builtin_amdgcn_s_barrier()
; #define PG8_SCHED __builtin_amdgcn_sched_barrier(0)
; template <class Epi, class Sched, bool ALIGN_EPI = true, bool F8 = false>
; __device__ __forceinline__ void gemm_phase(PG8_LAS unsigned char* lds, const Sched& S, const Epi& E) {
;     ...
;             PG8_LDB(B0, 1, 0); PG8_LDB(B1, 1, 1); PG8_SCHED; PG8_LDA(At, 1, 0); PG8_STAGE(PG8_SA(0, 1), a2, vA2[1]);
;             PG8_WAIT_V(8); PG8_WAIT_L(0); PG8_BAR; PG8_MMA(0, 0, At, B0); PG8_MMA(0, 1, At, B1); PG8_BAR; PG8_SCHED;
;             PG8_LDA(At, 1, 1); PG8_STAGE(PG8_SB(1, 0), b3, voffB[0]); PG8_STAGE(PG8_SB(1, 1), b3, voffB[1]); PG8_STAGE(PG8_SA(1, 0), a3, vA2[0]);
;             PG8_WAIT_V(8); PG8_WAIT_L(0); PG8_BAR; PG8_MMA(1, 0, At, B0); PG8_MMA(1, 1, At, B1); PG8_BAR; PG8_SCHED;
;         }
	ds_read_b128 v[172:175], v167
	ds_read_b128 v[176:179], v167 offset:1024
	ds_read_b128 v[180:183], v167 offset:2048
	ds_read_b128 v[184:187], v167 offset:3072
	ds_read_b128 v[188:191], v168
	ds_read_b128 v[192:195], v168 offset:1024
	ds_read_b128 v[196:199], v168 offset:2048
	ds_read_b128 v[200:203], v168 offset:3072
	s_mov_b32 m0, s52
	v_lshl_add_u64 v[248:249], s[42:43], 0, v[142:143]
	ds_read_b128 v[204:207], v166 offset:32768
	ds_read_b128 v[208:211], v166 offset:33792
	ds_read_b128 v[212:215], v166 offset:34816
	ds_read_b128 v[216:219], v166 offset:35840
	ds_read_b128 v[220:223], v166 offset:36864
	ds_read_b128 v[224:227], v166 offset:37888
	ds_read_b128 v[228:231], v166 offset:38912
	ds_read_b128 v[232:235], v166 offset:39936
	global_load_lds_dwordx4 v[248:249], off
	v_lshl_add_u64 v[248:249], s[42:43], 0, v[144:145]
	s_mov_b32 m0, s53
	s_nop 0
	global_load_lds_dwordx4 v[248:249], off
	s_waitcnt vmcnt(8)
	s_waitcnt lgkmcnt(0)
	s_barrier
	s_setprio 1
	s_waitcnt lgkmcnt(0)
	v_mfma_f32_16x16x32_bf16 v[126:129], v[172:175], v[204:207], v[126:129]
	v_mfma_f32_16x16x32_bf16 v[122:125], v[180:183], v[204:207], v[122:125]
	v_mfma_f32_16x16x32_bf16 v[118:121], v[172:175], v[212:215], v[118:121]
	v_mfma_f32_16x16x32_bf16 v[114:117], v[180:183], v[212:215], v[114:117]
	v_mfma_f32_16x16x32_bf16 v[102:105], v[172:175], v[220:223], v[102:105]
	v_mfma_f32_16x16x32_bf16 v[98:101], v[180:183], v[220:223], v[98:101]
	v_mfma_f32_16x16x32_bf16 v[86:89], v[172:175], v[228:231], v[86:89]
	v_mfma_f32_16x16x32_bf16 v[82:85], v[180:183], v[228:231], v[82:85]
	v_mfma_f32_16x16x32_bf16 v[126:129], v[176:179], v[208:211], v[126:129]
	v_mfma_f32_16x16x32_bf16 v[122:125], v[184:187], v[208:211], v[122:125]
	v_mfma_f32_16x16x32_bf16 v[118:121], v[176:179], v[216:219], v[118:121]
	v_mfma_f32_16x16x32_bf16 v[114:117], v[184:187], v[216:219], v[114:117]
	v_mfma_f32_16x16x32_bf16 v[102:105], v[176:179], v[224:227], v[102:105]
	v_mfma_f32_16x16x32_bf16 v[98:101], v[184:187], v[224:227], v[98:101]
	v_mfma_f32_16x16x32_bf16 v[86:89], v[176:179], v[232:235], v[86:89]
	v_mfma_f32_16x16x32_bf16 v[82:85], v[184:187], v[232:235], v[82:85]
	v_mfma_f32_16x16x32_bf16 v[110:113], v[188:191], v[204:207], v[110:113]
	v_mfma_f32_16x16x32_bf16 v[106:109], v[196:199], v[204:207], v[106:109]
	v_mfma_f32_16x16x32_bf16 v[94:97], v[188:191], v[212:215], v[94:97]
	v_mfma_f32_16x16x32_bf16 v[90:93], v[196:199], v[212:215], v[90:93]
	v_mfma_f32_16x16x32_bf16 v[78:81], v[188:191], v[220:223], v[78:81]
	v_mfma_f32_16x16x32_bf16 v[74:77], v[196:199], v[220:223], v[74:77]
	v_mfma_f32_16x16x32_bf16 v[70:73], v[188:191], v[228:231], v[70:73]
	v_mfma_f32_16x16x32_bf16 v[66:69], v[196:199], v[228:231], v[66:69]
	v_mfma_f32_16x16x32_bf16 v[110:113], v[192:195], v[208:211], v[110:113]
	v_mfma_f32_16x16x32_bf16 v[106:109], v[200:203], v[208:211], v[106:109]
	v_mfma_f32_16x16x32_bf16 v[94:97], v[192:195], v[216:219], v[94:97]
	v_mfma_f32_16x16x32_bf16 v[90:93], v[200:203], v[216:219], v[90:93]
	v_mfma_f32_16x16x32_bf16 v[78:81], v[192:195], v[224:227], v[78:81]
	v_mfma_f32_16x16x32_bf16 v[74:77], v[200:203], v[224:227], v[74:77]
	v_mfma_f32_16x16x32_bf16 v[70:73], v[192:195], v[232:235], v[70:73]
	v_mfma_f32_16x16x32_bf16 v[66:69], v[200:203], v[232:235], v[66:69]
	s_setprio 0
	s_barrier
	s_mov_b32 m0, s67
	v_lshl_add_u64 v[236:237], v[236:237], 0, s[10:11]
	ds_read_b128 v[204:207], v166 offset:49152
	ds_read_b128 v[208:211], v166 offset:50176
	ds_read_b128 v[212:215], v166 offset:51200
	ds_read_b128 v[216:219], v166 offset:52224
	ds_read_b128 v[220:223], v166 offset:53248
	ds_read_b128 v[224:227], v166 offset:54272
	ds_read_b128 v[228:231], v166 offset:55296
	ds_read_b128 v[232:235], v166 offset:56320
	global_load_lds_dwordx4 v[236:237], off
	v_lshl_add_u64 v[236:237], v[238:239], 0, s[10:11]
	s_mov_b32 m0, s68
	s_nop 0
	global_load_lds_dwordx4 v[236:237], off
	v_lshl_add_u64 v[236:237], v[240:241], 0, s[10:11]
	s_mov_b32 m0, s69
	s_nop 0
	global_load_lds_dwordx4 v[236:237], off
	v_lshl_add_u64 v[236:237], v[242:243], 0, s[10:11]
	s_mov_b32 m0, s70
	s_nop 0
	global_load_lds_dwordx4 v[236:237], off
	v_lshl_add_u64 v[236:237], v[244:245], 0, s[10:11]
	s_mov_b32 m0, s59
	s_nop 0
	global_load_lds_dwordx4 v[236:237], off
	v_lshl_add_u64 v[236:237], v[246:247], 0, s[10:11]
	s_mov_b32 m0, s60
	s_nop 0
	global_load_lds_dwordx4 v[236:237], off
	s_waitcnt vmcnt(8)
	s_waitcnt lgkmcnt(0)
	s_barrier
	s_setprio 1
	s_waitcnt lgkmcnt(0)
	v_mfma_f32_16x16x32_bf16 v[62:65], v[172:175], v[204:207], v[62:65]
	v_mfma_f32_16x16x32_bf16 v[58:61], v[180:183], v[204:207], v[58:61]
	v_mfma_f32_16x16x32_bf16 v[54:57], v[172:175], v[212:215], v[54:57]
	v_mfma_f32_16x16x32_bf16 v[50:53], v[180:183], v[212:215], v[50:53]
	v_mfma_f32_16x16x32_bf16 v[38:41], v[172:175], v[220:223], v[38:41]
	v_mfma_f32_16x16x32_bf16 v[34:37], v[180:183], v[220:223], v[34:37]
	v_mfma_f32_16x16x32_bf16 v[22:25], v[172:175], v[228:231], v[22:25]
	v_mfma_f32_16x16x32_bf16 v[18:21], v[180:183], v[228:231], v[18:21]
	v_mfma_f32_16x16x32_bf16 v[62:65], v[176:179], v[208:211], v[62:65]
	v_mfma_f32_16x16x32_bf16 v[58:61], v[184:187], v[208:211], v[58:61]
	v_mfma_f32_16x16x32_bf16 v[54:57], v[176:179], v[216:219], v[54:57]
	v_mfma_f32_16x16x32_bf16 v[50:53], v[184:187], v[216:219], v[50:53]
	v_mfma_f32_16x16x32_bf16 v[38:41], v[176:179], v[224:227], v[38:41]
	v_mfma_f32_16x16x32_bf16 v[34:37], v[184:187], v[224:227], v[34:37]
	v_mfma_f32_16x16x32_bf16 v[22:25], v[176:179], v[232:235], v[22:25]
	v_mfma_f32_16x16x32_bf16 v[18:21], v[184:187], v[232:235], v[18:21]
	v_mfma_f32_16x16x32_bf16 v[46:49], v[188:191], v[204:207], v[46:49]
	v_mfma_f32_16x16x32_bf16 v[42:45], v[196:199], v[204:207], v[42:45]
	v_mfma_f32_16x16x32_bf16 v[30:33], v[188:191], v[212:215], v[30:33]
	v_mfma_f32_16x16x32_bf16 v[26:29], v[196:199], v[212:215], v[26:29]
	v_mfma_f32_16x16x32_bf16 v[14:17], v[188:191], v[220:223], v[14:17]
	v_mfma_f32_16x16x32_bf16 v[10:13], v[196:199], v[220:223], v[10:13]
	v_mfma_f32_16x16x32_bf16 v[6:9], v[188:191], v[228:231], v[6:9]
	v_mfma_f32_16x16x32_bf16 v[2:5], v[196:199], v[228:231], v[2:5]
	v_mfma_f32_16x16x32_bf16 v[46:49], v[192:195], v[208:211], v[46:49]
	v_mfma_f32_16x16x32_bf16 v[42:45], v[200:203], v[208:211], v[42:45]
	v_mfma_f32_16x16x32_bf16 v[30:33], v[192:195], v[216:219], v[30:33]
	v_mfma_f32_16x16x32_bf16 v[26:29], v[200:203], v[216:219], v[26:29]
	v_mfma_f32_16x16x32_bf16 v[14:17], v[192:195], v[224:227], v[14:17]
	v_mfma_f32_16x16x32_bf16 v[10:13], v[200:203], v[224:227], v[10:13]
	v_mfma_f32_16x16x32_bf16 v[6:9], v[192:195], v[232:235], v[6:9]
	v_mfma_f32_16x16x32_bf16 v[2:5], v[200:203], v[232:235], v[2:5]
	s_setprio 0
	s_barrier
	s_movk_i32 s15, 0x100
	s_andn2_b64 vcc, exec, s[30:31]
	s_mov_b64 s[40:41], -1
	s_mov_b64 s[30:31], 0
	s_cbranch_vccz .LBB0_514

; #define PG8_STAGE(bufoff, gbase, voff) do { _Pragma("unroll") for (int _i = 0; _i < 2; ++_i) \
;         __builtin_amdgcn_global_load_lds((const unsigned*)((const char*)(gbase) + (voff)[_i]), (PG8_LAS unsigned*)(lds + (bufoff) + ldsw + _i * 8192), 16, 0, 0); } while (0)
; #define PG8_WAIT_V(n) asm volatile("s_waitcnt vmcnt(" #n ")" ::: "memory")
; #define PG8_WAIT_L(n) asm volatile("s_waitcnt lgkmcnt(" #n ")" ::: "memory")
; #define PG8_BAR __builtin_amdgcn_s_barrier()
; #define PG8_SCHED __builtin_amdgcn_sched_barrier(0)
; template <class Epi, class Sched, bool ALIGN_EPI = true, bool F8 = false>
; __device__ __forceinline__ void gemm_phase(PG8_LAS unsigned char* lds, const Sched& S, const Epi& E) {
;     ...
;             PG8_LDB(B0, 0, 0); PG8_LDB(B1, 0, 1); PG8_SCHED; PG8_LDA(At, 0, 0); PG8_STAGE(PG8_SA(1, 1), a1, voffA[1]);
;             PG8_WAIT_V(8); PG8_WAIT_L(0); PG8_BAR; PG8_MMA(0, 0, At, B0); PG8_MMA(0, 1, At, B1); PG8_BAR; PG8_SCHED;
;             PG8_LDA(At, 0, 1); PG8_STAGE(PG8_SB(0, 0), b2, voffB[0]); PG8_STAGE(PG8_SB(0, 1), b2, voffB[1]); PG8_STAGE(PG8_SA(0, 0), a2, vA2[0]);
;             PG8_WAIT_V(8); PG8_WAIT_L(0); PG8_BAR; PG8_MMA(1, 0, At, B0); PG8_MMA(1, 1, At, B1); PG8_BAR; PG8_SCHED;
.LBB0_614:
	ds_read_b128 v[2:5], v100
	ds_read_b128 v[6:9], v100 offset:1024
	ds_read_b128 v[10:13], v100 offset:2048
	ds_read_b128 v[14:17], v100 offset:3072
	ds_read_b128 v[18:21], v101
	ds_read_b128 v[22:25], v101 offset:1024
	ds_read_b128 v[26:29], v101 offset:2048
	ds_read_b128 v[30:33], v101 offset:3072
	s_mov_b32 m0, s31
	ds_read_b128 v[34:37], v102
	ds_read_b128 v[38:41], v102 offset:1024
	ds_read_b128 v[42:45], v102 offset:2048
	ds_read_b128 v[46:49], v102 offset:3072
	ds_read_b128 v[50:53], v102 offset:4096
	ds_read_b128 v[54:57], v102 offset:5120
	ds_read_b128 v[58:61], v102 offset:6144
	ds_read_b128 v[62:65], v102 offset:7168
	global_load_lds_dwordx4 v[96:97], off
	s_mov_b32 m0, s40
	s_nop 0
	global_load_lds_dwordx4 v[98:99], off
	s_waitcnt vmcnt(8)
	s_waitcnt lgkmcnt(0)
	s_barrier
	s_setprio 1
	s_waitcnt lgkmcnt(0)
	v_mfma_f32_16x16x32_bf16 v[106:109], v[2:5], v[34:37], 0
	v_mfma_f32_16x16x32_bf16 v[114:117], v[2:5], v[42:45], 0
	v_mfma_f32_16x16x32_bf16 v[122:125], v[2:5], v[50:53], 0
	v_mfma_f32_16x16x32_bf16 v[2:5], v[2:5], v[58:61], 0
	v_mfma_f32_16x16x32_bf16 v[106:109], v[6:9], v[38:41], v[106:109]
	v_mfma_f32_16x16x32_bf16 v[114:117], v[6:9], v[46:49], v[114:117]
	v_mfma_f32_16x16x32_bf16 v[122:125], v[6:9], v[54:57], v[122:125]
	v_mfma_f32_16x16x32_bf16 v[2:5], v[6:9], v[62:65], v[2:5]
	v_mfma_f32_16x16x32_bf16 v[6:9], v[10:13], v[58:61], 0
	v_mfma_f32_16x16x32_bf16 v[110:113], v[10:13], v[34:37], 0
	v_mfma_f32_16x16x32_bf16 v[118:121], v[10:13], v[42:45], 0
	v_mfma_f32_16x16x32_bf16 v[126:129], v[10:13], v[50:53], 0
	v_mfma_f32_16x16x32_bf16 v[6:9], v[14:17], v[62:65], v[6:9]
	v_mfma_f32_16x16x32_bf16 v[110:113], v[14:17], v[38:41], v[110:113]
	v_mfma_f32_16x16x32_bf16 v[118:121], v[14:17], v[46:49], v[118:121]
	v_mfma_f32_16x16x32_bf16 v[126:129], v[14:17], v[54:57], v[126:129]
	v_mfma_f32_16x16x32_bf16 v[10:13], v[18:21], v[34:37], 0
	v_mfma_f32_16x16x32_bf16 v[14:17], v[26:29], v[34:37], 0
	v_mfma_f32_16x16x32_bf16 v[34:37], v[18:21], v[42:45], 0
	v_mfma_f32_16x16x32_bf16 v[130:133], v[22:25], v[46:49], v[34:37]
	v_mfma_f32_16x16x32_bf16 v[34:37], v[26:29], v[42:45], 0
	v_mfma_f32_16x16x32_bf16 v[46:49], v[30:33], v[46:49], v[34:37]
	v_mfma_f32_16x16x32_bf16 v[34:37], v[18:21], v[50:53], 0
	v_mfma_f32_16x16x32_bf16 v[18:21], v[18:21], v[58:61], 0
	v_mfma_f32_16x16x32_bf16 v[10:13], v[22:25], v[38:41], v[10:13]
	v_mfma_f32_16x16x32_bf16 v[14:17], v[30:33], v[38:41], v[14:17]
	v_mfma_f32_16x16x32_bf16 v[134:137], v[22:25], v[54:57], v[34:37]
	v_mfma_f32_16x16x32_bf16 v[34:37], v[26:29], v[50:53], 0
	v_mfma_f32_16x16x32_bf16 v[142:145], v[22:25], v[62:65], v[18:21]
	v_mfma_f32_16x16x32_bf16 v[18:21], v[26:29], v[58:61], 0
	v_mfma_f32_16x16x32_bf16 v[138:141], v[30:33], v[54:57], v[34:37]
	v_mfma_f32_16x16x32_bf16 v[146:149], v[30:33], v[62:65], v[18:21]
	s_setprio 0
	s_barrier
	s_mov_b32 m0, s41
	v_lshl_add_u64 v[196:197], s[6:7], 0, v[66:67]
	global_load_lds_dwordx4 v[196:197], off
	v_lshl_add_u64 v[198:199], s[6:7], 0, v[68:69]
	s_mov_b32 m0, s42
	v_lshl_add_u64 v[200:201], s[6:7], 0, v[72:73]
	global_load_lds_dwordx4 v[198:199], off
	s_mov_b32 m0, s43
	v_lshl_add_u64 v[202:203], s[6:7], 0, v[70:71]
	global_load_lds_dwordx4 v[200:201], off
	s_mov_b32 m0, s44
	s_nop 0
	global_load_lds_dwordx4 v[202:203], off
	s_mov_b32 m0, s21
	s_nop 0
	global_load_lds_dwordx4 v[78:79], off
	s_mov_b32 m0, s22
	s_nop 0
	global_load_lds_dwordx4 v[80:81], off
	s_waitcnt vmcnt(8)
	s_waitcnt lgkmcnt(0)
	s_barrier
	s_setprio 1
	s_setprio 0
	s_barrier
; #define PG8_STAGE(bufoff, gbase, voff) do { _Pragma("unroll") for (int _i = 0; _i < 2; ++_i) \
;         __builtin_amdgcn_global_load_lds((const unsigned*)((const char*)(gbase) + (voff)[_i]), (PG8_LAS unsigned*)(lds + (bufoff) + ldsw + _i * 8192), 16, 0, 0); } while (0)
; #define PG8_WAIT_V(n) asm volatile("s_waitcnt vmcnt(" #n ")" ::: "memory")
; #define PG8_WAIT_L(n) asm volatile("s_waitcnt lgkmcnt(" #n ")" ::: "memory")
; #define PG8_BAR __builtin_amdgcn_s_barrier()
; #define PG8_SCHED __builtin_amdgcn_sched_barrier(0)
; template <class Epi, class Sched, bool ALIGN_EPI = true, bool F8 = false>
; __device__ __forceinline__ void gemm_phase(PG8_LAS unsigned char* lds, const Sched& S, const Epi& E) {
;     ...
;             PG8_LDB(B0, 1, 0); PG8_LDB(B1, 1, 1); PG8_SCHED; PG8_LDA(At, 1, 0); PG8_STAGE(PG8_SA(0, 1), a2, vA2[1]);
;             PG8_WAIT_V(8); PG8_WAIT_L(0); PG8_BAR; PG8_MMA(0, 0, At, B0); PG8_MMA(0, 1, At, B1); PG8_BAR; PG8_SCHED;
;             PG8_LDA(At, 1, 1); PG8_STAGE(PG8_SB(1, 0), b3, voffB[0]); PG8_STAGE(PG8_SB(1, 1), b3, voffB[1]); PG8_STAGE(PG8_SA(1, 0), a3, vA2[0]);
;             PG8_WAIT_V(8); PG8_WAIT_L(0); PG8_BAR; PG8_MMA(1, 0, At, B0); PG8_MMA(1, 1, At, B1); PG8_BAR; PG8_SCHED;
;         }
	ds_read_b128 v[26:29], v103
	ds_read_b128 v[30:33], v103 offset:1024
	ds_read_b128 v[42:45], v103 offset:2048
	ds_read_b128 v[58:61], v103 offset:3072
	ds_read_b128 v[150:153], v104
	ds_read_b128 v[154:157], v104 offset:1024
	ds_read_b128 v[158:161], v104 offset:2048
	ds_read_b128 v[162:165], v104 offset:3072
	s_mov_b32 m0, s23
	ds_read_b128 v[62:65], v102 offset:32768
	ds_read_b128 v[166:169], v102 offset:33792
	ds_read_b128 v[172:175], v102 offset:34816
	ds_read_b128 v[176:179], v102 offset:35840
	ds_read_b128 v[180:183], v102 offset:36864
	ds_read_b128 v[184:187], v102 offset:37888
	ds_read_b128 v[188:191], v102 offset:38912
	ds_read_b128 v[192:195], v102 offset:39936
	global_load_lds_dwordx4 v[82:83], off
	s_mov_b32 m0, s24
	s_nop 0
	global_load_lds_dwordx4 v[84:85], off
	s_waitcnt vmcnt(8)
	s_waitcnt lgkmcnt(0)
	s_barrier
	s_setprio 1
	s_waitcnt lgkmcnt(0)
	v_mfma_f32_16x16x32_bf16 v[18:21], v[26:29], v[62:65], v[106:109]
	v_mfma_f32_16x16x32_bf16 v[50:53], v[30:33], v[166:169], v[18:21]
	v_mfma_f32_16x16x32_bf16 v[18:21], v[42:45], v[62:65], v[110:113]
	v_mfma_f32_16x16x32_bf16 v[54:57], v[58:61], v[166:169], v[18:21]
	v_mfma_f32_16x16x32_bf16 v[18:21], v[26:29], v[172:175], v[114:117]
	v_mfma_f32_16x16x32_bf16 v[34:37], v[30:33], v[176:179], v[18:21]
	v_mfma_f32_16x16x32_bf16 v[18:21], v[42:45], v[172:175], v[118:121]
	v_mfma_f32_16x16x32_bf16 v[38:41], v[58:61], v[176:179], v[18:21]
	v_mfma_f32_16x16x32_bf16 v[18:21], v[26:29], v[180:183], v[122:125]
	v_mfma_f32_16x16x32_bf16 v[22:25], v[42:45], v[180:183], v[126:129]
	v_mfma_f32_16x16x32_bf16 v[2:5], v[26:29], v[188:191], v[2:5]
	v_mfma_f32_16x16x32_bf16 v[6:9], v[42:45], v[188:191], v[6:9]
	v_mfma_f32_16x16x32_bf16 v[18:21], v[30:33], v[184:187], v[18:21]
	v_mfma_f32_16x16x32_bf16 v[22:25], v[58:61], v[184:187], v[22:25]
	v_mfma_f32_16x16x32_bf16 v[2:5], v[30:33], v[192:195], v[2:5]
	v_mfma_f32_16x16x32_bf16 v[6:9], v[58:61], v[192:195], v[6:9]
	v_mfma_f32_16x16x32_bf16 v[10:13], v[150:153], v[62:65], v[10:13]
	v_mfma_f32_16x16x32_bf16 v[58:61], v[154:157], v[166:169], v[10:13]
	v_mfma_f32_16x16x32_bf16 v[10:13], v[158:161], v[62:65], v[14:17]
	v_mfma_f32_16x16x32_bf16 v[62:65], v[162:165], v[166:169], v[10:13]
	v_mfma_f32_16x16x32_bf16 v[10:13], v[150:153], v[172:175], v[130:133]
	v_mfma_f32_16x16x32_bf16 v[42:45], v[154:157], v[176:179], v[10:13]
	v_mfma_f32_16x16x32_bf16 v[10:13], v[158:161], v[172:175], v[46:49]
	v_mfma_f32_16x16x32_bf16 v[46:49], v[162:165], v[176:179], v[10:13]
	v_mfma_f32_16x16x32_bf16 v[10:13], v[150:153], v[180:183], v[134:137]
	v_mfma_f32_16x16x32_bf16 v[26:29], v[154:157], v[184:187], v[10:13]
	v_mfma_f32_16x16x32_bf16 v[10:13], v[158:161], v[180:183], v[138:141]
	v_mfma_f32_16x16x32_bf16 v[30:33], v[162:165], v[184:187], v[10:13]
	v_mfma_f32_16x16x32_bf16 v[10:13], v[150:153], v[188:191], v[142:145]
	v_mfma_f32_16x16x32_bf16 v[14:17], v[158:161], v[188:191], v[146:149]
	v_mfma_f32_16x16x32_bf16 v[10:13], v[154:157], v[192:195], v[10:13]
	v_mfma_f32_16x16x32_bf16 v[14:17], v[162:165], v[192:195], v[14:17]
	s_setprio 0
	s_barrier
	s_mov_b32 m0, s45
	v_lshl_add_u64 v[106:107], v[196:197], 0, s[10:11]
	global_load_lds_dwordx4 v[106:107], off
	v_lshl_add_u64 v[106:107], v[198:199], 0, s[10:11]
	s_mov_b32 m0, s46
	s_nop 0
	global_load_lds_dwordx4 v[106:107], off
	v_lshl_add_u64 v[106:107], v[200:201], 0, s[10:11]
	s_mov_b32 m0, s47
	s_nop 0
	global_load_lds_dwordx4 v[106:107], off
	v_lshl_add_u64 v[106:107], v[202:203], 0, s[10:11]
	s_mov_b32 m0, s48
	s_nop 0
	global_load_lds_dwordx4 v[106:107], off
	s_mov_b32 m0, s25
	s_nop 0
	global_load_lds_dwordx4 v[74:75], off
	s_mov_b32 m0, s26
	s_nop 0
	global_load_lds_dwordx4 v[76:77], off
	s_waitcnt vmcnt(8)
	s_waitcnt lgkmcnt(0)
	s_barrier
	s_setprio 1
	s_setprio 0
	s_barrier
	s_and_b64 vcc, exec, s[0:1]
	s_cbranch_vccnz .LBB0_616
	s_barrier

; #define PG8_STAGE(bufoff, gbase, voff) do { _Pragma("unroll") for (int _i = 0; _i < 2; ++_i) \
;         __builtin_amdgcn_global_load_lds((const unsigned*)((const char*)(gbase) + (voff)[_i]), (PG8_LAS unsigned*)(lds + (bufoff) + ldsw + _i * 8192), 16, 0, 0); } while (0)
; #define PG8_WAIT_V(n) asm volatile("s_waitcnt vmcnt(" #n ")" ::: "memory")
; #define PG8_WAIT_L(n) asm volatile("s_waitcnt lgkmcnt(" #n ")" ::: "memory")
; #define PG8_BAR __builtin_amdgcn_s_barrier()
; #define PG8_SCHED __builtin_amdgcn_sched_barrier(0)
; template <class Epi, class Sched, bool ALIGN_EPI = true, bool F8 = false>
; __device__ __forceinline__ void gemm_phase(PG8_LAS unsigned char* lds, const Sched& S, const Epi& E) {
;     ...
;             PG8_LDB(B0, 0, 0); PG8_LDB(B1, 0, 1); PG8_SCHED; PG8_LDA(At, 0, 0); PG8_STAGE(PG8_SA(1, 1), a1, voffA[1]);
;             PG8_WAIT_V(8); PG8_WAIT_L(0); PG8_BAR; PG8_MMA(0, 0, At, B0); PG8_MMA(0, 1, At, B1); PG8_BAR; PG8_SCHED;
;             PG8_LDA(At, 0, 1); PG8_STAGE(PG8_SB(0, 0), b2, voffB[0]); PG8_STAGE(PG8_SB(0, 1), b2, voffB[1]); PG8_STAGE(PG8_SA(0, 0), a2, vA2[0]);
;             PG8_WAIT_V(8); PG8_WAIT_L(0); PG8_BAR; PG8_MMA(1, 0, At, B0); PG8_MMA(1, 1, At, B1); PG8_BAR; PG8_SCHED;
.Lpkb_676:
	ds_read_b128 v[180:183], v174
	ds_read_b128 v[184:187], v174 offset:1024
	ds_read_b128 v[188:191], v174 offset:2048
	ds_read_b128 v[192:195], v174 offset:3072
	ds_read_b128 v[196:199], v175
	ds_read_b128 v[200:203], v175 offset:1024
	ds_read_b128 v[204:207], v175 offset:2048
	ds_read_b128 v[208:211], v175 offset:3072
	s_add_u32 s22, s20, 0x100
	s_addc_u32 s23, s21, 0
	s_cmp_eq_u32 s65, 8
	s_cselect_b32 s25, s13, s23
	s_cselect_b32 s24, s12, s22
	s_cselect_b32 s67, s15, s64
	s_cselect_b32 s66, s14, s63
	s_mov_b32 m0, s45
	v_lshl_add_u64 v[166:167], s[20:21], 0, v[164:165]
	ds_read_b128 v[212:215], v176
	ds_read_b128 v[216:219], v176 offset:1024
	ds_read_b128 v[220:223], v176 offset:2048
	ds_read_b128 v[224:227], v176 offset:3072
	ds_read_b128 v[228:231], v176 offset:4096
	ds_read_b128 v[232:235], v176 offset:5120
	ds_read_b128 v[236:239], v176 offset:6144
	ds_read_b128 v[240:243], v176 offset:7168
	global_load_lds_dwordx4 v[166:167], off
	v_lshl_add_u64 v[166:167], s[20:21], 0, v[162:163]
	s_mov_b32 m0, s46
	s_nop 0
	global_load_lds_dwordx4 v[166:167], off
	s_waitcnt vmcnt(8)
	s_waitcnt lgkmcnt(0)
	s_barrier
	s_setprio 1
	s_waitcnt lgkmcnt(0)
	v_mfma_f32_16x16x32_bf16 v[126:129], v[180:183], v[212:215], 0
	v_mfma_f32_16x16x32_bf16 v[122:125], v[188:191], v[212:215], 0
	v_mfma_f32_16x16x32_bf16 v[110:113], v[180:183], v[220:223], 0
	v_mfma_f32_16x16x32_bf16 v[106:109], v[188:191], v[220:223], 0
	v_mfma_f32_16x16x32_bf16 v[94:97], v[180:183], v[228:231], 0
	v_mfma_f32_16x16x32_bf16 v[90:93], v[188:191], v[228:231], 0
	v_mfma_f32_16x16x32_bf16 v[78:81], v[180:183], v[236:239], 0
	v_mfma_f32_16x16x32_bf16 v[74:77], v[188:191], v[236:239], 0
	v_mfma_f32_16x16x32_bf16 v[126:129], v[184:187], v[216:219], v[126:129]
	v_mfma_f32_16x16x32_bf16 v[122:125], v[192:195], v[216:219], v[122:125]
	v_mfma_f32_16x16x32_bf16 v[110:113], v[184:187], v[224:227], v[110:113]
	v_mfma_f32_16x16x32_bf16 v[106:109], v[192:195], v[224:227], v[106:109]
	v_mfma_f32_16x16x32_bf16 v[94:97], v[184:187], v[232:235], v[94:97]
	v_mfma_f32_16x16x32_bf16 v[90:93], v[192:195], v[232:235], v[90:93]
	v_mfma_f32_16x16x32_bf16 v[78:81], v[184:187], v[240:243], v[78:81]
	v_mfma_f32_16x16x32_bf16 v[74:77], v[192:195], v[240:243], v[74:77]
	v_mfma_f32_16x16x32_bf16 v[118:121], v[196:199], v[212:215], 0
	v_mfma_f32_16x16x32_bf16 v[114:117], v[204:207], v[212:215], 0
	v_mfma_f32_16x16x32_bf16 v[102:105], v[196:199], v[220:223], 0
	v_mfma_f32_16x16x32_bf16 v[98:101], v[204:207], v[220:223], 0
	v_mfma_f32_16x16x32_bf16 v[86:89], v[196:199], v[228:231], 0
	v_mfma_f32_16x16x32_bf16 v[82:85], v[204:207], v[228:231], 0
	v_mfma_f32_16x16x32_bf16 v[70:73], v[196:199], v[236:239], 0
	v_mfma_f32_16x16x32_bf16 v[66:69], v[204:207], v[236:239], 0
	v_mfma_f32_16x16x32_bf16 v[118:121], v[200:203], v[216:219], v[118:121]
	v_mfma_f32_16x16x32_bf16 v[114:117], v[208:211], v[216:219], v[114:117]
	v_mfma_f32_16x16x32_bf16 v[102:105], v[200:203], v[224:227], v[102:105]
	v_mfma_f32_16x16x32_bf16 v[98:101], v[208:211], v[224:227], v[98:101]
	v_mfma_f32_16x16x32_bf16 v[86:89], v[200:203], v[232:235], v[86:89]
	v_mfma_f32_16x16x32_bf16 v[82:85], v[208:211], v[232:235], v[82:85]
	v_mfma_f32_16x16x32_bf16 v[70:73], v[200:203], v[240:243], v[70:73]
	v_mfma_f32_16x16x32_bf16 v[66:69], v[208:211], v[240:243], v[66:69]
	s_setprio 0
	s_barrier
	s_mov_b32 m0, s47
	v_lshl_add_u64 v[166:167], s[66:67], 0, v[134:135]
	ds_read_b128 v[212:215], v176 offset:16384
	ds_read_b128 v[216:219], v176 offset:17408
	ds_read_b128 v[220:223], v176 offset:18432
	ds_read_b128 v[224:227], v176 offset:19456
	ds_read_b128 v[228:231], v176 offset:20480
	ds_read_b128 v[232:235], v176 offset:21504
	ds_read_b128 v[236:239], v176 offset:22528
	ds_read_b128 v[240:243], v176 offset:23552
	global_load_lds_dwordx4 v[166:167], off
	v_lshl_add_u64 v[244:245], s[66:67], 0, v[130:131]
	s_mov_b32 m0, s48
	v_lshl_add_u64 v[246:247], s[66:67], 0, v[136:137]
	global_load_lds_dwordx4 v[244:245], off
	s_mov_b32 m0, s49
	v_lshl_add_u64 v[248:249], s[66:67], 0, v[132:133]
	global_load_lds_dwordx4 v[246:247], off
	s_mov_b32 m0, s50
	v_lshl_add_u64 v[250:251], s[24:25], 0, v[138:139]
	global_load_lds_dwordx4 v[248:249], off
	s_mov_b32 m0, s30
	v_lshl_add_u64 v[252:253], s[24:25], 0, v[140:141]
	global_load_lds_dwordx4 v[250:251], off
	s_mov_b32 m0, s31
	s_nop 0
	global_load_lds_dwordx4 v[252:253], off
	s_waitcnt vmcnt(8)
	s_waitcnt lgkmcnt(0)
	s_barrier
	s_setprio 1
	s_waitcnt lgkmcnt(0)
	v_mfma_f32_16x16x32_bf16 v[62:65], v[180:183], v[212:215], 0
	v_mfma_f32_16x16x32_bf16 v[58:61], v[188:191], v[212:215], 0
	v_mfma_f32_16x16x32_bf16 v[46:49], v[180:183], v[220:223], 0
	v_mfma_f32_16x16x32_bf16 v[42:45], v[188:191], v[220:223], 0
	v_mfma_f32_16x16x32_bf16 v[30:33], v[180:183], v[228:231], 0
	v_mfma_f32_16x16x32_bf16 v[26:29], v[188:191], v[228:231], 0
	v_mfma_f32_16x16x32_bf16 v[14:17], v[180:183], v[236:239], 0
	v_mfma_f32_16x16x32_bf16 v[10:13], v[188:191], v[236:239], 0
	v_mfma_f32_16x16x32_bf16 v[62:65], v[184:187], v[216:219], v[62:65]
	v_mfma_f32_16x16x32_bf16 v[58:61], v[192:195], v[216:219], v[58:61]
	v_mfma_f32_16x16x32_bf16 v[46:49], v[184:187], v[224:227], v[46:49]
	v_mfma_f32_16x16x32_bf16 v[42:45], v[192:195], v[224:227], v[42:45]
	v_mfma_f32_16x16x32_bf16 v[30:33], v[184:187], v[232:235], v[30:33]
	v_mfma_f32_16x16x32_bf16 v[26:29], v[192:195], v[232:235], v[26:29]
	v_mfma_f32_16x16x32_bf16 v[14:17], v[184:187], v[240:243], v[14:17]
	v_mfma_f32_16x16x32_bf16 v[10:13], v[192:195], v[240:243], v[10:13]
	v_mfma_f32_16x16x32_bf16 v[54:57], v[196:199], v[212:215], 0
	v_mfma_f32_16x16x32_bf16 v[50:53], v[204:207], v[212:215], 0
	v_mfma_f32_16x16x32_bf16 v[38:41], v[196:199], v[220:223], 0
	v_mfma_f32_16x16x32_bf16 v[34:37], v[204:207], v[220:223], 0
	v_mfma_f32_16x16x32_bf16 v[22:25], v[196:199], v[228:231], 0
	v_mfma_f32_16x16x32_bf16 v[18:21], v[204:207], v[228:231], 0
	v_mfma_f32_16x16x32_bf16 v[6:9], v[196:199], v[236:239], 0
	v_mfma_f32_16x16x32_bf16 v[2:5], v[204:207], v[236:239], 0
	v_mfma_f32_16x16x32_bf16 v[54:57], v[200:203], v[216:219], v[54:57]
	v_mfma_f32_16x16x32_bf16 v[50:53], v[208:211], v[216:219], v[50:53]
	v_mfma_f32_16x16x32_bf16 v[38:41], v[200:203], v[224:227], v[38:41]
	v_mfma_f32_16x16x32_bf16 v[34:37], v[208:211], v[224:227], v[34:37]
	v_mfma_f32_16x16x32_bf16 v[22:25], v[200:203], v[232:235], v[22:25]
	v_mfma_f32_16x16x32_bf16 v[18:21], v[208:211], v[232:235], v[18:21]
	v_mfma_f32_16x16x32_bf16 v[6:9], v[200:203], v[240:243], v[6:9]
	v_mfma_f32_16x16x32_bf16 v[2:5], v[208:211], v[240:243], v[2:5]
	s_setprio 0
	s_barrier
; #define PG8_STAGE(bufoff, gbase, voff) do { _Pragma("unroll") for (int _i = 0; _i < 2; ++_i) \
;         __builtin_amdgcn_global_load_lds((const unsigned*)((const char*)(gbase) + (voff)[_i]), (PG8_LAS unsigned*)(lds + (bufoff) + ldsw + _i * 8192), 16, 0, 0); } while (0)
; #define PG8_WAIT_V(n) asm volatile("s_waitcnt vmcnt(" #n ")" ::: "memory")
; #define PG8_WAIT_L(n) asm volatile("s_waitcnt lgkmcnt(" #n ")" ::: "memory")
; #define PG8_BAR __builtin_amdgcn_s_barrier()
; #define PG8_SCHED __builtin_amdgcn_sched_barrier(0)
; template <class Epi, class Sched, bool ALIGN_EPI = true, bool F8 = false>
; __device__ __forceinline__ void gemm_phase(PG8_LAS unsigned char* lds, const Sched& S, const Epi& E) {
;     ...
;             PG8_LDB(B0, 1, 0); PG8_LDB(B1, 1, 1); PG8_SCHED; PG8_LDA(At, 1, 0); PG8_STAGE(PG8_SA(0, 1), a2, vA2[1]);
;             PG8_WAIT_V(8); PG8_WAIT_L(0); PG8_BAR; PG8_MMA(0, 0, At, B0); PG8_MMA(0, 1, At, B1); PG8_BAR; PG8_SCHED;
;             PG8_LDA(At, 1, 1); PG8_STAGE(PG8_SB(1, 0), b3, voffB[0]); PG8_STAGE(PG8_SB(1, 1), b3, voffB[1]); PG8_STAGE(PG8_SA(1, 0), a3, vA2[0]);
;             PG8_WAIT_V(8); PG8_WAIT_L(0); PG8_BAR; PG8_MMA(1, 0, At, B0); PG8_MMA(1, 1, At, B1); PG8_BAR; PG8_SCHED;
;         }
	ds_read_b128 v[180:183], v177
	ds_read_b128 v[184:187], v177 offset:1024
	ds_read_b128 v[188:191], v177 offset:2048
	ds_read_b128 v[192:195], v177 offset:3072
	ds_read_b128 v[196:199], v178
	ds_read_b128 v[200:203], v178 offset:1024
	ds_read_b128 v[204:207], v178 offset:2048
	ds_read_b128 v[208:211], v178 offset:3072
	s_mov_b32 m0, s40
	v_lshl_add_u64 v[254:255], s[24:25], 0, v[142:143]
	ds_read_b128 v[212:215], v176 offset:32768
	ds_read_b128 v[216:219], v176 offset:33792
	ds_read_b128 v[220:223], v176 offset:34816
	ds_read_b128 v[224:227], v176 offset:35840
	ds_read_b128 v[228:231], v176 offset:36864
	ds_read_b128 v[232:235], v176 offset:37888
	ds_read_b128 v[236:239], v176 offset:38912
	ds_read_b128 v[240:243], v176 offset:39936
	global_load_lds_dwordx4 v[254:255], off
	v_lshl_add_u64 v[254:255], s[24:25], 0, v[144:145]
	s_mov_b32 m0, s41
	s_nop 0
	global_load_lds_dwordx4 v[254:255], off
	s_waitcnt vmcnt(8)
	s_waitcnt lgkmcnt(0)
	s_barrier
	s_setprio 1
	s_waitcnt lgkmcnt(0)
	v_mfma_f32_16x16x32_bf16 v[126:129], v[180:183], v[212:215], v[126:129]
	v_mfma_f32_16x16x32_bf16 v[122:125], v[188:191], v[212:215], v[122:125]
	v_mfma_f32_16x16x32_bf16 v[110:113], v[180:183], v[220:223], v[110:113]
	v_mfma_f32_16x16x32_bf16 v[106:109], v[188:191], v[220:223], v[106:109]
	v_mfma_f32_16x16x32_bf16 v[94:97], v[180:183], v[228:231], v[94:97]
	v_mfma_f32_16x16x32_bf16 v[90:93], v[188:191], v[228:231], v[90:93]
	v_mfma_f32_16x16x32_bf16 v[78:81], v[180:183], v[236:239], v[78:81]
	v_mfma_f32_16x16x32_bf16 v[74:77], v[188:191], v[236:239], v[74:77]
	v_mfma_f32_16x16x32_bf16 v[126:129], v[184:187], v[216:219], v[126:129]
	v_mfma_f32_16x16x32_bf16 v[122:125], v[192:195], v[216:219], v[122:125]
	v_mfma_f32_16x16x32_bf16 v[110:113], v[184:187], v[224:227], v[110:113]
	v_mfma_f32_16x16x32_bf16 v[106:109], v[192:195], v[224:227], v[106:109]
	v_mfma_f32_16x16x32_bf16 v[94:97], v[184:187], v[232:235], v[94:97]
	v_mfma_f32_16x16x32_bf16 v[90:93], v[192:195], v[232:235], v[90:93]
	v_mfma_f32_16x16x32_bf16 v[78:81], v[184:187], v[240:243], v[78:81]
	v_mfma_f32_16x16x32_bf16 v[74:77], v[192:195], v[240:243], v[74:77]
	v_mfma_f32_16x16x32_bf16 v[118:121], v[196:199], v[212:215], v[118:121]
	v_mfma_f32_16x16x32_bf16 v[114:117], v[204:207], v[212:215], v[114:117]
	v_mfma_f32_16x16x32_bf16 v[102:105], v[196:199], v[220:223], v[102:105]
	v_mfma_f32_16x16x32_bf16 v[98:101], v[204:207], v[220:223], v[98:101]
	v_mfma_f32_16x16x32_bf16 v[86:89], v[196:199], v[228:231], v[86:89]
	v_mfma_f32_16x16x32_bf16 v[82:85], v[204:207], v[228:231], v[82:85]
	v_mfma_f32_16x16x32_bf16 v[70:73], v[196:199], v[236:239], v[70:73]
	v_mfma_f32_16x16x32_bf16 v[66:69], v[204:207], v[236:239], v[66:69]
	v_mfma_f32_16x16x32_bf16 v[118:121], v[200:203], v[216:219], v[118:121]
	v_mfma_f32_16x16x32_bf16 v[114:117], v[208:211], v[216:219], v[114:117]
	v_mfma_f32_16x16x32_bf16 v[102:105], v[200:203], v[224:227], v[102:105]
	v_mfma_f32_16x16x32_bf16 v[98:101], v[208:211], v[224:227], v[98:101]
	v_mfma_f32_16x16x32_bf16 v[86:89], v[200:203], v[232:235], v[86:89]
	v_mfma_f32_16x16x32_bf16 v[82:85], v[208:211], v[232:235], v[82:85]
	v_mfma_f32_16x16x32_bf16 v[70:73], v[200:203], v[240:243], v[70:73]
	v_mfma_f32_16x16x32_bf16 v[66:69], v[208:211], v[240:243], v[66:69]
	s_setprio 0
	s_barrier
	s_mov_b32 m0, s51
	v_lshl_add_u64 v[166:167], v[166:167], 0, s[8:9]
	ds_read_b128 v[212:215], v176 offset:49152
	ds_read_b128 v[216:219], v176 offset:50176
	ds_read_b128 v[220:223], v176 offset:51200
	ds_read_b128 v[224:227], v176 offset:52224
	ds_read_b128 v[228:231], v176 offset:53248
	ds_read_b128 v[232:235], v176 offset:54272
	ds_read_b128 v[236:239], v176 offset:55296
	ds_read_b128 v[240:243], v176 offset:56320
	global_load_lds_dwordx4 v[166:167], off
	v_lshl_add_u64 v[166:167], v[244:245], 0, s[8:9]
	s_mov_b32 m0, s52
	s_nop 0
	global_load_lds_dwordx4 v[166:167], off
	v_lshl_add_u64 v[166:167], v[246:247], 0, s[8:9]
	s_mov_b32 m0, s53
	s_nop 0
	global_load_lds_dwordx4 v[166:167], off
	v_lshl_add_u64 v[166:167], v[248:249], 0, s[8:9]
	s_mov_b32 m0, s58
	s_nop 0
	global_load_lds_dwordx4 v[166:167], off
	v_lshl_add_u64 v[166:167], v[250:251], 0, s[8:9]
	s_mov_b32 m0, s43
	s_nop 0
	global_load_lds_dwordx4 v[166:167], off
	v_lshl_add_u64 v[166:167], v[252:253], 0, s[8:9]
	s_mov_b32 m0, s44
	s_nop 0
	global_load_lds_dwordx4 v[166:167], off
	s_waitcnt vmcnt(8)
	s_waitcnt lgkmcnt(0)
	s_barrier
	s_setprio 1
	s_waitcnt lgkmcnt(0)
	v_mfma_f32_16x16x32_bf16 v[62:65], v[180:183], v[212:215], v[62:65]
	v_mfma_f32_16x16x32_bf16 v[58:61], v[188:191], v[212:215], v[58:61]
	v_mfma_f32_16x16x32_bf16 v[46:49], v[180:183], v[220:223], v[46:49]
	v_mfma_f32_16x16x32_bf16 v[42:45], v[188:191], v[220:223], v[42:45]
	v_mfma_f32_16x16x32_bf16 v[30:33], v[180:183], v[228:231], v[30:33]
	v_mfma_f32_16x16x32_bf16 v[26:29], v[188:191], v[228:231], v[26:29]
	v_mfma_f32_16x16x32_bf16 v[14:17], v[180:183], v[236:239], v[14:17]
	v_mfma_f32_16x16x32_bf16 v[10:13], v[188:191], v[236:239], v[10:13]
	v_mfma_f32_16x16x32_bf16 v[62:65], v[184:187], v[216:219], v[62:65]
	v_mfma_f32_16x16x32_bf16 v[58:61], v[192:195], v[216:219], v[58:61]
	v_mfma_f32_16x16x32_bf16 v[46:49], v[184:187], v[224:227], v[46:49]
	v_mfma_f32_16x16x32_bf16 v[42:45], v[192:195], v[224:227], v[42:45]
	v_mfma_f32_16x16x32_bf16 v[30:33], v[184:187], v[232:235], v[30:33]
	v_mfma_f32_16x16x32_bf16 v[26:29], v[192:195], v[232:235], v[26:29]
	v_mfma_f32_16x16x32_bf16 v[14:17], v[184:187], v[240:243], v[14:17]
	v_mfma_f32_16x16x32_bf16 v[10:13], v[192:195], v[240:243], v[10:13]
	v_mfma_f32_16x16x32_bf16 v[54:57], v[196:199], v[212:215], v[54:57]
	v_mfma_f32_16x16x32_bf16 v[50:53], v[204:207], v[212:215], v[50:53]
	v_mfma_f32_16x16x32_bf16 v[38:41], v[196:199], v[220:223], v[38:41]
	v_mfma_f32_16x16x32_bf16 v[34:37], v[204:207], v[220:223], v[34:37]
	v_mfma_f32_16x16x32_bf16 v[22:25], v[196:199], v[228:231], v[22:25]
	v_mfma_f32_16x16x32_bf16 v[18:21], v[204:207], v[228:231], v[18:21]
	v_mfma_f32_16x16x32_bf16 v[6:9], v[196:199], v[236:239], v[6:9]
	v_mfma_f32_16x16x32_bf16 v[2:5], v[204:207], v[236:239], v[2:5]
	v_mfma_f32_16x16x32_bf16 v[54:57], v[200:203], v[216:219], v[54:57]
	v_mfma_f32_16x16x32_bf16 v[50:53], v[208:211], v[216:219], v[50:53]
	v_mfma_f32_16x16x32_bf16 v[38:41], v[200:203], v[224:227], v[38:41]
	v_mfma_f32_16x16x32_bf16 v[34:37], v[208:211], v[224:227], v[34:37]
	v_mfma_f32_16x16x32_bf16 v[22:25], v[200:203], v[232:235], v[22:25]
	v_mfma_f32_16x16x32_bf16 v[18:21], v[208:211], v[232:235], v[18:21]
	v_mfma_f32_16x16x32_bf16 v[6:9], v[200:203], v[240:243], v[6:9]
	v_mfma_f32_16x16x32_bf16 v[2:5], v[208:211], v[240:243], v[2:5]
	s_setprio 0
	s_barrier
	s_add_i32 s65, s65, 2
	s_add_u32 s63, s63, 0x100
	s_addc_u32 s64, s64, 0
	s_cmp_gt_u32 s65, 9
	s_mov_b64 s[20:21], s[22:23]
	s_cbranch_scc0 .LBB0_676
	s_branch .Lpx_17518
; #define PG8_STAGE(bufoff, gbase, voff) do { _Pragma("unroll") for (int _i = 0; _i < 2; ++_i) \
;         __builtin_amdgcn_global_load_lds((const unsigned*)((const char*)(gbase) + (voff)[_i]), (PG8_LAS unsigned*)(lds + (bufoff) + ldsw + _i * 8192), 16, 0, 0); } while (0)
; #define PG8_WAIT_V(n) asm volatile("s_waitcnt vmcnt(" #n ")" ::: "memory")
; #define PG8_WAIT_L(n) asm volatile("s_waitcnt lgkmcnt(" #n ")" ::: "memory")
; #define PG8_BAR __builtin_amdgcn_s_barrier()
; #define PG8_SCHED __builtin_amdgcn_sched_barrier(0)
; template <class Epi, class Sched, bool ALIGN_EPI = true, bool F8 = false>
; __device__ __forceinline__ void gemm_phase(PG8_LAS unsigned char* lds, const Sched& S, const Epi& E) {
;     ...
;             PG8_LDB(B0, 0, 0); PG8_LDB(B1, 0, 1); PG8_SCHED; PG8_LDA(At, 0, 0); PG8_STAGE(PG8_SA(1, 1), a1, voffA[1]);
;             PG8_WAIT_V(8); PG8_WAIT_L(0); PG8_BAR; PG8_MMA(0, 0, At, B0); PG8_MMA(0, 1, At, B1); PG8_BAR; PG8_SCHED;
;             PG8_LDA(At, 0, 1); PG8_STAGE(PG8_SB(0, 0), b2, voffB[0]); PG8_STAGE(PG8_SB(0, 1), b2, voffB[1]); PG8_STAGE(PG8_SA(0, 0), a2, vA2[0]);
.LBB0_676:
	ds_read_b128 v[180:183], v174
	ds_read_b128 v[184:187], v174 offset:1024
	ds_read_b128 v[188:191], v174 offset:2048
	ds_read_b128 v[192:195], v174 offset:3072
	ds_read_b128 v[196:199], v175
	ds_read_b128 v[200:203], v175 offset:1024
	ds_read_b128 v[204:207], v175 offset:2048
	ds_read_b128 v[208:211], v175 offset:3072
	s_add_u32 s22, s20, 0x100
	s_addc_u32 s23, s21, 0
	s_cmp_eq_u32 s65, 8
	s_cselect_b32 s25, s13, s23
	s_cselect_b32 s24, s12, s22
	s_cselect_b32 s67, s15, s64
	s_cselect_b32 s66, s14, s63
	s_mov_b32 m0, s45
	v_lshl_add_u64 v[166:167], s[20:21], 0, v[164:165]
	ds_read_b128 v[212:215], v176
	ds_read_b128 v[216:219], v176 offset:1024
	ds_read_b128 v[220:223], v176 offset:2048
	ds_read_b128 v[224:227], v176 offset:3072
	ds_read_b128 v[228:231], v176 offset:4096
	ds_read_b128 v[232:235], v176 offset:5120
	ds_read_b128 v[236:239], v176 offset:6144
	ds_read_b128 v[240:243], v176 offset:7168
	global_load_lds_dwordx4 v[166:167], off
	v_lshl_add_u64 v[166:167], s[20:21], 0, v[162:163]
	s_mov_b32 m0, s46
	s_nop 0
	global_load_lds_dwordx4 v[166:167], off
	s_waitcnt vmcnt(8)
	s_waitcnt lgkmcnt(0)
	s_barrier
	s_setprio 1
	s_waitcnt lgkmcnt(0)
	v_mfma_f32_16x16x32_bf16 v[126:129], v[180:183], v[212:215], v[126:129]
	v_mfma_f32_16x16x32_bf16 v[122:125], v[188:191], v[212:215], v[122:125]
	v_mfma_f32_16x16x32_bf16 v[110:113], v[180:183], v[220:223], v[110:113]
	v_mfma_f32_16x16x32_bf16 v[106:109], v[188:191], v[220:223], v[106:109]
	v_mfma_f32_16x16x32_bf16 v[94:97], v[180:183], v[228:231], v[94:97]
	v_mfma_f32_16x16x32_bf16 v[90:93], v[188:191], v[228:231], v[90:93]
	v_mfma_f32_16x16x32_bf16 v[78:81], v[180:183], v[236:239], v[78:81]
	v_mfma_f32_16x16x32_bf16 v[74:77], v[188:191], v[236:239], v[74:77]
	v_mfma_f32_16x16x32_bf16 v[126:129], v[184:187], v[216:219], v[126:129]
	v_mfma_f32_16x16x32_bf16 v[122:125], v[192:195], v[216:219], v[122:125]
	v_mfma_f32_16x16x32_bf16 v[110:113], v[184:187], v[224:227], v[110:113]
	v_mfma_f32_16x16x32_bf16 v[106:109], v[192:195], v[224:227], v[106:109]
	v_mfma_f32_16x16x32_bf16 v[94:97], v[184:187], v[232:235], v[94:97]
	v_mfma_f32_16x16x32_bf16 v[90:93], v[192:195], v[232:235], v[90:93]
	v_mfma_f32_16x16x32_bf16 v[78:81], v[184:187], v[240:243], v[78:81]
	v_mfma_f32_16x16x32_bf16 v[74:77], v[192:195], v[240:243], v[74:77]
	v_mfma_f32_16x16x32_bf16 v[118:121], v[196:199], v[212:215], v[118:121]
	v_mfma_f32_16x16x32_bf16 v[114:117], v[204:207], v[212:215], v[114:117]
	v_mfma_f32_16x16x32_bf16 v[102:105], v[196:199], v[220:223], v[102:105]
	v_mfma_f32_16x16x32_bf16 v[98:101], v[204:207], v[220:223], v[98:101]
	v_mfma_f32_16x16x32_bf16 v[86:89], v[196:199], v[228:231], v[86:89]
	v_mfma_f32_16x16x32_bf16 v[82:85], v[204:207], v[228:231], v[82:85]
	v_mfma_f32_16x16x32_bf16 v[70:73], v[196:199], v[236:239], v[70:73]
	v_mfma_f32_16x16x32_bf16 v[66:69], v[204:207], v[236:239], v[66:69]
	v_mfma_f32_16x16x32_bf16 v[118:121], v[200:203], v[216:219], v[118:121]
	v_mfma_f32_16x16x32_bf16 v[114:117], v[208:211], v[216:219], v[114:117]
	v_mfma_f32_16x16x32_bf16 v[102:105], v[200:203], v[224:227], v[102:105]
	v_mfma_f32_16x16x32_bf16 v[98:101], v[208:211], v[224:227], v[98:101]
	v_mfma_f32_16x16x32_bf16 v[86:89], v[200:203], v[232:235], v[86:89]
	v_mfma_f32_16x16x32_bf16 v[82:85], v[208:211], v[232:235], v[82:85]
	v_mfma_f32_16x16x32_bf16 v[70:73], v[200:203], v[240:243], v[70:73]
	v_mfma_f32_16x16x32_bf16 v[66:69], v[208:211], v[240:243], v[66:69]
	s_setprio 0
	s_barrier
	s_mov_b32 m0, s47
	v_lshl_add_u64 v[166:167], s[66:67], 0, v[134:135]
	ds_read_b128 v[212:215], v176 offset:16384
	ds_read_b128 v[216:219], v176 offset:17408
	ds_read_b128 v[220:223], v176 offset:18432
	ds_read_b128 v[224:227], v176 offset:19456
	ds_read_b128 v[228:231], v176 offset:20480
	ds_read_b128 v[232:235], v176 offset:21504
	ds_read_b128 v[236:239], v176 offset:22528
	ds_read_b128 v[240:243], v176 offset:23552
	global_load_lds_dwordx4 v[166:167], off
	v_lshl_add_u64 v[244:245], s[66:67], 0, v[130:131]
	s_mov_b32 m0, s48
	v_lshl_add_u64 v[246:247], s[66:67], 0, v[136:137]
	global_load_lds_dwordx4 v[244:245], off
	s_mov_b32 m0, s49
	v_lshl_add_u64 v[248:249], s[66:67], 0, v[132:133]
	global_load_lds_dwordx4 v[246:247], off
	s_mov_b32 m0, s50
	v_lshl_add_u64 v[250:251], s[24:25], 0, v[138:139]
	global_load_lds_dwordx4 v[248:249], off
	s_mov_b32 m0, s30
	v_lshl_add_u64 v[252:253], s[24:25], 0, v[140:141]
	global_load_lds_dwordx4 v[250:251], off
	s_mov_b32 m0, s31
	s_nop 0
	global_load_lds_dwordx4 v[252:253], off
	s_waitcnt vmcnt(8)
	s_waitcnt lgkmcnt(0)
	s_barrier
; #define PG8_STAGE(bufoff, gbase, voff) do { _Pragma("unroll") for (int _i = 0; _i < 2; ++_i) \
;         __builtin_amdgcn_global_load_lds((const unsigned*)((const char*)(gbase) + (voff)[_i]), (PG8_LAS unsigned*)(lds + (bufoff) + ldsw + _i * 8192), 16, 0, 0); } while (0)
; #define PG8_WAIT_V(n) asm volatile("s_waitcnt vmcnt(" #n ")" ::: "memory")
; #define PG8_WAIT_L(n) asm volatile("s_waitcnt lgkmcnt(" #n ")" ::: "memory")
; #define PG8_BAR __builtin_amdgcn_s_barrier()
; #define PG8_SCHED __builtin_amdgcn_sched_barrier(0)
; template <class Epi, class Sched, bool ALIGN_EPI = true, bool F8 = false>
; __device__ __forceinline__ void gemm_phase(PG8_LAS unsigned char* lds, const Sched& S, const Epi& E) {
;     ...
;             PG8_WAIT_V(8); PG8_WAIT_L(0); PG8_BAR; PG8_MMA(1, 0, At, B0); PG8_MMA(1, 1, At, B1); PG8_BAR; PG8_SCHED;
;             PG8_LDB(B0, 1, 0); PG8_LDB(B1, 1, 1); PG8_SCHED; PG8_LDA(At, 1, 0); PG8_STAGE(PG8_SA(0, 1), a2, vA2[1]);
;             PG8_WAIT_V(8); PG8_WAIT_L(0); PG8_BAR; PG8_MMA(0, 0, At, B0); PG8_MMA(0, 1, At, B1); PG8_BAR; PG8_SCHED;
	s_setprio 1
	s_waitcnt lgkmcnt(0)
	v_mfma_f32_16x16x32_bf16 v[62:65], v[180:183], v[212:215], v[62:65]
	v_mfma_f32_16x16x32_bf16 v[58:61], v[188:191], v[212:215], v[58:61]
	v_mfma_f32_16x16x32_bf16 v[46:49], v[180:183], v[220:223], v[46:49]
	v_mfma_f32_16x16x32_bf16 v[42:45], v[188:191], v[220:223], v[42:45]
	v_mfma_f32_16x16x32_bf16 v[30:33], v[180:183], v[228:231], v[30:33]
	v_mfma_f32_16x16x32_bf16 v[26:29], v[188:191], v[228:231], v[26:29]
	v_mfma_f32_16x16x32_bf16 v[14:17], v[180:183], v[236:239], v[14:17]
	v_mfma_f32_16x16x32_bf16 v[10:13], v[188:191], v[236:239], v[10:13]
	v_mfma_f32_16x16x32_bf16 v[62:65], v[184:187], v[216:219], v[62:65]
	v_mfma_f32_16x16x32_bf16 v[58:61], v[192:195], v[216:219], v[58:61]
	v_mfma_f32_16x16x32_bf16 v[46:49], v[184:187], v[224:227], v[46:49]
	v_mfma_f32_16x16x32_bf16 v[42:45], v[192:195], v[224:227], v[42:45]
	v_mfma_f32_16x16x32_bf16 v[30:33], v[184:187], v[232:235], v[30:33]
	v_mfma_f32_16x16x32_bf16 v[26:29], v[192:195], v[232:235], v[26:29]
	v_mfma_f32_16x16x32_bf16 v[14:17], v[184:187], v[240:243], v[14:17]
	v_mfma_f32_16x16x32_bf16 v[10:13], v[192:195], v[240:243], v[10:13]
	v_mfma_f32_16x16x32_bf16 v[54:57], v[196:199], v[212:215], v[54:57]
	v_mfma_f32_16x16x32_bf16 v[50:53], v[204:207], v[212:215], v[50:53]
	v_mfma_f32_16x16x32_bf16 v[38:41], v[196:199], v[220:223], v[38:41]
	v_mfma_f32_16x16x32_bf16 v[34:37], v[204:207], v[220:223], v[34:37]
	v_mfma_f32_16x16x32_bf16 v[22:25], v[196:199], v[228:231], v[22:25]
	v_mfma_f32_16x16x32_bf16 v[18:21], v[204:207], v[228:231], v[18:21]
	v_mfma_f32_16x16x32_bf16 v[6:9], v[196:199], v[236:239], v[6:9]
	v_mfma_f32_16x16x32_bf16 v[2:5], v[204:207], v[236:239], v[2:5]
	v_mfma_f32_16x16x32_bf16 v[54:57], v[200:203], v[216:219], v[54:57]
	v_mfma_f32_16x16x32_bf16 v[50:53], v[208:211], v[216:219], v[50:53]
	v_mfma_f32_16x16x32_bf16 v[38:41], v[200:203], v[224:227], v[38:41]
	v_mfma_f32_16x16x32_bf16 v[34:37], v[208:211], v[224:227], v[34:37]
	v_mfma_f32_16x16x32_bf16 v[22:25], v[200:203], v[232:235], v[22:25]
	v_mfma_f32_16x16x32_bf16 v[18:21], v[208:211], v[232:235], v[18:21]
	v_mfma_f32_16x16x32_bf16 v[6:9], v[200:203], v[240:243], v[6:9]
	v_mfma_f32_16x16x32_bf16 v[2:5], v[208:211], v[240:243], v[2:5]
	s_setprio 0
	s_barrier
	ds_read_b128 v[180:183], v177
	ds_read_b128 v[184:187], v177 offset:1024
	ds_read_b128 v[188:191], v177 offset:2048
	ds_read_b128 v[192:195], v177 offset:3072
	ds_read_b128 v[196:199], v178
	ds_read_b128 v[200:203], v178 offset:1024
	ds_read_b128 v[204:207], v178 offset:2048
	ds_read_b128 v[208:211], v178 offset:3072
	s_mov_b32 m0, s40
	v_lshl_add_u64 v[254:255], s[24:25], 0, v[142:143]
	ds_read_b128 v[212:215], v176 offset:32768
	ds_read_b128 v[216:219], v176 offset:33792
	ds_read_b128 v[220:223], v176 offset:34816
	ds_read_b128 v[224:227], v176 offset:35840
	ds_read_b128 v[228:231], v176 offset:36864
	ds_read_b128 v[232:235], v176 offset:37888
	ds_read_b128 v[236:239], v176 offset:38912
	ds_read_b128 v[240:243], v176 offset:39936
	global_load_lds_dwordx4 v[254:255], off
	v_lshl_add_u64 v[254:255], s[24:25], 0, v[144:145]
	s_mov_b32 m0, s41
	s_nop 0
	global_load_lds_dwordx4 v[254:255], off
	s_waitcnt vmcnt(8)
	s_waitcnt lgkmcnt(0)
	s_barrier
	s_setprio 1
	s_waitcnt lgkmcnt(0)
	v_mfma_f32_16x16x32_bf16 v[126:129], v[180:183], v[212:215], v[126:129]
	v_mfma_f32_16x16x32_bf16 v[122:125], v[188:191], v[212:215], v[122:125]
	v_mfma_f32_16x16x32_bf16 v[110:113], v[180:183], v[220:223], v[110:113]
	v_mfma_f32_16x16x32_bf16 v[106:109], v[188:191], v[220:223], v[106:109]
	v_mfma_f32_16x16x32_bf16 v[94:97], v[180:183], v[228:231], v[94:97]
	v_mfma_f32_16x16x32_bf16 v[90:93], v[188:191], v[228:231], v[90:93]
	v_mfma_f32_16x16x32_bf16 v[78:81], v[180:183], v[236:239], v[78:81]
	v_mfma_f32_16x16x32_bf16 v[74:77], v[188:191], v[236:239], v[74:77]
	v_mfma_f32_16x16x32_bf16 v[126:129], v[184:187], v[216:219], v[126:129]
	v_mfma_f32_16x16x32_bf16 v[122:125], v[192:195], v[216:219], v[122:125]
	v_mfma_f32_16x16x32_bf16 v[110:113], v[184:187], v[224:227], v[110:113]
	v_mfma_f32_16x16x32_bf16 v[106:109], v[192:195], v[224:227], v[106:109]
	v_mfma_f32_16x16x32_bf16 v[94:97], v[184:187], v[232:235], v[94:97]
	v_mfma_f32_16x16x32_bf16 v[90:93], v[192:195], v[232:235], v[90:93]
	v_mfma_f32_16x16x32_bf16 v[78:81], v[184:187], v[240:243], v[78:81]
	v_mfma_f32_16x16x32_bf16 v[74:77], v[192:195], v[240:243], v[74:77]
	v_mfma_f32_16x16x32_bf16 v[118:121], v[196:199], v[212:215], v[118:121]
	v_mfma_f32_16x16x32_bf16 v[114:117], v[204:207], v[212:215], v[114:117]
	v_mfma_f32_16x16x32_bf16 v[102:105], v[196:199], v[220:223], v[102:105]
	v_mfma_f32_16x16x32_bf16 v[98:101], v[204:207], v[220:223], v[98:101]
	v_mfma_f32_16x16x32_bf16 v[86:89], v[196:199], v[228:231], v[86:89]
	v_mfma_f32_16x16x32_bf16 v[82:85], v[204:207], v[228:231], v[82:85]
	v_mfma_f32_16x16x32_bf16 v[70:73], v[196:199], v[236:239], v[70:73]
	v_mfma_f32_16x16x32_bf16 v[66:69], v[204:207], v[236:239], v[66:69]
	v_mfma_f32_16x16x32_bf16 v[118:121], v[200:203], v[216:219], v[118:121]
	v_mfma_f32_16x16x32_bf16 v[114:117], v[208:211], v[216:219], v[114:117]
	v_mfma_f32_16x16x32_bf16 v[102:105], v[200:203], v[224:227], v[102:105]
	v_mfma_f32_16x16x32_bf16 v[98:101], v[208:211], v[224:227], v[98:101]
	v_mfma_f32_16x16x32_bf16 v[86:89], v[200:203], v[232:235], v[86:89]
	v_mfma_f32_16x16x32_bf16 v[82:85], v[208:211], v[232:235], v[82:85]
	v_mfma_f32_16x16x32_bf16 v[70:73], v[200:203], v[240:243], v[70:73]
	v_mfma_f32_16x16x32_bf16 v[66:69], v[208:211], v[240:243], v[66:69]
	s_setprio 0
	s_barrier
; #define PG8_STAGE(bufoff, gbase, voff) do { _Pragma("unroll") for (int _i = 0; _i < 2; ++_i) \
;         __builtin_amdgcn_global_load_lds((const unsigned*)((const char*)(gbase) + (voff)[_i]), (PG8_LAS unsigned*)(lds + (bufoff) + ldsw + _i * 8192), 16, 0, 0); } while (0)
; #define PG8_WAIT_V(n) asm volatile("s_waitcnt vmcnt(" #n ")" ::: "memory")
; #define PG8_WAIT_L(n) asm volatile("s_waitcnt lgkmcnt(" #n ")" ::: "memory")
; #define PG8_BAR __builtin_amdgcn_s_barrier()
; #define PG8_SCHED __builtin_amdgcn_sched_barrier(0)
; template <class Epi, class Sched, bool ALIGN_EPI = true, bool F8 = false>
; __device__ __forceinline__ void gemm_phase(PG8_LAS unsigned char* lds, const Sched& S, const Epi& E) {
;     ...
;             PG8_LDA(At, 1, 1); PG8_STAGE(PG8_SB(1, 0), b3, voffB[0]); PG8_STAGE(PG8_SB(1, 1), b3, voffB[1]); PG8_STAGE(PG8_SA(1, 0), a3, vA2[0]);
;             PG8_WAIT_V(8); PG8_WAIT_L(0); PG8_BAR; PG8_MMA(1, 0, At, B0); PG8_MMA(1, 1, At, B1); PG8_BAR; PG8_SCHED;
;         }
	s_mov_b32 m0, s51
	v_lshl_add_u64 v[166:167], v[166:167], 0, s[8:9]
	ds_read_b128 v[212:215], v176 offset:49152
	ds_read_b128 v[216:219], v176 offset:50176
	ds_read_b128 v[220:223], v176 offset:51200
	ds_read_b128 v[224:227], v176 offset:52224
	ds_read_b128 v[228:231], v176 offset:53248
	ds_read_b128 v[232:235], v176 offset:54272
	ds_read_b128 v[236:239], v176 offset:55296
	ds_read_b128 v[240:243], v176 offset:56320
	global_load_lds_dwordx4 v[166:167], off
	v_lshl_add_u64 v[166:167], v[244:245], 0, s[8:9]
	s_mov_b32 m0, s52
	s_nop 0
	global_load_lds_dwordx4 v[166:167], off
	v_lshl_add_u64 v[166:167], v[246:247], 0, s[8:9]
	s_mov_b32 m0, s53
	s_nop 0
	global_load_lds_dwordx4 v[166:167], off
	v_lshl_add_u64 v[166:167], v[248:249], 0, s[8:9]
	s_mov_b32 m0, s58
	s_nop 0
	global_load_lds_dwordx4 v[166:167], off
	v_lshl_add_u64 v[166:167], v[250:251], 0, s[8:9]
	s_mov_b32 m0, s43
	s_nop 0
	global_load_lds_dwordx4 v[166:167], off
	v_lshl_add_u64 v[166:167], v[252:253], 0, s[8:9]
	s_mov_b32 m0, s44
	s_nop 0
	global_load_lds_dwordx4 v[166:167], off
	s_waitcnt vmcnt(8)
	s_waitcnt lgkmcnt(0)
	s_barrier
	s_setprio 1
	s_waitcnt lgkmcnt(0)
	v_mfma_f32_16x16x32_bf16 v[62:65], v[180:183], v[212:215], v[62:65]
	v_mfma_f32_16x16x32_bf16 v[58:61], v[188:191], v[212:215], v[58:61]
	v_mfma_f32_16x16x32_bf16 v[46:49], v[180:183], v[220:223], v[46:49]
	v_mfma_f32_16x16x32_bf16 v[42:45], v[188:191], v[220:223], v[42:45]
	v_mfma_f32_16x16x32_bf16 v[30:33], v[180:183], v[228:231], v[30:33]
	v_mfma_f32_16x16x32_bf16 v[26:29], v[188:191], v[228:231], v[26:29]
	v_mfma_f32_16x16x32_bf16 v[14:17], v[180:183], v[236:239], v[14:17]
	v_mfma_f32_16x16x32_bf16 v[10:13], v[188:191], v[236:239], v[10:13]
	v_mfma_f32_16x16x32_bf16 v[62:65], v[184:187], v[216:219], v[62:65]
	v_mfma_f32_16x16x32_bf16 v[58:61], v[192:195], v[216:219], v[58:61]
	v_mfma_f32_16x16x32_bf16 v[46:49], v[184:187], v[224:227], v[46:49]
	v_mfma_f32_16x16x32_bf16 v[42:45], v[192:195], v[224:227], v[42:45]
	v_mfma_f32_16x16x32_bf16 v[30:33], v[184:187], v[232:235], v[30:33]
	v_mfma_f32_16x16x32_bf16 v[26:29], v[192:195], v[232:235], v[26:29]
	v_mfma_f32_16x16x32_bf16 v[14:17], v[184:187], v[240:243], v[14:17]
	v_mfma_f32_16x16x32_bf16 v[10:13], v[192:195], v[240:243], v[10:13]
	v_mfma_f32_16x16x32_bf16 v[54:57], v[196:199], v[212:215], v[54:57]
	v_mfma_f32_16x16x32_bf16 v[50:53], v[204:207], v[212:215], v[50:53]
	v_mfma_f32_16x16x32_bf16 v[38:41], v[196:199], v[220:223], v[38:41]
	v_mfma_f32_16x16x32_bf16 v[34:37], v[204:207], v[220:223], v[34:37]
	v_mfma_f32_16x16x32_bf16 v[22:25], v[196:199], v[228:231], v[22:25]
	v_mfma_f32_16x16x32_bf16 v[18:21], v[204:207], v[228:231], v[18:21]
	v_mfma_f32_16x16x32_bf16 v[6:9], v[196:199], v[236:239], v[6:9]
	v_mfma_f32_16x16x32_bf16 v[2:5], v[204:207], v[236:239], v[2:5]
	v_mfma_f32_16x16x32_bf16 v[54:57], v[200:203], v[216:219], v[54:57]
	v_mfma_f32_16x16x32_bf16 v[50:53], v[208:211], v[216:219], v[50:53]
	v_mfma_f32_16x16x32_bf16 v[38:41], v[200:203], v[224:227], v[38:41]
	v_mfma_f32_16x16x32_bf16 v[34:37], v[208:211], v[224:227], v[34:37]
	v_mfma_f32_16x16x32_bf16 v[22:25], v[200:203], v[232:235], v[22:25]
	v_mfma_f32_16x16x32_bf16 v[18:21], v[208:211], v[232:235], v[18:21]
	v_mfma_f32_16x16x32_bf16 v[6:9], v[200:203], v[240:243], v[6:9]
	v_mfma_f32_16x16x32_bf16 v[2:5], v[208:211], v[240:243], v[2:5]
	s_setprio 0
	s_barrier
	s_add_i32 s65, s65, 2
	s_add_u32 s63, s63, 0x100
	s_addc_u32 s64, s64, 0
	s_cmp_gt_u32 s65, 9
	s_mov_b64 s[20:21], s[22:23]
	s_cbranch_scc0 .LBB0_676

; #define PG8_STAGE(bufoff, gbase, voff) do { _Pragma("unroll") for (int _i = 0; _i < 2; ++_i) \
;         __builtin_amdgcn_global_load_lds((const unsigned*)((const char*)(gbase) + (voff)[_i]), (PG8_LAS unsigned*)(lds + (bufoff) + ldsw + _i * 8192), 16, 0, 0); } while (0)
; #define PG8_WAIT_V(n) asm volatile("s_waitcnt vmcnt(" #n ")" ::: "memory")
; #define PG8_WAIT_L(n) asm volatile("s_waitcnt lgkmcnt(" #n ")" ::: "memory")
; #define PG8_BAR __builtin_amdgcn_s_barrier()
; #define PG8_SCHED __builtin_amdgcn_sched_barrier(0)
; template <class Epi, class Sched, bool ALIGN_EPI = true, bool F8 = false>
; __device__ __forceinline__ void gemm_phase(PG8_LAS unsigned char* lds, const Sched& S, const Epi& E) {
;     ...
;             PG8_LDB(B0, 0, 0); PG8_LDB(B1, 0, 1); PG8_SCHED; PG8_LDA(At, 0, 0); PG8_STAGE(PG8_SA(1, 1), a1, voffA[1]);
;             PG8_WAIT_V(8); PG8_WAIT_L(0); PG8_BAR; PG8_MMA(0, 0, At, B0); PG8_MMA(0, 1, At, B1); PG8_BAR; PG8_SCHED;
;             PG8_LDA(At, 0, 1); PG8_STAGE(PG8_SB(0, 0), b2, voffB[0]); PG8_STAGE(PG8_SB(0, 1), b2, voffB[1]); PG8_STAGE(PG8_SA(0, 0), a2, vA2[0]);
;             PG8_WAIT_V(8); PG8_WAIT_L(0); PG8_BAR; PG8_MMA(1, 0, At, B0); PG8_MMA(1, 1, At, B1); PG8_BAR; PG8_SCHED;
;             PG8_LDB(B0, 1, 0); PG8_LDB(B1, 1, 1); PG8_SCHED; PG8_LDA(At, 1, 0); PG8_STAGE(PG8_SA(0, 1), a2, vA2[1]);
;             PG8_WAIT_V(8); PG8_WAIT_L(0); PG8_BAR; PG8_MMA(0, 0, At, B0); PG8_MMA(0, 1, At, B1); PG8_BAR; PG8_SCHED;
.Lpkb_692:
	s_add_u32 s30, s4, s19
	s_addc_u32 s31, s5, 0
	s_add_i32 s28, s19, 0x100
	s_and_b64 s[26:27], s[24:25], exec
	s_cselect_b32 s26, 0, s28
	s_cselect_b32 s27, 0, 0
	s_add_u32 s26, s4, s26
	ds_read_b128 v[100:103], v94
	ds_read_b128 v[104:107], v94 offset:1024
	ds_read_b128 v[108:111], v94 offset:2048
	ds_read_b128 v[112:115], v94 offset:3072
	ds_read_b128 v[116:119], v95
	ds_read_b128 v[120:123], v95 offset:1024
	ds_read_b128 v[124:127], v95 offset:2048
	ds_read_b128 v[128:131], v95 offset:3072
	s_addc_u32 s27, s5, s27
	s_add_u32 s19, s20, s19
	s_addc_u32 s28, s21, 0
	s_add_u32 s19, s19, 0x100
	s_addc_u32 s28, s28, 0
	s_and_b64 s[24:25], s[24:25], exec
	s_cselect_b32 s29, s15, s28
	s_cselect_b32 s28, s14, s19
	s_add_u32 s30, s30, 0x80
	s_addc_u32 s31, s31, 0
	s_add_u32 s24, s28, 0x80
	s_addc_u32 s25, s29, 0
	s_mov_b32 m0, s51
	v_lshl_add_u64 v[164:165], s[30:31], 0, v[78:79]
	ds_read_b128 v[132:135], v96
	ds_read_b128 v[136:139], v96 offset:1024
	ds_read_b128 v[140:143], v96 offset:2048
	ds_read_b128 v[144:147], v96 offset:3072
	ds_read_b128 v[148:151], v96 offset:4096
	ds_read_b128 v[152:155], v96 offset:5120
	ds_read_b128 v[156:159], v96 offset:6144
	ds_read_b128 v[160:163], v96 offset:7168
	global_load_lds_dwordx4 v[164:165], off
	v_lshl_add_u64 v[164:165], s[30:31], 0, v[80:81]
	s_mov_b32 m0, s52
	s_nop 0
	global_load_lds_dwordx4 v[164:165], off
	s_waitcnt vmcnt(8)
	s_waitcnt lgkmcnt(0)
	s_barrier
	s_setprio 1
	s_waitcnt lgkmcnt(0)
	v_mfma_f32_16x16x32_bf16 v[62:65], v[100:103], v[132:135], 0
	v_mfma_f32_16x16x32_bf16 v[58:61], v[108:111], v[132:135], 0
	v_mfma_f32_16x16x32_bf16 v[50:53], v[100:103], v[140:143], 0
	v_mfma_f32_16x16x32_bf16 v[42:45], v[108:111], v[140:143], 0
	v_mfma_f32_16x16x32_bf16 v[34:37], v[100:103], v[148:151], 0
	v_mfma_f32_16x16x32_bf16 v[26:29], v[108:111], v[148:151], 0
	v_mfma_f32_16x16x32_bf16 v[18:21], v[100:103], v[156:159], 0
	v_mfma_f32_16x16x32_bf16 v[10:13], v[108:111], v[156:159], 0
	v_mfma_f32_16x16x32_bf16 v[62:65], v[104:107], v[136:139], v[62:65]
	v_mfma_f32_16x16x32_bf16 v[58:61], v[112:115], v[136:139], v[58:61]
	v_mfma_f32_16x16x32_bf16 v[50:53], v[104:107], v[144:147], v[50:53]
	v_mfma_f32_16x16x32_bf16 v[42:45], v[112:115], v[144:147], v[42:45]
	v_mfma_f32_16x16x32_bf16 v[34:37], v[104:107], v[152:155], v[34:37]
	v_mfma_f32_16x16x32_bf16 v[26:29], v[112:115], v[152:155], v[26:29]
	v_mfma_f32_16x16x32_bf16 v[18:21], v[104:107], v[160:163], v[18:21]
	v_mfma_f32_16x16x32_bf16 v[10:13], v[112:115], v[160:163], v[10:13]
	v_mfma_f32_16x16x32_bf16 v[54:57], v[116:119], v[132:135], 0
	v_mfma_f32_16x16x32_bf16 v[46:49], v[124:127], v[132:135], 0
	v_mfma_f32_16x16x32_bf16 v[38:41], v[116:119], v[140:143], 0
	v_mfma_f32_16x16x32_bf16 v[30:33], v[124:127], v[140:143], 0
	v_mfma_f32_16x16x32_bf16 v[22:25], v[116:119], v[148:151], 0
	v_mfma_f32_16x16x32_bf16 v[14:17], v[124:127], v[148:151], 0
	v_mfma_f32_16x16x32_bf16 v[6:9], v[116:119], v[156:159], 0
	v_mfma_f32_16x16x32_bf16 v[2:5], v[124:127], v[156:159], 0
	v_mfma_f32_16x16x32_bf16 v[54:57], v[120:123], v[136:139], v[54:57]
	v_mfma_f32_16x16x32_bf16 v[46:49], v[128:131], v[136:139], v[46:49]
	v_mfma_f32_16x16x32_bf16 v[38:41], v[120:123], v[144:147], v[38:41]
	v_mfma_f32_16x16x32_bf16 v[30:33], v[128:131], v[144:147], v[30:33]
	v_mfma_f32_16x16x32_bf16 v[22:25], v[120:123], v[152:155], v[22:25]
	v_mfma_f32_16x16x32_bf16 v[14:17], v[128:131], v[152:155], v[14:17]
	v_mfma_f32_16x16x32_bf16 v[6:9], v[120:123], v[160:163], v[6:9]
	v_mfma_f32_16x16x32_bf16 v[2:5], v[128:131], v[160:163], v[2:5]
	s_setprio 0
	s_barrier
	s_mov_b32 m0, s53
	v_lshl_add_u64 v[164:165], s[28:29], 0, v[70:71]
	global_load_lds_dwordx4 v[164:165], off
	v_lshl_add_u64 v[166:167], s[28:29], 0, v[66:67]
	s_mov_b32 m0, s58
	v_lshl_add_u64 v[100:101], s[28:29], 0, v[72:73]
	global_load_lds_dwordx4 v[166:167], off
	s_mov_b32 m0, s59
	v_lshl_add_u64 v[168:169], s[26:27], 0, v[74:75]
	global_load_lds_dwordx4 v[100:101], off
	v_lshl_add_u64 v[100:101], s[28:29], 0, v[68:69]
	s_mov_b32 m0, s60
	v_lshl_add_u64 v[172:173], s[26:27], 0, v[76:77]
	global_load_lds_dwordx4 v[100:101], off
	s_mov_b32 m0, s42
	s_nop 0
	global_load_lds_dwordx4 v[168:169], off
	s_mov_b32 m0, s43
	s_nop 0
	global_load_lds_dwordx4 v[172:173], off
	s_waitcnt vmcnt(8)
	s_waitcnt lgkmcnt(0)
	s_barrier
	s_setprio 1
	s_setprio 0
	s_barrier
	ds_read_b128 v[100:103], v97
	ds_read_b128 v[104:107], v97 offset:1024
	ds_read_b128 v[108:111], v97 offset:2048
	ds_read_b128 v[112:115], v97 offset:3072
	ds_read_b128 v[116:119], v98
	ds_read_b128 v[120:123], v98 offset:1024
	ds_read_b128 v[124:127], v98 offset:2048
	ds_read_b128 v[128:131], v98 offset:3072
	s_mov_b32 m0, s44
	v_lshl_add_u64 v[174:175], s[26:27], 0, v[78:79]
	ds_read_b128 v[132:135], v96 offset:32768
	ds_read_b128 v[136:139], v96 offset:33792
	ds_read_b128 v[140:143], v96 offset:34816
	ds_read_b128 v[144:147], v96 offset:35840
	ds_read_b128 v[148:151], v96 offset:36864
	ds_read_b128 v[152:155], v96 offset:37888
	ds_read_b128 v[156:159], v96 offset:38912
	ds_read_b128 v[160:163], v96 offset:39936
	global_load_lds_dwordx4 v[174:175], off
	v_lshl_add_u64 v[174:175], s[26:27], 0, v[80:81]
	s_mov_b32 m0, s45
	s_nop 0
	global_load_lds_dwordx4 v[174:175], off
	s_waitcnt vmcnt(8)
	s_waitcnt lgkmcnt(0)
	s_barrier
; #define PG8_STAGE(bufoff, gbase, voff) do { _Pragma("unroll") for (int _i = 0; _i < 2; ++_i) \
;         __builtin_amdgcn_global_load_lds((const unsigned*)((const char*)(gbase) + (voff)[_i]), (PG8_LAS unsigned*)(lds + (bufoff) + ldsw + _i * 8192), 16, 0, 0); } while (0)
; #define PG8_WAIT_V(n) asm volatile("s_waitcnt vmcnt(" #n ")" ::: "memory")
; #define PG8_WAIT_L(n) asm volatile("s_waitcnt lgkmcnt(" #n ")" ::: "memory")
; template <class Epi, class Sched, bool ALIGN_EPI = true, bool F8 = false>
; __device__ __forceinline__ void gemm_phase(PG8_LAS unsigned char* lds, const Sched& S, const Epi& E) {
;     ...
;         for (int t = 0; t < nt; t += 2) {
;             const bool last = (t == nt - 2);
;             if constexpr (Sched::GATHER) { if (last && has_next) S.a_off(nxt, Rs, Cs, voffAn); }
;             const char* a1 = cA + (size_t)(t + 1) * kstep;
;             const char* a2 = last ? nA : cA + (size_t)(t + 2) * kstep; const char* b2 = last ? nB : cB + (size_t)(t + 2) * kstepB;
;             const char* a3 = a2 + kstep; const char* b3 = b2 + kstepB;
;             unsigned vA2[2][2];
; #pragma unroll
;             for (int h = 0; h < 2; ++h)
; #pragma unroll
;                 for (int i = 0; i < 2; ++i) { if constexpr (Sched::GATHER) vA2[h][i] = (last && has_next) ? voffAn[h][i] : voffA[h][i]; else vA2[h][i] = voffA[h][i]; }
;             PG8_LDB(B0, 0, 0); PG8_LDB(B1, 0, 1); PG8_SCHED; PG8_LDA(At, 0, 0); PG8_STAGE(PG8_SA(1, 1), a1, voffA[1]);
;             PG8_WAIT_V(8); PG8_WAIT_L(0); PG8_BAR; PG8_MMA(0, 0, At, B0); PG8_MMA(0, 1, At, B1); PG8_BAR; PG8_SCHED;
;             PG8_LDA(At, 0, 1); PG8_STAGE(PG8_SB(0, 0), b2, voffB[0]); PG8_STAGE(PG8_SB(0, 1), b2, voffB[1]); PG8_STAGE(PG8_SA(0, 0), a2, vA2[0]);
;             PG8_WAIT_V(8); PG8_WAIT_L(0); PG8_BAR; PG8_MMA(1, 0, At, B0); PG8_MMA(1, 1, At, B1); PG8_BAR; PG8_SCHED;
;             PG8_LDB(B0, 1, 0); PG8_LDB(B1, 1, 1); PG8_SCHED; PG8_LDA(At, 1, 0); PG8_STAGE(PG8_SA(0, 1), a2, vA2[1]);
;             PG8_WAIT_V(8); PG8_WAIT_L(0); PG8_BAR; PG8_MMA(0, 0, At, B0); PG8_MMA(0, 1, At, B1); PG8_BAR; PG8_SCHED;
;             PG8_LDA(At, 1, 1); PG8_STAGE(PG8_SB(1, 0), b3, voffB[0]); PG8_STAGE(PG8_SB(1, 1), b3, voffB[1]); PG8_STAGE(PG8_SA(1, 0), a3, vA2[0]);
;             PG8_WAIT_V(8); PG8_WAIT_L(0); PG8_BAR; PG8_MMA(1, 0, At, B0); PG8_MMA(1, 1, At, B1); PG8_BAR; PG8_SCHED;
	s_setprio 1
	s_waitcnt lgkmcnt(0)
	v_mfma_f32_16x16x32_bf16 v[62:65], v[100:103], v[132:135], v[62:65]
	v_mfma_f32_16x16x32_bf16 v[58:61], v[108:111], v[132:135], v[58:61]
	v_mfma_f32_16x16x32_bf16 v[50:53], v[100:103], v[140:143], v[50:53]
	v_mfma_f32_16x16x32_bf16 v[42:45], v[108:111], v[140:143], v[42:45]
	v_mfma_f32_16x16x32_bf16 v[34:37], v[100:103], v[148:151], v[34:37]
	v_mfma_f32_16x16x32_bf16 v[26:29], v[108:111], v[148:151], v[26:29]
	v_mfma_f32_16x16x32_bf16 v[18:21], v[100:103], v[156:159], v[18:21]
	v_mfma_f32_16x16x32_bf16 v[10:13], v[108:111], v[156:159], v[10:13]
	v_mfma_f32_16x16x32_bf16 v[62:65], v[104:107], v[136:139], v[62:65]
	v_mfma_f32_16x16x32_bf16 v[58:61], v[112:115], v[136:139], v[58:61]
	v_mfma_f32_16x16x32_bf16 v[50:53], v[104:107], v[144:147], v[50:53]
	v_mfma_f32_16x16x32_bf16 v[42:45], v[112:115], v[144:147], v[42:45]
	v_mfma_f32_16x16x32_bf16 v[34:37], v[104:107], v[152:155], v[34:37]
	v_mfma_f32_16x16x32_bf16 v[26:29], v[112:115], v[152:155], v[26:29]
	v_mfma_f32_16x16x32_bf16 v[18:21], v[104:107], v[160:163], v[18:21]
	v_mfma_f32_16x16x32_bf16 v[10:13], v[112:115], v[160:163], v[10:13]
	v_mfma_f32_16x16x32_bf16 v[54:57], v[116:119], v[132:135], v[54:57]
	v_mfma_f32_16x16x32_bf16 v[46:49], v[124:127], v[132:135], v[46:49]
	v_mfma_f32_16x16x32_bf16 v[38:41], v[116:119], v[140:143], v[38:41]
	v_mfma_f32_16x16x32_bf16 v[30:33], v[124:127], v[140:143], v[30:33]
	v_mfma_f32_16x16x32_bf16 v[22:25], v[116:119], v[148:151], v[22:25]
	v_mfma_f32_16x16x32_bf16 v[14:17], v[124:127], v[148:151], v[14:17]
	v_mfma_f32_16x16x32_bf16 v[6:9], v[116:119], v[156:159], v[6:9]
	v_mfma_f32_16x16x32_bf16 v[2:5], v[124:127], v[156:159], v[2:5]
	v_mfma_f32_16x16x32_bf16 v[54:57], v[120:123], v[136:139], v[54:57]
	v_mfma_f32_16x16x32_bf16 v[46:49], v[128:131], v[136:139], v[46:49]
	v_mfma_f32_16x16x32_bf16 v[38:41], v[120:123], v[144:147], v[38:41]
	v_mfma_f32_16x16x32_bf16 v[30:33], v[128:131], v[144:147], v[30:33]
	v_mfma_f32_16x16x32_bf16 v[22:25], v[120:123], v[152:155], v[22:25]
	v_mfma_f32_16x16x32_bf16 v[14:17], v[128:131], v[152:155], v[14:17]
	v_mfma_f32_16x16x32_bf16 v[6:9], v[120:123], v[160:163], v[6:9]
	v_mfma_f32_16x16x32_bf16 v[2:5], v[128:131], v[160:163], v[2:5]
	s_setprio 0
	s_barrier
	s_mov_b32 m0, s61
	v_lshl_add_u64 v[100:101], v[164:165], 0, s[10:11]
	global_load_lds_dwordx4 v[100:101], off
	v_lshl_add_u64 v[100:101], v[166:167], 0, s[10:11]
	s_mov_b32 m0, s62
	s_nop 0
	global_load_lds_dwordx4 v[100:101], off
	v_lshl_add_u64 v[100:101], s[24:25], 0, v[72:73]
	s_mov_b32 m0, s63
	s_nop 0
	global_load_lds_dwordx4 v[100:101], off
	v_lshl_add_u64 v[100:101], s[24:25], 0, v[68:69]
	s_mov_b32 m0, s64
	s_nop 0
	global_load_lds_dwordx4 v[100:101], off
	v_lshl_add_u64 v[100:101], v[168:169], 0, s[10:11]
	s_mov_b32 m0, s47
	s_nop 0
	global_load_lds_dwordx4 v[100:101], off
	v_lshl_add_u64 v[100:101], v[172:173], 0, s[10:11]
	s_mov_b32 m0, s48
	s_nop 0
	global_load_lds_dwordx4 v[100:101], off
	s_waitcnt vmcnt(8)
	s_waitcnt lgkmcnt(0)
	s_barrier
	s_setprio 1
	s_setprio 0
	s_barrier
	s_andn2_b64 vcc, exec, s[22:23]
	s_mov_b64 s[24:25], -1
	s_mov_b64 s[22:23], 0
	s_movk_i32 s19, 0x100
	s_cbranch_vccz .LBB0_692
	s_branch .Lpx_19328
.LBB0_692:
	s_add_u32 s30, s4, s19
	s_addc_u32 s31, s5, 0
	s_add_i32 s28, s19, 0x100
	s_and_b64 s[26:27], s[24:25], exec
	s_cselect_b32 s26, 0, s28
	s_cselect_b32 s27, 0, 0
	s_add_u32 s26, s4, s26
	ds_read_b128 v[100:103], v94
	ds_read_b128 v[104:107], v94 offset:1024
	ds_read_b128 v[108:111], v94 offset:2048
	ds_read_b128 v[112:115], v94 offset:3072
	ds_read_b128 v[116:119], v95
	ds_read_b128 v[120:123], v95 offset:1024
	ds_read_b128 v[124:127], v95 offset:2048
	ds_read_b128 v[128:131], v95 offset:3072
	s_addc_u32 s27, s5, s27
	s_add_u32 s19, s20, s19
	s_addc_u32 s28, s21, 0
	s_add_u32 s19, s19, 0x100
	s_addc_u32 s28, s28, 0
	s_and_b64 s[24:25], s[24:25], exec
	s_cselect_b32 s29, s15, s28
	s_cselect_b32 s28, s14, s19
	s_add_u32 s30, s30, 0x80
	s_addc_u32 s31, s31, 0
	s_add_u32 s24, s28, 0x80
	s_addc_u32 s25, s29, 0
	s_mov_b32 m0, s51
	v_lshl_add_u64 v[164:165], s[30:31], 0, v[78:79]
	ds_read_b128 v[132:135], v96
	ds_read_b128 v[136:139], v96 offset:1024
	ds_read_b128 v[140:143], v96 offset:2048
	ds_read_b128 v[144:147], v96 offset:3072
	ds_read_b128 v[148:151], v96 offset:4096
	ds_read_b128 v[152:155], v96 offset:5120
	ds_read_b128 v[156:159], v96 offset:6144
	ds_read_b128 v[160:163], v96 offset:7168
	global_load_lds_dwordx4 v[164:165], off
	v_lshl_add_u64 v[164:165], s[30:31], 0, v[80:81]
	s_mov_b32 m0, s52
	s_nop 0
	global_load_lds_dwordx4 v[164:165], off
	s_waitcnt vmcnt(8)
	s_waitcnt lgkmcnt(0)
	s_barrier
; #define PG8_STAGE(bufoff, gbase, voff) do { _Pragma("unroll") for (int _i = 0; _i < 2; ++_i) \
;         __builtin_amdgcn_global_load_lds((const unsigned*)((const char*)(gbase) + (voff)[_i]), (PG8_LAS unsigned*)(lds + (bufoff) + ldsw + _i * 8192), 16, 0, 0); } while (0)
; #define PG8_WAIT_V(n) asm volatile("s_waitcnt vmcnt(" #n ")" ::: "memory")
; #define PG8_WAIT_L(n) asm volatile("s_waitcnt lgkmcnt(" #n ")" ::: "memory")
; template <class Epi, class Sched, bool ALIGN_EPI = true, bool F8 = false>
; __device__ __forceinline__ void gemm_phase(PG8_LAS unsigned char* lds, const Sched& S, const Epi& E) {
;     ...
;         for (int t = 0; t < nt; t += 2) {
;             const bool last = (t == nt - 2);
;             if constexpr (Sched::GATHER) { if (last && has_next) S.a_off(nxt, Rs, Cs, voffAn); }
;             const char* a1 = cA + (size_t)(t + 1) * kstep;
;             const char* a2 = last ? nA : cA + (size_t)(t + 2) * kstep; const char* b2 = last ? nB : cB + (size_t)(t + 2) * kstepB;
;             const char* a3 = a2 + kstep; const char* b3 = b2 + kstepB;
;             unsigned vA2[2][2];
; #pragma unroll
;             for (int h = 0; h < 2; ++h)
; #pragma unroll
;                 for (int i = 0; i < 2; ++i) { if constexpr (Sched::GATHER) vA2[h][i] = (last && has_next) ? voffAn[h][i] : voffA[h][i]; else vA2[h][i] = voffA[h][i]; }
;             PG8_LDB(B0, 0, 0); PG8_LDB(B1, 0, 1); PG8_SCHED; PG8_LDA(At, 0, 0); PG8_STAGE(PG8_SA(1, 1), a1, voffA[1]);
;             PG8_WAIT_V(8); PG8_WAIT_L(0); PG8_BAR; PG8_MMA(0, 0, At, B0); PG8_MMA(0, 1, At, B1); PG8_BAR; PG8_SCHED;
;             PG8_LDA(At, 0, 1); PG8_STAGE(PG8_SB(0, 0), b2, voffB[0]); PG8_STAGE(PG8_SB(0, 1), b2, voffB[1]); PG8_STAGE(PG8_SA(0, 0), a2, vA2[0]);
;             PG8_WAIT_V(8); PG8_WAIT_L(0); PG8_BAR; PG8_MMA(1, 0, At, B0); PG8_MMA(1, 1, At, B1); PG8_BAR; PG8_SCHED;
;             PG8_LDB(B0, 1, 0); PG8_LDB(B1, 1, 1); PG8_SCHED; PG8_LDA(At, 1, 0); PG8_STAGE(PG8_SA(0, 1), a2, vA2[1]);
;             PG8_WAIT_V(8); PG8_WAIT_L(0); PG8_BAR; PG8_MMA(0, 0, At, B0); PG8_MMA(0, 1, At, B1); PG8_BAR; PG8_SCHED;
;             PG8_LDA(At, 1, 1); PG8_STAGE(PG8_SB(1, 0), b3, voffB[0]); PG8_STAGE(PG8_SB(1, 1), b3, voffB[1]); PG8_STAGE(PG8_SA(1, 0), a3, vA2[0]);
;             PG8_WAIT_V(8); PG8_WAIT_L(0); PG8_BAR; PG8_MMA(1, 0, At, B0); PG8_MMA(1, 1, At, B1); PG8_BAR; PG8_SCHED;
	s_setprio 1
	s_waitcnt lgkmcnt(0)
	v_mfma_f32_16x16x32_bf16 v[62:65], v[100:103], v[132:135], v[62:65]
	v_mfma_f32_16x16x32_bf16 v[58:61], v[108:111], v[132:135], v[58:61]
	v_mfma_f32_16x16x32_bf16 v[50:53], v[100:103], v[140:143], v[50:53]
	v_mfma_f32_16x16x32_bf16 v[42:45], v[108:111], v[140:143], v[42:45]
	v_mfma_f32_16x16x32_bf16 v[34:37], v[100:103], v[148:151], v[34:37]
	v_mfma_f32_16x16x32_bf16 v[26:29], v[108:111], v[148:151], v[26:29]
	v_mfma_f32_16x16x32_bf16 v[18:21], v[100:103], v[156:159], v[18:21]
	v_mfma_f32_16x16x32_bf16 v[10:13], v[108:111], v[156:159], v[10:13]
	v_mfma_f32_16x16x32_bf16 v[62:65], v[104:107], v[136:139], v[62:65]
	v_mfma_f32_16x16x32_bf16 v[58:61], v[112:115], v[136:139], v[58:61]
	v_mfma_f32_16x16x32_bf16 v[50:53], v[104:107], v[144:147], v[50:53]
	v_mfma_f32_16x16x32_bf16 v[42:45], v[112:115], v[144:147], v[42:45]
	v_mfma_f32_16x16x32_bf16 v[34:37], v[104:107], v[152:155], v[34:37]
	v_mfma_f32_16x16x32_bf16 v[26:29], v[112:115], v[152:155], v[26:29]
	v_mfma_f32_16x16x32_bf16 v[18:21], v[104:107], v[160:163], v[18:21]
	v_mfma_f32_16x16x32_bf16 v[10:13], v[112:115], v[160:163], v[10:13]
	v_mfma_f32_16x16x32_bf16 v[54:57], v[116:119], v[132:135], v[54:57]
	v_mfma_f32_16x16x32_bf16 v[46:49], v[124:127], v[132:135], v[46:49]
	v_mfma_f32_16x16x32_bf16 v[38:41], v[116:119], v[140:143], v[38:41]
	v_mfma_f32_16x16x32_bf16 v[30:33], v[124:127], v[140:143], v[30:33]
	v_mfma_f32_16x16x32_bf16 v[22:25], v[116:119], v[148:151], v[22:25]
	v_mfma_f32_16x16x32_bf16 v[14:17], v[124:127], v[148:151], v[14:17]
	v_mfma_f32_16x16x32_bf16 v[6:9], v[116:119], v[156:159], v[6:9]
	v_mfma_f32_16x16x32_bf16 v[2:5], v[124:127], v[156:159], v[2:5]
	v_mfma_f32_16x16x32_bf16 v[54:57], v[120:123], v[136:139], v[54:57]
	v_mfma_f32_16x16x32_bf16 v[46:49], v[128:131], v[136:139], v[46:49]
	v_mfma_f32_16x16x32_bf16 v[38:41], v[120:123], v[144:147], v[38:41]
	v_mfma_f32_16x16x32_bf16 v[30:33], v[128:131], v[144:147], v[30:33]
	v_mfma_f32_16x16x32_bf16 v[22:25], v[120:123], v[152:155], v[22:25]
	v_mfma_f32_16x16x32_bf16 v[14:17], v[128:131], v[152:155], v[14:17]
	v_mfma_f32_16x16x32_bf16 v[6:9], v[120:123], v[160:163], v[6:9]
	v_mfma_f32_16x16x32_bf16 v[2:5], v[128:131], v[160:163], v[2:5]
	s_setprio 0
	s_barrier
	s_mov_b32 m0, s53
	v_lshl_add_u64 v[164:165], s[28:29], 0, v[70:71]
	global_load_lds_dwordx4 v[164:165], off
	v_lshl_add_u64 v[166:167], s[28:29], 0, v[66:67]
	s_mov_b32 m0, s58
	v_lshl_add_u64 v[100:101], s[28:29], 0, v[72:73]
	global_load_lds_dwordx4 v[166:167], off
	s_mov_b32 m0, s59
	v_lshl_add_u64 v[168:169], s[26:27], 0, v[74:75]
	global_load_lds_dwordx4 v[100:101], off
	v_lshl_add_u64 v[100:101], s[28:29], 0, v[68:69]
	s_mov_b32 m0, s60
	v_lshl_add_u64 v[172:173], s[26:27], 0, v[76:77]
	global_load_lds_dwordx4 v[100:101], off
	s_mov_b32 m0, s42
	s_nop 0
	global_load_lds_dwordx4 v[168:169], off
	s_mov_b32 m0, s43
	s_nop 0
	global_load_lds_dwordx4 v[172:173], off
	s_waitcnt vmcnt(8)
	s_waitcnt lgkmcnt(0)
	s_barrier
	s_setprio 1
	s_setprio 0
	s_barrier
	ds_read_b128 v[100:103], v97
	ds_read_b128 v[104:107], v97 offset:1024
	ds_read_b128 v[108:111], v97 offset:2048
	ds_read_b128 v[112:115], v97 offset:3072
	ds_read_b128 v[116:119], v98
	ds_read_b128 v[120:123], v98 offset:1024
	ds_read_b128 v[124:127], v98 offset:2048
	ds_read_b128 v[128:131], v98 offset:3072
	s_mov_b32 m0, s44
	v_lshl_add_u64 v[174:175], s[26:27], 0, v[78:79]
	ds_read_b128 v[132:135], v96 offset:32768
	ds_read_b128 v[136:139], v96 offset:33792
	ds_read_b128 v[140:143], v96 offset:34816
	ds_read_b128 v[144:147], v96 offset:35840
	ds_read_b128 v[148:151], v96 offset:36864
	ds_read_b128 v[152:155], v96 offset:37888
	ds_read_b128 v[156:159], v96 offset:38912
	ds_read_b128 v[160:163], v96 offset:39936
	global_load_lds_dwordx4 v[174:175], off
	v_lshl_add_u64 v[174:175], s[26:27], 0, v[80:81]
	s_mov_b32 m0, s45
	s_nop 0
	global_load_lds_dwordx4 v[174:175], off
	s_waitcnt vmcnt(8)
	s_waitcnt lgkmcnt(0)
	s_barrier
; #define PG8_STAGE(bufoff, gbase, voff) do { _Pragma("unroll") for (int _i = 0; _i < 2; ++_i) \
;         __builtin_amdgcn_global_load_lds((const unsigned*)((const char*)(gbase) + (voff)[_i]), (PG8_LAS unsigned*)(lds + (bufoff) + ldsw + _i * 8192), 16, 0, 0); } while (0)
; #define PG8_WAIT_V(n) asm volatile("s_waitcnt vmcnt(" #n ")" ::: "memory")
; #define PG8_WAIT_L(n) asm volatile("s_waitcnt lgkmcnt(" #n ")" ::: "memory")
; template <class Epi, class Sched, bool ALIGN_EPI = true, bool F8 = false>
; __device__ __forceinline__ void gemm_phase(PG8_LAS unsigned char* lds, const Sched& S, const Epi& E) {
;     ...
;         for (int t = 0; t < nt; t += 2) {
;             const bool last = (t == nt - 2);
;             if constexpr (Sched::GATHER) { if (last && has_next) S.a_off(nxt, Rs, Cs, voffAn); }
;             const char* a1 = cA + (size_t)(t + 1) * kstep;
;             const char* a2 = last ? nA : cA + (size_t)(t + 2) * kstep; const char* b2 = last ? nB : cB + (size_t)(t + 2) * kstepB;
;             const char* a3 = a2 + kstep; const char* b3 = b2 + kstepB;
;             unsigned vA2[2][2];
; #pragma unroll
;             for (int h = 0; h < 2; ++h)
; #pragma unroll
;                 for (int i = 0; i < 2; ++i) { if constexpr (Sched::GATHER) vA2[h][i] = (last && has_next) ? voffAn[h][i] : voffA[h][i]; else vA2[h][i] = voffA[h][i]; }
;             PG8_LDB(B0, 0, 0); PG8_LDB(B1, 0, 1); PG8_SCHED; PG8_LDA(At, 0, 0); PG8_STAGE(PG8_SA(1, 1), a1, voffA[1]);
;             PG8_WAIT_V(8); PG8_WAIT_L(0); PG8_BAR; PG8_MMA(0, 0, At, B0); PG8_MMA(0, 1, At, B1); PG8_BAR; PG8_SCHED;
;             PG8_LDA(At, 0, 1); PG8_STAGE(PG8_SB(0, 0), b2, voffB[0]); PG8_STAGE(PG8_SB(0, 1), b2, voffB[1]); PG8_STAGE(PG8_SA(0, 0), a2, vA2[0]);
;             PG8_WAIT_V(8); PG8_WAIT_L(0); PG8_BAR; PG8_MMA(1, 0, At, B0); PG8_MMA(1, 1, At, B1); PG8_BAR; PG8_SCHED;
;             PG8_LDB(B0, 1, 0); PG8_LDB(B1, 1, 1); PG8_SCHED; PG8_LDA(At, 1, 0); PG8_STAGE(PG8_SA(0, 1), a2, vA2[1]);
;             PG8_WAIT_V(8); PG8_WAIT_L(0); PG8_BAR; PG8_MMA(0, 0, At, B0); PG8_MMA(0, 1, At, B1); PG8_BAR; PG8_SCHED;
;             PG8_LDA(At, 1, 1); PG8_STAGE(PG8_SB(1, 0), b3, voffB[0]); PG8_STAGE(PG8_SB(1, 1), b3, voffB[1]); PG8_STAGE(PG8_SA(1, 0), a3, vA2[0]);
;             PG8_WAIT_V(8); PG8_WAIT_L(0); PG8_BAR; PG8_MMA(1, 0, At, B0); PG8_MMA(1, 1, At, B1); PG8_BAR; PG8_SCHED;
	s_setprio 1
	s_waitcnt lgkmcnt(0)
	v_mfma_f32_16x16x32_bf16 v[62:65], v[100:103], v[132:135], v[62:65]
	v_mfma_f32_16x16x32_bf16 v[58:61], v[108:111], v[132:135], v[58:61]
	v_mfma_f32_16x16x32_bf16 v[50:53], v[100:103], v[140:143], v[50:53]
	v_mfma_f32_16x16x32_bf16 v[42:45], v[108:111], v[140:143], v[42:45]
	v_mfma_f32_16x16x32_bf16 v[34:37], v[100:103], v[148:151], v[34:37]
	v_mfma_f32_16x16x32_bf16 v[26:29], v[108:111], v[148:151], v[26:29]
	v_mfma_f32_16x16x32_bf16 v[18:21], v[100:103], v[156:159], v[18:21]
	v_mfma_f32_16x16x32_bf16 v[10:13], v[108:111], v[156:159], v[10:13]
	v_mfma_f32_16x16x32_bf16 v[62:65], v[104:107], v[136:139], v[62:65]
	v_mfma_f32_16x16x32_bf16 v[58:61], v[112:115], v[136:139], v[58:61]
	v_mfma_f32_16x16x32_bf16 v[50:53], v[104:107], v[144:147], v[50:53]
	v_mfma_f32_16x16x32_bf16 v[42:45], v[112:115], v[144:147], v[42:45]
	v_mfma_f32_16x16x32_bf16 v[34:37], v[104:107], v[152:155], v[34:37]
	v_mfma_f32_16x16x32_bf16 v[26:29], v[112:115], v[152:155], v[26:29]
	v_mfma_f32_16x16x32_bf16 v[18:21], v[104:107], v[160:163], v[18:21]
	v_mfma_f32_16x16x32_bf16 v[10:13], v[112:115], v[160:163], v[10:13]
	v_mfma_f32_16x16x32_bf16 v[54:57], v[116:119], v[132:135], v[54:57]
	v_mfma_f32_16x16x32_bf16 v[46:49], v[124:127], v[132:135], v[46:49]
	v_mfma_f32_16x16x32_bf16 v[38:41], v[116:119], v[140:143], v[38:41]
	v_mfma_f32_16x16x32_bf16 v[30:33], v[124:127], v[140:143], v[30:33]
	v_mfma_f32_16x16x32_bf16 v[22:25], v[116:119], v[148:151], v[22:25]
	v_mfma_f32_16x16x32_bf16 v[14:17], v[124:127], v[148:151], v[14:17]
	v_mfma_f32_16x16x32_bf16 v[6:9], v[116:119], v[156:159], v[6:9]
	v_mfma_f32_16x16x32_bf16 v[2:5], v[124:127], v[156:159], v[2:5]
	v_mfma_f32_16x16x32_bf16 v[54:57], v[120:123], v[136:139], v[54:57]
	v_mfma_f32_16x16x32_bf16 v[46:49], v[128:131], v[136:139], v[46:49]
	v_mfma_f32_16x16x32_bf16 v[38:41], v[120:123], v[144:147], v[38:41]
	v_mfma_f32_16x16x32_bf16 v[30:33], v[128:131], v[144:147], v[30:33]
	v_mfma_f32_16x16x32_bf16 v[22:25], v[120:123], v[152:155], v[22:25]
	v_mfma_f32_16x16x32_bf16 v[14:17], v[128:131], v[152:155], v[14:17]
	v_mfma_f32_16x16x32_bf16 v[6:9], v[120:123], v[160:163], v[6:9]
	v_mfma_f32_16x16x32_bf16 v[2:5], v[128:131], v[160:163], v[2:5]
	s_setprio 0
	s_barrier
	s_mov_b32 m0, s61
	v_lshl_add_u64 v[100:101], v[164:165], 0, s[10:11]
	global_load_lds_dwordx4 v[100:101], off
	v_lshl_add_u64 v[100:101], v[166:167], 0, s[10:11]
	s_mov_b32 m0, s62
	s_nop 0
	global_load_lds_dwordx4 v[100:101], off
	v_lshl_add_u64 v[100:101], s[24:25], 0, v[72:73]
	s_mov_b32 m0, s63
	s_nop 0
	global_load_lds_dwordx4 v[100:101], off
	v_lshl_add_u64 v[100:101], s[24:25], 0, v[68:69]
	s_mov_b32 m0, s64
	s_nop 0
	global_load_lds_dwordx4 v[100:101], off
	v_lshl_add_u64 v[100:101], v[168:169], 0, s[10:11]
	s_mov_b32 m0, s47
	s_nop 0
	global_load_lds_dwordx4 v[100:101], off
	v_lshl_add_u64 v[100:101], v[172:173], 0, s[10:11]
	s_mov_b32 m0, s48
	s_nop 0
	global_load_lds_dwordx4 v[100:101], off
	s_waitcnt vmcnt(8)
	s_waitcnt lgkmcnt(0)
	s_barrier
	s_setprio 1
	s_setprio 0
	s_barrier
	s_andn2_b64 vcc, exec, s[22:23]
	s_mov_b64 s[24:25], -1
	s_mov_b64 s[22:23], 0
	s_movk_i32 s19, 0x100
	s_cbranch_vccz .LBB0_692

; #define PG8_STAGE(bufoff, gbase, voff) do { _Pragma("unroll") for (int _i = 0; _i < 2; ++_i) \
;         __builtin_amdgcn_global_load_lds((const unsigned*)((const char*)(gbase) + (voff)[_i]), (PG8_LAS unsigned*)(lds + (bufoff) + ldsw + _i * 8192), 16, 0, 0); } while (0)
; #define PG8_WAIT_V(n) asm volatile("s_waitcnt vmcnt(" #n ")" ::: "memory")
; #define PG8_WAIT_L(n) asm volatile("s_waitcnt lgkmcnt(" #n ")" ::: "memory")
; template <class Epi, class Sched, bool ALIGN_EPI = true, bool F8 = false>
; __device__ __forceinline__ void gemm_phase(PG8_LAS unsigned char* lds, const Sched& S, const Epi& E) {
;     ...
;         for (int t = 0; t < nt; t += 2) {
;             const bool last = (t == nt - 2);
;             if constexpr (Sched::GATHER) { if (last && has_next) S.a_off(nxt, Rs, Cs, voffAn); }
;             const char* a1 = cA + (size_t)(t + 1) * kstep;
;             const char* a2 = last ? nA : cA + (size_t)(t + 2) * kstep; const char* b2 = last ? nB : cB + (size_t)(t + 2) * kstepB;
;             const char* a3 = a2 + kstep; const char* b3 = b2 + kstepB;
;             unsigned vA2[2][2];
; #pragma unroll
;             for (int h = 0; h < 2; ++h)
; #pragma unroll
;                 for (int i = 0; i < 2; ++i) { if constexpr (Sched::GATHER) vA2[h][i] = (last && has_next) ? voffAn[h][i] : voffA[h][i]; else vA2[h][i] = voffA[h][i]; }
;             PG8_LDB(B0, 0, 0); PG8_LDB(B1, 0, 1); PG8_SCHED; PG8_LDA(At, 0, 0); PG8_STAGE(PG8_SA(1, 1), a1, voffA[1]);
;             PG8_WAIT_V(8); PG8_WAIT_L(0); PG8_BAR; PG8_MMA(0, 0, At, B0); PG8_MMA(0, 1, At, B1); PG8_BAR; PG8_SCHED;
;             PG8_LDA(At, 0, 1); PG8_STAGE(PG8_SB(0, 0), b2, voffB[0]); PG8_STAGE(PG8_SB(0, 1), b2, voffB[1]); PG8_STAGE(PG8_SA(0, 0), a2, vA2[0]);
;             PG8_WAIT_V(8); PG8_WAIT_L(0); PG8_BAR; PG8_MMA(1, 0, At, B0); PG8_MMA(1, 1, At, B1); PG8_BAR; PG8_SCHED;
;             PG8_LDB(B0, 1, 0); PG8_LDB(B1, 1, 1); PG8_SCHED; PG8_LDA(At, 1, 0); PG8_STAGE(PG8_SA(0, 1), a2, vA2[1]);
;             PG8_WAIT_V(8); PG8_WAIT_L(0); PG8_BAR; PG8_MMA(0, 0, At, B0); PG8_MMA(0, 1, At, B1); PG8_BAR; PG8_SCHED;
;             PG8_LDA(At, 1, 1); PG8_STAGE(PG8_SB(1, 0), b3, voffB[0]); PG8_STAGE(PG8_SB(1, 1), b3, voffB[1]); PG8_STAGE(PG8_SA(1, 0), a3, vA2[0]);
;             PG8_WAIT_V(8); PG8_WAIT_L(0); PG8_BAR; PG8_MMA(1, 0, At, B0); PG8_MMA(1, 1, At, B1); PG8_BAR; PG8_SCHED;
.Lpkb_763:
	ds_read_b128 v[62:65], v208
	ds_read_b128 v[70:73], v208 offset:1024
	ds_read_b128 v[74:77], v208 offset:2048
	ds_read_b128 v[78:81], v208 offset:3072
	ds_read_b128 v[138:141], v209
	ds_read_b128 v[150:153], v209 offset:1024
	ds_read_b128 v[154:157], v209 offset:2048
	ds_read_b128 v[158:161], v209 offset:3072
	s_add_u32 s28, s26, 0x80
	s_addc_u32 s29, s27, 0
	s_cmp_eq_u32 s69, 4
	s_cselect_b32 s31, s23, s29
	s_cselect_b32 s30, s22, s28
	s_cselect_b32 s29, s25, s21
	s_cselect_b32 s28, s24, s19
	v_lshl_add_u64 v[236:237], s[26:27], 0, v[196:197]
	s_add_i32 m0, s44, 0xc000
	ds_read_b128 v[162:165], v210
	ds_read_b128 v[166:169], v210 offset:1024
	ds_read_b128 v[202:205], v210 offset:2048
	ds_read_b128 v[216:219], v210 offset:3072
	ds_read_b128 v[220:223], v210 offset:4096
	ds_read_b128 v[224:227], v210 offset:5120
	ds_read_b128 v[228:231], v210 offset:6144
	ds_read_b128 v[232:235], v210 offset:7168
	global_load_lds_dwordx4 v[236:237], off
	v_lshl_add_u64 v[236:237], s[26:27], 0, v[194:195]
	s_add_i32 m0, s44, 0xe000
	s_nop 0
	global_load_lds_dwordx4 v[236:237], off
	s_waitcnt vmcnt(8)
	s_waitcnt lgkmcnt(0)
	s_barrier
	s_setprio 1
	s_waitcnt lgkmcnt(0)
	v_mfma_f32_16x16x32_bf16 v[146:149], v[62:65], v[162:165], 0
	v_mfma_f32_16x16x32_bf16 v[142:145], v[74:77], v[162:165], 0
	v_mfma_f32_16x16x32_bf16 v[126:129], v[62:65], v[202:205], 0
	v_mfma_f32_16x16x32_bf16 v[122:125], v[74:77], v[202:205], 0
	v_mfma_f32_16x16x32_bf16 v[110:113], v[62:65], v[220:223], 0
	v_mfma_f32_16x16x32_bf16 v[106:109], v[74:77], v[220:223], 0
	v_mfma_f32_16x16x32_bf16 v[94:97], v[62:65], v[228:231], 0
	v_mfma_f32_16x16x32_bf16 v[90:93], v[74:77], v[228:231], 0
	v_mfma_f32_16x16x32_bf16 v[146:149], v[70:73], v[166:169], v[146:149]
	v_mfma_f32_16x16x32_bf16 v[142:145], v[78:81], v[166:169], v[142:145]
	v_mfma_f32_16x16x32_bf16 v[126:129], v[70:73], v[216:219], v[126:129]
	v_mfma_f32_16x16x32_bf16 v[122:125], v[78:81], v[216:219], v[122:125]
	v_mfma_f32_16x16x32_bf16 v[110:113], v[70:73], v[224:227], v[110:113]
	v_mfma_f32_16x16x32_bf16 v[106:109], v[78:81], v[224:227], v[106:109]
	v_mfma_f32_16x16x32_bf16 v[94:97], v[70:73], v[232:235], v[94:97]
	v_mfma_f32_16x16x32_bf16 v[90:93], v[78:81], v[232:235], v[90:93]
	v_mfma_f32_16x16x32_bf16 v[134:137], v[138:141], v[162:165], 0
	v_mfma_f32_16x16x32_bf16 v[130:133], v[154:157], v[162:165], 0
	v_mfma_f32_16x16x32_bf16 v[118:121], v[138:141], v[202:205], 0
	v_mfma_f32_16x16x32_bf16 v[114:117], v[154:157], v[202:205], 0
	v_mfma_f32_16x16x32_bf16 v[102:105], v[138:141], v[220:223], 0
	v_mfma_f32_16x16x32_bf16 v[98:101], v[154:157], v[220:223], 0
	v_mfma_f32_16x16x32_bf16 v[86:89], v[138:141], v[228:231], 0
	v_mfma_f32_16x16x32_bf16 v[82:85], v[154:157], v[228:231], 0
	v_mfma_f32_16x16x32_bf16 v[134:137], v[150:153], v[166:169], v[134:137]
	v_mfma_f32_16x16x32_bf16 v[130:133], v[158:161], v[166:169], v[130:133]
	v_mfma_f32_16x16x32_bf16 v[118:121], v[150:153], v[216:219], v[118:121]
	v_mfma_f32_16x16x32_bf16 v[114:117], v[158:161], v[216:219], v[114:117]
	v_mfma_f32_16x16x32_bf16 v[102:105], v[150:153], v[224:227], v[102:105]
	v_mfma_f32_16x16x32_bf16 v[98:101], v[158:161], v[224:227], v[98:101]
	v_mfma_f32_16x16x32_bf16 v[86:89], v[150:153], v[232:235], v[86:89]
	v_mfma_f32_16x16x32_bf16 v[82:85], v[158:161], v[232:235], v[82:85]
	s_setprio 0
	s_barrier
	s_add_i32 s70, s60, s43
	v_lshl_add_u64 v[236:237], s[28:29], 0, v[172:173]
	s_mov_b32 m0, s70
	ds_read_b128 v[162:165], v210 offset:16384
	ds_read_b128 v[166:169], v210 offset:17408
	ds_read_b128 v[202:205], v210 offset:18432
	ds_read_b128 v[216:219], v210 offset:19456
	ds_read_b128 v[220:223], v210 offset:20480
	ds_read_b128 v[224:227], v210 offset:21504
	ds_read_b128 v[228:231], v210 offset:22528
	ds_read_b128 v[232:235], v210 offset:23552
	global_load_lds_dwordx4 v[236:237], off
	v_lshl_add_u64 v[238:239], s[28:29], 0, v[174:175]
	s_add_i32 m0, s70, 0x2000
	s_add_i32 s70, s61, s43
	global_load_lds_dwordx4 v[238:239], off
	v_lshl_add_u64 v[240:241], s[28:29], 0, v[176:177]
	s_mov_b32 m0, s70
	v_lshl_add_u64 v[242:243], s[30:31], 0, v[182:183]
	global_load_lds_dwordx4 v[240:241], off
	v_lshl_add_u64 v[240:241], s[28:29], 0, v[178:179]
	s_add_i32 m0, s70, 0x2000
	s_nop 0
	global_load_lds_dwordx4 v[240:241], off
	v_lshl_add_u64 v[240:241], s[30:31], 0, v[180:181]
	s_mov_b32 m0, s44
	s_nop 0
	global_load_lds_dwordx4 v[240:241], off
	s_mov_b32 m0, s45
	s_nop 0
	global_load_lds_dwordx4 v[242:243], off
	s_waitcnt vmcnt(8)
	s_waitcnt lgkmcnt(0)
	s_barrier
	s_setprio 1
	s_waitcnt lgkmcnt(0)
	v_mfma_f32_16x16x32_bf16 v[66:69], v[62:65], v[162:165], 0
	v_mfma_f32_16x16x32_bf16 v[58:61], v[74:77], v[162:165], 0
	v_mfma_f32_16x16x32_bf16 v[46:49], v[62:65], v[202:205], 0
	v_mfma_f32_16x16x32_bf16 v[42:45], v[74:77], v[202:205], 0
	v_mfma_f32_16x16x32_bf16 v[30:33], v[62:65], v[220:223], 0
	v_mfma_f32_16x16x32_bf16 v[26:29], v[74:77], v[220:223], 0
	v_mfma_f32_16x16x32_bf16 v[14:17], v[62:65], v[228:231], 0
	v_mfma_f32_16x16x32_bf16 v[10:13], v[74:77], v[228:231], 0
	v_mfma_f32_16x16x32_bf16 v[66:69], v[70:73], v[166:169], v[66:69]
	v_mfma_f32_16x16x32_bf16 v[58:61], v[78:81], v[166:169], v[58:61]
	v_mfma_f32_16x16x32_bf16 v[46:49], v[70:73], v[216:219], v[46:49]
	v_mfma_f32_16x16x32_bf16 v[42:45], v[78:81], v[216:219], v[42:45]
	v_mfma_f32_16x16x32_bf16 v[30:33], v[70:73], v[224:227], v[30:33]
	v_mfma_f32_16x16x32_bf16 v[26:29], v[78:81], v[224:227], v[26:29]
	v_mfma_f32_16x16x32_bf16 v[14:17], v[70:73], v[232:235], v[14:17]
	v_mfma_f32_16x16x32_bf16 v[10:13], v[78:81], v[232:235], v[10:13]
	v_mfma_f32_16x16x32_bf16 v[54:57], v[138:141], v[162:165], 0
	v_mfma_f32_16x16x32_bf16 v[50:53], v[154:157], v[162:165], 0
	v_mfma_f32_16x16x32_bf16 v[38:41], v[138:141], v[202:205], 0
	v_mfma_f32_16x16x32_bf16 v[34:37], v[154:157], v[202:205], 0
	v_mfma_f32_16x16x32_bf16 v[22:25], v[138:141], v[220:223], 0
	v_mfma_f32_16x16x32_bf16 v[18:21], v[154:157], v[220:223], 0
	v_mfma_f32_16x16x32_bf16 v[6:9], v[138:141], v[228:231], 0
	v_mfma_f32_16x16x32_bf16 v[2:5], v[154:157], v[228:231], 0
	v_mfma_f32_16x16x32_bf16 v[54:57], v[150:153], v[166:169], v[54:57]
	v_mfma_f32_16x16x32_bf16 v[50:53], v[158:161], v[166:169], v[50:53]
	v_mfma_f32_16x16x32_bf16 v[38:41], v[150:153], v[216:219], v[38:41]
	v_mfma_f32_16x16x32_bf16 v[34:37], v[158:161], v[216:219], v[34:37]
	v_mfma_f32_16x16x32_bf16 v[22:25], v[150:153], v[224:227], v[22:25]
	v_mfma_f32_16x16x32_bf16 v[18:21], v[158:161], v[224:227], v[18:21]
	v_mfma_f32_16x16x32_bf16 v[6:9], v[150:153], v[232:235], v[6:9]
	v_mfma_f32_16x16x32_bf16 v[2:5], v[158:161], v[232:235], v[2:5]
	s_setprio 0
	s_barrier
; #define PG8_STAGE(bufoff, gbase, voff) do { _Pragma("unroll") for (int _i = 0; _i < 2; ++_i) \
;         __builtin_amdgcn_global_load_lds((const unsigned*)((const char*)(gbase) + (voff)[_i]), (PG8_LAS unsigned*)(lds + (bufoff) + ldsw + _i * 8192), 16, 0, 0); } while (0)
; #define PG8_WAIT_V(n) asm volatile("s_waitcnt vmcnt(" #n ")" ::: "memory")
; #define PG8_WAIT_L(n) asm volatile("s_waitcnt lgkmcnt(" #n ")" ::: "memory")
; template <class Epi, class Sched, bool ALIGN_EPI = true, bool F8 = false>
; __device__ __forceinline__ void gemm_phase(PG8_LAS unsigned char* lds, const Sched& S, const Epi& E) {
;     ...
;         for (int t = 0; t < nt; t += 2) {
;             const bool last = (t == nt - 2);
;             if constexpr (Sched::GATHER) { if (last && has_next) S.a_off(nxt, Rs, Cs, voffAn); }
;             const char* a1 = cA + (size_t)(t + 1) * kstep;
;             const char* a2 = last ? nA : cA + (size_t)(t + 2) * kstep; const char* b2 = last ? nB : cB + (size_t)(t + 2) * kstepB;
;             const char* a3 = a2 + kstep; const char* b3 = b2 + kstepB;
;             unsigned vA2[2][2];
; #pragma unroll
;             for (int h = 0; h < 2; ++h)
; #pragma unroll
;                 for (int i = 0; i < 2; ++i) { if constexpr (Sched::GATHER) vA2[h][i] = (last && has_next) ? voffAn[h][i] : voffA[h][i]; else vA2[h][i] = voffA[h][i]; }
;             PG8_LDB(B0, 0, 0); PG8_LDB(B1, 0, 1); PG8_SCHED; PG8_LDA(At, 0, 0); PG8_STAGE(PG8_SA(1, 1), a1, voffA[1]);
;             PG8_WAIT_V(8); PG8_WAIT_L(0); PG8_BAR; PG8_MMA(0, 0, At, B0); PG8_MMA(0, 1, At, B1); PG8_BAR; PG8_SCHED;
;             PG8_LDA(At, 0, 1); PG8_STAGE(PG8_SB(0, 0), b2, voffB[0]); PG8_STAGE(PG8_SB(0, 1), b2, voffB[1]); PG8_STAGE(PG8_SA(0, 0), a2, vA2[0]);
;             PG8_WAIT_V(8); PG8_WAIT_L(0); PG8_BAR; PG8_MMA(1, 0, At, B0); PG8_MMA(1, 1, At, B1); PG8_BAR; PG8_SCHED;
;             PG8_LDB(B0, 1, 0); PG8_LDB(B1, 1, 1); PG8_SCHED; PG8_LDA(At, 1, 0); PG8_STAGE(PG8_SA(0, 1), a2, vA2[1]);
;             PG8_WAIT_V(8); PG8_WAIT_L(0); PG8_BAR; PG8_MMA(0, 0, At, B0); PG8_MMA(0, 1, At, B1); PG8_BAR; PG8_SCHED;
;             PG8_LDA(At, 1, 1); PG8_STAGE(PG8_SB(1, 0), b3, voffB[0]); PG8_STAGE(PG8_SB(1, 1), b3, voffB[1]); PG8_STAGE(PG8_SA(1, 0), a3, vA2[0]);
;             PG8_WAIT_V(8); PG8_WAIT_L(0); PG8_BAR; PG8_MMA(1, 0, At, B0); PG8_MMA(1, 1, At, B1); PG8_BAR; PG8_SCHED;
	s_add_i32 s70, 0, 0x18000
	s_add_i32 s71, 0, 0x1c000
	v_add_u32_e32 v78, s70, v207
	v_add_u32_e32 v158, s71, v207
	ds_read_b128 v[62:65], v78
	ds_read_b128 v[70:73], v78 offset:1024
	ds_read_b128 v[74:77], v78 offset:2048
	ds_read_b128 v[78:81], v78 offset:3072
	ds_read_b128 v[138:141], v158
	ds_read_b128 v[150:153], v158 offset:1024
	ds_read_b128 v[154:157], v158 offset:2048
	ds_read_b128 v[158:161], v158 offset:3072
	s_mov_b32 m0, s46
	v_lshl_add_u64 v[244:245], s[30:31], 0, v[184:185]
	ds_read_b128 v[162:165], v210 offset:32768
	ds_read_b128 v[166:169], v210 offset:33792
	ds_read_b128 v[202:205], v210 offset:34816
	ds_read_b128 v[216:219], v210 offset:35840
	ds_read_b128 v[220:223], v210 offset:36864
	ds_read_b128 v[224:227], v210 offset:37888
	ds_read_b128 v[228:231], v210 offset:38912
	ds_read_b128 v[232:235], v210 offset:39936
	global_load_lds_dwordx4 v[244:245], off
	v_lshl_add_u64 v[244:245], s[30:31], 0, v[186:187]
	s_mov_b32 m0, s47
	s_nop 0
	global_load_lds_dwordx4 v[244:245], off
	s_waitcnt vmcnt(8)
	s_waitcnt lgkmcnt(0)
	s_barrier
	s_setprio 1
	s_waitcnt lgkmcnt(0)
	v_mfma_f32_16x16x32_bf16 v[146:149], v[62:65], v[162:165], v[146:149]
	v_mfma_f32_16x16x32_bf16 v[142:145], v[74:77], v[162:165], v[142:145]
	v_mfma_f32_16x16x32_bf16 v[126:129], v[62:65], v[202:205], v[126:129]
	v_mfma_f32_16x16x32_bf16 v[122:125], v[74:77], v[202:205], v[122:125]
	v_mfma_f32_16x16x32_bf16 v[110:113], v[62:65], v[220:223], v[110:113]
	v_mfma_f32_16x16x32_bf16 v[106:109], v[74:77], v[220:223], v[106:109]
	v_mfma_f32_16x16x32_bf16 v[94:97], v[62:65], v[228:231], v[94:97]
	v_mfma_f32_16x16x32_bf16 v[90:93], v[74:77], v[228:231], v[90:93]
	v_mfma_f32_16x16x32_bf16 v[146:149], v[70:73], v[166:169], v[146:149]
	v_mfma_f32_16x16x32_bf16 v[142:145], v[78:81], v[166:169], v[142:145]
	v_mfma_f32_16x16x32_bf16 v[126:129], v[70:73], v[216:219], v[126:129]
	v_mfma_f32_16x16x32_bf16 v[122:125], v[78:81], v[216:219], v[122:125]
	v_mfma_f32_16x16x32_bf16 v[110:113], v[70:73], v[224:227], v[110:113]
	v_mfma_f32_16x16x32_bf16 v[106:109], v[78:81], v[224:227], v[106:109]
	v_mfma_f32_16x16x32_bf16 v[94:97], v[70:73], v[232:235], v[94:97]
	v_mfma_f32_16x16x32_bf16 v[90:93], v[78:81], v[232:235], v[90:93]
	v_mfma_f32_16x16x32_bf16 v[134:137], v[138:141], v[162:165], v[134:137]
	v_mfma_f32_16x16x32_bf16 v[130:133], v[154:157], v[162:165], v[130:133]
	v_mfma_f32_16x16x32_bf16 v[118:121], v[138:141], v[202:205], v[118:121]
	v_mfma_f32_16x16x32_bf16 v[114:117], v[154:157], v[202:205], v[114:117]
	v_mfma_f32_16x16x32_bf16 v[102:105], v[138:141], v[220:223], v[102:105]
	v_mfma_f32_16x16x32_bf16 v[98:101], v[154:157], v[220:223], v[98:101]
	v_mfma_f32_16x16x32_bf16 v[86:89], v[138:141], v[228:231], v[86:89]
	v_mfma_f32_16x16x32_bf16 v[82:85], v[154:157], v[228:231], v[82:85]
	v_mfma_f32_16x16x32_bf16 v[134:137], v[150:153], v[166:169], v[134:137]
	v_mfma_f32_16x16x32_bf16 v[130:133], v[158:161], v[166:169], v[130:133]
	v_mfma_f32_16x16x32_bf16 v[118:121], v[150:153], v[216:219], v[118:121]
	v_mfma_f32_16x16x32_bf16 v[114:117], v[158:161], v[216:219], v[114:117]
	v_mfma_f32_16x16x32_bf16 v[102:105], v[150:153], v[224:227], v[102:105]
	v_mfma_f32_16x16x32_bf16 v[98:101], v[158:161], v[224:227], v[98:101]
	v_mfma_f32_16x16x32_bf16 v[86:89], v[150:153], v[232:235], v[86:89]
	v_mfma_f32_16x16x32_bf16 v[82:85], v[158:161], v[232:235], v[82:85]
	s_setprio 0
	s_barrier
	s_add_u32 s28, s28, 0x80
	s_addc_u32 s29, s29, 0
	s_add_i32 s30, s70, s43
	v_lshl_add_u64 v[236:237], v[236:237], 0, s[14:15]
	s_mov_b32 m0, s30
	ds_read_b128 v[162:165], v210 offset:49152
	ds_read_b128 v[166:169], v210 offset:50176
	ds_read_b128 v[202:205], v210 offset:51200
	ds_read_b128 v[216:219], v210 offset:52224
	ds_read_b128 v[220:223], v210 offset:53248
	ds_read_b128 v[224:227], v210 offset:54272
	ds_read_b128 v[228:231], v210 offset:55296
	ds_read_b128 v[232:235], v210 offset:56320
	global_load_lds_dwordx4 v[236:237], off
	v_lshl_add_u64 v[236:237], v[238:239], 0, s[14:15]
	s_add_i32 m0, s30, 0x2000
	s_add_i32 s30, s71, s43
	global_load_lds_dwordx4 v[236:237], off
	v_lshl_add_u64 v[236:237], s[28:29], 0, v[176:177]
	s_mov_b32 m0, s30
	s_nop 0
	global_load_lds_dwordx4 v[236:237], off
	v_lshl_add_u64 v[236:237], s[28:29], 0, v[178:179]
	s_add_i32 m0, s30, 0x2000
	s_nop 0
	global_load_lds_dwordx4 v[236:237], off
	v_lshl_add_u64 v[236:237], v[240:241], 0, s[14:15]
	s_mov_b32 m0, s50
	s_nop 0
	global_load_lds_dwordx4 v[236:237], off
	v_lshl_add_u64 v[236:237], v[242:243], 0, s[14:15]
	s_mov_b32 m0, s51
	s_nop 0
	global_load_lds_dwordx4 v[236:237], off
	s_waitcnt vmcnt(8)
	s_waitcnt lgkmcnt(0)
	s_barrier
	s_setprio 1
	s_waitcnt lgkmcnt(0)
	v_mfma_f32_16x16x32_bf16 v[66:69], v[62:65], v[162:165], v[66:69]
	v_mfma_f32_16x16x32_bf16 v[58:61], v[74:77], v[162:165], v[58:61]
	v_mfma_f32_16x16x32_bf16 v[46:49], v[62:65], v[202:205], v[46:49]
	v_mfma_f32_16x16x32_bf16 v[42:45], v[74:77], v[202:205], v[42:45]
	v_mfma_f32_16x16x32_bf16 v[30:33], v[62:65], v[220:223], v[30:33]
	v_mfma_f32_16x16x32_bf16 v[26:29], v[74:77], v[220:223], v[26:29]
	v_mfma_f32_16x16x32_bf16 v[14:17], v[62:65], v[228:231], v[14:17]
	v_mfma_f32_16x16x32_bf16 v[10:13], v[74:77], v[228:231], v[10:13]
	v_mfma_f32_16x16x32_bf16 v[66:69], v[70:73], v[166:169], v[66:69]
	v_mfma_f32_16x16x32_bf16 v[58:61], v[78:81], v[166:169], v[58:61]
	v_mfma_f32_16x16x32_bf16 v[46:49], v[70:73], v[216:219], v[46:49]
	v_mfma_f32_16x16x32_bf16 v[42:45], v[78:81], v[216:219], v[42:45]
	v_mfma_f32_16x16x32_bf16 v[30:33], v[70:73], v[224:227], v[30:33]
	v_mfma_f32_16x16x32_bf16 v[26:29], v[78:81], v[224:227], v[26:29]
	v_mfma_f32_16x16x32_bf16 v[14:17], v[70:73], v[232:235], v[14:17]
	v_mfma_f32_16x16x32_bf16 v[10:13], v[78:81], v[232:235], v[10:13]
	v_mfma_f32_16x16x32_bf16 v[54:57], v[138:141], v[162:165], v[54:57]
	v_mfma_f32_16x16x32_bf16 v[50:53], v[154:157], v[162:165], v[50:53]
	v_mfma_f32_16x16x32_bf16 v[38:41], v[138:141], v[202:205], v[38:41]
	v_mfma_f32_16x16x32_bf16 v[34:37], v[154:157], v[202:205], v[34:37]
	v_mfma_f32_16x16x32_bf16 v[22:25], v[138:141], v[220:223], v[22:25]
	v_mfma_f32_16x16x32_bf16 v[18:21], v[154:157], v[220:223], v[18:21]
	v_mfma_f32_16x16x32_bf16 v[6:9], v[138:141], v[228:231], v[6:9]
	v_mfma_f32_16x16x32_bf16 v[2:5], v[154:157], v[228:231], v[2:5]
	v_mfma_f32_16x16x32_bf16 v[54:57], v[150:153], v[166:169], v[54:57]
	v_mfma_f32_16x16x32_bf16 v[50:53], v[158:161], v[166:169], v[50:53]
	v_mfma_f32_16x16x32_bf16 v[38:41], v[150:153], v[216:219], v[38:41]
	v_mfma_f32_16x16x32_bf16 v[34:37], v[158:161], v[216:219], v[34:37]
	v_mfma_f32_16x16x32_bf16 v[22:25], v[150:153], v[224:227], v[22:25]
	v_mfma_f32_16x16x32_bf16 v[18:21], v[158:161], v[224:227], v[18:21]
	v_mfma_f32_16x16x32_bf16 v[6:9], v[150:153], v[232:235], v[6:9]
	v_mfma_f32_16x16x32_bf16 v[2:5], v[158:161], v[232:235], v[2:5]
	s_setprio 0
	s_barrier
	s_add_i32 s69, s69, 2
	s_add_u32 s19, s19, 0x100
	s_addc_u32 s21, s21, 0
	s_add_u32 s26, s26, 0x100
	s_addc_u32 s27, s27, 0
	s_cmp_gt_u32 s69, 5
	s_cbranch_scc0 .LBB0_763
	s_branch .Lpx_20766
; #define PG8_STAGE(bufoff, gbase, voff) do { _Pragma("unroll") for (int _i = 0; _i < 2; ++_i) \
;         __builtin_amdgcn_global_load_lds((const unsigned*)((const char*)(gbase) + (voff)[_i]), (PG8_LAS unsigned*)(lds + (bufoff) + ldsw + _i * 8192), 16, 0, 0); } while (0)
; #define PG8_WAIT_V(n) asm volatile("s_waitcnt vmcnt(" #n ")" ::: "memory")
; #define PG8_WAIT_L(n) asm volatile("s_waitcnt lgkmcnt(" #n ")" ::: "memory")
; template <class Epi, class Sched, bool ALIGN_EPI = true, bool F8 = false>
; __device__ __forceinline__ void gemm_phase(PG8_LAS unsigned char* lds, const Sched& S, const Epi& E) {
;     ...
;         for (int t = 0; t < nt; t += 2) {
;             const bool last = (t == nt - 2);
;             if constexpr (Sched::GATHER) { if (last && has_next) S.a_off(nxt, Rs, Cs, voffAn); }
;             const char* a1 = cA + (size_t)(t + 1) * kstep;
;             const char* a2 = last ? nA : cA + (size_t)(t + 2) * kstep; const char* b2 = last ? nB : cB + (size_t)(t + 2) * kstepB;
;             const char* a3 = a2 + kstep; const char* b3 = b2 + kstepB;
;             unsigned vA2[2][2];
; #pragma unroll
;             for (int h = 0; h < 2; ++h)
; #pragma unroll
;                 for (int i = 0; i < 2; ++i) { if constexpr (Sched::GATHER) vA2[h][i] = (last && has_next) ? voffAn[h][i] : voffA[h][i]; else vA2[h][i] = voffA[h][i]; }
;             PG8_LDB(B0, 0, 0); PG8_LDB(B1, 0, 1); PG8_SCHED; PG8_LDA(At, 0, 0); PG8_STAGE(PG8_SA(1, 1), a1, voffA[1]);
;             PG8_WAIT_V(8); PG8_WAIT_L(0); PG8_BAR; PG8_MMA(0, 0, At, B0); PG8_MMA(0, 1, At, B1); PG8_BAR; PG8_SCHED;
;             PG8_LDA(At, 0, 1); PG8_STAGE(PG8_SB(0, 0), b2, voffB[0]); PG8_STAGE(PG8_SB(0, 1), b2, voffB[1]); PG8_STAGE(PG8_SA(0, 0), a2, vA2[0]);
;             PG8_WAIT_V(8); PG8_WAIT_L(0); PG8_BAR; PG8_MMA(1, 0, At, B0); PG8_MMA(1, 1, At, B1); PG8_BAR; PG8_SCHED;
;             PG8_LDB(B0, 1, 0); PG8_LDB(B1, 1, 1); PG8_SCHED; PG8_LDA(At, 1, 0); PG8_STAGE(PG8_SA(0, 1), a2, vA2[1]);
;             PG8_WAIT_V(8); PG8_WAIT_L(0); PG8_BAR; PG8_MMA(0, 0, At, B0); PG8_MMA(0, 1, At, B1); PG8_BAR; PG8_SCHED;
;             PG8_LDA(At, 1, 1); PG8_STAGE(PG8_SB(1, 0), b3, voffB[0]); PG8_STAGE(PG8_SB(1, 1), b3, voffB[1]); PG8_STAGE(PG8_SA(1, 0), a3, vA2[0]);
;             PG8_WAIT_V(8); PG8_WAIT_L(0); PG8_BAR; PG8_MMA(1, 0, At, B0); PG8_MMA(1, 1, At, B1); PG8_BAR; PG8_SCHED;
.LBB0_763:
	ds_read_b128 v[62:65], v208
	ds_read_b128 v[70:73], v208 offset:1024
	ds_read_b128 v[74:77], v208 offset:2048
	ds_read_b128 v[78:81], v208 offset:3072
	ds_read_b128 v[138:141], v209
	ds_read_b128 v[150:153], v209 offset:1024
	ds_read_b128 v[154:157], v209 offset:2048
	ds_read_b128 v[158:161], v209 offset:3072
	s_add_u32 s28, s26, 0x80
	s_addc_u32 s29, s27, 0
	s_cmp_eq_u32 s69, 4
	s_cselect_b32 s31, s23, s29
	s_cselect_b32 s30, s22, s28
	s_cselect_b32 s29, s25, s21
	s_cselect_b32 s28, s24, s19
	v_lshl_add_u64 v[236:237], s[26:27], 0, v[196:197]
	s_add_i32 m0, s44, 0xc000
	ds_read_b128 v[162:165], v210
	ds_read_b128 v[166:169], v210 offset:1024
	ds_read_b128 v[202:205], v210 offset:2048
	ds_read_b128 v[216:219], v210 offset:3072
	ds_read_b128 v[220:223], v210 offset:4096
	ds_read_b128 v[224:227], v210 offset:5120
	ds_read_b128 v[228:231], v210 offset:6144
	ds_read_b128 v[232:235], v210 offset:7168
	global_load_lds_dwordx4 v[236:237], off
	v_lshl_add_u64 v[236:237], s[26:27], 0, v[194:195]
	s_add_i32 m0, s44, 0xe000
	s_nop 0
	global_load_lds_dwordx4 v[236:237], off
	s_waitcnt vmcnt(8)
	s_waitcnt lgkmcnt(0)
	s_barrier
	s_setprio 1
	s_waitcnt lgkmcnt(0)
	v_mfma_f32_16x16x32_bf16 v[146:149], v[62:65], v[162:165], v[146:149]
	v_mfma_f32_16x16x32_bf16 v[142:145], v[74:77], v[162:165], v[142:145]
	v_mfma_f32_16x16x32_bf16 v[126:129], v[62:65], v[202:205], v[126:129]
	v_mfma_f32_16x16x32_bf16 v[122:125], v[74:77], v[202:205], v[122:125]
	v_mfma_f32_16x16x32_bf16 v[110:113], v[62:65], v[220:223], v[110:113]
	v_mfma_f32_16x16x32_bf16 v[106:109], v[74:77], v[220:223], v[106:109]
	v_mfma_f32_16x16x32_bf16 v[94:97], v[62:65], v[228:231], v[94:97]
	v_mfma_f32_16x16x32_bf16 v[90:93], v[74:77], v[228:231], v[90:93]
	v_mfma_f32_16x16x32_bf16 v[146:149], v[70:73], v[166:169], v[146:149]
	v_mfma_f32_16x16x32_bf16 v[142:145], v[78:81], v[166:169], v[142:145]
	v_mfma_f32_16x16x32_bf16 v[126:129], v[70:73], v[216:219], v[126:129]
	v_mfma_f32_16x16x32_bf16 v[122:125], v[78:81], v[216:219], v[122:125]
	v_mfma_f32_16x16x32_bf16 v[110:113], v[70:73], v[224:227], v[110:113]
	v_mfma_f32_16x16x32_bf16 v[106:109], v[78:81], v[224:227], v[106:109]
	v_mfma_f32_16x16x32_bf16 v[94:97], v[70:73], v[232:235], v[94:97]
	v_mfma_f32_16x16x32_bf16 v[90:93], v[78:81], v[232:235], v[90:93]
	v_mfma_f32_16x16x32_bf16 v[134:137], v[138:141], v[162:165], v[134:137]
	v_mfma_f32_16x16x32_bf16 v[130:133], v[154:157], v[162:165], v[130:133]
	v_mfma_f32_16x16x32_bf16 v[118:121], v[138:141], v[202:205], v[118:121]
	v_mfma_f32_16x16x32_bf16 v[114:117], v[154:157], v[202:205], v[114:117]
	v_mfma_f32_16x16x32_bf16 v[102:105], v[138:141], v[220:223], v[102:105]
	v_mfma_f32_16x16x32_bf16 v[98:101], v[154:157], v[220:223], v[98:101]
	v_mfma_f32_16x16x32_bf16 v[86:89], v[138:141], v[228:231], v[86:89]
	v_mfma_f32_16x16x32_bf16 v[82:85], v[154:157], v[228:231], v[82:85]
	v_mfma_f32_16x16x32_bf16 v[134:137], v[150:153], v[166:169], v[134:137]
	v_mfma_f32_16x16x32_bf16 v[130:133], v[158:161], v[166:169], v[130:133]
	v_mfma_f32_16x16x32_bf16 v[118:121], v[150:153], v[216:219], v[118:121]
	v_mfma_f32_16x16x32_bf16 v[114:117], v[158:161], v[216:219], v[114:117]
	v_mfma_f32_16x16x32_bf16 v[102:105], v[150:153], v[224:227], v[102:105]
	v_mfma_f32_16x16x32_bf16 v[98:101], v[158:161], v[224:227], v[98:101]
	v_mfma_f32_16x16x32_bf16 v[86:89], v[150:153], v[232:235], v[86:89]
	v_mfma_f32_16x16x32_bf16 v[82:85], v[158:161], v[232:235], v[82:85]
	s_setprio 0
	s_barrier
	s_add_i32 s70, s60, s43
	v_lshl_add_u64 v[236:237], s[28:29], 0, v[172:173]
	s_mov_b32 m0, s70
	ds_read_b128 v[162:165], v210 offset:16384
	ds_read_b128 v[166:169], v210 offset:17408
	ds_read_b128 v[202:205], v210 offset:18432
	ds_read_b128 v[216:219], v210 offset:19456
	ds_read_b128 v[220:223], v210 offset:20480
	ds_read_b128 v[224:227], v210 offset:21504
	ds_read_b128 v[228:231], v210 offset:22528
	ds_read_b128 v[232:235], v210 offset:23552
	global_load_lds_dwordx4 v[236:237], off
	v_lshl_add_u64 v[238:239], s[28:29], 0, v[174:175]
	s_add_i32 m0, s70, 0x2000
	s_add_i32 s70, s61, s43
	global_load_lds_dwordx4 v[238:239], off
	v_lshl_add_u64 v[240:241], s[28:29], 0, v[176:177]
	s_mov_b32 m0, s70
	v_lshl_add_u64 v[242:243], s[30:31], 0, v[182:183]
	global_load_lds_dwordx4 v[240:241], off
	v_lshl_add_u64 v[240:241], s[28:29], 0, v[178:179]
	s_add_i32 m0, s70, 0x2000
	s_nop 0
	global_load_lds_dwordx4 v[240:241], off
	v_lshl_add_u64 v[240:241], s[30:31], 0, v[180:181]
	s_mov_b32 m0, s44
	s_nop 0
	global_load_lds_dwordx4 v[240:241], off
	s_mov_b32 m0, s45
	s_nop 0
	global_load_lds_dwordx4 v[242:243], off
	s_waitcnt vmcnt(8)
	s_waitcnt lgkmcnt(0)
	s_barrier
; #define PG8_STAGE(bufoff, gbase, voff) do { _Pragma("unroll") for (int _i = 0; _i < 2; ++_i) \
;         __builtin_amdgcn_global_load_lds((const unsigned*)((const char*)(gbase) + (voff)[_i]), (PG8_LAS unsigned*)(lds + (bufoff) + ldsw + _i * 8192), 16, 0, 0); } while (0)
; #define PG8_WAIT_V(n) asm volatile("s_waitcnt vmcnt(" #n ")" ::: "memory")
; #define PG8_WAIT_L(n) asm volatile("s_waitcnt lgkmcnt(" #n ")" ::: "memory")
; template <class Epi, class Sched, bool ALIGN_EPI = true, bool F8 = false>
; __device__ __forceinline__ void gemm_phase(PG8_LAS unsigned char* lds, const Sched& S, const Epi& E) {
;     ...
;         for (int t = 0; t < nt; t += 2) {
;             const bool last = (t == nt - 2);
;             if constexpr (Sched::GATHER) { if (last && has_next) S.a_off(nxt, Rs, Cs, voffAn); }
;             const char* a1 = cA + (size_t)(t + 1) * kstep;
;             const char* a2 = last ? nA : cA + (size_t)(t + 2) * kstep; const char* b2 = last ? nB : cB + (size_t)(t + 2) * kstepB;
;             const char* a3 = a2 + kstep; const char* b3 = b2 + kstepB;
;             unsigned vA2[2][2];
; #pragma unroll
;             for (int h = 0; h < 2; ++h)
; #pragma unroll
;                 for (int i = 0; i < 2; ++i) { if constexpr (Sched::GATHER) vA2[h][i] = (last && has_next) ? voffAn[h][i] : voffA[h][i]; else vA2[h][i] = voffA[h][i]; }
;             PG8_LDB(B0, 0, 0); PG8_LDB(B1, 0, 1); PG8_SCHED; PG8_LDA(At, 0, 0); PG8_STAGE(PG8_SA(1, 1), a1, voffA[1]);
;             PG8_WAIT_V(8); PG8_WAIT_L(0); PG8_BAR; PG8_MMA(0, 0, At, B0); PG8_MMA(0, 1, At, B1); PG8_BAR; PG8_SCHED;
;             PG8_LDA(At, 0, 1); PG8_STAGE(PG8_SB(0, 0), b2, voffB[0]); PG8_STAGE(PG8_SB(0, 1), b2, voffB[1]); PG8_STAGE(PG8_SA(0, 0), a2, vA2[0]);
;             PG8_WAIT_V(8); PG8_WAIT_L(0); PG8_BAR; PG8_MMA(1, 0, At, B0); PG8_MMA(1, 1, At, B1); PG8_BAR; PG8_SCHED;
;             PG8_LDB(B0, 1, 0); PG8_LDB(B1, 1, 1); PG8_SCHED; PG8_LDA(At, 1, 0); PG8_STAGE(PG8_SA(0, 1), a2, vA2[1]);
;             PG8_WAIT_V(8); PG8_WAIT_L(0); PG8_BAR; PG8_MMA(0, 0, At, B0); PG8_MMA(0, 1, At, B1); PG8_BAR; PG8_SCHED;
;             PG8_LDA(At, 1, 1); PG8_STAGE(PG8_SB(1, 0), b3, voffB[0]); PG8_STAGE(PG8_SB(1, 1), b3, voffB[1]); PG8_STAGE(PG8_SA(1, 0), a3, vA2[0]);
;             PG8_WAIT_V(8); PG8_WAIT_L(0); PG8_BAR; PG8_MMA(1, 0, At, B0); PG8_MMA(1, 1, At, B1); PG8_BAR; PG8_SCHED;
	s_setprio 1
	s_waitcnt lgkmcnt(0)
	v_mfma_f32_16x16x32_bf16 v[66:69], v[62:65], v[162:165], v[66:69]
	v_mfma_f32_16x16x32_bf16 v[58:61], v[74:77], v[162:165], v[58:61]
	v_mfma_f32_16x16x32_bf16 v[46:49], v[62:65], v[202:205], v[46:49]
	v_mfma_f32_16x16x32_bf16 v[42:45], v[74:77], v[202:205], v[42:45]
	v_mfma_f32_16x16x32_bf16 v[30:33], v[62:65], v[220:223], v[30:33]
	v_mfma_f32_16x16x32_bf16 v[26:29], v[74:77], v[220:223], v[26:29]
	v_mfma_f32_16x16x32_bf16 v[14:17], v[62:65], v[228:231], v[14:17]
	v_mfma_f32_16x16x32_bf16 v[10:13], v[74:77], v[228:231], v[10:13]
	v_mfma_f32_16x16x32_bf16 v[66:69], v[70:73], v[166:169], v[66:69]
	v_mfma_f32_16x16x32_bf16 v[58:61], v[78:81], v[166:169], v[58:61]
	v_mfma_f32_16x16x32_bf16 v[46:49], v[70:73], v[216:219], v[46:49]
	v_mfma_f32_16x16x32_bf16 v[42:45], v[78:81], v[216:219], v[42:45]
	v_mfma_f32_16x16x32_bf16 v[30:33], v[70:73], v[224:227], v[30:33]
	v_mfma_f32_16x16x32_bf16 v[26:29], v[78:81], v[224:227], v[26:29]
	v_mfma_f32_16x16x32_bf16 v[14:17], v[70:73], v[232:235], v[14:17]
	v_mfma_f32_16x16x32_bf16 v[10:13], v[78:81], v[232:235], v[10:13]
	v_mfma_f32_16x16x32_bf16 v[54:57], v[138:141], v[162:165], v[54:57]
	v_mfma_f32_16x16x32_bf16 v[50:53], v[154:157], v[162:165], v[50:53]
	v_mfma_f32_16x16x32_bf16 v[38:41], v[138:141], v[202:205], v[38:41]
	v_mfma_f32_16x16x32_bf16 v[34:37], v[154:157], v[202:205], v[34:37]
	v_mfma_f32_16x16x32_bf16 v[22:25], v[138:141], v[220:223], v[22:25]
	v_mfma_f32_16x16x32_bf16 v[18:21], v[154:157], v[220:223], v[18:21]
	v_mfma_f32_16x16x32_bf16 v[6:9], v[138:141], v[228:231], v[6:9]
	v_mfma_f32_16x16x32_bf16 v[2:5], v[154:157], v[228:231], v[2:5]
	v_mfma_f32_16x16x32_bf16 v[54:57], v[150:153], v[166:169], v[54:57]
	v_mfma_f32_16x16x32_bf16 v[50:53], v[158:161], v[166:169], v[50:53]
	v_mfma_f32_16x16x32_bf16 v[38:41], v[150:153], v[216:219], v[38:41]
	v_mfma_f32_16x16x32_bf16 v[34:37], v[158:161], v[216:219], v[34:37]
	v_mfma_f32_16x16x32_bf16 v[22:25], v[150:153], v[224:227], v[22:25]
	v_mfma_f32_16x16x32_bf16 v[18:21], v[158:161], v[224:227], v[18:21]
	v_mfma_f32_16x16x32_bf16 v[6:9], v[150:153], v[232:235], v[6:9]
	v_mfma_f32_16x16x32_bf16 v[2:5], v[158:161], v[232:235], v[2:5]
	s_setprio 0
	s_barrier
	s_add_i32 s70, 0, 0x18000
	s_add_i32 s71, 0, 0x1c000
	v_add_u32_e32 v78, s70, v207
	v_add_u32_e32 v158, s71, v207
	ds_read_b128 v[62:65], v78
	ds_read_b128 v[70:73], v78 offset:1024
	ds_read_b128 v[74:77], v78 offset:2048
	ds_read_b128 v[78:81], v78 offset:3072
	ds_read_b128 v[138:141], v158
	ds_read_b128 v[150:153], v158 offset:1024
	ds_read_b128 v[154:157], v158 offset:2048
	ds_read_b128 v[158:161], v158 offset:3072
	s_mov_b32 m0, s46
	v_lshl_add_u64 v[244:245], s[30:31], 0, v[184:185]
	ds_read_b128 v[162:165], v210 offset:32768
	ds_read_b128 v[166:169], v210 offset:33792
	ds_read_b128 v[202:205], v210 offset:34816
	ds_read_b128 v[216:219], v210 offset:35840
	ds_read_b128 v[220:223], v210 offset:36864
	ds_read_b128 v[224:227], v210 offset:37888
	ds_read_b128 v[228:231], v210 offset:38912
	ds_read_b128 v[232:235], v210 offset:39936
	global_load_lds_dwordx4 v[244:245], off
	v_lshl_add_u64 v[244:245], s[30:31], 0, v[186:187]
	s_mov_b32 m0, s47
	s_nop 0
	global_load_lds_dwordx4 v[244:245], off
	s_waitcnt vmcnt(8)
	s_waitcnt lgkmcnt(0)
	s_barrier
	s_setprio 1
	s_waitcnt lgkmcnt(0)
	v_mfma_f32_16x16x32_bf16 v[146:149], v[62:65], v[162:165], v[146:149]
	v_mfma_f32_16x16x32_bf16 v[142:145], v[74:77], v[162:165], v[142:145]
	v_mfma_f32_16x16x32_bf16 v[126:129], v[62:65], v[202:205], v[126:129]
	v_mfma_f32_16x16x32_bf16 v[122:125], v[74:77], v[202:205], v[122:125]
	v_mfma_f32_16x16x32_bf16 v[110:113], v[62:65], v[220:223], v[110:113]
	v_mfma_f32_16x16x32_bf16 v[106:109], v[74:77], v[220:223], v[106:109]
	v_mfma_f32_16x16x32_bf16 v[94:97], v[62:65], v[228:231], v[94:97]
	v_mfma_f32_16x16x32_bf16 v[90:93], v[74:77], v[228:231], v[90:93]
	v_mfma_f32_16x16x32_bf16 v[146:149], v[70:73], v[166:169], v[146:149]
	v_mfma_f32_16x16x32_bf16 v[142:145], v[78:81], v[166:169], v[142:145]
	v_mfma_f32_16x16x32_bf16 v[126:129], v[70:73], v[216:219], v[126:129]
	v_mfma_f32_16x16x32_bf16 v[122:125], v[78:81], v[216:219], v[122:125]
	v_mfma_f32_16x16x32_bf16 v[110:113], v[70:73], v[224:227], v[110:113]
	v_mfma_f32_16x16x32_bf16 v[106:109], v[78:81], v[224:227], v[106:109]
	v_mfma_f32_16x16x32_bf16 v[94:97], v[70:73], v[232:235], v[94:97]
	v_mfma_f32_16x16x32_bf16 v[90:93], v[78:81], v[232:235], v[90:93]
	v_mfma_f32_16x16x32_bf16 v[134:137], v[138:141], v[162:165], v[134:137]
	v_mfma_f32_16x16x32_bf16 v[130:133], v[154:157], v[162:165], v[130:133]
	v_mfma_f32_16x16x32_bf16 v[118:121], v[138:141], v[202:205], v[118:121]
	v_mfma_f32_16x16x32_bf16 v[114:117], v[154:157], v[202:205], v[114:117]
	v_mfma_f32_16x16x32_bf16 v[102:105], v[138:141], v[220:223], v[102:105]
	v_mfma_f32_16x16x32_bf16 v[98:101], v[154:157], v[220:223], v[98:101]
	v_mfma_f32_16x16x32_bf16 v[86:89], v[138:141], v[228:231], v[86:89]
	v_mfma_f32_16x16x32_bf16 v[82:85], v[154:157], v[228:231], v[82:85]
	v_mfma_f32_16x16x32_bf16 v[134:137], v[150:153], v[166:169], v[134:137]
	v_mfma_f32_16x16x32_bf16 v[130:133], v[158:161], v[166:169], v[130:133]
	v_mfma_f32_16x16x32_bf16 v[118:121], v[150:153], v[216:219], v[118:121]
	v_mfma_f32_16x16x32_bf16 v[114:117], v[158:161], v[216:219], v[114:117]
	v_mfma_f32_16x16x32_bf16 v[102:105], v[150:153], v[224:227], v[102:105]
	v_mfma_f32_16x16x32_bf16 v[98:101], v[158:161], v[224:227], v[98:101]
	v_mfma_f32_16x16x32_bf16 v[86:89], v[150:153], v[232:235], v[86:89]
	v_mfma_f32_16x16x32_bf16 v[82:85], v[158:161], v[232:235], v[82:85]
	s_setprio 0
	s_barrier
; #define PG8_STAGE(bufoff, gbase, voff) do { _Pragma("unroll") for (int _i = 0; _i < 2; ++_i) \
;         __builtin_amdgcn_global_load_lds((const unsigned*)((const char*)(gbase) + (voff)[_i]), (PG8_LAS unsigned*)(lds + (bufoff) + ldsw + _i * 8192), 16, 0, 0); } while (0)
; #define PG8_WAIT_V(n) asm volatile("s_waitcnt vmcnt(" #n ")" ::: "memory")
; #define PG8_WAIT_L(n) asm volatile("s_waitcnt lgkmcnt(" #n ")" ::: "memory")
; template <class Epi, class Sched, bool ALIGN_EPI = true, bool F8 = false>
; __device__ __forceinline__ void gemm_phase(PG8_LAS unsigned char* lds, const Sched& S, const Epi& E) {
;     ...
;         for (int t = 0; t < nt; t += 2) {
;             const bool last = (t == nt - 2);
;             if constexpr (Sched::GATHER) { if (last && has_next) S.a_off(nxt, Rs, Cs, voffAn); }
;             const char* a1 = cA + (size_t)(t + 1) * kstep;
;             const char* a2 = last ? nA : cA + (size_t)(t + 2) * kstep; const char* b2 = last ? nB : cB + (size_t)(t + 2) * kstepB;
;             const char* a3 = a2 + kstep; const char* b3 = b2 + kstepB;
;             unsigned vA2[2][2];
; #pragma unroll
;             for (int h = 0; h < 2; ++h)
; #pragma unroll
;                 for (int i = 0; i < 2; ++i) { if constexpr (Sched::GATHER) vA2[h][i] = (last && has_next) ? voffAn[h][i] : voffA[h][i]; else vA2[h][i] = voffA[h][i]; }
;             PG8_LDB(B0, 0, 0); PG8_LDB(B1, 0, 1); PG8_SCHED; PG8_LDA(At, 0, 0); PG8_STAGE(PG8_SA(1, 1), a1, voffA[1]);
;             PG8_WAIT_V(8); PG8_WAIT_L(0); PG8_BAR; PG8_MMA(0, 0, At, B0); PG8_MMA(0, 1, At, B1); PG8_BAR; PG8_SCHED;
;             PG8_LDA(At, 0, 1); PG8_STAGE(PG8_SB(0, 0), b2, voffB[0]); PG8_STAGE(PG8_SB(0, 1), b2, voffB[1]); PG8_STAGE(PG8_SA(0, 0), a2, vA2[0]);
;             PG8_WAIT_V(8); PG8_WAIT_L(0); PG8_BAR; PG8_MMA(1, 0, At, B0); PG8_MMA(1, 1, At, B1); PG8_BAR; PG8_SCHED;
;             PG8_LDB(B0, 1, 0); PG8_LDB(B1, 1, 1); PG8_SCHED; PG8_LDA(At, 1, 0); PG8_STAGE(PG8_SA(0, 1), a2, vA2[1]);
;             PG8_WAIT_V(8); PG8_WAIT_L(0); PG8_BAR; PG8_MMA(0, 0, At, B0); PG8_MMA(0, 1, At, B1); PG8_BAR; PG8_SCHED;
;             PG8_LDA(At, 1, 1); PG8_STAGE(PG8_SB(1, 0), b3, voffB[0]); PG8_STAGE(PG8_SB(1, 1), b3, voffB[1]); PG8_STAGE(PG8_SA(1, 0), a3, vA2[0]);
;             PG8_WAIT_V(8); PG8_WAIT_L(0); PG8_BAR; PG8_MMA(1, 0, At, B0); PG8_MMA(1, 1, At, B1); PG8_BAR; PG8_SCHED;
	s_add_u32 s28, s28, 0x80
	s_addc_u32 s29, s29, 0
	s_add_i32 s30, s70, s43
	v_lshl_add_u64 v[236:237], v[236:237], 0, s[14:15]
	s_mov_b32 m0, s30
	ds_read_b128 v[162:165], v210 offset:49152
	ds_read_b128 v[166:169], v210 offset:50176
	ds_read_b128 v[202:205], v210 offset:51200
	ds_read_b128 v[216:219], v210 offset:52224
	ds_read_b128 v[220:223], v210 offset:53248
	ds_read_b128 v[224:227], v210 offset:54272
	ds_read_b128 v[228:231], v210 offset:55296
	ds_read_b128 v[232:235], v210 offset:56320
	global_load_lds_dwordx4 v[236:237], off
	v_lshl_add_u64 v[236:237], v[238:239], 0, s[14:15]
	s_add_i32 m0, s30, 0x2000
	s_add_i32 s30, s71, s43
	global_load_lds_dwordx4 v[236:237], off
	v_lshl_add_u64 v[236:237], s[28:29], 0, v[176:177]
	s_mov_b32 m0, s30
	s_nop 0
	global_load_lds_dwordx4 v[236:237], off
	v_lshl_add_u64 v[236:237], s[28:29], 0, v[178:179]
	s_add_i32 m0, s30, 0x2000
	s_nop 0
	global_load_lds_dwordx4 v[236:237], off
	v_lshl_add_u64 v[236:237], v[240:241], 0, s[14:15]
	s_mov_b32 m0, s50
	s_nop 0
	global_load_lds_dwordx4 v[236:237], off
	v_lshl_add_u64 v[236:237], v[242:243], 0, s[14:15]
	s_mov_b32 m0, s51
	s_nop 0
	global_load_lds_dwordx4 v[236:237], off
	s_waitcnt vmcnt(8)
	s_waitcnt lgkmcnt(0)
	s_barrier
	s_setprio 1
	s_waitcnt lgkmcnt(0)
	v_mfma_f32_16x16x32_bf16 v[66:69], v[62:65], v[162:165], v[66:69]
	v_mfma_f32_16x16x32_bf16 v[58:61], v[74:77], v[162:165], v[58:61]
	v_mfma_f32_16x16x32_bf16 v[46:49], v[62:65], v[202:205], v[46:49]
	v_mfma_f32_16x16x32_bf16 v[42:45], v[74:77], v[202:205], v[42:45]
	v_mfma_f32_16x16x32_bf16 v[30:33], v[62:65], v[220:223], v[30:33]
	v_mfma_f32_16x16x32_bf16 v[26:29], v[74:77], v[220:223], v[26:29]
	v_mfma_f32_16x16x32_bf16 v[14:17], v[62:65], v[228:231], v[14:17]
	v_mfma_f32_16x16x32_bf16 v[10:13], v[74:77], v[228:231], v[10:13]
	v_mfma_f32_16x16x32_bf16 v[66:69], v[70:73], v[166:169], v[66:69]
	v_mfma_f32_16x16x32_bf16 v[58:61], v[78:81], v[166:169], v[58:61]
	v_mfma_f32_16x16x32_bf16 v[46:49], v[70:73], v[216:219], v[46:49]
	v_mfma_f32_16x16x32_bf16 v[42:45], v[78:81], v[216:219], v[42:45]
	v_mfma_f32_16x16x32_bf16 v[30:33], v[70:73], v[224:227], v[30:33]
	v_mfma_f32_16x16x32_bf16 v[26:29], v[78:81], v[224:227], v[26:29]
	v_mfma_f32_16x16x32_bf16 v[14:17], v[70:73], v[232:235], v[14:17]
	v_mfma_f32_16x16x32_bf16 v[10:13], v[78:81], v[232:235], v[10:13]
	v_mfma_f32_16x16x32_bf16 v[54:57], v[138:141], v[162:165], v[54:57]
	v_mfma_f32_16x16x32_bf16 v[50:53], v[154:157], v[162:165], v[50:53]
	v_mfma_f32_16x16x32_bf16 v[38:41], v[138:141], v[202:205], v[38:41]
	v_mfma_f32_16x16x32_bf16 v[34:37], v[154:157], v[202:205], v[34:37]
	v_mfma_f32_16x16x32_bf16 v[22:25], v[138:141], v[220:223], v[22:25]
	v_mfma_f32_16x16x32_bf16 v[18:21], v[154:157], v[220:223], v[18:21]
	v_mfma_f32_16x16x32_bf16 v[6:9], v[138:141], v[228:231], v[6:9]
	v_mfma_f32_16x16x32_bf16 v[2:5], v[154:157], v[228:231], v[2:5]
	v_mfma_f32_16x16x32_bf16 v[54:57], v[150:153], v[166:169], v[54:57]
	v_mfma_f32_16x16x32_bf16 v[50:53], v[158:161], v[166:169], v[50:53]
	v_mfma_f32_16x16x32_bf16 v[38:41], v[150:153], v[216:219], v[38:41]
	v_mfma_f32_16x16x32_bf16 v[34:37], v[158:161], v[216:219], v[34:37]
	v_mfma_f32_16x16x32_bf16 v[22:25], v[150:153], v[224:227], v[22:25]
	v_mfma_f32_16x16x32_bf16 v[18:21], v[158:161], v[224:227], v[18:21]
	v_mfma_f32_16x16x32_bf16 v[6:9], v[150:153], v[232:235], v[6:9]
	v_mfma_f32_16x16x32_bf16 v[2:5], v[158:161], v[232:235], v[2:5]
	s_setprio 0
	s_barrier
	s_add_i32 s69, s69, 2
	s_add_u32 s19, s19, 0x100
	s_addc_u32 s21, s21, 0
	s_add_u32 s26, s26, 0x100
	s_addc_u32 s27, s27, 0
	s_cmp_gt_u32 s69, 5
	s_cbranch_scc0 .LBB0_763

; #define PG8_STAGE(bufoff, gbase, voff) do { _Pragma("unroll") for (int _i = 0; _i < 2; ++_i) \
;         __builtin_amdgcn_global_load_lds((const unsigned*)((const char*)(gbase) + (voff)[_i]), (PG8_LAS unsigned*)(lds + (bufoff) + ldsw + _i * 8192), 16, 0, 0); } while (0)
; #define PG8_WAIT_V(n) asm volatile("s_waitcnt vmcnt(" #n ")" ::: "memory")
; #define PG8_WAIT_L(n) asm volatile("s_waitcnt lgkmcnt(" #n ")" ::: "memory")
; template <class Epi, class Sched, bool ALIGN_EPI = true, bool F8 = false>
; __device__ __forceinline__ void gemm_phase(PG8_LAS unsigned char* lds, const Sched& S, const Epi& E) {
;     ...
;         for (int t = 0; t < nt; t += 2) {
;             const bool last = (t == nt - 2);
;             if constexpr (Sched::GATHER) { if (last && has_next) S.a_off(nxt, Rs, Cs, voffAn); }
;             const char* a1 = cA + (size_t)(t + 1) * kstep;
;             const char* a2 = last ? nA : cA + (size_t)(t + 2) * kstep; const char* b2 = last ? nB : cB + (size_t)(t + 2) * kstepB;
;             const char* a3 = a2 + kstep; const char* b3 = b2 + kstepB;
;             unsigned vA2[2][2];
; #pragma unroll
;             for (int h = 0; h < 2; ++h)
; #pragma unroll
;                 for (int i = 0; i < 2; ++i) { if constexpr (Sched::GATHER) vA2[h][i] = (last && has_next) ? voffAn[h][i] : voffA[h][i]; else vA2[h][i] = voffA[h][i]; }
;             PG8_LDB(B0, 0, 0); PG8_LDB(B1, 0, 1); PG8_SCHED; PG8_LDA(At, 0, 0); PG8_STAGE(PG8_SA(1, 1), a1, voffA[1]);
;             PG8_WAIT_V(8); PG8_WAIT_L(0); PG8_BAR; PG8_MMA(0, 0, At, B0); PG8_MMA(0, 1, At, B1); PG8_BAR; PG8_SCHED;
;             PG8_LDA(At, 0, 1); PG8_STAGE(PG8_SB(0, 0), b2, voffB[0]); PG8_STAGE(PG8_SB(0, 1), b2, voffB[1]); PG8_STAGE(PG8_SA(0, 0), a2, vA2[0]);
;             PG8_WAIT_V(8); PG8_WAIT_L(0); PG8_BAR; PG8_MMA(1, 0, At, B0); PG8_MMA(1, 1, At, B1); PG8_BAR; PG8_SCHED;
;             PG8_LDB(B0, 1, 0); PG8_LDB(B1, 1, 1); PG8_SCHED; PG8_LDA(At, 1, 0); PG8_STAGE(PG8_SA(0, 1), a2, vA2[1]);
;             PG8_WAIT_V(8); PG8_WAIT_L(0); PG8_BAR; PG8_MMA(0, 0, At, B0); PG8_MMA(0, 1, At, B1); PG8_BAR; PG8_SCHED;
;             PG8_LDA(At, 1, 1); PG8_STAGE(PG8_SB(1, 0), b3, voffB[0]); PG8_STAGE(PG8_SB(1, 1), b3, voffB[1]); PG8_STAGE(PG8_SA(1, 0), a3, vA2[0]);
;             PG8_WAIT_V(8); PG8_WAIT_L(0); PG8_BAR; PG8_MMA(1, 0, At, B0); PG8_MMA(1, 1, At, B1); PG8_BAR; PG8_SCHED;
.LBB0_834:
	v_add_u32_e32 v10, s58, v190
	ds_read_b128 v[2:5], v10
	ds_read_b128 v[6:9], v10 offset:1024
	ds_read_b128 v[142:145], v10 offset:2048
	ds_read_b128 v[146:149], v10 offset:3072
	v_add_u32_e32 v10, s59, v190
	ds_read_b128 v[150:153], v10
	ds_read_b128 v[154:157], v10 offset:1024
	ds_read_b128 v[202:205], v10 offset:2048
	ds_read_b128 v[206:209], v10 offset:3072
	s_add_i32 s77, s26, 2
	s_add_u32 s27, s24, 0x8000
	s_addc_u32 s28, s25, 0
	s_cmp_eq_u32 s74, s26
	s_cselect_b32 s30, s20, s27
	s_cselect_b32 s31, s21, s28
	s_cselect_b32 s28, s22, s75
	s_cselect_b32 s29, s23, s76
	s_add_u32 s26, s30, 0x8000
	s_addc_u32 s27, s31, 0
	s_add_i32 m0, s45, 0xc000
	ds_read_b128 v[210:213], v198
	ds_read_b128 v[214:217], v198 offset:1024
	ds_read_b128 v[218:221], v198 offset:2048
	ds_read_b128 v[222:225], v198 offset:3072
	ds_read_b128 v[226:229], v198 offset:4096
	ds_read_b128 v[230:233], v198 offset:5120
	ds_read_b128 v[234:237], v198 offset:6144
	ds_read_b128 v[238:241], v198 offset:7168
	global_load_lds_dwordx4 v182, s[24:25]
	s_add_i32 m0, s45, 0xe000
	s_nop 0
	global_load_lds_dwordx4 v180, s[24:25]
	s_waitcnt vmcnt(8)
	s_waitcnt lgkmcnt(0)
	s_setprio 1
	v_mfma_f32_16x16x128_f8f6f4 v[138:141], v[2:9], v[210:217], v[138:141]
	v_mfma_f32_16x16x128_f8f6f4 v[134:137], v[142:149], v[210:217], v[134:137]
	v_mfma_f32_16x16x128_f8f6f4 v[130:133], v[2:9], v[218:225], v[130:133]
	v_mfma_f32_16x16x128_f8f6f4 v[126:129], v[142:149], v[218:225], v[126:129]
	v_mfma_f32_16x16x128_f8f6f4 v[122:125], v[2:9], v[226:233], v[122:125]
	v_mfma_f32_16x16x128_f8f6f4 v[118:121], v[142:149], v[226:233], v[118:121]
	v_mfma_f32_16x16x128_f8f6f4 v[114:117], v[2:9], v[234:241], v[114:117]
	v_mfma_f32_16x16x128_f8f6f4 v[110:113], v[142:149], v[234:241], v[110:113]
	s_nop 3
	v_mfma_f32_16x16x128_f8f6f4 v[106:109], v[150:157], v[210:217], v[106:109]
	v_mfma_f32_16x16x128_f8f6f4 v[102:105], v[202:209], v[210:217], v[102:105]
	v_mfma_f32_16x16x128_f8f6f4 v[98:101], v[150:157], v[218:225], v[98:101]
	v_mfma_f32_16x16x128_f8f6f4 v[94:97], v[202:209], v[218:225], v[94:97]
	v_mfma_f32_16x16x128_f8f6f4 v[90:93], v[150:157], v[226:233], v[90:93]
	v_mfma_f32_16x16x128_f8f6f4 v[86:89], v[202:209], v[226:233], v[86:89]
	v_mfma_f32_16x16x128_f8f6f4 v[82:85], v[150:157], v[234:241], v[82:85]
	v_mfma_f32_16x16x128_f8f6f4 v[78:81], v[202:209], v[234:241], v[78:81]
	s_setprio 0
	s_barrier
	s_add_i32 s78, s58, s44
	s_mov_b32 m0, s78
	ds_read_b128 v[210:213], v198 offset:16384
	ds_read_b128 v[214:217], v198 offset:17408
	ds_read_b128 v[218:221], v198 offset:18432
	ds_read_b128 v[222:225], v198 offset:19456
	ds_read_b128 v[226:229], v198 offset:20480
	ds_read_b128 v[230:233], v198 offset:21504
	ds_read_b128 v[234:237], v198 offset:22528
	ds_read_b128 v[238:241], v198 offset:23552
	global_load_lds_dwordx4 v158, s[28:29]
	s_add_i32 m0, s78, 0x2000
	s_add_i32 s78, s59, s44
	global_load_lds_dwordx4 v160, s[28:29]
	s_add_u32 s98, s28, s8
	s_addc_u32 s99, s29, s9
	s_mov_b32 m0, s78
	s_nop 0
	global_load_lds_dwordx4 v158, s[98:99]
	s_add_u32 s100, s28, s8
	s_addc_u32 s101, s29, s9
	s_add_i32 m0, s78, 0x2000
	s_nop 0
	global_load_lds_dwordx4 v160, s[100:101]
	s_mov_b32 m0, s45
	s_nop 0
	global_load_lds_dwordx4 v162, s[30:31]
	s_mov_b32 m0, s46
	s_nop 0
	global_load_lds_dwordx4 v164, s[30:31]
	s_waitcnt vmcnt(8)
	s_waitcnt lgkmcnt(0)
	s_setprio 1
	v_mfma_f32_16x16x128_f8f6f4 v[74:77], v[2:9], v[210:217], v[74:77]
	v_mfma_f32_16x16x128_f8f6f4 v[70:73], v[142:149], v[210:217], v[70:73]
	v_mfma_f32_16x16x128_f8f6f4 v[66:69], v[2:9], v[218:225], v[66:69]
	v_mfma_f32_16x16x128_f8f6f4 v[62:65], v[142:149], v[218:225], v[62:65]
	v_mfma_f32_16x16x128_f8f6f4 v[58:61], v[2:9], v[226:233], v[58:61]
	v_mfma_f32_16x16x128_f8f6f4 v[54:57], v[142:149], v[226:233], v[54:57]
	v_mfma_f32_16x16x128_f8f6f4 v[50:53], v[2:9], v[234:241], v[50:53]
	v_mfma_f32_16x16x128_f8f6f4 v[46:49], v[142:149], v[234:241], v[46:49]
	s_nop 3
	v_mfma_f32_16x16x128_f8f6f4 v[42:45], v[150:157], v[210:217], v[42:45]
	v_mfma_f32_16x16x128_f8f6f4 v[38:41], v[202:209], v[210:217], v[38:41]
	v_mfma_f32_16x16x128_f8f6f4 v[34:37], v[150:157], v[218:225], v[34:37]
	v_mfma_f32_16x16x128_f8f6f4 v[30:33], v[202:209], v[218:225], v[30:33]
	v_mfma_f32_16x16x128_f8f6f4 v[26:29], v[150:157], v[226:233], v[26:29]
	v_mfma_f32_16x16x128_f8f6f4 v[22:25], v[202:209], v[226:233], v[22:25]
	v_mfma_f32_16x16x128_f8f6f4 v[18:21], v[150:157], v[234:241], v[18:21]
	v_mfma_f32_16x16x128_f8f6f4 v[14:17], v[202:209], v[234:241], v[14:17]
	s_setprio 0
	s_barrier
	s_add_i32 s78, 0, 0x18000
	s_add_i32 s79, 0, 0x1c000
	v_add_u32_e32 v2, s78, v190
	v_add_u32_e32 v10, s79, v190
	ds_read_b128 v[142:145], v2
	ds_read_b128 v[146:149], v2 offset:1024
	ds_read_b128 v[150:153], v2 offset:2048
	ds_read_b128 v[154:157], v2 offset:3072
	ds_read_b128 v[2:5], v10
	ds_read_b128 v[6:9], v10 offset:1024
	ds_read_b128 v[202:205], v10 offset:2048
	ds_read_b128 v[206:209], v10 offset:3072
	s_mov_b32 m0, s47
	ds_read_b128 v[210:213], v198 offset:32768
	ds_read_b128 v[214:217], v198 offset:33792
	ds_read_b128 v[218:221], v198 offset:34816
	ds_read_b128 v[222:225], v198 offset:35840
	ds_read_b128 v[226:229], v198 offset:36864
	ds_read_b128 v[230:233], v198 offset:37888
	ds_read_b128 v[234:237], v198 offset:38912
	ds_read_b128 v[238:241], v198 offset:39936
	global_load_lds_dwordx4 v166, s[30:31]
	s_mov_b32 m0, s48
	s_nop 0
	global_load_lds_dwordx4 v168, s[30:31]
	s_waitcnt vmcnt(8)
	s_waitcnt lgkmcnt(0)
	s_setprio 1
	v_mfma_f32_16x16x128_f8f6f4 v[138:141], v[142:149], v[210:217], v[138:141]
	v_mfma_f32_16x16x128_f8f6f4 v[134:137], v[150:157], v[210:217], v[134:137]
	v_mfma_f32_16x16x128_f8f6f4 v[130:133], v[142:149], v[218:225], v[130:133]
	v_mfma_f32_16x16x128_f8f6f4 v[126:129], v[150:157], v[218:225], v[126:129]
	v_mfma_f32_16x16x128_f8f6f4 v[122:125], v[142:149], v[226:233], v[122:125]
	v_mfma_f32_16x16x128_f8f6f4 v[118:121], v[150:157], v[226:233], v[118:121]
	v_mfma_f32_16x16x128_f8f6f4 v[114:117], v[142:149], v[234:241], v[114:117]
	v_mfma_f32_16x16x128_f8f6f4 v[110:113], v[150:157], v[234:241], v[110:113]
	s_nop 3
	v_mfma_f32_16x16x128_f8f6f4 v[106:109], v[2:9], v[210:217], v[106:109]
	v_mfma_f32_16x16x128_f8f6f4 v[102:105], v[202:209], v[210:217], v[102:105]
	v_mfma_f32_16x16x128_f8f6f4 v[98:101], v[2:9], v[218:225], v[98:101]
	v_mfma_f32_16x16x128_f8f6f4 v[94:97], v[202:209], v[218:225], v[94:97]
	v_mfma_f32_16x16x128_f8f6f4 v[90:93], v[2:9], v[226:233], v[90:93]
	v_mfma_f32_16x16x128_f8f6f4 v[86:89], v[202:209], v[226:233], v[86:89]
	v_mfma_f32_16x16x128_f8f6f4 v[82:85], v[2:9], v[234:241], v[82:85]
	v_mfma_f32_16x16x128_f8f6f4 v[78:81], v[202:209], v[234:241], v[78:81]
	s_setprio 0
	s_barrier
; #define PG8_STAGE(bufoff, gbase, voff) do { _Pragma("unroll") for (int _i = 0; _i < 2; ++_i) \
;         __builtin_amdgcn_global_load_lds((const unsigned*)((const char*)(gbase) + (voff)[_i]), (PG8_LAS unsigned*)(lds + (bufoff) + ldsw + _i * 8192), 16, 0, 0); } while (0)
; #define PG8_WAIT_V(n) asm volatile("s_waitcnt vmcnt(" #n ")" ::: "memory")
; #define PG8_WAIT_L(n) asm volatile("s_waitcnt lgkmcnt(" #n ")" ::: "memory")
; template <class Epi, class Sched, bool ALIGN_EPI = true, bool F8 = false>
; __device__ __forceinline__ void gemm_phase(PG8_LAS unsigned char* lds, const Sched& S, const Epi& E) {
;     ...
;         for (int t = 0; t < nt; t += 2) {
;             const bool last = (t == nt - 2);
;             if constexpr (Sched::GATHER) { if (last && has_next) S.a_off(nxt, Rs, Cs, voffAn); }
;             const char* a1 = cA + (size_t)(t + 1) * kstep;
;             const char* a2 = last ? nA : cA + (size_t)(t + 2) * kstep; const char* b2 = last ? nB : cB + (size_t)(t + 2) * kstepB;
;             const char* a3 = a2 + kstep; const char* b3 = b2 + kstepB;
;             unsigned vA2[2][2];
; #pragma unroll
;             for (int h = 0; h < 2; ++h)
; #pragma unroll
;                 for (int i = 0; i < 2; ++i) { if constexpr (Sched::GATHER) vA2[h][i] = (last && has_next) ? voffAn[h][i] : voffA[h][i]; else vA2[h][i] = voffA[h][i]; }
;             PG8_LDB(B0, 0, 0); PG8_LDB(B1, 0, 1); PG8_SCHED; PG8_LDA(At, 0, 0); PG8_STAGE(PG8_SA(1, 1), a1, voffA[1]);
;             PG8_WAIT_V(8); PG8_WAIT_L(0); PG8_BAR; PG8_MMA(0, 0, At, B0); PG8_MMA(0, 1, At, B1); PG8_BAR; PG8_SCHED;
;             PG8_LDA(At, 0, 1); PG8_STAGE(PG8_SB(0, 0), b2, voffB[0]); PG8_STAGE(PG8_SB(0, 1), b2, voffB[1]); PG8_STAGE(PG8_SA(0, 0), a2, vA2[0]);
;             PG8_WAIT_V(8); PG8_WAIT_L(0); PG8_BAR; PG8_MMA(1, 0, At, B0); PG8_MMA(1, 1, At, B1); PG8_BAR; PG8_SCHED;
;             PG8_LDB(B0, 1, 0); PG8_LDB(B1, 1, 1); PG8_SCHED; PG8_LDA(At, 1, 0); PG8_STAGE(PG8_SA(0, 1), a2, vA2[1]);
;             PG8_WAIT_V(8); PG8_WAIT_L(0); PG8_BAR; PG8_MMA(0, 0, At, B0); PG8_MMA(0, 1, At, B1); PG8_BAR; PG8_SCHED;
;             PG8_LDA(At, 1, 1); PG8_STAGE(PG8_SB(1, 0), b3, voffB[0]); PG8_STAGE(PG8_SB(1, 1), b3, voffB[1]); PG8_STAGE(PG8_SA(1, 0), a3, vA2[0]);
;             PG8_WAIT_V(8); PG8_WAIT_L(0); PG8_BAR; PG8_MMA(1, 0, At, B0); PG8_MMA(1, 1, At, B1); PG8_BAR; PG8_SCHED;
	s_add_u32 s28, s28, 0x8000
	s_addc_u32 s29, s29, 0
	s_add_i32 s30, s78, s44
	s_mov_b32 m0, s30
	ds_read_b128 v[210:213], v198 offset:49152
	ds_read_b128 v[214:217], v198 offset:50176
	ds_read_b128 v[218:221], v198 offset:51200
	ds_read_b128 v[222:225], v198 offset:52224
	ds_read_b128 v[226:229], v198 offset:53248
	ds_read_b128 v[230:233], v198 offset:54272
	ds_read_b128 v[234:237], v198 offset:55296
	ds_read_b128 v[238:241], v198 offset:56320
	global_load_lds_dwordx4 v158, s[28:29]
	s_add_i32 m0, s30, 0x2000
	s_add_i32 s30, s79, s44
	global_load_lds_dwordx4 v160, s[28:29]
	s_mov_b32 m0, s30
	s_nop 0
	global_load_lds_dwordx4 v172, s[28:29]
	s_add_i32 m0, s30, 0x2000
	s_nop 0
	global_load_lds_dwordx4 v174, s[28:29]
	s_mov_b32 m0, s50
	s_nop 0
	global_load_lds_dwordx4 v162, s[26:27]
	s_mov_b32 m0, s51
	s_nop 0
	global_load_lds_dwordx4 v164, s[26:27]
	s_waitcnt vmcnt(8)
	s_waitcnt lgkmcnt(0)
	s_setprio 1
	v_mfma_f32_16x16x128_f8f6f4 v[74:77], v[142:149], v[210:217], v[74:77]
	v_mfma_f32_16x16x128_f8f6f4 v[70:73], v[150:157], v[210:217], v[70:73]
	v_mfma_f32_16x16x128_f8f6f4 v[66:69], v[142:149], v[218:225], v[66:69]
	v_mfma_f32_16x16x128_f8f6f4 v[62:65], v[150:157], v[218:225], v[62:65]
	v_mfma_f32_16x16x128_f8f6f4 v[58:61], v[142:149], v[226:233], v[58:61]
	v_mfma_f32_16x16x128_f8f6f4 v[54:57], v[150:157], v[226:233], v[54:57]
	v_mfma_f32_16x16x128_f8f6f4 v[50:53], v[142:149], v[234:241], v[50:53]
	v_mfma_f32_16x16x128_f8f6f4 v[46:49], v[150:157], v[234:241], v[46:49]
	s_nop 3
	v_mfma_f32_16x16x128_f8f6f4 v[42:45], v[2:9], v[210:217], v[42:45]
	v_mfma_f32_16x16x128_f8f6f4 v[38:41], v[202:209], v[210:217], v[38:41]
	v_mfma_f32_16x16x128_f8f6f4 v[34:37], v[2:9], v[218:225], v[34:37]
	v_mfma_f32_16x16x128_f8f6f4 v[30:33], v[202:209], v[218:225], v[30:33]
	v_mfma_f32_16x16x128_f8f6f4 v[26:29], v[2:9], v[226:233], v[26:29]
	v_mfma_f32_16x16x128_f8f6f4 v[22:25], v[202:209], v[226:233], v[22:25]
	v_mfma_f32_16x16x128_f8f6f4 v[18:21], v[2:9], v[234:241], v[18:21]
	v_mfma_f32_16x16x128_f8f6f4 v[14:17], v[202:209], v[234:241], v[14:17]
	s_setprio 0
	s_barrier
	s_add_u32 s75, s75, 0x10000
	s_addc_u32 s76, s76, 0
	s_add_u32 s24, s24, 0x10000
	s_addc_u32 s25, s25, 0
	s_cmp_ge_i32 s77, s72
	s_mov_b32 s26, s77
	s_cbranch_scc0 .LBB0_834
	s_branch .Lfx_23459
.Lh1e_23459:
.Lh1_834:
	v_add_u32_e32 v10, s58, v190
	ds_read_b128 v[2:5], v10
	ds_read_b128 v[6:9], v10 offset:1024
	ds_read_b128 v[142:145], v10 offset:2048
	ds_read_b128 v[146:149], v10 offset:3072
	v_add_u32_e32 v10, s59, v190
	ds_read_b128 v[150:153], v10
	ds_read_b128 v[154:157], v10 offset:1024
	ds_read_b128 v[202:205], v10 offset:2048
	ds_read_b128 v[206:209], v10 offset:3072
	s_add_i32 s77, s26, 2
	s_add_u32 s27, s24, 0x8000
	s_addc_u32 s28, s25, 0
	s_cmp_eq_u32 s74, s26
	s_cselect_b32 s30, s20, s27
	s_cselect_b32 s31, s21, s28
	s_cselect_b32 s28, s22, s75
	s_cselect_b32 s29, s23, s76
	s_add_u32 s26, s30, 0x8000
	s_addc_u32 s27, s31, 0
	s_add_i32 m0, s45, 0xc000
	ds_read_b128 v[210:213], v198
	ds_read_b128 v[214:217], v198 offset:1024
	ds_read_b128 v[218:221], v198 offset:2048
	ds_read_b128 v[222:225], v198 offset:3072
	ds_read_b128 v[226:229], v198 offset:4096
	ds_read_b128 v[230:233], v198 offset:5120
	ds_read_b128 v[234:237], v198 offset:6144
	ds_read_b128 v[238:241], v198 offset:7168
	global_load_lds_dwordx4 v182, s[24:25]
	s_add_i32 m0, s45, 0xe000
	s_nop 0
	global_load_lds_dwordx4 v180, s[24:25]
	s_waitcnt vmcnt(8)
	s_waitcnt lgkmcnt(0)
	s_barrier
	s_setprio 2
	v_mfma_f32_16x16x128_f8f6f4 v[138:141], v[2:9], v[210:217], v[138:141]
	v_mfma_f32_16x16x128_f8f6f4 v[134:137], v[142:149], v[210:217], v[134:137]
	v_mfma_f32_16x16x128_f8f6f4 v[130:133], v[2:9], v[218:225], v[130:133]
	v_mfma_f32_16x16x128_f8f6f4 v[126:129], v[142:149], v[218:225], v[126:129]
	v_mfma_f32_16x16x128_f8f6f4 v[122:125], v[2:9], v[226:233], v[122:125]
	v_mfma_f32_16x16x128_f8f6f4 v[118:121], v[142:149], v[226:233], v[118:121]
	v_mfma_f32_16x16x128_f8f6f4 v[114:117], v[2:9], v[234:241], v[114:117]
	v_mfma_f32_16x16x128_f8f6f4 v[110:113], v[142:149], v[234:241], v[110:113]
	s_nop 3
	v_mfma_f32_16x16x128_f8f6f4 v[106:109], v[150:157], v[210:217], v[106:109]
	v_mfma_f32_16x16x128_f8f6f4 v[102:105], v[202:209], v[210:217], v[102:105]
	v_mfma_f32_16x16x128_f8f6f4 v[98:101], v[150:157], v[218:225], v[98:101]
	v_mfma_f32_16x16x128_f8f6f4 v[94:97], v[202:209], v[218:225], v[94:97]
	v_mfma_f32_16x16x128_f8f6f4 v[90:93], v[150:157], v[226:233], v[90:93]
	v_mfma_f32_16x16x128_f8f6f4 v[86:89], v[202:209], v[226:233], v[86:89]
	v_mfma_f32_16x16x128_f8f6f4 v[82:85], v[150:157], v[234:241], v[82:85]
	v_mfma_f32_16x16x128_f8f6f4 v[78:81], v[202:209], v[234:241], v[78:81]
	s_setprio 0
	s_add_i32 s78, s58, s44
	s_mov_b32 m0, s78
	ds_read_b128 v[210:213], v198 offset:16384
	ds_read_b128 v[214:217], v198 offset:17408
	ds_read_b128 v[218:221], v198 offset:18432
	ds_read_b128 v[222:225], v198 offset:19456
	ds_read_b128 v[226:229], v198 offset:20480
	ds_read_b128 v[230:233], v198 offset:21504
	ds_read_b128 v[234:237], v198 offset:22528
	ds_read_b128 v[238:241], v198 offset:23552
	global_load_lds_dwordx4 v158, s[28:29]
	s_add_i32 m0, s78, 0x2000
	s_add_i32 s78, s59, s44
	global_load_lds_dwordx4 v160, s[28:29]
	s_add_u32 s98, s28, s8
	s_addc_u32 s99, s29, s9
	s_mov_b32 m0, s78
	s_nop 0
	global_load_lds_dwordx4 v158, s[98:99]
	s_add_u32 s100, s28, s8
	s_addc_u32 s101, s29, s9
	s_add_i32 m0, s78, 0x2000
	s_nop 0
	global_load_lds_dwordx4 v160, s[100:101]
	s_mov_b32 m0, s45
	s_nop 0
	global_load_lds_dwordx4 v162, s[30:31]
	s_mov_b32 m0, s46
	s_nop 0
	global_load_lds_dwordx4 v164, s[30:31]
	s_waitcnt vmcnt(8)
	s_waitcnt lgkmcnt(0)
	s_barrier
; #define PG8_STAGE(bufoff, gbase, voff) do { _Pragma("unroll") for (int _i = 0; _i < 2; ++_i) \
;         __builtin_amdgcn_global_load_lds((const unsigned*)((const char*)(gbase) + (voff)[_i]), (PG8_LAS unsigned*)(lds + (bufoff) + ldsw + _i * 8192), 16, 0, 0); } while (0)
; #define PG8_WAIT_V(n) asm volatile("s_waitcnt vmcnt(" #n ")" ::: "memory")
; #define PG8_WAIT_L(n) asm volatile("s_waitcnt lgkmcnt(" #n ")" ::: "memory")
; template <class Epi, class Sched, bool ALIGN_EPI = true, bool F8 = false>
; __device__ __forceinline__ void gemm_phase(PG8_LAS unsigned char* lds, const Sched& S, const Epi& E) {
;     ...
;         for (int t = 0; t < nt; t += 2) {
;             const bool last = (t == nt - 2);
;             if constexpr (Sched::GATHER) { if (last && has_next) S.a_off(nxt, Rs, Cs, voffAn); }
;             const char* a1 = cA + (size_t)(t + 1) * kstep;
;             const char* a2 = last ? nA : cA + (size_t)(t + 2) * kstep; const char* b2 = last ? nB : cB + (size_t)(t + 2) * kstepB;
;             const char* a3 = a2 + kstep; const char* b3 = b2 + kstepB;
;             unsigned vA2[2][2];
; #pragma unroll
;             for (int h = 0; h < 2; ++h)
; #pragma unroll
;                 for (int i = 0; i < 2; ++i) { if constexpr (Sched::GATHER) vA2[h][i] = (last && has_next) ? voffAn[h][i] : voffA[h][i]; else vA2[h][i] = voffA[h][i]; }
;             PG8_LDB(B0, 0, 0); PG8_LDB(B1, 0, 1); PG8_SCHED; PG8_LDA(At, 0, 0); PG8_STAGE(PG8_SA(1, 1), a1, voffA[1]);
;             PG8_WAIT_V(8); PG8_WAIT_L(0); PG8_BAR; PG8_MMA(0, 0, At, B0); PG8_MMA(0, 1, At, B1); PG8_BAR; PG8_SCHED;
;             PG8_LDA(At, 0, 1); PG8_STAGE(PG8_SB(0, 0), b2, voffB[0]); PG8_STAGE(PG8_SB(0, 1), b2, voffB[1]); PG8_STAGE(PG8_SA(0, 0), a2, vA2[0]);
;             PG8_WAIT_V(8); PG8_WAIT_L(0); PG8_BAR; PG8_MMA(1, 0, At, B0); PG8_MMA(1, 1, At, B1); PG8_BAR; PG8_SCHED;
;             PG8_LDB(B0, 1, 0); PG8_LDB(B1, 1, 1); PG8_SCHED; PG8_LDA(At, 1, 0); PG8_STAGE(PG8_SA(0, 1), a2, vA2[1]);
;             PG8_WAIT_V(8); PG8_WAIT_L(0); PG8_BAR; PG8_MMA(0, 0, At, B0); PG8_MMA(0, 1, At, B1); PG8_BAR; PG8_SCHED;
;             PG8_LDA(At, 1, 1); PG8_STAGE(PG8_SB(1, 0), b3, voffB[0]); PG8_STAGE(PG8_SB(1, 1), b3, voffB[1]); PG8_STAGE(PG8_SA(1, 0), a3, vA2[0]);
;             PG8_WAIT_V(8); PG8_WAIT_L(0); PG8_BAR; PG8_MMA(1, 0, At, B0); PG8_MMA(1, 1, At, B1); PG8_BAR; PG8_SCHED;
	s_setprio 2
	v_mfma_f32_16x16x128_f8f6f4 v[74:77], v[2:9], v[210:217], v[74:77]
	v_mfma_f32_16x16x128_f8f6f4 v[70:73], v[142:149], v[210:217], v[70:73]
	v_mfma_f32_16x16x128_f8f6f4 v[66:69], v[2:9], v[218:225], v[66:69]
	v_mfma_f32_16x16x128_f8f6f4 v[62:65], v[142:149], v[218:225], v[62:65]
	v_mfma_f32_16x16x128_f8f6f4 v[58:61], v[2:9], v[226:233], v[58:61]
	v_mfma_f32_16x16x128_f8f6f4 v[54:57], v[142:149], v[226:233], v[54:57]
	v_mfma_f32_16x16x128_f8f6f4 v[50:53], v[2:9], v[234:241], v[50:53]
	v_mfma_f32_16x16x128_f8f6f4 v[46:49], v[142:149], v[234:241], v[46:49]
	s_nop 3
	v_mfma_f32_16x16x128_f8f6f4 v[42:45], v[150:157], v[210:217], v[42:45]
	v_mfma_f32_16x16x128_f8f6f4 v[38:41], v[202:209], v[210:217], v[38:41]
	v_mfma_f32_16x16x128_f8f6f4 v[34:37], v[150:157], v[218:225], v[34:37]
	v_mfma_f32_16x16x128_f8f6f4 v[30:33], v[202:209], v[218:225], v[30:33]
	v_mfma_f32_16x16x128_f8f6f4 v[26:29], v[150:157], v[226:233], v[26:29]
	v_mfma_f32_16x16x128_f8f6f4 v[22:25], v[202:209], v[226:233], v[22:25]
	v_mfma_f32_16x16x128_f8f6f4 v[18:21], v[150:157], v[234:241], v[18:21]
	v_mfma_f32_16x16x128_f8f6f4 v[14:17], v[202:209], v[234:241], v[14:17]
	s_setprio 0
	s_add_i32 s78, 0, 0x18000
	s_add_i32 s79, 0, 0x1c000
	v_add_u32_e32 v2, s78, v190
	v_add_u32_e32 v10, s79, v190
	ds_read_b128 v[142:145], v2
	ds_read_b128 v[146:149], v2 offset:1024
	ds_read_b128 v[150:153], v2 offset:2048
	ds_read_b128 v[154:157], v2 offset:3072
	ds_read_b128 v[2:5], v10
	ds_read_b128 v[6:9], v10 offset:1024
	ds_read_b128 v[202:205], v10 offset:2048
	ds_read_b128 v[206:209], v10 offset:3072
	s_mov_b32 m0, s47
	ds_read_b128 v[210:213], v198 offset:32768
	ds_read_b128 v[214:217], v198 offset:33792
	ds_read_b128 v[218:221], v198 offset:34816
	ds_read_b128 v[222:225], v198 offset:35840
	ds_read_b128 v[226:229], v198 offset:36864
	ds_read_b128 v[230:233], v198 offset:37888
	ds_read_b128 v[234:237], v198 offset:38912
	ds_read_b128 v[238:241], v198 offset:39936
	global_load_lds_dwordx4 v166, s[30:31]
	s_mov_b32 m0, s48
	s_nop 0
	global_load_lds_dwordx4 v168, s[30:31]
	s_waitcnt vmcnt(8)
	s_waitcnt lgkmcnt(0)
	s_barrier
	s_setprio 2
	v_mfma_f32_16x16x128_f8f6f4 v[138:141], v[142:149], v[210:217], v[138:141]
	v_mfma_f32_16x16x128_f8f6f4 v[134:137], v[150:157], v[210:217], v[134:137]
	v_mfma_f32_16x16x128_f8f6f4 v[130:133], v[142:149], v[218:225], v[130:133]
	v_mfma_f32_16x16x128_f8f6f4 v[126:129], v[150:157], v[218:225], v[126:129]
	v_mfma_f32_16x16x128_f8f6f4 v[122:125], v[142:149], v[226:233], v[122:125]
	v_mfma_f32_16x16x128_f8f6f4 v[118:121], v[150:157], v[226:233], v[118:121]
	v_mfma_f32_16x16x128_f8f6f4 v[114:117], v[142:149], v[234:241], v[114:117]
	v_mfma_f32_16x16x128_f8f6f4 v[110:113], v[150:157], v[234:241], v[110:113]
	s_nop 3
	v_mfma_f32_16x16x128_f8f6f4 v[106:109], v[2:9], v[210:217], v[106:109]
	v_mfma_f32_16x16x128_f8f6f4 v[102:105], v[202:209], v[210:217], v[102:105]
	v_mfma_f32_16x16x128_f8f6f4 v[98:101], v[2:9], v[218:225], v[98:101]
	v_mfma_f32_16x16x128_f8f6f4 v[94:97], v[202:209], v[218:225], v[94:97]
	v_mfma_f32_16x16x128_f8f6f4 v[90:93], v[2:9], v[226:233], v[90:93]
	v_mfma_f32_16x16x128_f8f6f4 v[86:89], v[202:209], v[226:233], v[86:89]
	v_mfma_f32_16x16x128_f8f6f4 v[82:85], v[2:9], v[234:241], v[82:85]
	v_mfma_f32_16x16x128_f8f6f4 v[78:81], v[202:209], v[234:241], v[78:81]
	s_setprio 0
	s_add_u32 s28, s28, 0x8000
	s_addc_u32 s29, s29, 0
	s_add_i32 s30, s78, s44
	s_mov_b32 m0, s30
	ds_read_b128 v[210:213], v198 offset:49152
	ds_read_b128 v[214:217], v198 offset:50176
	ds_read_b128 v[218:221], v198 offset:51200
	ds_read_b128 v[222:225], v198 offset:52224
	ds_read_b128 v[226:229], v198 offset:53248
	ds_read_b128 v[230:233], v198 offset:54272
	ds_read_b128 v[234:237], v198 offset:55296
	ds_read_b128 v[238:241], v198 offset:56320
	global_load_lds_dwordx4 v158, s[28:29]
	s_add_i32 m0, s30, 0x2000
	s_add_i32 s30, s79, s44
	global_load_lds_dwordx4 v160, s[28:29]
	s_mov_b32 m0, s30
	s_nop 0
	global_load_lds_dwordx4 v172, s[28:29]
	s_add_i32 m0, s30, 0x2000
	s_nop 0
	global_load_lds_dwordx4 v174, s[28:29]
	s_mov_b32 m0, s50
	s_nop 0
	global_load_lds_dwordx4 v162, s[26:27]
	s_mov_b32 m0, s51
	s_nop 0
	global_load_lds_dwordx4 v164, s[26:27]
	s_waitcnt vmcnt(8)
	s_waitcnt lgkmcnt(0)
	s_barrier
	s_setprio 2
	v_mfma_f32_16x16x128_f8f6f4 v[74:77], v[142:149], v[210:217], v[74:77]
	v_mfma_f32_16x16x128_f8f6f4 v[70:73], v[150:157], v[210:217], v[70:73]
	v_mfma_f32_16x16x128_f8f6f4 v[66:69], v[142:149], v[218:225], v[66:69]
	v_mfma_f32_16x16x128_f8f6f4 v[62:65], v[150:157], v[218:225], v[62:65]
	v_mfma_f32_16x16x128_f8f6f4 v[58:61], v[142:149], v[226:233], v[58:61]
	v_mfma_f32_16x16x128_f8f6f4 v[54:57], v[150:157], v[226:233], v[54:57]
	v_mfma_f32_16x16x128_f8f6f4 v[50:53], v[142:149], v[234:241], v[50:53]
	v_mfma_f32_16x16x128_f8f6f4 v[46:49], v[150:157], v[234:241], v[46:49]
	s_nop 3
	v_mfma_f32_16x16x128_f8f6f4 v[42:45], v[2:9], v[210:217], v[42:45]
	v_mfma_f32_16x16x128_f8f6f4 v[38:41], v[202:209], v[210:217], v[38:41]
	v_mfma_f32_16x16x128_f8f6f4 v[34:37], v[2:9], v[218:225], v[34:37]
	v_mfma_f32_16x16x128_f8f6f4 v[30:33], v[202:209], v[218:225], v[30:33]
	v_mfma_f32_16x16x128_f8f6f4 v[26:29], v[2:9], v[226:233], v[26:29]
	v_mfma_f32_16x16x128_f8f6f4 v[22:25], v[202:209], v[226:233], v[22:25]
	v_mfma_f32_16x16x128_f8f6f4 v[18:21], v[2:9], v[234:241], v[18:21]
	v_mfma_f32_16x16x128_f8f6f4 v[14:17], v[202:209], v[234:241], v[14:17]
	s_setprio 0
	s_add_u32 s75, s75, 0x10000
	s_addc_u32 s76, s76, 0
	s_add_u32 s24, s24, 0x10000
	s_addc_u32 s25, s25, 0
	s_cmp_ge_i32 s77, s72
	s_mov_b32 s26, s77
	s_cbranch_scc0 .Lh1_834

; #define PG8_STAGE(bufoff, gbase, voff) do { _Pragma("unroll") for (int _i = 0; _i < 2; ++_i) \
;         __builtin_amdgcn_global_load_lds((const unsigned*)((const char*)(gbase) + (voff)[_i]), (PG8_LAS unsigned*)(lds + (bufoff) + ldsw + _i * 8192), 16, 0, 0); } while (0)
; #define PG8_WAIT_V(n) asm volatile("s_waitcnt vmcnt(" #n ")" ::: "memory")
; #define PG8_WAIT_L(n) asm volatile("s_waitcnt lgkmcnt(" #n ")" ::: "memory")
; template <class Epi, class Sched, bool ALIGN_EPI = true, bool F8 = false>
; __device__ __forceinline__ void gemm_phase(PG8_LAS unsigned char* lds, const Sched& S, const Epi& E) {
;     ...
;         for (int t = 0; t < nt; t += 2) {
;             const bool last = (t == nt - 2);
;             if constexpr (Sched::GATHER) { if (last && has_next) S.a_off(nxt, Rs, Cs, voffAn); }
;             const char* a1 = cA + (size_t)(t + 1) * kstep;
;             const char* a2 = last ? nA : cA + (size_t)(t + 2) * kstep; const char* b2 = last ? nB : cB + (size_t)(t + 2) * kstepB;
;             const char* a3 = a2 + kstep; const char* b3 = b2 + kstepB;
;             unsigned vA2[2][2];
; #pragma unroll
;             for (int h = 0; h < 2; ++h)
; #pragma unroll
;                 for (int i = 0; i < 2; ++i) { if constexpr (Sched::GATHER) vA2[h][i] = (last && has_next) ? voffAn[h][i] : voffA[h][i]; else vA2[h][i] = voffA[h][i]; }
;             PG8_LDB(B0, 0, 0); PG8_LDB(B1, 0, 1); PG8_SCHED; PG8_LDA(At, 0, 0); PG8_STAGE(PG8_SA(1, 1), a1, voffA[1]);
;             PG8_WAIT_V(8); PG8_WAIT_L(0); PG8_BAR; PG8_MMA(0, 0, At, B0); PG8_MMA(0, 1, At, B1); PG8_BAR; PG8_SCHED;
;             PG8_LDA(At, 0, 1); PG8_STAGE(PG8_SB(0, 0), b2, voffB[0]); PG8_STAGE(PG8_SB(0, 1), b2, voffB[1]); PG8_STAGE(PG8_SA(0, 0), a2, vA2[0]);
;             PG8_WAIT_V(8); PG8_WAIT_L(0); PG8_BAR; PG8_MMA(1, 0, At, B0); PG8_MMA(1, 1, At, B1); PG8_BAR; PG8_SCHED;
;             PG8_LDB(B0, 1, 0); PG8_LDB(B1, 1, 1); PG8_SCHED; PG8_LDA(At, 1, 0); PG8_STAGE(PG8_SA(0, 1), a2, vA2[1]);
;             PG8_WAIT_V(8); PG8_WAIT_L(0); PG8_BAR; PG8_MMA(0, 0, At, B0); PG8_MMA(0, 1, At, B1); PG8_BAR; PG8_SCHED;
;             PG8_LDA(At, 1, 1); PG8_STAGE(PG8_SB(1, 0), b3, voffB[0]); PG8_STAGE(PG8_SB(1, 1), b3, voffB[1]); PG8_STAGE(PG8_SA(1, 0), a3, vA2[0]);
;             PG8_WAIT_V(8); PG8_WAIT_L(0); PG8_BAR; PG8_MMA(1, 0, At, B0); PG8_MMA(1, 1, At, B1); PG8_BAR; PG8_SCHED;
.Lpk0_911:
	ds_read_b128 v[18:21], v191
	ds_read_b128 v[22:25], v191 offset:1024
	ds_read_b128 v[26:29], v191 offset:2048
	ds_read_b128 v[30:33], v191 offset:3072
	ds_read_b128 v[2:5], v192
	ds_read_b128 v[6:9], v192 offset:1024
	ds_read_b128 v[10:13], v192 offset:2048
	ds_read_b128 v[14:17], v192 offset:3072
	s_add_u32 s30, s28, 0x8000
	s_addc_u32 s31, s29, 0
	s_cmp_eq_u32 s65, 12
	s_cselect_b32 s42, s22, s30
	s_cselect_b32 s43, s23, s31
	s_cselect_b32 s40, s24, s19
	s_cselect_b32 s41, s25, s21
	s_add_u32 s30, s42, 0x8000
	s_addc_u32 s31, s43, 0
	s_add_i32 m0, s27, 0xc000
	ds_read_b128 v[196:199], v193
	ds_read_b128 v[200:203], v193 offset:1024
	ds_read_b128 v[204:207], v193 offset:2048
	ds_read_b128 v[208:211], v193 offset:3072
	ds_read_b128 v[212:215], v193 offset:4096
	ds_read_b128 v[216:219], v193 offset:5120
	ds_read_b128 v[220:223], v193 offset:6144
	ds_read_b128 v[224:227], v193 offset:7168
	global_load_lds_dwordx4 v182, s[28:29]
	s_add_i32 m0, s27, 0xe000
	s_nop 0
	global_load_lds_dwordx4 v180, s[28:29]
	s_waitcnt vmcnt(8)
	s_waitcnt lgkmcnt(0)
	s_setprio 1
	v_mfma_f32_16x16x128_f8f6f4 v[158:161], v[18:25], v[196:203], 0
	v_mfma_f32_16x16x128_f8f6f4 v[154:157], v[26:33], v[196:203], 0
	v_mfma_f32_16x16x128_f8f6f4 v[150:153], v[18:25], v[204:211], 0
	v_mfma_f32_16x16x128_f8f6f4 v[146:149], v[26:33], v[204:211], 0
	v_mfma_f32_16x16x128_f8f6f4 v[130:133], v[18:25], v[212:219], 0
	v_mfma_f32_16x16x128_f8f6f4 v[122:125], v[26:33], v[212:219], 0
	v_mfma_f32_16x16x128_f8f6f4 v[114:117], v[18:25], v[220:227], 0
	v_mfma_f32_16x16x128_f8f6f4 v[106:109], v[26:33], v[220:227], 0
	s_nop 3
	v_mfma_f32_16x16x128_f8f6f4 v[142:145], v[2:9], v[196:203], 0
	v_mfma_f32_16x16x128_f8f6f4 v[138:141], v[10:17], v[196:203], 0
	v_mfma_f32_16x16x128_f8f6f4 v[134:137], v[2:9], v[204:211], 0
	v_mfma_f32_16x16x128_f8f6f4 v[126:129], v[10:17], v[204:211], 0
	v_mfma_f32_16x16x128_f8f6f4 v[118:121], v[2:9], v[212:219], 0
	v_mfma_f32_16x16x128_f8f6f4 v[110:113], v[10:17], v[212:219], 0
	v_mfma_f32_16x16x128_f8f6f4 v[102:105], v[2:9], v[220:227], 0
	v_mfma_f32_16x16x128_f8f6f4 v[98:101], v[10:17], v[220:227], 0
	s_setprio 0
	s_barrier
	s_add_i32 s66, s60, s48
	s_mov_b32 m0, s66
	ds_read_b128 v[196:199], v193 offset:16384
	ds_read_b128 v[200:203], v193 offset:17408
	ds_read_b128 v[204:207], v193 offset:18432
	ds_read_b128 v[208:211], v193 offset:19456
	ds_read_b128 v[212:215], v193 offset:20480
	ds_read_b128 v[216:219], v193 offset:21504
	ds_read_b128 v[220:223], v193 offset:22528
	ds_read_b128 v[224:227], v193 offset:23552
	global_load_lds_dwordx4 v162, s[40:41]
	s_add_i32 m0, s66, 0x2000
	s_add_i32 s66, s61, s48
	global_load_lds_dwordx4 v164, s[40:41]
	s_add_u32 s98, s40, s6
	s_addc_u32 s99, s41, s7
	s_mov_b32 m0, s66
	s_nop 0
	global_load_lds_dwordx4 v162, s[98:99]
	s_add_u32 s100, s40, s6
	s_addc_u32 s101, s41, s7
	s_add_i32 m0, s66, 0x2000
	s_nop 0
	global_load_lds_dwordx4 v164, s[100:101]
	s_mov_b32 m0, s27
	s_nop 0
	global_load_lds_dwordx4 v166, s[42:43]
	s_mov_b32 m0, s49
	s_nop 0
	global_load_lds_dwordx4 v168, s[42:43]
	s_waitcnt vmcnt(8)
	s_waitcnt lgkmcnt(0)
	s_setprio 1
	v_mfma_f32_16x16x128_f8f6f4 v[94:97], v[18:25], v[196:203], 0
	v_mfma_f32_16x16x128_f8f6f4 v[90:93], v[26:33], v[196:203], 0
	v_mfma_f32_16x16x128_f8f6f4 v[82:85], v[18:25], v[204:211], 0
	v_mfma_f32_16x16x128_f8f6f4 v[74:77], v[26:33], v[204:211], 0
	v_mfma_f32_16x16x128_f8f6f4 v[66:69], v[18:25], v[212:219], 0
	v_mfma_f32_16x16x128_f8f6f4 v[58:61], v[26:33], v[212:219], 0
	v_mfma_f32_16x16x128_f8f6f4 v[50:53], v[18:25], v[220:227], 0
	v_mfma_f32_16x16x128_f8f6f4 v[42:45], v[26:33], v[220:227], 0
	s_nop 3
	v_mfma_f32_16x16x128_f8f6f4 v[86:89], v[2:9], v[196:203], 0
	v_mfma_f32_16x16x128_f8f6f4 v[78:81], v[10:17], v[196:203], 0
	v_mfma_f32_16x16x128_f8f6f4 v[70:73], v[2:9], v[204:211], 0
	v_mfma_f32_16x16x128_f8f6f4 v[62:65], v[10:17], v[204:211], 0
	v_mfma_f32_16x16x128_f8f6f4 v[54:57], v[2:9], v[212:219], 0
	v_mfma_f32_16x16x128_f8f6f4 v[46:49], v[10:17], v[212:219], 0
	v_mfma_f32_16x16x128_f8f6f4 v[38:41], v[2:9], v[220:227], 0
	v_mfma_f32_16x16x128_f8f6f4 v[34:37], v[10:17], v[220:227], 0
	s_setprio 0
	s_barrier
	s_add_i32 s66, 0, 0x18000
	s_add_i32 s67, 0, 0x1c000
	v_add_u32_e32 v14, s66, v189
	v_add_u32_e32 v30, s67, v189
	ds_read_b128 v[2:5], v14
	ds_read_b128 v[6:9], v14 offset:1024
	ds_read_b128 v[10:13], v14 offset:2048
	ds_read_b128 v[14:17], v14 offset:3072
	ds_read_b128 v[18:21], v30
	ds_read_b128 v[22:25], v30 offset:1024
	ds_read_b128 v[26:29], v30 offset:2048
	ds_read_b128 v[30:33], v30 offset:3072
	s_mov_b32 m0, s50
	ds_read_b128 v[196:199], v193 offset:32768
	ds_read_b128 v[200:203], v193 offset:33792
	ds_read_b128 v[204:207], v193 offset:34816
	ds_read_b128 v[208:211], v193 offset:35840
	ds_read_b128 v[212:215], v193 offset:36864
	ds_read_b128 v[216:219], v193 offset:37888
	ds_read_b128 v[220:223], v193 offset:38912
	ds_read_b128 v[224:227], v193 offset:39936
	global_load_lds_dwordx4 v172, s[42:43]
	s_mov_b32 m0, s51
	s_nop 0
	global_load_lds_dwordx4 v174, s[42:43]
	s_waitcnt vmcnt(8)
	s_waitcnt lgkmcnt(0)
	s_setprio 1
	v_mfma_f32_16x16x128_f8f6f4 v[158:161], v[2:9], v[196:203], v[158:161]
	v_mfma_f32_16x16x128_f8f6f4 v[154:157], v[10:17], v[196:203], v[154:157]
	v_mfma_f32_16x16x128_f8f6f4 v[150:153], v[2:9], v[204:211], v[150:153]
	v_mfma_f32_16x16x128_f8f6f4 v[146:149], v[10:17], v[204:211], v[146:149]
	v_mfma_f32_16x16x128_f8f6f4 v[130:133], v[2:9], v[212:219], v[130:133]
	v_mfma_f32_16x16x128_f8f6f4 v[122:125], v[10:17], v[212:219], v[122:125]
	v_mfma_f32_16x16x128_f8f6f4 v[114:117], v[2:9], v[220:227], v[114:117]
	v_mfma_f32_16x16x128_f8f6f4 v[106:109], v[10:17], v[220:227], v[106:109]
	s_nop 3
	v_mfma_f32_16x16x128_f8f6f4 v[142:145], v[18:25], v[196:203], v[142:145]
	v_mfma_f32_16x16x128_f8f6f4 v[138:141], v[26:33], v[196:203], v[138:141]
	v_mfma_f32_16x16x128_f8f6f4 v[134:137], v[18:25], v[204:211], v[134:137]
	v_mfma_f32_16x16x128_f8f6f4 v[126:129], v[26:33], v[204:211], v[126:129]
	v_mfma_f32_16x16x128_f8f6f4 v[118:121], v[18:25], v[212:219], v[118:121]
	v_mfma_f32_16x16x128_f8f6f4 v[110:113], v[26:33], v[212:219], v[110:113]
	v_mfma_f32_16x16x128_f8f6f4 v[102:105], v[18:25], v[220:227], v[102:105]
	v_mfma_f32_16x16x128_f8f6f4 v[98:101], v[26:33], v[220:227], v[98:101]
	s_setprio 0
	s_barrier
; #define PG8_STAGE(bufoff, gbase, voff) do { _Pragma("unroll") for (int _i = 0; _i < 2; ++_i) \
;         __builtin_amdgcn_global_load_lds((const unsigned*)((const char*)(gbase) + (voff)[_i]), (PG8_LAS unsigned*)(lds + (bufoff) + ldsw + _i * 8192), 16, 0, 0); } while (0)
; #define PG8_WAIT_V(n) asm volatile("s_waitcnt vmcnt(" #n ")" ::: "memory")
; #define PG8_WAIT_L(n) asm volatile("s_waitcnt lgkmcnt(" #n ")" ::: "memory")
; template <class Epi, class Sched, bool ALIGN_EPI = true, bool F8 = false>
; __device__ __forceinline__ void gemm_phase(PG8_LAS unsigned char* lds, const Sched& S, const Epi& E) {
;     ...
;         for (int t = 0; t < nt; t += 2) {
;             const bool last = (t == nt - 2);
;             if constexpr (Sched::GATHER) { if (last && has_next) S.a_off(nxt, Rs, Cs, voffAn); }
;             const char* a1 = cA + (size_t)(t + 1) * kstep;
;             const char* a2 = last ? nA : cA + (size_t)(t + 2) * kstep; const char* b2 = last ? nB : cB + (size_t)(t + 2) * kstepB;
;             const char* a3 = a2 + kstep; const char* b3 = b2 + kstepB;
;             unsigned vA2[2][2];
; #pragma unroll
;             for (int h = 0; h < 2; ++h)
; #pragma unroll
;                 for (int i = 0; i < 2; ++i) { if constexpr (Sched::GATHER) vA2[h][i] = (last && has_next) ? voffAn[h][i] : voffA[h][i]; else vA2[h][i] = voffA[h][i]; }
;             PG8_LDB(B0, 0, 0); PG8_LDB(B1, 0, 1); PG8_SCHED; PG8_LDA(At, 0, 0); PG8_STAGE(PG8_SA(1, 1), a1, voffA[1]);
;             PG8_WAIT_V(8); PG8_WAIT_L(0); PG8_BAR; PG8_MMA(0, 0, At, B0); PG8_MMA(0, 1, At, B1); PG8_BAR; PG8_SCHED;
;             PG8_LDA(At, 0, 1); PG8_STAGE(PG8_SB(0, 0), b2, voffB[0]); PG8_STAGE(PG8_SB(0, 1), b2, voffB[1]); PG8_STAGE(PG8_SA(0, 0), a2, vA2[0]);
;             PG8_WAIT_V(8); PG8_WAIT_L(0); PG8_BAR; PG8_MMA(1, 0, At, B0); PG8_MMA(1, 1, At, B1); PG8_BAR; PG8_SCHED;
;             PG8_LDB(B0, 1, 0); PG8_LDB(B1, 1, 1); PG8_SCHED; PG8_LDA(At, 1, 0); PG8_STAGE(PG8_SA(0, 1), a2, vA2[1]);
;             PG8_WAIT_V(8); PG8_WAIT_L(0); PG8_BAR; PG8_MMA(0, 0, At, B0); PG8_MMA(0, 1, At, B1); PG8_BAR; PG8_SCHED;
;             PG8_LDA(At, 1, 1); PG8_STAGE(PG8_SB(1, 0), b3, voffB[0]); PG8_STAGE(PG8_SB(1, 1), b3, voffB[1]); PG8_STAGE(PG8_SA(1, 0), a3, vA2[0]);
;             PG8_WAIT_V(8); PG8_WAIT_L(0); PG8_BAR; PG8_MMA(1, 0, At, B0); PG8_MMA(1, 1, At, B1); PG8_BAR; PG8_SCHED;
	s_add_u32 s40, s40, 0x8000
	s_addc_u32 s41, s41, 0
	s_add_i32 s42, s66, s48
	s_mov_b32 m0, s42
	ds_read_b128 v[196:199], v193 offset:49152
	ds_read_b128 v[200:203], v193 offset:50176
	ds_read_b128 v[204:207], v193 offset:51200
	ds_read_b128 v[208:211], v193 offset:52224
	ds_read_b128 v[212:215], v193 offset:53248
	ds_read_b128 v[216:219], v193 offset:54272
	ds_read_b128 v[220:223], v193 offset:55296
	ds_read_b128 v[224:227], v193 offset:56320
	global_load_lds_dwordx4 v162, s[40:41]
	s_add_i32 m0, s42, 0x2000
	s_add_i32 s42, s67, s48
	global_load_lds_dwordx4 v164, s[40:41]
	s_mov_b32 m0, s42
	s_nop 0
	global_load_lds_dwordx4 v176, s[40:41]
	s_add_i32 m0, s42, 0x2000
	s_nop 0
	global_load_lds_dwordx4 v178, s[40:41]
	s_mov_b32 m0, s53
	s_nop 0
	global_load_lds_dwordx4 v166, s[30:31]
	s_mov_b32 m0, s58
	s_nop 0
	global_load_lds_dwordx4 v168, s[30:31]
	s_waitcnt vmcnt(8)
	s_waitcnt lgkmcnt(0)
	s_setprio 1
	v_mfma_f32_16x16x128_f8f6f4 v[94:97], v[2:9], v[196:203], v[94:97]
	v_mfma_f32_16x16x128_f8f6f4 v[90:93], v[10:17], v[196:203], v[90:93]
	v_mfma_f32_16x16x128_f8f6f4 v[82:85], v[2:9], v[204:211], v[82:85]
	v_mfma_f32_16x16x128_f8f6f4 v[74:77], v[10:17], v[204:211], v[74:77]
	v_mfma_f32_16x16x128_f8f6f4 v[66:69], v[2:9], v[212:219], v[66:69]
	v_mfma_f32_16x16x128_f8f6f4 v[58:61], v[10:17], v[212:219], v[58:61]
	v_mfma_f32_16x16x128_f8f6f4 v[50:53], v[2:9], v[220:227], v[50:53]
	v_mfma_f32_16x16x128_f8f6f4 v[42:45], v[10:17], v[220:227], v[42:45]
	s_nop 3
	v_mfma_f32_16x16x128_f8f6f4 v[86:89], v[18:25], v[196:203], v[86:89]
	v_mfma_f32_16x16x128_f8f6f4 v[78:81], v[26:33], v[196:203], v[78:81]
	v_mfma_f32_16x16x128_f8f6f4 v[70:73], v[18:25], v[204:211], v[70:73]
	v_mfma_f32_16x16x128_f8f6f4 v[62:65], v[26:33], v[204:211], v[62:65]
	v_mfma_f32_16x16x128_f8f6f4 v[54:57], v[18:25], v[212:219], v[54:57]
	v_mfma_f32_16x16x128_f8f6f4 v[46:49], v[26:33], v[212:219], v[46:49]
	v_mfma_f32_16x16x128_f8f6f4 v[38:41], v[18:25], v[220:227], v[38:41]
	v_mfma_f32_16x16x128_f8f6f4 v[34:37], v[26:33], v[220:227], v[34:37]
	s_setprio 0
	s_barrier
	s_add_i32 s65, s65, 2
	s_add_u32 s19, s19, 0x10000
	s_addc_u32 s21, s21, 0
	s_add_u32 s28, s28, 0x10000
	s_addc_u32 s29, s29, 0
	s_cmp_gt_u32 s65, 13
	s_cbranch_scc0 .LBB0_911
	s_branch .Lfx_26630
.LBB0_911:
	ds_read_b128 v[18:21], v191
	ds_read_b128 v[22:25], v191 offset:1024
	ds_read_b128 v[26:29], v191 offset:2048
	ds_read_b128 v[30:33], v191 offset:3072
	ds_read_b128 v[2:5], v192
	ds_read_b128 v[6:9], v192 offset:1024
	ds_read_b128 v[10:13], v192 offset:2048
	ds_read_b128 v[14:17], v192 offset:3072
	s_add_u32 s30, s28, 0x8000
	s_addc_u32 s31, s29, 0
	s_cmp_eq_u32 s65, 12
	s_cselect_b32 s42, s22, s30
	s_cselect_b32 s43, s23, s31
	s_cselect_b32 s40, s24, s19
	s_cselect_b32 s41, s25, s21
	s_add_u32 s30, s42, 0x8000
	s_addc_u32 s31, s43, 0
	s_add_i32 m0, s27, 0xc000
	ds_read_b128 v[196:199], v193
	ds_read_b128 v[200:203], v193 offset:1024
	ds_read_b128 v[204:207], v193 offset:2048
	ds_read_b128 v[208:211], v193 offset:3072
	ds_read_b128 v[212:215], v193 offset:4096
	ds_read_b128 v[216:219], v193 offset:5120
	ds_read_b128 v[220:223], v193 offset:6144
	ds_read_b128 v[224:227], v193 offset:7168
	global_load_lds_dwordx4 v182, s[28:29]
	s_add_i32 m0, s27, 0xe000
	s_nop 0
	global_load_lds_dwordx4 v180, s[28:29]
	s_waitcnt vmcnt(8)
	s_waitcnt lgkmcnt(0)
	s_setprio 1
	v_mfma_f32_16x16x128_f8f6f4 v[158:161], v[18:25], v[196:203], v[158:161]
	v_mfma_f32_16x16x128_f8f6f4 v[154:157], v[26:33], v[196:203], v[154:157]
	v_mfma_f32_16x16x128_f8f6f4 v[150:153], v[18:25], v[204:211], v[150:153]
	v_mfma_f32_16x16x128_f8f6f4 v[146:149], v[26:33], v[204:211], v[146:149]
	v_mfma_f32_16x16x128_f8f6f4 v[130:133], v[18:25], v[212:219], v[130:133]
	v_mfma_f32_16x16x128_f8f6f4 v[122:125], v[26:33], v[212:219], v[122:125]
	v_mfma_f32_16x16x128_f8f6f4 v[114:117], v[18:25], v[220:227], v[114:117]
	v_mfma_f32_16x16x128_f8f6f4 v[106:109], v[26:33], v[220:227], v[106:109]
	s_nop 3
	v_mfma_f32_16x16x128_f8f6f4 v[142:145], v[2:9], v[196:203], v[142:145]
	v_mfma_f32_16x16x128_f8f6f4 v[138:141], v[10:17], v[196:203], v[138:141]
	v_mfma_f32_16x16x128_f8f6f4 v[134:137], v[2:9], v[204:211], v[134:137]
	v_mfma_f32_16x16x128_f8f6f4 v[126:129], v[10:17], v[204:211], v[126:129]
	v_mfma_f32_16x16x128_f8f6f4 v[118:121], v[2:9], v[212:219], v[118:121]
	v_mfma_f32_16x16x128_f8f6f4 v[110:113], v[10:17], v[212:219], v[110:113]
	v_mfma_f32_16x16x128_f8f6f4 v[102:105], v[2:9], v[220:227], v[102:105]
	v_mfma_f32_16x16x128_f8f6f4 v[98:101], v[10:17], v[220:227], v[98:101]
	s_setprio 0
	s_barrier
	s_add_i32 s66, s60, s48
	s_mov_b32 m0, s66
	ds_read_b128 v[196:199], v193 offset:16384
	ds_read_b128 v[200:203], v193 offset:17408
	ds_read_b128 v[204:207], v193 offset:18432
	ds_read_b128 v[208:211], v193 offset:19456
	ds_read_b128 v[212:215], v193 offset:20480
	ds_read_b128 v[216:219], v193 offset:21504
	ds_read_b128 v[220:223], v193 offset:22528
	ds_read_b128 v[224:227], v193 offset:23552
	global_load_lds_dwordx4 v162, s[40:41]
	s_add_i32 m0, s66, 0x2000
	s_add_i32 s66, s61, s48
	global_load_lds_dwordx4 v164, s[40:41]
	s_add_u32 s98, s40, s6
	s_addc_u32 s99, s41, s7
	s_mov_b32 m0, s66
	s_nop 0
	global_load_lds_dwordx4 v162, s[98:99]
	s_add_u32 s100, s40, s6
	s_addc_u32 s101, s41, s7
	s_add_i32 m0, s66, 0x2000
	s_nop 0
	global_load_lds_dwordx4 v164, s[100:101]
	s_mov_b32 m0, s27
	s_nop 0
	global_load_lds_dwordx4 v166, s[42:43]
	s_mov_b32 m0, s49
	s_nop 0
	global_load_lds_dwordx4 v168, s[42:43]
	s_waitcnt vmcnt(8)
	s_waitcnt lgkmcnt(0)
	s_setprio 1
	v_mfma_f32_16x16x128_f8f6f4 v[94:97], v[18:25], v[196:203], v[94:97]
	v_mfma_f32_16x16x128_f8f6f4 v[90:93], v[26:33], v[196:203], v[90:93]
	v_mfma_f32_16x16x128_f8f6f4 v[82:85], v[18:25], v[204:211], v[82:85]
	v_mfma_f32_16x16x128_f8f6f4 v[74:77], v[26:33], v[204:211], v[74:77]
	v_mfma_f32_16x16x128_f8f6f4 v[66:69], v[18:25], v[212:219], v[66:69]
	v_mfma_f32_16x16x128_f8f6f4 v[58:61], v[26:33], v[212:219], v[58:61]
	v_mfma_f32_16x16x128_f8f6f4 v[50:53], v[18:25], v[220:227], v[50:53]
	v_mfma_f32_16x16x128_f8f6f4 v[42:45], v[26:33], v[220:227], v[42:45]
	s_nop 3
	v_mfma_f32_16x16x128_f8f6f4 v[86:89], v[2:9], v[196:203], v[86:89]
	v_mfma_f32_16x16x128_f8f6f4 v[78:81], v[10:17], v[196:203], v[78:81]
	v_mfma_f32_16x16x128_f8f6f4 v[70:73], v[2:9], v[204:211], v[70:73]
	v_mfma_f32_16x16x128_f8f6f4 v[62:65], v[10:17], v[204:211], v[62:65]
	v_mfma_f32_16x16x128_f8f6f4 v[54:57], v[2:9], v[212:219], v[54:57]
	v_mfma_f32_16x16x128_f8f6f4 v[46:49], v[10:17], v[212:219], v[46:49]
	v_mfma_f32_16x16x128_f8f6f4 v[38:41], v[2:9], v[220:227], v[38:41]
	v_mfma_f32_16x16x128_f8f6f4 v[34:37], v[10:17], v[220:227], v[34:37]
	s_setprio 0
	s_barrier
; #define PG8_STAGE(bufoff, gbase, voff) do { _Pragma("unroll") for (int _i = 0; _i < 2; ++_i) \
;         __builtin_amdgcn_global_load_lds((const unsigned*)((const char*)(gbase) + (voff)[_i]), (PG8_LAS unsigned*)(lds + (bufoff) + ldsw + _i * 8192), 16, 0, 0); } while (0)
; #define PG8_WAIT_V(n) asm volatile("s_waitcnt vmcnt(" #n ")" ::: "memory")
; #define PG8_WAIT_L(n) asm volatile("s_waitcnt lgkmcnt(" #n ")" ::: "memory")
; template <class Epi, class Sched, bool ALIGN_EPI = true, bool F8 = false>
; __device__ __forceinline__ void gemm_phase(PG8_LAS unsigned char* lds, const Sched& S, const Epi& E) {
;     ...
;         for (int t = 0; t < nt; t += 2) {
;             const bool last = (t == nt - 2);
;             if constexpr (Sched::GATHER) { if (last && has_next) S.a_off(nxt, Rs, Cs, voffAn); }
;             const char* a1 = cA + (size_t)(t + 1) * kstep;
;             const char* a2 = last ? nA : cA + (size_t)(t + 2) * kstep; const char* b2 = last ? nB : cB + (size_t)(t + 2) * kstepB;
;             const char* a3 = a2 + kstep; const char* b3 = b2 + kstepB;
;             unsigned vA2[2][2];
; #pragma unroll
;             for (int h = 0; h < 2; ++h)
; #pragma unroll
;                 for (int i = 0; i < 2; ++i) { if constexpr (Sched::GATHER) vA2[h][i] = (last && has_next) ? voffAn[h][i] : voffA[h][i]; else vA2[h][i] = voffA[h][i]; }
;             PG8_LDB(B0, 0, 0); PG8_LDB(B1, 0, 1); PG8_SCHED; PG8_LDA(At, 0, 0); PG8_STAGE(PG8_SA(1, 1), a1, voffA[1]);
;             PG8_WAIT_V(8); PG8_WAIT_L(0); PG8_BAR; PG8_MMA(0, 0, At, B0); PG8_MMA(0, 1, At, B1); PG8_BAR; PG8_SCHED;
;             PG8_LDA(At, 0, 1); PG8_STAGE(PG8_SB(0, 0), b2, voffB[0]); PG8_STAGE(PG8_SB(0, 1), b2, voffB[1]); PG8_STAGE(PG8_SA(0, 0), a2, vA2[0]);
;             PG8_WAIT_V(8); PG8_WAIT_L(0); PG8_BAR; PG8_MMA(1, 0, At, B0); PG8_MMA(1, 1, At, B1); PG8_BAR; PG8_SCHED;
;             PG8_LDB(B0, 1, 0); PG8_LDB(B1, 1, 1); PG8_SCHED; PG8_LDA(At, 1, 0); PG8_STAGE(PG8_SA(0, 1), a2, vA2[1]);
;             PG8_WAIT_V(8); PG8_WAIT_L(0); PG8_BAR; PG8_MMA(0, 0, At, B0); PG8_MMA(0, 1, At, B1); PG8_BAR; PG8_SCHED;
;             PG8_LDA(At, 1, 1); PG8_STAGE(PG8_SB(1, 0), b3, voffB[0]); PG8_STAGE(PG8_SB(1, 1), b3, voffB[1]); PG8_STAGE(PG8_SA(1, 0), a3, vA2[0]);
;             PG8_WAIT_V(8); PG8_WAIT_L(0); PG8_BAR; PG8_MMA(1, 0, At, B0); PG8_MMA(1, 1, At, B1); PG8_BAR; PG8_SCHED;
	s_add_i32 s66, 0, 0x18000
	s_add_i32 s67, 0, 0x1c000
	v_add_u32_e32 v14, s66, v189
	v_add_u32_e32 v30, s67, v189
	ds_read_b128 v[2:5], v14
	ds_read_b128 v[6:9], v14 offset:1024
	ds_read_b128 v[10:13], v14 offset:2048
	ds_read_b128 v[14:17], v14 offset:3072
	ds_read_b128 v[18:21], v30
	ds_read_b128 v[22:25], v30 offset:1024
	ds_read_b128 v[26:29], v30 offset:2048
	ds_read_b128 v[30:33], v30 offset:3072
	s_mov_b32 m0, s50
	ds_read_b128 v[196:199], v193 offset:32768
	ds_read_b128 v[200:203], v193 offset:33792
	ds_read_b128 v[204:207], v193 offset:34816
	ds_read_b128 v[208:211], v193 offset:35840
	ds_read_b128 v[212:215], v193 offset:36864
	ds_read_b128 v[216:219], v193 offset:37888
	ds_read_b128 v[220:223], v193 offset:38912
	ds_read_b128 v[224:227], v193 offset:39936
	global_load_lds_dwordx4 v172, s[42:43]
	s_mov_b32 m0, s51
	s_nop 0
	global_load_lds_dwordx4 v174, s[42:43]
	s_waitcnt vmcnt(8)
	s_waitcnt lgkmcnt(0)
	s_setprio 1
	v_mfma_f32_16x16x128_f8f6f4 v[158:161], v[2:9], v[196:203], v[158:161]
	v_mfma_f32_16x16x128_f8f6f4 v[154:157], v[10:17], v[196:203], v[154:157]
	v_mfma_f32_16x16x128_f8f6f4 v[150:153], v[2:9], v[204:211], v[150:153]
	v_mfma_f32_16x16x128_f8f6f4 v[146:149], v[10:17], v[204:211], v[146:149]
	v_mfma_f32_16x16x128_f8f6f4 v[130:133], v[2:9], v[212:219], v[130:133]
	v_mfma_f32_16x16x128_f8f6f4 v[122:125], v[10:17], v[212:219], v[122:125]
	v_mfma_f32_16x16x128_f8f6f4 v[114:117], v[2:9], v[220:227], v[114:117]
	v_mfma_f32_16x16x128_f8f6f4 v[106:109], v[10:17], v[220:227], v[106:109]
	s_nop 3
	v_mfma_f32_16x16x128_f8f6f4 v[142:145], v[18:25], v[196:203], v[142:145]
	v_mfma_f32_16x16x128_f8f6f4 v[138:141], v[26:33], v[196:203], v[138:141]
	v_mfma_f32_16x16x128_f8f6f4 v[134:137], v[18:25], v[204:211], v[134:137]
	v_mfma_f32_16x16x128_f8f6f4 v[126:129], v[26:33], v[204:211], v[126:129]
	v_mfma_f32_16x16x128_f8f6f4 v[118:121], v[18:25], v[212:219], v[118:121]
	v_mfma_f32_16x16x128_f8f6f4 v[110:113], v[26:33], v[212:219], v[110:113]
	v_mfma_f32_16x16x128_f8f6f4 v[102:105], v[18:25], v[220:227], v[102:105]
	v_mfma_f32_16x16x128_f8f6f4 v[98:101], v[26:33], v[220:227], v[98:101]
	s_setprio 0
	s_barrier
	s_add_u32 s40, s40, 0x8000
	s_addc_u32 s41, s41, 0
	s_add_i32 s42, s66, s48
	s_mov_b32 m0, s42
	ds_read_b128 v[196:199], v193 offset:49152
	ds_read_b128 v[200:203], v193 offset:50176
	ds_read_b128 v[204:207], v193 offset:51200
	ds_read_b128 v[208:211], v193 offset:52224
	ds_read_b128 v[212:215], v193 offset:53248
	ds_read_b128 v[216:219], v193 offset:54272
	ds_read_b128 v[220:223], v193 offset:55296
	ds_read_b128 v[224:227], v193 offset:56320
	global_load_lds_dwordx4 v162, s[40:41]
	s_add_i32 m0, s42, 0x2000
	s_add_i32 s42, s67, s48
	global_load_lds_dwordx4 v164, s[40:41]
	s_mov_b32 m0, s42
	s_nop 0
	global_load_lds_dwordx4 v176, s[40:41]
	s_add_i32 m0, s42, 0x2000
	s_nop 0
	global_load_lds_dwordx4 v178, s[40:41]
	s_mov_b32 m0, s53
	s_nop 0
	global_load_lds_dwordx4 v166, s[30:31]
	s_mov_b32 m0, s58
	s_nop 0
	global_load_lds_dwordx4 v168, s[30:31]
	s_waitcnt vmcnt(8)
	s_waitcnt lgkmcnt(0)
	s_setprio 1
	v_mfma_f32_16x16x128_f8f6f4 v[94:97], v[2:9], v[196:203], v[94:97]
	v_mfma_f32_16x16x128_f8f6f4 v[90:93], v[10:17], v[196:203], v[90:93]
	v_mfma_f32_16x16x128_f8f6f4 v[82:85], v[2:9], v[204:211], v[82:85]
	v_mfma_f32_16x16x128_f8f6f4 v[74:77], v[10:17], v[204:211], v[74:77]
	v_mfma_f32_16x16x128_f8f6f4 v[66:69], v[2:9], v[212:219], v[66:69]
	v_mfma_f32_16x16x128_f8f6f4 v[58:61], v[10:17], v[212:219], v[58:61]
	v_mfma_f32_16x16x128_f8f6f4 v[50:53], v[2:9], v[220:227], v[50:53]
	v_mfma_f32_16x16x128_f8f6f4 v[42:45], v[10:17], v[220:227], v[42:45]
	s_nop 3
	v_mfma_f32_16x16x128_f8f6f4 v[86:89], v[18:25], v[196:203], v[86:89]
	v_mfma_f32_16x16x128_f8f6f4 v[78:81], v[26:33], v[196:203], v[78:81]
	v_mfma_f32_16x16x128_f8f6f4 v[70:73], v[18:25], v[204:211], v[70:73]
	v_mfma_f32_16x16x128_f8f6f4 v[62:65], v[26:33], v[204:211], v[62:65]
	v_mfma_f32_16x16x128_f8f6f4 v[54:57], v[18:25], v[212:219], v[54:57]
	v_mfma_f32_16x16x128_f8f6f4 v[46:49], v[26:33], v[212:219], v[46:49]
	v_mfma_f32_16x16x128_f8f6f4 v[38:41], v[18:25], v[220:227], v[38:41]
	v_mfma_f32_16x16x128_f8f6f4 v[34:37], v[26:33], v[220:227], v[34:37]
	s_setprio 0
	s_barrier
	s_add_i32 s65, s65, 2
	s_add_u32 s19, s19, 0x10000
	s_addc_u32 s21, s21, 0
	s_add_u32 s28, s28, 0x10000
	s_addc_u32 s29, s29, 0
	s_cmp_gt_u32 s65, 13
	s_cbranch_scc0 .LBB0_911
	s_branch .Lfx_26630
; #define PG8_STAGE(bufoff, gbase, voff) do { _Pragma("unroll") for (int _i = 0; _i < 2; ++_i) \
;         __builtin_amdgcn_global_load_lds((const unsigned*)((const char*)(gbase) + (voff)[_i]), (PG8_LAS unsigned*)(lds + (bufoff) + ldsw + _i * 8192), 16, 0, 0); } while (0)
; #define PG8_WAIT_V(n) asm volatile("s_waitcnt vmcnt(" #n ")" ::: "memory")
; #define PG8_WAIT_L(n) asm volatile("s_waitcnt lgkmcnt(" #n ")" ::: "memory")
; template <class Epi, class Sched, bool ALIGN_EPI = true, bool F8 = false>
; __device__ __forceinline__ void gemm_phase(PG8_LAS unsigned char* lds, const Sched& S, const Epi& E) {
;     ...
;         for (int t = 0; t < nt; t += 2) {
;             const bool last = (t == nt - 2);
;             if constexpr (Sched::GATHER) { if (last && has_next) S.a_off(nxt, Rs, Cs, voffAn); }
;             const char* a1 = cA + (size_t)(t + 1) * kstep;
;             const char* a2 = last ? nA : cA + (size_t)(t + 2) * kstep; const char* b2 = last ? nB : cB + (size_t)(t + 2) * kstepB;
;             const char* a3 = a2 + kstep; const char* b3 = b2 + kstepB;
;             unsigned vA2[2][2];
; #pragma unroll
;             for (int h = 0; h < 2; ++h)
; #pragma unroll
;                 for (int i = 0; i < 2; ++i) { if constexpr (Sched::GATHER) vA2[h][i] = (last && has_next) ? voffAn[h][i] : voffA[h][i]; else vA2[h][i] = voffA[h][i]; }
;             PG8_LDB(B0, 0, 0); PG8_LDB(B1, 0, 1); PG8_SCHED; PG8_LDA(At, 0, 0); PG8_STAGE(PG8_SA(1, 1), a1, voffA[1]);
;             PG8_WAIT_V(8); PG8_WAIT_L(0); PG8_BAR; PG8_MMA(0, 0, At, B0); PG8_MMA(0, 1, At, B1); PG8_BAR; PG8_SCHED;
;             PG8_LDA(At, 0, 1); PG8_STAGE(PG8_SB(0, 0), b2, voffB[0]); PG8_STAGE(PG8_SB(0, 1), b2, voffB[1]); PG8_STAGE(PG8_SA(0, 0), a2, vA2[0]);
;             PG8_WAIT_V(8); PG8_WAIT_L(0); PG8_BAR; PG8_MMA(1, 0, At, B0); PG8_MMA(1, 1, At, B1); PG8_BAR; PG8_SCHED;
;             PG8_LDB(B0, 1, 0); PG8_LDB(B1, 1, 1); PG8_SCHED; PG8_LDA(At, 1, 0); PG8_STAGE(PG8_SA(0, 1), a2, vA2[1]);
;             PG8_WAIT_V(8); PG8_WAIT_L(0); PG8_BAR; PG8_MMA(0, 0, At, B0); PG8_MMA(0, 1, At, B1); PG8_BAR; PG8_SCHED;
;             PG8_LDA(At, 1, 1); PG8_STAGE(PG8_SB(1, 0), b3, voffB[0]); PG8_STAGE(PG8_SB(1, 1), b3, voffB[1]); PG8_STAGE(PG8_SA(1, 0), a3, vA2[0]);
;             PG8_WAIT_V(8); PG8_WAIT_L(0); PG8_BAR; PG8_MMA(1, 0, At, B0); PG8_MMA(1, 1, At, B1); PG8_BAR; PG8_SCHED;
.Lh1e_26630:
.Lpk1_911:
	ds_read_b128 v[18:21], v191
	ds_read_b128 v[22:25], v191 offset:1024
	ds_read_b128 v[26:29], v191 offset:2048
	ds_read_b128 v[30:33], v191 offset:3072
	ds_read_b128 v[2:5], v192
	ds_read_b128 v[6:9], v192 offset:1024
	ds_read_b128 v[10:13], v192 offset:2048
	ds_read_b128 v[14:17], v192 offset:3072
	s_add_u32 s30, s28, 0x8000
	s_addc_u32 s31, s29, 0
	s_cmp_eq_u32 s65, 12
	s_cselect_b32 s42, s22, s30
	s_cselect_b32 s43, s23, s31
	s_cselect_b32 s40, s24, s19
	s_cselect_b32 s41, s25, s21
	s_add_u32 s30, s42, 0x8000
	s_addc_u32 s31, s43, 0
	s_add_i32 m0, s27, 0xc000
	ds_read_b128 v[196:199], v193
	ds_read_b128 v[200:203], v193 offset:1024
	ds_read_b128 v[204:207], v193 offset:2048
	ds_read_b128 v[208:211], v193 offset:3072
	ds_read_b128 v[212:215], v193 offset:4096
	ds_read_b128 v[216:219], v193 offset:5120
	ds_read_b128 v[220:223], v193 offset:6144
	ds_read_b128 v[224:227], v193 offset:7168
	global_load_lds_dwordx4 v182, s[28:29]
	s_add_i32 m0, s27, 0xe000
	s_nop 0
	global_load_lds_dwordx4 v180, s[28:29]
	s_waitcnt vmcnt(8)
	s_waitcnt lgkmcnt(0)
	s_barrier
	s_setprio 2
	v_mfma_f32_16x16x128_f8f6f4 v[158:161], v[18:25], v[196:203], 0
	v_mfma_f32_16x16x128_f8f6f4 v[154:157], v[26:33], v[196:203], 0
	v_mfma_f32_16x16x128_f8f6f4 v[150:153], v[18:25], v[204:211], 0
	v_mfma_f32_16x16x128_f8f6f4 v[146:149], v[26:33], v[204:211], 0
	v_mfma_f32_16x16x128_f8f6f4 v[130:133], v[18:25], v[212:219], 0
	v_mfma_f32_16x16x128_f8f6f4 v[122:125], v[26:33], v[212:219], 0
	v_mfma_f32_16x16x128_f8f6f4 v[114:117], v[18:25], v[220:227], 0
	v_mfma_f32_16x16x128_f8f6f4 v[106:109], v[26:33], v[220:227], 0
	s_nop 3
	v_mfma_f32_16x16x128_f8f6f4 v[142:145], v[2:9], v[196:203], 0
	v_mfma_f32_16x16x128_f8f6f4 v[138:141], v[10:17], v[196:203], 0
	v_mfma_f32_16x16x128_f8f6f4 v[134:137], v[2:9], v[204:211], 0
	v_mfma_f32_16x16x128_f8f6f4 v[126:129], v[10:17], v[204:211], 0
	v_mfma_f32_16x16x128_f8f6f4 v[118:121], v[2:9], v[212:219], 0
	v_mfma_f32_16x16x128_f8f6f4 v[110:113], v[10:17], v[212:219], 0
	v_mfma_f32_16x16x128_f8f6f4 v[102:105], v[2:9], v[220:227], 0
	v_mfma_f32_16x16x128_f8f6f4 v[98:101], v[10:17], v[220:227], 0
	s_setprio 0
	s_add_i32 s66, s60, s48
	s_mov_b32 m0, s66
	ds_read_b128 v[196:199], v193 offset:16384
	ds_read_b128 v[200:203], v193 offset:17408
	ds_read_b128 v[204:207], v193 offset:18432
	ds_read_b128 v[208:211], v193 offset:19456
	ds_read_b128 v[212:215], v193 offset:20480
	ds_read_b128 v[216:219], v193 offset:21504
	ds_read_b128 v[220:223], v193 offset:22528
	ds_read_b128 v[224:227], v193 offset:23552
	global_load_lds_dwordx4 v162, s[40:41]
	s_add_i32 m0, s66, 0x2000
	s_add_i32 s66, s61, s48
	global_load_lds_dwordx4 v164, s[40:41]
	s_add_u32 s98, s40, s6
	s_addc_u32 s99, s41, s7
	s_mov_b32 m0, s66
	s_nop 0
	global_load_lds_dwordx4 v162, s[98:99]
	s_add_u32 s100, s40, s6
	s_addc_u32 s101, s41, s7
	s_add_i32 m0, s66, 0x2000
	s_nop 0
	global_load_lds_dwordx4 v164, s[100:101]
	s_mov_b32 m0, s27
	s_nop 0
	global_load_lds_dwordx4 v166, s[42:43]
	s_mov_b32 m0, s49
	s_nop 0
	global_load_lds_dwordx4 v168, s[42:43]
	s_waitcnt vmcnt(8)
	s_waitcnt lgkmcnt(0)
	s_barrier
	s_setprio 2
	v_mfma_f32_16x16x128_f8f6f4 v[94:97], v[18:25], v[196:203], 0
	v_mfma_f32_16x16x128_f8f6f4 v[90:93], v[26:33], v[196:203], 0
	v_mfma_f32_16x16x128_f8f6f4 v[82:85], v[18:25], v[204:211], 0
	v_mfma_f32_16x16x128_f8f6f4 v[74:77], v[26:33], v[204:211], 0
	v_mfma_f32_16x16x128_f8f6f4 v[66:69], v[18:25], v[212:219], 0
	v_mfma_f32_16x16x128_f8f6f4 v[58:61], v[26:33], v[212:219], 0
	v_mfma_f32_16x16x128_f8f6f4 v[50:53], v[18:25], v[220:227], 0
	v_mfma_f32_16x16x128_f8f6f4 v[42:45], v[26:33], v[220:227], 0
	s_nop 3
	v_mfma_f32_16x16x128_f8f6f4 v[86:89], v[2:9], v[196:203], 0
	v_mfma_f32_16x16x128_f8f6f4 v[78:81], v[10:17], v[196:203], 0
	v_mfma_f32_16x16x128_f8f6f4 v[70:73], v[2:9], v[204:211], 0
	v_mfma_f32_16x16x128_f8f6f4 v[62:65], v[10:17], v[204:211], 0
	v_mfma_f32_16x16x128_f8f6f4 v[54:57], v[2:9], v[212:219], 0
	v_mfma_f32_16x16x128_f8f6f4 v[46:49], v[10:17], v[212:219], 0
	v_mfma_f32_16x16x128_f8f6f4 v[38:41], v[2:9], v[220:227], 0
	v_mfma_f32_16x16x128_f8f6f4 v[34:37], v[10:17], v[220:227], 0
	s_setprio 0
	s_add_i32 s66, 0, 0x18000
	s_add_i32 s67, 0, 0x1c000
	v_add_u32_e32 v14, s66, v189
	v_add_u32_e32 v30, s67, v189
	ds_read_b128 v[2:5], v14
	ds_read_b128 v[6:9], v14 offset:1024
	ds_read_b128 v[10:13], v14 offset:2048
	ds_read_b128 v[14:17], v14 offset:3072
	ds_read_b128 v[18:21], v30
	ds_read_b128 v[22:25], v30 offset:1024
	ds_read_b128 v[26:29], v30 offset:2048
	ds_read_b128 v[30:33], v30 offset:3072
	s_mov_b32 m0, s50
	ds_read_b128 v[196:199], v193 offset:32768
	ds_read_b128 v[200:203], v193 offset:33792
	ds_read_b128 v[204:207], v193 offset:34816
	ds_read_b128 v[208:211], v193 offset:35840
	ds_read_b128 v[212:215], v193 offset:36864
	ds_read_b128 v[216:219], v193 offset:37888
	ds_read_b128 v[220:223], v193 offset:38912
	ds_read_b128 v[224:227], v193 offset:39936
	global_load_lds_dwordx4 v172, s[42:43]
	s_mov_b32 m0, s51
	s_nop 0
	global_load_lds_dwordx4 v174, s[42:43]
	s_waitcnt vmcnt(8)
	s_waitcnt lgkmcnt(0)
	s_barrier
; #define PG8_STAGE(bufoff, gbase, voff) do { _Pragma("unroll") for (int _i = 0; _i < 2; ++_i) \
;         __builtin_amdgcn_global_load_lds((const unsigned*)((const char*)(gbase) + (voff)[_i]), (PG8_LAS unsigned*)(lds + (bufoff) + ldsw + _i * 8192), 16, 0, 0); } while (0)
; #define PG8_WAIT_V(n) asm volatile("s_waitcnt vmcnt(" #n ")" ::: "memory")
; #define PG8_WAIT_L(n) asm volatile("s_waitcnt lgkmcnt(" #n ")" ::: "memory")
; template <class Epi, class Sched, bool ALIGN_EPI = true, bool F8 = false>
; __device__ __forceinline__ void gemm_phase(PG8_LAS unsigned char* lds, const Sched& S, const Epi& E) {
;     ...
;         for (int t = 0; t < nt; t += 2) {
;             const bool last = (t == nt - 2);
;             if constexpr (Sched::GATHER) { if (last && has_next) S.a_off(nxt, Rs, Cs, voffAn); }
;             const char* a1 = cA + (size_t)(t + 1) * kstep;
;             const char* a2 = last ? nA : cA + (size_t)(t + 2) * kstep; const char* b2 = last ? nB : cB + (size_t)(t + 2) * kstepB;
;             const char* a3 = a2 + kstep; const char* b3 = b2 + kstepB;
;             unsigned vA2[2][2];
; #pragma unroll
;             for (int h = 0; h < 2; ++h)
; #pragma unroll
;                 for (int i = 0; i < 2; ++i) { if constexpr (Sched::GATHER) vA2[h][i] = (last && has_next) ? voffAn[h][i] : voffA[h][i]; else vA2[h][i] = voffA[h][i]; }
;             PG8_LDB(B0, 0, 0); PG8_LDB(B1, 0, 1); PG8_SCHED; PG8_LDA(At, 0, 0); PG8_STAGE(PG8_SA(1, 1), a1, voffA[1]);
;             PG8_WAIT_V(8); PG8_WAIT_L(0); PG8_BAR; PG8_MMA(0, 0, At, B0); PG8_MMA(0, 1, At, B1); PG8_BAR; PG8_SCHED;
;             PG8_LDA(At, 0, 1); PG8_STAGE(PG8_SB(0, 0), b2, voffB[0]); PG8_STAGE(PG8_SB(0, 1), b2, voffB[1]); PG8_STAGE(PG8_SA(0, 0), a2, vA2[0]);
;             PG8_WAIT_V(8); PG8_WAIT_L(0); PG8_BAR; PG8_MMA(1, 0, At, B0); PG8_MMA(1, 1, At, B1); PG8_BAR; PG8_SCHED;
;             PG8_LDB(B0, 1, 0); PG8_LDB(B1, 1, 1); PG8_SCHED; PG8_LDA(At, 1, 0); PG8_STAGE(PG8_SA(0, 1), a2, vA2[1]);
;             PG8_WAIT_V(8); PG8_WAIT_L(0); PG8_BAR; PG8_MMA(0, 0, At, B0); PG8_MMA(0, 1, At, B1); PG8_BAR; PG8_SCHED;
;             PG8_LDA(At, 1, 1); PG8_STAGE(PG8_SB(1, 0), b3, voffB[0]); PG8_STAGE(PG8_SB(1, 1), b3, voffB[1]); PG8_STAGE(PG8_SA(1, 0), a3, vA2[0]);
;             PG8_WAIT_V(8); PG8_WAIT_L(0); PG8_BAR; PG8_MMA(1, 0, At, B0); PG8_MMA(1, 1, At, B1); PG8_BAR; PG8_SCHED;
	s_setprio 2
	v_mfma_f32_16x16x128_f8f6f4 v[158:161], v[2:9], v[196:203], v[158:161]
	v_mfma_f32_16x16x128_f8f6f4 v[154:157], v[10:17], v[196:203], v[154:157]
	v_mfma_f32_16x16x128_f8f6f4 v[150:153], v[2:9], v[204:211], v[150:153]
	v_mfma_f32_16x16x128_f8f6f4 v[146:149], v[10:17], v[204:211], v[146:149]
	v_mfma_f32_16x16x128_f8f6f4 v[130:133], v[2:9], v[212:219], v[130:133]
	v_mfma_f32_16x16x128_f8f6f4 v[122:125], v[10:17], v[212:219], v[122:125]
	v_mfma_f32_16x16x128_f8f6f4 v[114:117], v[2:9], v[220:227], v[114:117]
	v_mfma_f32_16x16x128_f8f6f4 v[106:109], v[10:17], v[220:227], v[106:109]
	s_nop 3
	v_mfma_f32_16x16x128_f8f6f4 v[142:145], v[18:25], v[196:203], v[142:145]
	v_mfma_f32_16x16x128_f8f6f4 v[138:141], v[26:33], v[196:203], v[138:141]
	v_mfma_f32_16x16x128_f8f6f4 v[134:137], v[18:25], v[204:211], v[134:137]
	v_mfma_f32_16x16x128_f8f6f4 v[126:129], v[26:33], v[204:211], v[126:129]
	v_mfma_f32_16x16x128_f8f6f4 v[118:121], v[18:25], v[212:219], v[118:121]
	v_mfma_f32_16x16x128_f8f6f4 v[110:113], v[26:33], v[212:219], v[110:113]
	v_mfma_f32_16x16x128_f8f6f4 v[102:105], v[18:25], v[220:227], v[102:105]
	v_mfma_f32_16x16x128_f8f6f4 v[98:101], v[26:33], v[220:227], v[98:101]
	s_setprio 0
	s_add_u32 s40, s40, 0x8000
	s_addc_u32 s41, s41, 0
	s_add_i32 s42, s66, s48
	s_mov_b32 m0, s42
	ds_read_b128 v[196:199], v193 offset:49152
	ds_read_b128 v[200:203], v193 offset:50176
	ds_read_b128 v[204:207], v193 offset:51200
	ds_read_b128 v[208:211], v193 offset:52224
	ds_read_b128 v[212:215], v193 offset:53248
	ds_read_b128 v[216:219], v193 offset:54272
	ds_read_b128 v[220:223], v193 offset:55296
	ds_read_b128 v[224:227], v193 offset:56320
	global_load_lds_dwordx4 v162, s[40:41]
	s_add_i32 m0, s42, 0x2000
	s_add_i32 s42, s67, s48
	global_load_lds_dwordx4 v164, s[40:41]
	s_mov_b32 m0, s42
	s_nop 0
	global_load_lds_dwordx4 v176, s[40:41]
	s_add_i32 m0, s42, 0x2000
	s_nop 0
	global_load_lds_dwordx4 v178, s[40:41]
	s_mov_b32 m0, s53
	s_nop 0
	global_load_lds_dwordx4 v166, s[30:31]
	s_mov_b32 m0, s58
	s_nop 0
	global_load_lds_dwordx4 v168, s[30:31]
	s_waitcnt vmcnt(8)
	s_waitcnt lgkmcnt(0)
	s_barrier
	s_setprio 2
	v_mfma_f32_16x16x128_f8f6f4 v[94:97], v[2:9], v[196:203], v[94:97]
	v_mfma_f32_16x16x128_f8f6f4 v[90:93], v[10:17], v[196:203], v[90:93]
	v_mfma_f32_16x16x128_f8f6f4 v[82:85], v[2:9], v[204:211], v[82:85]
	v_mfma_f32_16x16x128_f8f6f4 v[74:77], v[10:17], v[204:211], v[74:77]
	v_mfma_f32_16x16x128_f8f6f4 v[66:69], v[2:9], v[212:219], v[66:69]
	v_mfma_f32_16x16x128_f8f6f4 v[58:61], v[10:17], v[212:219], v[58:61]
	v_mfma_f32_16x16x128_f8f6f4 v[50:53], v[2:9], v[220:227], v[50:53]
	v_mfma_f32_16x16x128_f8f6f4 v[42:45], v[10:17], v[220:227], v[42:45]
	s_nop 3
	v_mfma_f32_16x16x128_f8f6f4 v[86:89], v[18:25], v[196:203], v[86:89]
	v_mfma_f32_16x16x128_f8f6f4 v[78:81], v[26:33], v[196:203], v[78:81]
	v_mfma_f32_16x16x128_f8f6f4 v[70:73], v[18:25], v[204:211], v[70:73]
	v_mfma_f32_16x16x128_f8f6f4 v[62:65], v[26:33], v[204:211], v[62:65]
	v_mfma_f32_16x16x128_f8f6f4 v[54:57], v[18:25], v[212:219], v[54:57]
	v_mfma_f32_16x16x128_f8f6f4 v[46:49], v[26:33], v[212:219], v[46:49]
	v_mfma_f32_16x16x128_f8f6f4 v[38:41], v[18:25], v[220:227], v[38:41]
	v_mfma_f32_16x16x128_f8f6f4 v[34:37], v[26:33], v[220:227], v[34:37]
	s_setprio 0
	s_add_i32 s65, s65, 2
	s_add_u32 s19, s19, 0x10000
	s_addc_u32 s21, s21, 0
	s_add_u32 s28, s28, 0x10000
	s_addc_u32 s29, s29, 0
	s_cmp_gt_u32 s65, 13
	s_cbranch_scc0 .Lh1_911
	s_branch .Lfx_26630
.Lh1_911:
	ds_read_b128 v[18:21], v191
	ds_read_b128 v[22:25], v191 offset:1024
	ds_read_b128 v[26:29], v191 offset:2048
	ds_read_b128 v[30:33], v191 offset:3072
	ds_read_b128 v[2:5], v192
	ds_read_b128 v[6:9], v192 offset:1024
	ds_read_b128 v[10:13], v192 offset:2048
	ds_read_b128 v[14:17], v192 offset:3072
	s_add_u32 s30, s28, 0x8000
	s_addc_u32 s31, s29, 0
	s_cmp_eq_u32 s65, 12
	s_cselect_b32 s42, s22, s30
	s_cselect_b32 s43, s23, s31
	s_cselect_b32 s40, s24, s19
	s_cselect_b32 s41, s25, s21
	s_add_u32 s30, s42, 0x8000
	s_addc_u32 s31, s43, 0
	s_add_i32 m0, s27, 0xc000
	ds_read_b128 v[196:199], v193
	ds_read_b128 v[200:203], v193 offset:1024
	ds_read_b128 v[204:207], v193 offset:2048
	ds_read_b128 v[208:211], v193 offset:3072
	ds_read_b128 v[212:215], v193 offset:4096
	ds_read_b128 v[216:219], v193 offset:5120
	ds_read_b128 v[220:223], v193 offset:6144
	ds_read_b128 v[224:227], v193 offset:7168
	global_load_lds_dwordx4 v182, s[28:29]
	s_add_i32 m0, s27, 0xe000
	s_nop 0
	global_load_lds_dwordx4 v180, s[28:29]
	s_waitcnt vmcnt(8)
	s_waitcnt lgkmcnt(0)
	s_barrier
	s_setprio 2
	v_mfma_f32_16x16x128_f8f6f4 v[158:161], v[18:25], v[196:203], v[158:161]
	v_mfma_f32_16x16x128_f8f6f4 v[154:157], v[26:33], v[196:203], v[154:157]
	v_mfma_f32_16x16x128_f8f6f4 v[150:153], v[18:25], v[204:211], v[150:153]
	v_mfma_f32_16x16x128_f8f6f4 v[146:149], v[26:33], v[204:211], v[146:149]
	v_mfma_f32_16x16x128_f8f6f4 v[130:133], v[18:25], v[212:219], v[130:133]
	v_mfma_f32_16x16x128_f8f6f4 v[122:125], v[26:33], v[212:219], v[122:125]
	v_mfma_f32_16x16x128_f8f6f4 v[114:117], v[18:25], v[220:227], v[114:117]
	v_mfma_f32_16x16x128_f8f6f4 v[106:109], v[26:33], v[220:227], v[106:109]
	s_nop 3
	v_mfma_f32_16x16x128_f8f6f4 v[142:145], v[2:9], v[196:203], v[142:145]
	v_mfma_f32_16x16x128_f8f6f4 v[138:141], v[10:17], v[196:203], v[138:141]
	v_mfma_f32_16x16x128_f8f6f4 v[134:137], v[2:9], v[204:211], v[134:137]
	v_mfma_f32_16x16x128_f8f6f4 v[126:129], v[10:17], v[204:211], v[126:129]
	v_mfma_f32_16x16x128_f8f6f4 v[118:121], v[2:9], v[212:219], v[118:121]
	v_mfma_f32_16x16x128_f8f6f4 v[110:113], v[10:17], v[212:219], v[110:113]
	v_mfma_f32_16x16x128_f8f6f4 v[102:105], v[2:9], v[220:227], v[102:105]
	v_mfma_f32_16x16x128_f8f6f4 v[98:101], v[10:17], v[220:227], v[98:101]
	s_setprio 0
	s_add_i32 s66, s60, s48
	s_mov_b32 m0, s66
	ds_read_b128 v[196:199], v193 offset:16384
	ds_read_b128 v[200:203], v193 offset:17408
	ds_read_b128 v[204:207], v193 offset:18432
	ds_read_b128 v[208:211], v193 offset:19456
	ds_read_b128 v[212:215], v193 offset:20480
	ds_read_b128 v[216:219], v193 offset:21504
	ds_read_b128 v[220:223], v193 offset:22528
	ds_read_b128 v[224:227], v193 offset:23552
	global_load_lds_dwordx4 v162, s[40:41]
	s_add_i32 m0, s66, 0x2000
	s_add_i32 s66, s61, s48
	global_load_lds_dwordx4 v164, s[40:41]
	s_add_u32 s98, s40, s6
	s_addc_u32 s99, s41, s7
	s_mov_b32 m0, s66
	s_nop 0
	global_load_lds_dwordx4 v162, s[98:99]
	s_add_u32 s100, s40, s6
	s_addc_u32 s101, s41, s7
	s_add_i32 m0, s66, 0x2000
	s_nop 0
	global_load_lds_dwordx4 v164, s[100:101]
	s_mov_b32 m0, s27
	s_nop 0
	global_load_lds_dwordx4 v166, s[42:43]
	s_mov_b32 m0, s49
	s_nop 0
	global_load_lds_dwordx4 v168, s[42:43]
	s_waitcnt vmcnt(8)
	s_waitcnt lgkmcnt(0)
	s_barrier
; #define PG8_STAGE(bufoff, gbase, voff) do { _Pragma("unroll") for (int _i = 0; _i < 2; ++_i) \
;         __builtin_amdgcn_global_load_lds((const unsigned*)((const char*)(gbase) + (voff)[_i]), (PG8_LAS unsigned*)(lds + (bufoff) + ldsw + _i * 8192), 16, 0, 0); } while (0)
; #define PG8_WAIT_V(n) asm volatile("s_waitcnt vmcnt(" #n ")" ::: "memory")
; #define PG8_WAIT_L(n) asm volatile("s_waitcnt lgkmcnt(" #n ")" ::: "memory")
; template <class Epi, class Sched, bool ALIGN_EPI = true, bool F8 = false>
; __device__ __forceinline__ void gemm_phase(PG8_LAS unsigned char* lds, const Sched& S, const Epi& E) {
;     ...
;         for (int t = 0; t < nt; t += 2) {
;             const bool last = (t == nt - 2);
;             if constexpr (Sched::GATHER) { if (last && has_next) S.a_off(nxt, Rs, Cs, voffAn); }
;             const char* a1 = cA + (size_t)(t + 1) * kstep;
;             const char* a2 = last ? nA : cA + (size_t)(t + 2) * kstep; const char* b2 = last ? nB : cB + (size_t)(t + 2) * kstepB;
;             const char* a3 = a2 + kstep; const char* b3 = b2 + kstepB;
;             unsigned vA2[2][2];
; #pragma unroll
;             for (int h = 0; h < 2; ++h)
; #pragma unroll
;                 for (int i = 0; i < 2; ++i) { if constexpr (Sched::GATHER) vA2[h][i] = (last && has_next) ? voffAn[h][i] : voffA[h][i]; else vA2[h][i] = voffA[h][i]; }
;             PG8_LDB(B0, 0, 0); PG8_LDB(B1, 0, 1); PG8_SCHED; PG8_LDA(At, 0, 0); PG8_STAGE(PG8_SA(1, 1), a1, voffA[1]);
;             PG8_WAIT_V(8); PG8_WAIT_L(0); PG8_BAR; PG8_MMA(0, 0, At, B0); PG8_MMA(0, 1, At, B1); PG8_BAR; PG8_SCHED;
;             PG8_LDA(At, 0, 1); PG8_STAGE(PG8_SB(0, 0), b2, voffB[0]); PG8_STAGE(PG8_SB(0, 1), b2, voffB[1]); PG8_STAGE(PG8_SA(0, 0), a2, vA2[0]);
;             PG8_WAIT_V(8); PG8_WAIT_L(0); PG8_BAR; PG8_MMA(1, 0, At, B0); PG8_MMA(1, 1, At, B1); PG8_BAR; PG8_SCHED;
;             PG8_LDB(B0, 1, 0); PG8_LDB(B1, 1, 1); PG8_SCHED; PG8_LDA(At, 1, 0); PG8_STAGE(PG8_SA(0, 1), a2, vA2[1]);
;             PG8_WAIT_V(8); PG8_WAIT_L(0); PG8_BAR; PG8_MMA(0, 0, At, B0); PG8_MMA(0, 1, At, B1); PG8_BAR; PG8_SCHED;
;             PG8_LDA(At, 1, 1); PG8_STAGE(PG8_SB(1, 0), b3, voffB[0]); PG8_STAGE(PG8_SB(1, 1), b3, voffB[1]); PG8_STAGE(PG8_SA(1, 0), a3, vA2[0]);
;             PG8_WAIT_V(8); PG8_WAIT_L(0); PG8_BAR; PG8_MMA(1, 0, At, B0); PG8_MMA(1, 1, At, B1); PG8_BAR; PG8_SCHED;
	s_setprio 2
	v_mfma_f32_16x16x128_f8f6f4 v[94:97], v[18:25], v[196:203], v[94:97]
	v_mfma_f32_16x16x128_f8f6f4 v[90:93], v[26:33], v[196:203], v[90:93]
	v_mfma_f32_16x16x128_f8f6f4 v[82:85], v[18:25], v[204:211], v[82:85]
	v_mfma_f32_16x16x128_f8f6f4 v[74:77], v[26:33], v[204:211], v[74:77]
	v_mfma_f32_16x16x128_f8f6f4 v[66:69], v[18:25], v[212:219], v[66:69]
	v_mfma_f32_16x16x128_f8f6f4 v[58:61], v[26:33], v[212:219], v[58:61]
	v_mfma_f32_16x16x128_f8f6f4 v[50:53], v[18:25], v[220:227], v[50:53]
	v_mfma_f32_16x16x128_f8f6f4 v[42:45], v[26:33], v[220:227], v[42:45]
	s_nop 3
	v_mfma_f32_16x16x128_f8f6f4 v[86:89], v[2:9], v[196:203], v[86:89]
	v_mfma_f32_16x16x128_f8f6f4 v[78:81], v[10:17], v[196:203], v[78:81]
	v_mfma_f32_16x16x128_f8f6f4 v[70:73], v[2:9], v[204:211], v[70:73]
	v_mfma_f32_16x16x128_f8f6f4 v[62:65], v[10:17], v[204:211], v[62:65]
	v_mfma_f32_16x16x128_f8f6f4 v[54:57], v[2:9], v[212:219], v[54:57]
	v_mfma_f32_16x16x128_f8f6f4 v[46:49], v[10:17], v[212:219], v[46:49]
	v_mfma_f32_16x16x128_f8f6f4 v[38:41], v[2:9], v[220:227], v[38:41]
	v_mfma_f32_16x16x128_f8f6f4 v[34:37], v[10:17], v[220:227], v[34:37]
	s_setprio 0
	s_add_i32 s66, 0, 0x18000
	s_add_i32 s67, 0, 0x1c000
	v_add_u32_e32 v14, s66, v189
	v_add_u32_e32 v30, s67, v189
	ds_read_b128 v[2:5], v14
	ds_read_b128 v[6:9], v14 offset:1024
	ds_read_b128 v[10:13], v14 offset:2048
	ds_read_b128 v[14:17], v14 offset:3072
	ds_read_b128 v[18:21], v30
	ds_read_b128 v[22:25], v30 offset:1024
	ds_read_b128 v[26:29], v30 offset:2048
	ds_read_b128 v[30:33], v30 offset:3072
	s_mov_b32 m0, s50
	ds_read_b128 v[196:199], v193 offset:32768
	ds_read_b128 v[200:203], v193 offset:33792
	ds_read_b128 v[204:207], v193 offset:34816
	ds_read_b128 v[208:211], v193 offset:35840
	ds_read_b128 v[212:215], v193 offset:36864
	ds_read_b128 v[216:219], v193 offset:37888
	ds_read_b128 v[220:223], v193 offset:38912
	ds_read_b128 v[224:227], v193 offset:39936
	global_load_lds_dwordx4 v172, s[42:43]
	s_mov_b32 m0, s51
	s_nop 0
	global_load_lds_dwordx4 v174, s[42:43]
	s_waitcnt vmcnt(8)
	s_waitcnt lgkmcnt(0)
	s_barrier
	s_setprio 2
	v_mfma_f32_16x16x128_f8f6f4 v[158:161], v[2:9], v[196:203], v[158:161]
	v_mfma_f32_16x16x128_f8f6f4 v[154:157], v[10:17], v[196:203], v[154:157]
	v_mfma_f32_16x16x128_f8f6f4 v[150:153], v[2:9], v[204:211], v[150:153]
	v_mfma_f32_16x16x128_f8f6f4 v[146:149], v[10:17], v[204:211], v[146:149]
	v_mfma_f32_16x16x128_f8f6f4 v[130:133], v[2:9], v[212:219], v[130:133]
	v_mfma_f32_16x16x128_f8f6f4 v[122:125], v[10:17], v[212:219], v[122:125]
	v_mfma_f32_16x16x128_f8f6f4 v[114:117], v[2:9], v[220:227], v[114:117]
	v_mfma_f32_16x16x128_f8f6f4 v[106:109], v[10:17], v[220:227], v[106:109]
	s_nop 3
	v_mfma_f32_16x16x128_f8f6f4 v[142:145], v[18:25], v[196:203], v[142:145]
	v_mfma_f32_16x16x128_f8f6f4 v[138:141], v[26:33], v[196:203], v[138:141]
	v_mfma_f32_16x16x128_f8f6f4 v[134:137], v[18:25], v[204:211], v[134:137]
	v_mfma_f32_16x16x128_f8f6f4 v[126:129], v[26:33], v[204:211], v[126:129]
	v_mfma_f32_16x16x128_f8f6f4 v[118:121], v[18:25], v[212:219], v[118:121]
	v_mfma_f32_16x16x128_f8f6f4 v[110:113], v[26:33], v[212:219], v[110:113]
	v_mfma_f32_16x16x128_f8f6f4 v[102:105], v[18:25], v[220:227], v[102:105]
	v_mfma_f32_16x16x128_f8f6f4 v[98:101], v[26:33], v[220:227], v[98:101]
	s_setprio 0
	s_add_u32 s40, s40, 0x8000
	s_addc_u32 s41, s41, 0
	s_add_i32 s42, s66, s48
	s_mov_b32 m0, s42
	ds_read_b128 v[196:199], v193 offset:49152
	ds_read_b128 v[200:203], v193 offset:50176
	ds_read_b128 v[204:207], v193 offset:51200
	ds_read_b128 v[208:211], v193 offset:52224
	ds_read_b128 v[212:215], v193 offset:53248
	ds_read_b128 v[216:219], v193 offset:54272
	ds_read_b128 v[220:223], v193 offset:55296
	ds_read_b128 v[224:227], v193 offset:56320
	global_load_lds_dwordx4 v162, s[40:41]
	s_add_i32 m0, s42, 0x2000
	s_add_i32 s42, s67, s48
	global_load_lds_dwordx4 v164, s[40:41]
	s_mov_b32 m0, s42
	s_nop 0
	global_load_lds_dwordx4 v176, s[40:41]
	s_add_i32 m0, s42, 0x2000
	s_nop 0
	global_load_lds_dwordx4 v178, s[40:41]
	s_mov_b32 m0, s53
	s_nop 0
	global_load_lds_dwordx4 v166, s[30:31]
	s_mov_b32 m0, s58
	s_nop 0
	global_load_lds_dwordx4 v168, s[30:31]
	s_waitcnt vmcnt(8)
	s_waitcnt lgkmcnt(0)
	s_barrier
	s_setprio 2
	v_mfma_f32_16x16x128_f8f6f4 v[94:97], v[2:9], v[196:203], v[94:97]
	v_mfma_f32_16x16x128_f8f6f4 v[90:93], v[10:17], v[196:203], v[90:93]
	v_mfma_f32_16x16x128_f8f6f4 v[82:85], v[2:9], v[204:211], v[82:85]
	v_mfma_f32_16x16x128_f8f6f4 v[74:77], v[10:17], v[204:211], v[74:77]
	v_mfma_f32_16x16x128_f8f6f4 v[66:69], v[2:9], v[212:219], v[66:69]
	v_mfma_f32_16x16x128_f8f6f4 v[58:61], v[10:17], v[212:219], v[58:61]
	v_mfma_f32_16x16x128_f8f6f4 v[50:53], v[2:9], v[220:227], v[50:53]
	v_mfma_f32_16x16x128_f8f6f4 v[42:45], v[10:17], v[220:227], v[42:45]
	s_nop 3
	v_mfma_f32_16x16x128_f8f6f4 v[86:89], v[18:25], v[196:203], v[86:89]
	v_mfma_f32_16x16x128_f8f6f4 v[78:81], v[26:33], v[196:203], v[78:81]
	v_mfma_f32_16x16x128_f8f6f4 v[70:73], v[18:25], v[204:211], v[70:73]
	v_mfma_f32_16x16x128_f8f6f4 v[62:65], v[26:33], v[204:211], v[62:65]
	v_mfma_f32_16x16x128_f8f6f4 v[54:57], v[18:25], v[212:219], v[54:57]
	v_mfma_f32_16x16x128_f8f6f4 v[46:49], v[26:33], v[212:219], v[46:49]
	v_mfma_f32_16x16x128_f8f6f4 v[38:41], v[18:25], v[220:227], v[38:41]
	v_mfma_f32_16x16x128_f8f6f4 v[34:37], v[26:33], v[220:227], v[34:37]
	s_setprio 0
	s_add_i32 s65, s65, 2
	s_add_u32 s19, s19, 0x10000
	s_addc_u32 s21, s21, 0
	s_add_u32 s28, s28, 0x10000
	s_addc_u32 s29, s29, 0
	s_cmp_gt_u32 s65, 13
	s_cbranch_scc0 .Lh1_911

; #define PG8_WAIT_V(n) asm volatile("s_waitcnt vmcnt(" #n ")" ::: "memory")
; template <class Epi, class Sched, bool ALIGN_EPI = true, bool F8 = false>
; __device__ __forceinline__ void gemm_phase(PG8_LAS unsigned char* lds, const Sched& S, const Epi& E) {
;     ...
;         for (int t = 0; t < nt; t += 2) {
;             const bool last = (t == nt - 2);
;             if constexpr (Sched::GATHER) { if (last && has_next) S.a_off(nxt, Rs, Cs, voffAn); }
;             const char* a1 = cA + (size_t)(t + 1) * kstep;
;             const char* a2 = last ? nA : cA + (size_t)(t + 2) * kstep; const char* b2 = last ? nB : cB + (size_t)(t + 2) * kstepB;
;             const char* a3 = a2 + kstep; const char* b3 = b2 + kstepB;
;             unsigned vA2[2][2];
; #pragma unroll
;             for (int h = 0; h < 2; ++h)
; #pragma unroll
;                 for (int i = 0; i < 2; ++i) { if constexpr (Sched::GATHER) vA2[h][i] = (last && has_next) ? voffAn[h][i] : voffA[h][i]; else vA2[h][i] = voffA[h][i]; }
;             PG8_LDB(B0, 0, 0); PG8_LDB(B1, 0, 1); PG8_SCHED; PG8_LDA(At, 0, 0); PG8_STAGE(PG8_SA(1, 1), a1, voffA[1]);
;             PG8_WAIT_V(8); PG8_WAIT_L(0); PG8_BAR; PG8_MMA(0, 0, At, B0); PG8_MMA(0, 1, At, B1); PG8_BAR; PG8_SCHED;
;             PG8_LDA(At, 0, 1); PG8_STAGE(PG8_SB(0, 0), b2, voffB[0]); PG8_STAGE(PG8_SB(0, 1), b2, voffB[1]); PG8_STAGE(PG8_SA(0, 0), a2, vA2[0]);
;             PG8_WAIT_V(8); PG8_WAIT_L(0); PG8_BAR; PG8_MMA(1, 0, At, B0); PG8_MMA(1, 1, At, B1); PG8_BAR; PG8_SCHED;
;             PG8_LDB(B0, 1, 0); PG8_LDB(B1, 1, 1); PG8_SCHED; PG8_LDA(At, 1, 0); PG8_STAGE(PG8_SA(0, 1), a2, vA2[1]);
;             PG8_WAIT_V(8); PG8_WAIT_L(0); PG8_BAR; PG8_MMA(0, 0, At, B0); PG8_MMA(0, 1, At, B1); PG8_BAR; PG8_SCHED;
;             PG8_LDA(At, 1, 1); PG8_STAGE(PG8_SB(1, 0), b3, voffB[0]); PG8_STAGE(PG8_SB(1, 1), b3, voffB[1]); PG8_STAGE(PG8_SA(1, 0), a3, vA2[0]);
;             PG8_WAIT_V(8); PG8_WAIT_L(0); PG8_BAR; PG8_MMA(1, 0, At, B0); PG8_MMA(1, 1, At, B1); PG8_BAR; PG8_SCHED;
;     __device__ __forceinline__ bool next(int i, GUnit& u) const { const int L = i * G + c; const int ti = L >> 3, ct = L & 7; if (ti >= __builtin_amdgcn_readfirstlane(pre[NE])) return false;
;         int e = 0;
; #pragma unroll 1
;         for (int s = 16; s >= 1; s >>= 1) if (pre[e + s] <= ti) e += s;
;         e = __builtin_amdgcn_readfirstlane(e);
.Lpk0_1060:
	v_add_u32_e32 v2, s12, v210
	v_add_u32_e32 v14, s62, v210
	s_add_u32 s28, s30, 0x100
	ds_read_b128 v[18:21], v2
	ds_read_b128 v[22:25], v2 offset:1024
	ds_read_b128 v[26:29], v2 offset:2048
	ds_read_b128 v[30:33], v2 offset:3072
	ds_read_b128 v[2:5], v14
	ds_read_b128 v[6:9], v14 offset:1024
	ds_read_b128 v[10:13], v14 offset:2048
	ds_read_b128 v[14:17], v14 offset:3072
	s_addc_u32 s29, s31, 0
	s_and_b64 s[42:43], s[40:41], exec
	s_cselect_b32 s42, 0, s28
	s_cselect_b32 s43, 0, s29
	s_add_u32 s42, s6, s42
	s_addc_u32 s43, s7, s43
	s_and_b64 s[40:41], s[40:41], exec
	s_cselect_b32 s41, s25, s68
	s_cselect_b32 s40, s24, s21
	v_lshl_add_u64 v[204:205], v[196:197], 0, s[30:31]
	s_add_i32 m0, s52, 0xc000
	ds_read_b128 v[222:225], v213
	ds_read_b128 v[226:229], v213 offset:1024
	ds_read_b128 v[230:233], v213 offset:2048
	ds_read_b128 v[234:237], v213 offset:3072
	ds_read_b128 v[238:241], v213 offset:4096
	ds_read_b128 v[242:245], v213 offset:5120
	ds_read_b128 v[246:249], v213 offset:6144
	ds_read_b128 v[250:253], v213 offset:7168
	global_load_lds_dwordx4 v[204:205], off
	v_lshl_add_u64 v[204:205], v[194:195], 0, s[30:31]
	s_add_i32 m0, s52, 0xe000
	s_nop 0
	global_load_lds_dwordx4 v[204:205], off
	s_waitcnt vmcnt(8)
	s_waitcnt lgkmcnt(0)
	s_setprio 1
	v_mfma_f32_16x16x128_f8f6f4 v[142:145], v[18:25], v[222:229], 0
	v_mfma_f32_16x16x128_f8f6f4 v[138:141], v[26:33], v[222:229], 0
	v_mfma_f32_16x16x128_f8f6f4 v[134:137], v[18:25], v[230:237], 0
	v_mfma_f32_16x16x128_f8f6f4 v[130:133], v[26:33], v[230:237], 0
	v_mfma_f32_16x16x128_f8f6f4 v[126:129], v[18:25], v[238:245], 0
	v_mfma_f32_16x16x128_f8f6f4 v[122:125], v[26:33], v[238:245], 0
	v_mfma_f32_16x16x128_f8f6f4 v[118:121], v[18:25], v[246:253], 0
	v_mfma_f32_16x16x128_f8f6f4 v[114:117], v[26:33], v[246:253], 0
	s_nop 3
	v_mfma_f32_16x16x128_f8f6f4 v[110:113], v[2:9], v[222:229], 0
	v_mfma_f32_16x16x128_f8f6f4 v[106:109], v[10:17], v[222:229], 0
	v_mfma_f32_16x16x128_f8f6f4 v[102:105], v[2:9], v[230:237], 0
	v_mfma_f32_16x16x128_f8f6f4 v[98:101], v[10:17], v[230:237], 0
	v_mfma_f32_16x16x128_f8f6f4 v[94:97], v[2:9], v[238:245], 0
	v_mfma_f32_16x16x128_f8f6f4 v[90:93], v[10:17], v[238:245], 0
	v_mfma_f32_16x16x128_f8f6f4 v[86:89], v[2:9], v[246:253], 0
	v_mfma_f32_16x16x128_f8f6f4 v[82:85], v[10:17], v[246:253], 0
	s_setprio 0
	s_barrier
	s_add_i32 s30, s12, s48
	v_lshl_add_u64 v[204:205], s[40:41], 0, v[162:163]
	s_mov_b32 m0, s30
	ds_read_b128 v[222:225], v213 offset:16384
	ds_read_b128 v[226:229], v213 offset:17408
	ds_read_b128 v[230:233], v213 offset:18432
	ds_read_b128 v[234:237], v213 offset:19456
	ds_read_b128 v[238:241], v213 offset:20480
	ds_read_b128 v[242:245], v213 offset:21504
	ds_read_b128 v[246:249], v213 offset:22528
	ds_read_b128 v[250:253], v213 offset:23552
	global_load_lds_dwordx4 v[204:205], off
	v_lshl_add_u64 v[204:205], s[40:41], 0, v[164:165]
	s_add_i32 m0, s30, 0x2000
	s_add_i32 s30, s62, s48
	global_load_lds_dwordx4 v[204:205], off
	v_lshl_add_u64 v[204:205], s[40:41], 0, v[166:167]
	s_mov_b32 m0, s30
	v_mov_b32_e32 v203, v171
	global_load_lds_dwordx4 v[204:205], off
	v_lshl_add_u64 v[204:205], s[40:41], 0, v[168:169]
	s_add_i32 m0, s30, 0x2000
	s_nop 0
	global_load_lds_dwordx4 v[204:205], off
	s_mov_b32 m0, s52
	v_lshl_add_u64 v[204:205], s[42:43], 0, v[170:171]
	global_load_lds_dwordx4 v170, s[42:43]
	s_mov_b32 m0, s53
	s_nop 0
	global_load_lds_dwordx4 v202, s[42:43]
	s_waitcnt vmcnt(8)
	s_waitcnt lgkmcnt(0)
	v_lshl_add_u64 v[202:203], s[42:43], 0, v[202:203]
	s_setprio 1
	v_mfma_f32_16x16x128_f8f6f4 v[78:81], v[18:25], v[222:229], 0
	v_mfma_f32_16x16x128_f8f6f4 v[74:77], v[26:33], v[222:229], 0
	v_mfma_f32_16x16x128_f8f6f4 v[70:73], v[18:25], v[230:237], 0
	v_mfma_f32_16x16x128_f8f6f4 v[66:69], v[26:33], v[230:237], 0
	v_mfma_f32_16x16x128_f8f6f4 v[62:65], v[18:25], v[238:245], 0
	v_mfma_f32_16x16x128_f8f6f4 v[58:61], v[26:33], v[238:245], 0
	v_mfma_f32_16x16x128_f8f6f4 v[54:57], v[18:25], v[246:253], 0
	v_mfma_f32_16x16x128_f8f6f4 v[50:53], v[26:33], v[246:253], 0
	s_nop 3
	v_mfma_f32_16x16x128_f8f6f4 v[46:49], v[2:9], v[222:229], 0
	v_mfma_f32_16x16x128_f8f6f4 v[42:45], v[10:17], v[222:229], 0
	v_mfma_f32_16x16x128_f8f6f4 v[38:41], v[2:9], v[230:237], 0
	v_mfma_f32_16x16x128_f8f6f4 v[34:37], v[10:17], v[230:237], 0
	v_mfma_f32_16x16x128_f8f6f4 v[146:149], v[2:9], v[238:245], 0
	v_mfma_f32_16x16x128_f8f6f4 v[150:153], v[10:17], v[238:245], 0
	v_mfma_f32_16x16x128_f8f6f4 v[154:157], v[2:9], v[246:253], 0
	v_mfma_f32_16x16x128_f8f6f4 v[158:161], v[10:17], v[246:253], 0
	s_setprio 0
	s_barrier
; #define PG8_WAIT_V(n) asm volatile("s_waitcnt vmcnt(" #n ")" ::: "memory")
; template <class Epi, class Sched, bool ALIGN_EPI = true, bool F8 = false>
; __device__ __forceinline__ void gemm_phase(PG8_LAS unsigned char* lds, const Sched& S, const Epi& E) {
;     ...
;         for (int t = 0; t < nt; t += 2) {
;             const bool last = (t == nt - 2);
;             if constexpr (Sched::GATHER) { if (last && has_next) S.a_off(nxt, Rs, Cs, voffAn); }
;             const char* a1 = cA + (size_t)(t + 1) * kstep;
;             const char* a2 = last ? nA : cA + (size_t)(t + 2) * kstep; const char* b2 = last ? nB : cB + (size_t)(t + 2) * kstepB;
;             const char* a3 = a2 + kstep; const char* b3 = b2 + kstepB;
;             unsigned vA2[2][2];
; #pragma unroll
;             for (int h = 0; h < 2; ++h)
; #pragma unroll
;                 for (int i = 0; i < 2; ++i) { if constexpr (Sched::GATHER) vA2[h][i] = (last && has_next) ? voffAn[h][i] : voffA[h][i]; else vA2[h][i] = voffA[h][i]; }
;             PG8_LDB(B0, 0, 0); PG8_LDB(B1, 0, 1); PG8_SCHED; PG8_LDA(At, 0, 0); PG8_STAGE(PG8_SA(1, 1), a1, voffA[1]);
;             PG8_WAIT_V(8); PG8_WAIT_L(0); PG8_BAR; PG8_MMA(0, 0, At, B0); PG8_MMA(0, 1, At, B1); PG8_BAR; PG8_SCHED;
;             PG8_LDA(At, 0, 1); PG8_STAGE(PG8_SB(0, 0), b2, voffB[0]); PG8_STAGE(PG8_SB(0, 1), b2, voffB[1]); PG8_STAGE(PG8_SA(0, 0), a2, vA2[0]);
;             PG8_WAIT_V(8); PG8_WAIT_L(0); PG8_BAR; PG8_MMA(1, 0, At, B0); PG8_MMA(1, 1, At, B1); PG8_BAR; PG8_SCHED;
;             PG8_LDB(B0, 1, 0); PG8_LDB(B1, 1, 1); PG8_SCHED; PG8_LDA(At, 1, 0); PG8_STAGE(PG8_SA(0, 1), a2, vA2[1]);
;             PG8_WAIT_V(8); PG8_WAIT_L(0); PG8_BAR; PG8_MMA(0, 0, At, B0); PG8_MMA(0, 1, At, B1); PG8_BAR; PG8_SCHED;
;             PG8_LDA(At, 1, 1); PG8_STAGE(PG8_SB(1, 0), b3, voffB[0]); PG8_STAGE(PG8_SB(1, 1), b3, voffB[1]); PG8_STAGE(PG8_SA(1, 0), a3, vA2[0]);
;             PG8_WAIT_V(8); PG8_WAIT_L(0); PG8_BAR; PG8_MMA(1, 0, At, B0); PG8_MMA(1, 1, At, B1); PG8_BAR; PG8_SCHED;
;     __device__ __forceinline__ bool next(int i, GUnit& u) const { const int L = i * G + c; const int ti = L >> 3, ct = L & 7; if (ti >= __builtin_amdgcn_readfirstlane(pre[NE])) return false;
;         int e = 0;
; #pragma unroll 1
;         for (int s = 16; s >= 1; s >>= 1) if (pre[e + s] <= ti) e += s;
;         e = __builtin_amdgcn_readfirstlane(e);
	s_add_i32 s70, 0, 0x18000
	s_add_i32 s71, 0, 0x1c000
	v_add_u32_e32 v14, s70, v210
	v_add_u32_e32 v30, s71, v210
	ds_read_b128 v[2:5], v14
	ds_read_b128 v[6:9], v14 offset:1024
	ds_read_b128 v[10:13], v14 offset:2048
	ds_read_b128 v[14:17], v14 offset:3072
	ds_read_b128 v[18:21], v30
	ds_read_b128 v[22:25], v30 offset:1024
	ds_read_b128 v[26:29], v30 offset:2048
	ds_read_b128 v[30:33], v30 offset:3072
	s_mov_b32 m0, s58
	v_lshl_add_u64 v[200:201], s[42:43], 0, v[200:201]
	ds_read_b128 v[222:225], v213 offset:32768
	ds_read_b128 v[226:229], v213 offset:33792
	ds_read_b128 v[230:233], v213 offset:34816
	ds_read_b128 v[234:237], v213 offset:35840
	ds_read_b128 v[238:241], v213 offset:36864
	ds_read_b128 v[242:245], v213 offset:37888
	ds_read_b128 v[246:249], v213 offset:38912
	ds_read_b128 v[250:253], v213 offset:39936
	global_load_lds_dwordx4 v[200:201], off
	v_lshl_add_u64 v[198:199], s[42:43], 0, v[198:199]
	s_mov_b32 m0, s59
	s_nop 0
	global_load_lds_dwordx4 v[198:199], off
	s_waitcnt vmcnt(8)
	s_waitcnt lgkmcnt(0)
	s_setprio 1
	v_mfma_f32_16x16x128_f8f6f4 v[142:145], v[2:9], v[222:229], v[142:145]
	v_mfma_f32_16x16x128_f8f6f4 v[138:141], v[10:17], v[222:229], v[138:141]
	v_mfma_f32_16x16x128_f8f6f4 v[134:137], v[2:9], v[230:237], v[134:137]
	v_mfma_f32_16x16x128_f8f6f4 v[130:133], v[10:17], v[230:237], v[130:133]
	v_mfma_f32_16x16x128_f8f6f4 v[126:129], v[2:9], v[238:245], v[126:129]
	v_mfma_f32_16x16x128_f8f6f4 v[122:125], v[10:17], v[238:245], v[122:125]
	v_mfma_f32_16x16x128_f8f6f4 v[118:121], v[2:9], v[246:253], v[118:121]
	v_mfma_f32_16x16x128_f8f6f4 v[114:117], v[10:17], v[246:253], v[114:117]
	s_nop 3
	v_mfma_f32_16x16x128_f8f6f4 v[110:113], v[18:25], v[222:229], v[110:113]
	v_mfma_f32_16x16x128_f8f6f4 v[106:109], v[26:33], v[222:229], v[106:109]
	v_mfma_f32_16x16x128_f8f6f4 v[102:105], v[18:25], v[230:237], v[102:105]
	v_mfma_f32_16x16x128_f8f6f4 v[98:101], v[26:33], v[230:237], v[98:101]
	v_mfma_f32_16x16x128_f8f6f4 v[94:97], v[18:25], v[238:245], v[94:97]
	v_mfma_f32_16x16x128_f8f6f4 v[90:93], v[26:33], v[238:245], v[90:93]
	v_mfma_f32_16x16x128_f8f6f4 v[86:89], v[18:25], v[246:253], v[86:89]
	v_mfma_f32_16x16x128_f8f6f4 v[82:85], v[26:33], v[246:253], v[82:85]
	s_setprio 0
	s_barrier
	s_add_u32 s30, s40, 0x8000
	s_addc_u32 s31, s41, 0
	s_add_i32 s40, s70, s48
	v_lshl_add_u64 v[198:199], s[30:31], 0, v[162:163]
	s_mov_b32 m0, s40
	ds_read_b128 v[222:225], v213 offset:49152
	ds_read_b128 v[226:229], v213 offset:50176
	ds_read_b128 v[230:233], v213 offset:51200
	ds_read_b128 v[234:237], v213 offset:52224
	ds_read_b128 v[238:241], v213 offset:53248
	ds_read_b128 v[242:245], v213 offset:54272
	ds_read_b128 v[246:249], v213 offset:55296
	ds_read_b128 v[250:253], v213 offset:56320
	global_load_lds_dwordx4 v[198:199], off
	v_lshl_add_u64 v[198:199], s[30:31], 0, v[164:165]
	s_add_i32 m0, s40, 0x2000
	s_add_i32 s40, s71, s48
	global_load_lds_dwordx4 v[198:199], off
	v_lshl_add_u64 v[198:199], s[30:31], 0, v[166:167]
	s_mov_b32 m0, s40
	s_nop 0
	global_load_lds_dwordx4 v[198:199], off
	v_lshl_add_u64 v[198:199], s[30:31], 0, v[168:169]
	s_add_i32 m0, s40, 0x2000
	s_nop 0
	global_load_lds_dwordx4 v[198:199], off
	v_lshl_add_u64 v[198:199], v[204:205], 0, s[18:19]
	s_mov_b32 m0, s60
	s_nop 0
	global_load_lds_dwordx4 v[198:199], off
	v_lshl_add_u64 v[198:199], v[202:203], 0, s[18:19]
	s_mov_b32 m0, s61
	s_nop 0
	global_load_lds_dwordx4 v[198:199], off
	s_waitcnt vmcnt(8)
	s_waitcnt lgkmcnt(0)
	s_setprio 1
	v_mfma_f32_16x16x128_f8f6f4 v[78:81], v[2:9], v[222:229], v[78:81]
	v_mfma_f32_16x16x128_f8f6f4 v[74:77], v[10:17], v[222:229], v[74:77]
	v_mfma_f32_16x16x128_f8f6f4 v[70:73], v[2:9], v[230:237], v[70:73]
	v_mfma_f32_16x16x128_f8f6f4 v[66:69], v[10:17], v[230:237], v[66:69]
	v_mfma_f32_16x16x128_f8f6f4 v[62:65], v[2:9], v[238:245], v[62:65]
	v_mfma_f32_16x16x128_f8f6f4 v[58:61], v[10:17], v[238:245], v[58:61]
	v_mfma_f32_16x16x128_f8f6f4 v[54:57], v[2:9], v[246:253], v[54:57]
	v_mfma_f32_16x16x128_f8f6f4 v[50:53], v[10:17], v[246:253], v[50:53]
	s_nop 3
	v_mfma_f32_16x16x128_f8f6f4 v[46:49], v[18:25], v[222:229], v[46:49]
	v_mfma_f32_16x16x128_f8f6f4 v[42:45], v[26:33], v[222:229], v[42:45]
	v_mfma_f32_16x16x128_f8f6f4 v[38:41], v[18:25], v[230:237], v[38:41]
	v_mfma_f32_16x16x128_f8f6f4 v[34:37], v[26:33], v[230:237], v[34:37]
	v_mfma_f32_16x16x128_f8f6f4 v[146:149], v[18:25], v[238:245], v[146:149]
	v_mfma_f32_16x16x128_f8f6f4 v[150:153], v[26:33], v[238:245], v[150:153]
	v_mfma_f32_16x16x128_f8f6f4 v[154:157], v[18:25], v[246:253], v[154:157]
	v_mfma_f32_16x16x128_f8f6f4 v[158:161], v[26:33], v[246:253], v[158:161]
	s_setprio 0
	s_barrier
	s_add_i32 s69, s69, 2
	s_add_u32 s21, s21, 0x10000
	s_addc_u32 s68, s68, 0
	s_cmp_gt_u32 s69, 13
	s_cbranch_scc1 .LBB0_1062
	s_mov_b64 s[30:31], s[28:29]
	s_branch .LBB0_1058

; #define PG8_WAIT_V(n) asm volatile("s_waitcnt vmcnt(" #n ")" ::: "memory")
; template <class Epi, class Sched, bool ALIGN_EPI = true, bool F8 = false>
; __device__ __forceinline__ void gemm_phase(PG8_LAS unsigned char* lds, const Sched& S, const Epi& E) {
;     ...
;         for (int t = 0; t < nt; t += 2) {
;             const bool last = (t == nt - 2);
;             if constexpr (Sched::GATHER) { if (last && has_next) S.a_off(nxt, Rs, Cs, voffAn); }
;             const char* a1 = cA + (size_t)(t + 1) * kstep;
;             const char* a2 = last ? nA : cA + (size_t)(t + 2) * kstep; const char* b2 = last ? nB : cB + (size_t)(t + 2) * kstepB;
;             const char* a3 = a2 + kstep; const char* b3 = b2 + kstepB;
;             unsigned vA2[2][2];
; #pragma unroll
;             for (int h = 0; h < 2; ++h)
; #pragma unroll
;                 for (int i = 0; i < 2; ++i) { if constexpr (Sched::GATHER) vA2[h][i] = (last && has_next) ? voffAn[h][i] : voffA[h][i]; else vA2[h][i] = voffA[h][i]; }
;             PG8_LDB(B0, 0, 0); PG8_LDB(B1, 0, 1); PG8_SCHED; PG8_LDA(At, 0, 0); PG8_STAGE(PG8_SA(1, 1), a1, voffA[1]);
;             PG8_WAIT_V(8); PG8_WAIT_L(0); PG8_BAR; PG8_MMA(0, 0, At, B0); PG8_MMA(0, 1, At, B1); PG8_BAR; PG8_SCHED;
;             PG8_LDA(At, 0, 1); PG8_STAGE(PG8_SB(0, 0), b2, voffB[0]); PG8_STAGE(PG8_SB(0, 1), b2, voffB[1]); PG8_STAGE(PG8_SA(0, 0), a2, vA2[0]);
;             PG8_WAIT_V(8); PG8_WAIT_L(0); PG8_BAR; PG8_MMA(1, 0, At, B0); PG8_MMA(1, 1, At, B1); PG8_BAR; PG8_SCHED;
;             PG8_LDB(B0, 1, 0); PG8_LDB(B1, 1, 1); PG8_SCHED; PG8_LDA(At, 1, 0); PG8_STAGE(PG8_SA(0, 1), a2, vA2[1]);
;             PG8_WAIT_V(8); PG8_WAIT_L(0); PG8_BAR; PG8_MMA(0, 0, At, B0); PG8_MMA(0, 1, At, B1); PG8_BAR; PG8_SCHED;
;             PG8_LDA(At, 1, 1); PG8_STAGE(PG8_SB(1, 0), b3, voffB[0]); PG8_STAGE(PG8_SB(1, 1), b3, voffB[1]); PG8_STAGE(PG8_SA(1, 0), a3, vA2[0]);
;             PG8_WAIT_V(8); PG8_WAIT_L(0); PG8_BAR; PG8_MMA(1, 0, At, B0); PG8_MMA(1, 1, At, B1); PG8_BAR; PG8_SCHED;
;     __device__ __forceinline__ bool next(int i, GUnit& u) const { const int L = i * G + c; const int ti = L >> 3, ct = L & 7; if (ti >= __builtin_amdgcn_readfirstlane(pre[NE])) return false;
;         int e = 0;
; #pragma unroll 1
;         for (int s = 16; s >= 1; s >>= 1) if (pre[e + s] <= ti) e += s;
;         e = __builtin_amdgcn_readfirstlane(e);
.LBB0_1060:
	v_add_u32_e32 v2, s12, v210
	v_add_u32_e32 v14, s62, v210
	s_add_u32 s28, s30, 0x100
	ds_read_b128 v[18:21], v2
	ds_read_b128 v[22:25], v2 offset:1024
	ds_read_b128 v[26:29], v2 offset:2048
	ds_read_b128 v[30:33], v2 offset:3072
	ds_read_b128 v[2:5], v14
	ds_read_b128 v[6:9], v14 offset:1024
	ds_read_b128 v[10:13], v14 offset:2048
	ds_read_b128 v[14:17], v14 offset:3072
	s_addc_u32 s29, s31, 0
	s_and_b64 s[42:43], s[40:41], exec
	s_cselect_b32 s42, 0, s28
	s_cselect_b32 s43, 0, s29
	s_add_u32 s42, s6, s42
	s_addc_u32 s43, s7, s43
	s_and_b64 s[40:41], s[40:41], exec
	s_cselect_b32 s41, s25, s68
	s_cselect_b32 s40, s24, s21
	v_lshl_add_u64 v[204:205], v[196:197], 0, s[30:31]
	s_add_i32 m0, s52, 0xc000
	ds_read_b128 v[222:225], v213
	ds_read_b128 v[226:229], v213 offset:1024
	ds_read_b128 v[230:233], v213 offset:2048
	ds_read_b128 v[234:237], v213 offset:3072
	ds_read_b128 v[238:241], v213 offset:4096
	ds_read_b128 v[242:245], v213 offset:5120
	ds_read_b128 v[246:249], v213 offset:6144
	ds_read_b128 v[250:253], v213 offset:7168
	global_load_lds_dwordx4 v[204:205], off
	v_lshl_add_u64 v[204:205], v[194:195], 0, s[30:31]
	s_add_i32 m0, s52, 0xe000
	s_nop 0
	global_load_lds_dwordx4 v[204:205], off
	s_waitcnt vmcnt(8)
	s_waitcnt lgkmcnt(0)
	s_setprio 1
	v_mfma_f32_16x16x128_f8f6f4 v[142:145], v[18:25], v[222:229], v[142:145]
	v_mfma_f32_16x16x128_f8f6f4 v[138:141], v[26:33], v[222:229], v[138:141]
	v_mfma_f32_16x16x128_f8f6f4 v[134:137], v[18:25], v[230:237], v[134:137]
	v_mfma_f32_16x16x128_f8f6f4 v[130:133], v[26:33], v[230:237], v[130:133]
	v_mfma_f32_16x16x128_f8f6f4 v[126:129], v[18:25], v[238:245], v[126:129]
	v_mfma_f32_16x16x128_f8f6f4 v[122:125], v[26:33], v[238:245], v[122:125]
	v_mfma_f32_16x16x128_f8f6f4 v[118:121], v[18:25], v[246:253], v[118:121]
	v_mfma_f32_16x16x128_f8f6f4 v[114:117], v[26:33], v[246:253], v[114:117]
	s_nop 3
	v_mfma_f32_16x16x128_f8f6f4 v[110:113], v[2:9], v[222:229], v[110:113]
	v_mfma_f32_16x16x128_f8f6f4 v[106:109], v[10:17], v[222:229], v[106:109]
	v_mfma_f32_16x16x128_f8f6f4 v[102:105], v[2:9], v[230:237], v[102:105]
	v_mfma_f32_16x16x128_f8f6f4 v[98:101], v[10:17], v[230:237], v[98:101]
	v_mfma_f32_16x16x128_f8f6f4 v[94:97], v[2:9], v[238:245], v[94:97]
	v_mfma_f32_16x16x128_f8f6f4 v[90:93], v[10:17], v[238:245], v[90:93]
	v_mfma_f32_16x16x128_f8f6f4 v[86:89], v[2:9], v[246:253], v[86:89]
	v_mfma_f32_16x16x128_f8f6f4 v[82:85], v[10:17], v[246:253], v[82:85]
	s_setprio 0
	s_barrier
	s_add_i32 s30, s12, s48
	v_lshl_add_u64 v[204:205], s[40:41], 0, v[162:163]
	s_mov_b32 m0, s30
	ds_read_b128 v[222:225], v213 offset:16384
	ds_read_b128 v[226:229], v213 offset:17408
	ds_read_b128 v[230:233], v213 offset:18432
	ds_read_b128 v[234:237], v213 offset:19456
	ds_read_b128 v[238:241], v213 offset:20480
	ds_read_b128 v[242:245], v213 offset:21504
	ds_read_b128 v[246:249], v213 offset:22528
	ds_read_b128 v[250:253], v213 offset:23552
	global_load_lds_dwordx4 v[204:205], off
	v_lshl_add_u64 v[204:205], s[40:41], 0, v[164:165]
	s_add_i32 m0, s30, 0x2000
	s_add_i32 s30, s62, s48
	global_load_lds_dwordx4 v[204:205], off
	v_lshl_add_u64 v[204:205], s[40:41], 0, v[166:167]
	s_mov_b32 m0, s30
	v_mov_b32_e32 v203, v171
	global_load_lds_dwordx4 v[204:205], off
	v_lshl_add_u64 v[204:205], s[40:41], 0, v[168:169]
	s_add_i32 m0, s30, 0x2000
	s_nop 0
	global_load_lds_dwordx4 v[204:205], off
	s_mov_b32 m0, s52
	v_lshl_add_u64 v[204:205], s[42:43], 0, v[170:171]
	global_load_lds_dwordx4 v170, s[42:43]
	s_mov_b32 m0, s53
	s_nop 0
	global_load_lds_dwordx4 v202, s[42:43]
	s_waitcnt vmcnt(8)
	s_waitcnt lgkmcnt(0)
	v_lshl_add_u64 v[202:203], s[42:43], 0, v[202:203]
	s_setprio 1
	v_mfma_f32_16x16x128_f8f6f4 v[78:81], v[18:25], v[222:229], v[78:81]
	v_mfma_f32_16x16x128_f8f6f4 v[74:77], v[26:33], v[222:229], v[74:77]
	v_mfma_f32_16x16x128_f8f6f4 v[70:73], v[18:25], v[230:237], v[70:73]
	v_mfma_f32_16x16x128_f8f6f4 v[66:69], v[26:33], v[230:237], v[66:69]
	v_mfma_f32_16x16x128_f8f6f4 v[62:65], v[18:25], v[238:245], v[62:65]
	v_mfma_f32_16x16x128_f8f6f4 v[58:61], v[26:33], v[238:245], v[58:61]
	v_mfma_f32_16x16x128_f8f6f4 v[54:57], v[18:25], v[246:253], v[54:57]
	v_mfma_f32_16x16x128_f8f6f4 v[50:53], v[26:33], v[246:253], v[50:53]
	s_nop 3
	v_mfma_f32_16x16x128_f8f6f4 v[46:49], v[2:9], v[222:229], v[46:49]
	v_mfma_f32_16x16x128_f8f6f4 v[42:45], v[10:17], v[222:229], v[42:45]
	v_mfma_f32_16x16x128_f8f6f4 v[38:41], v[2:9], v[230:237], v[38:41]
	v_mfma_f32_16x16x128_f8f6f4 v[34:37], v[10:17], v[230:237], v[34:37]
	v_mfma_f32_16x16x128_f8f6f4 v[146:149], v[2:9], v[238:245], v[146:149]
	v_mfma_f32_16x16x128_f8f6f4 v[150:153], v[10:17], v[238:245], v[150:153]
	v_mfma_f32_16x16x128_f8f6f4 v[154:157], v[2:9], v[246:253], v[154:157]
	v_mfma_f32_16x16x128_f8f6f4 v[158:161], v[10:17], v[246:253], v[158:161]
	s_setprio 0
	s_barrier
; #define PG8_WAIT_V(n) asm volatile("s_waitcnt vmcnt(" #n ")" ::: "memory")
; template <class Epi, class Sched, bool ALIGN_EPI = true, bool F8 = false>
; __device__ __forceinline__ void gemm_phase(PG8_LAS unsigned char* lds, const Sched& S, const Epi& E) {
;     ...
;         for (int t = 0; t < nt; t += 2) {
;             const bool last = (t == nt - 2);
;             if constexpr (Sched::GATHER) { if (last && has_next) S.a_off(nxt, Rs, Cs, voffAn); }
;             const char* a1 = cA + (size_t)(t + 1) * kstep;
;             const char* a2 = last ? nA : cA + (size_t)(t + 2) * kstep; const char* b2 = last ? nB : cB + (size_t)(t + 2) * kstepB;
;             const char* a3 = a2 + kstep; const char* b3 = b2 + kstepB;
;             unsigned vA2[2][2];
; #pragma unroll
;             for (int h = 0; h < 2; ++h)
; #pragma unroll
;                 for (int i = 0; i < 2; ++i) { if constexpr (Sched::GATHER) vA2[h][i] = (last && has_next) ? voffAn[h][i] : voffA[h][i]; else vA2[h][i] = voffA[h][i]; }
;             PG8_LDB(B0, 0, 0); PG8_LDB(B1, 0, 1); PG8_SCHED; PG8_LDA(At, 0, 0); PG8_STAGE(PG8_SA(1, 1), a1, voffA[1]);
;             PG8_WAIT_V(8); PG8_WAIT_L(0); PG8_BAR; PG8_MMA(0, 0, At, B0); PG8_MMA(0, 1, At, B1); PG8_BAR; PG8_SCHED;
;             PG8_LDA(At, 0, 1); PG8_STAGE(PG8_SB(0, 0), b2, voffB[0]); PG8_STAGE(PG8_SB(0, 1), b2, voffB[1]); PG8_STAGE(PG8_SA(0, 0), a2, vA2[0]);
;             PG8_WAIT_V(8); PG8_WAIT_L(0); PG8_BAR; PG8_MMA(1, 0, At, B0); PG8_MMA(1, 1, At, B1); PG8_BAR; PG8_SCHED;
;             PG8_LDB(B0, 1, 0); PG8_LDB(B1, 1, 1); PG8_SCHED; PG8_LDA(At, 1, 0); PG8_STAGE(PG8_SA(0, 1), a2, vA2[1]);
;             PG8_WAIT_V(8); PG8_WAIT_L(0); PG8_BAR; PG8_MMA(0, 0, At, B0); PG8_MMA(0, 1, At, B1); PG8_BAR; PG8_SCHED;
;             PG8_LDA(At, 1, 1); PG8_STAGE(PG8_SB(1, 0), b3, voffB[0]); PG8_STAGE(PG8_SB(1, 1), b3, voffB[1]); PG8_STAGE(PG8_SA(1, 0), a3, vA2[0]);
;             PG8_WAIT_V(8); PG8_WAIT_L(0); PG8_BAR; PG8_MMA(1, 0, At, B0); PG8_MMA(1, 1, At, B1); PG8_BAR; PG8_SCHED;
;     __device__ __forceinline__ bool next(int i, GUnit& u) const { const int L = i * G + c; const int ti = L >> 3, ct = L & 7; if (ti >= __builtin_amdgcn_readfirstlane(pre[NE])) return false;
;         int e = 0;
; #pragma unroll 1
;         for (int s = 16; s >= 1; s >>= 1) if (pre[e + s] <= ti) e += s;
;         e = __builtin_amdgcn_readfirstlane(e);
	s_add_i32 s70, 0, 0x18000
	s_add_i32 s71, 0, 0x1c000
	v_add_u32_e32 v14, s70, v210
	v_add_u32_e32 v30, s71, v210
	ds_read_b128 v[2:5], v14
	ds_read_b128 v[6:9], v14 offset:1024
	ds_read_b128 v[10:13], v14 offset:2048
	ds_read_b128 v[14:17], v14 offset:3072
	ds_read_b128 v[18:21], v30
	ds_read_b128 v[22:25], v30 offset:1024
	ds_read_b128 v[26:29], v30 offset:2048
	ds_read_b128 v[30:33], v30 offset:3072
	s_mov_b32 m0, s58
	v_lshl_add_u64 v[200:201], s[42:43], 0, v[200:201]
	ds_read_b128 v[222:225], v213 offset:32768
	ds_read_b128 v[226:229], v213 offset:33792
	ds_read_b128 v[230:233], v213 offset:34816
	ds_read_b128 v[234:237], v213 offset:35840
	ds_read_b128 v[238:241], v213 offset:36864
	ds_read_b128 v[242:245], v213 offset:37888
	ds_read_b128 v[246:249], v213 offset:38912
	ds_read_b128 v[250:253], v213 offset:39936
	global_load_lds_dwordx4 v[200:201], off
	v_lshl_add_u64 v[198:199], s[42:43], 0, v[198:199]
	s_mov_b32 m0, s59
	s_nop 0
	global_load_lds_dwordx4 v[198:199], off
	s_waitcnt vmcnt(8)
	s_waitcnt lgkmcnt(0)
	s_setprio 1
	v_mfma_f32_16x16x128_f8f6f4 v[142:145], v[2:9], v[222:229], v[142:145]
	v_mfma_f32_16x16x128_f8f6f4 v[138:141], v[10:17], v[222:229], v[138:141]
	v_mfma_f32_16x16x128_f8f6f4 v[134:137], v[2:9], v[230:237], v[134:137]
	v_mfma_f32_16x16x128_f8f6f4 v[130:133], v[10:17], v[230:237], v[130:133]
	v_mfma_f32_16x16x128_f8f6f4 v[126:129], v[2:9], v[238:245], v[126:129]
	v_mfma_f32_16x16x128_f8f6f4 v[122:125], v[10:17], v[238:245], v[122:125]
	v_mfma_f32_16x16x128_f8f6f4 v[118:121], v[2:9], v[246:253], v[118:121]
	v_mfma_f32_16x16x128_f8f6f4 v[114:117], v[10:17], v[246:253], v[114:117]
	s_nop 3
	v_mfma_f32_16x16x128_f8f6f4 v[110:113], v[18:25], v[222:229], v[110:113]
	v_mfma_f32_16x16x128_f8f6f4 v[106:109], v[26:33], v[222:229], v[106:109]
	v_mfma_f32_16x16x128_f8f6f4 v[102:105], v[18:25], v[230:237], v[102:105]
	v_mfma_f32_16x16x128_f8f6f4 v[98:101], v[26:33], v[230:237], v[98:101]
	v_mfma_f32_16x16x128_f8f6f4 v[94:97], v[18:25], v[238:245], v[94:97]
	v_mfma_f32_16x16x128_f8f6f4 v[90:93], v[26:33], v[238:245], v[90:93]
	v_mfma_f32_16x16x128_f8f6f4 v[86:89], v[18:25], v[246:253], v[86:89]
	v_mfma_f32_16x16x128_f8f6f4 v[82:85], v[26:33], v[246:253], v[82:85]
	s_setprio 0
	s_barrier
	s_add_u32 s30, s40, 0x8000
	s_addc_u32 s31, s41, 0
	s_add_i32 s40, s70, s48
	v_lshl_add_u64 v[198:199], s[30:31], 0, v[162:163]
	s_mov_b32 m0, s40
	ds_read_b128 v[222:225], v213 offset:49152
	ds_read_b128 v[226:229], v213 offset:50176
	ds_read_b128 v[230:233], v213 offset:51200
	ds_read_b128 v[234:237], v213 offset:52224
	ds_read_b128 v[238:241], v213 offset:53248
	ds_read_b128 v[242:245], v213 offset:54272
	ds_read_b128 v[246:249], v213 offset:55296
	ds_read_b128 v[250:253], v213 offset:56320
	global_load_lds_dwordx4 v[198:199], off
	v_lshl_add_u64 v[198:199], s[30:31], 0, v[164:165]
	s_add_i32 m0, s40, 0x2000
	s_add_i32 s40, s71, s48
	global_load_lds_dwordx4 v[198:199], off
	v_lshl_add_u64 v[198:199], s[30:31], 0, v[166:167]
	s_mov_b32 m0, s40
	s_nop 0
	global_load_lds_dwordx4 v[198:199], off
	v_lshl_add_u64 v[198:199], s[30:31], 0, v[168:169]
	s_add_i32 m0, s40, 0x2000
	s_nop 0
	global_load_lds_dwordx4 v[198:199], off
	v_lshl_add_u64 v[198:199], v[204:205], 0, s[18:19]
	s_mov_b32 m0, s60
	s_nop 0
	global_load_lds_dwordx4 v[198:199], off
	v_lshl_add_u64 v[198:199], v[202:203], 0, s[18:19]
	s_mov_b32 m0, s61
	s_nop 0
	global_load_lds_dwordx4 v[198:199], off
	s_waitcnt vmcnt(8)
	s_waitcnt lgkmcnt(0)
	s_setprio 1
	v_mfma_f32_16x16x128_f8f6f4 v[78:81], v[2:9], v[222:229], v[78:81]
	v_mfma_f32_16x16x128_f8f6f4 v[74:77], v[10:17], v[222:229], v[74:77]
	v_mfma_f32_16x16x128_f8f6f4 v[70:73], v[2:9], v[230:237], v[70:73]
	v_mfma_f32_16x16x128_f8f6f4 v[66:69], v[10:17], v[230:237], v[66:69]
	v_mfma_f32_16x16x128_f8f6f4 v[62:65], v[2:9], v[238:245], v[62:65]
	v_mfma_f32_16x16x128_f8f6f4 v[58:61], v[10:17], v[238:245], v[58:61]
	v_mfma_f32_16x16x128_f8f6f4 v[54:57], v[2:9], v[246:253], v[54:57]
	v_mfma_f32_16x16x128_f8f6f4 v[50:53], v[10:17], v[246:253], v[50:53]
	s_nop 3
	v_mfma_f32_16x16x128_f8f6f4 v[46:49], v[18:25], v[222:229], v[46:49]
	v_mfma_f32_16x16x128_f8f6f4 v[42:45], v[26:33], v[222:229], v[42:45]
	v_mfma_f32_16x16x128_f8f6f4 v[38:41], v[18:25], v[230:237], v[38:41]
	v_mfma_f32_16x16x128_f8f6f4 v[34:37], v[26:33], v[230:237], v[34:37]
	v_mfma_f32_16x16x128_f8f6f4 v[146:149], v[18:25], v[238:245], v[146:149]
	v_mfma_f32_16x16x128_f8f6f4 v[150:153], v[26:33], v[238:245], v[150:153]
	v_mfma_f32_16x16x128_f8f6f4 v[154:157], v[18:25], v[246:253], v[154:157]
	v_mfma_f32_16x16x128_f8f6f4 v[158:161], v[26:33], v[246:253], v[158:161]
	s_setprio 0
	s_barrier
	s_add_i32 s69, s69, 2
	s_add_u32 s21, s21, 0x10000
	s_addc_u32 s68, s68, 0
	s_cmp_gt_u32 s69, 13
	s_cbranch_scc1 .LBB0_1062
	s_mov_b64 s[30:31], s[28:29]
	s_branch .LBB0_1058

; #define PG8_WAIT_V(n) asm volatile("s_waitcnt vmcnt(" #n ")" ::: "memory")
; template <class Epi, class Sched, bool ALIGN_EPI = true, bool F8 = false>
; __device__ __forceinline__ void gemm_phase(PG8_LAS unsigned char* lds, const Sched& S, const Epi& E) {
;     ...
;         for (int t = 0; t < nt; t += 2) {
;             const bool last = (t == nt - 2);
;             if constexpr (Sched::GATHER) { if (last && has_next) S.a_off(nxt, Rs, Cs, voffAn); }
;             const char* a1 = cA + (size_t)(t + 1) * kstep;
;             const char* a2 = last ? nA : cA + (size_t)(t + 2) * kstep; const char* b2 = last ? nB : cB + (size_t)(t + 2) * kstepB;
;             const char* a3 = a2 + kstep; const char* b3 = b2 + kstepB;
;             unsigned vA2[2][2];
; #pragma unroll
;             for (int h = 0; h < 2; ++h)
; #pragma unroll
;                 for (int i = 0; i < 2; ++i) { if constexpr (Sched::GATHER) vA2[h][i] = (last && has_next) ? voffAn[h][i] : voffA[h][i]; else vA2[h][i] = voffA[h][i]; }
;             PG8_LDB(B0, 0, 0); PG8_LDB(B1, 0, 1); PG8_SCHED; PG8_LDA(At, 0, 0); PG8_STAGE(PG8_SA(1, 1), a1, voffA[1]);
;             PG8_WAIT_V(8); PG8_WAIT_L(0); PG8_BAR; PG8_MMA(0, 0, At, B0); PG8_MMA(0, 1, At, B1); PG8_BAR; PG8_SCHED;
;             PG8_LDA(At, 0, 1); PG8_STAGE(PG8_SB(0, 0), b2, voffB[0]); PG8_STAGE(PG8_SB(0, 1), b2, voffB[1]); PG8_STAGE(PG8_SA(0, 0), a2, vA2[0]);
;             PG8_WAIT_V(8); PG8_WAIT_L(0); PG8_BAR; PG8_MMA(1, 0, At, B0); PG8_MMA(1, 1, At, B1); PG8_BAR; PG8_SCHED;
;             PG8_LDB(B0, 1, 0); PG8_LDB(B1, 1, 1); PG8_SCHED; PG8_LDA(At, 1, 0); PG8_STAGE(PG8_SA(0, 1), a2, vA2[1]);
;             PG8_WAIT_V(8); PG8_WAIT_L(0); PG8_BAR; PG8_MMA(0, 0, At, B0); PG8_MMA(0, 1, At, B1); PG8_BAR; PG8_SCHED;
;             PG8_LDA(At, 1, 1); PG8_STAGE(PG8_SB(1, 0), b3, voffB[0]); PG8_STAGE(PG8_SB(1, 1), b3, voffB[1]); PG8_STAGE(PG8_SA(1, 0), a3, vA2[0]);
;             PG8_WAIT_V(8); PG8_WAIT_L(0); PG8_BAR; PG8_MMA(1, 0, At, B0); PG8_MMA(1, 1, At, B1); PG8_BAR; PG8_SCHED;
;     __device__ __forceinline__ bool next(int i, GUnit& u) const { const int L = i * G + c; const int ti = L >> 3, ct = L & 7; if (ti >= __builtin_amdgcn_readfirstlane(pre[NE])) return false;
;         int e = 0;
; #pragma unroll 1
;         for (int s = 16; s >= 1; s >>= 1) if (pre[e + s] <= ti) e += s;
;         e = __builtin_amdgcn_readfirstlane(e);
.Lpk1_1060:
	v_add_u32_e32 v2, s12, v210
	v_add_u32_e32 v14, s62, v210
	s_add_u32 s28, s30, 0x100
	ds_read_b128 v[18:21], v2
	ds_read_b128 v[22:25], v2 offset:1024
	ds_read_b128 v[26:29], v2 offset:2048
	ds_read_b128 v[30:33], v2 offset:3072
	ds_read_b128 v[2:5], v14
	ds_read_b128 v[6:9], v14 offset:1024
	ds_read_b128 v[10:13], v14 offset:2048
	ds_read_b128 v[14:17], v14 offset:3072
	s_addc_u32 s29, s31, 0
	s_and_b64 s[42:43], s[40:41], exec
	s_cselect_b32 s42, 0, s28
	s_cselect_b32 s43, 0, s29
	s_add_u32 s42, s6, s42
	s_addc_u32 s43, s7, s43
	s_and_b64 s[40:41], s[40:41], exec
	s_cselect_b32 s41, s25, s68
	s_cselect_b32 s40, s24, s21
	v_lshl_add_u64 v[204:205], v[196:197], 0, s[30:31]
	s_add_i32 m0, s52, 0xc000
	ds_read_b128 v[222:225], v213
	ds_read_b128 v[226:229], v213 offset:1024
	ds_read_b128 v[230:233], v213 offset:2048
	ds_read_b128 v[234:237], v213 offset:3072
	ds_read_b128 v[238:241], v213 offset:4096
	ds_read_b128 v[242:245], v213 offset:5120
	ds_read_b128 v[246:249], v213 offset:6144
	ds_read_b128 v[250:253], v213 offset:7168
	global_load_lds_dwordx4 v[204:205], off
	v_lshl_add_u64 v[204:205], v[194:195], 0, s[30:31]
	s_add_i32 m0, s52, 0xe000
	s_nop 0
	global_load_lds_dwordx4 v[204:205], off
	s_waitcnt vmcnt(8)
	s_waitcnt lgkmcnt(0)
	s_barrier
	s_setprio 2
	v_mfma_f32_16x16x128_f8f6f4 v[142:145], v[18:25], v[222:229], 0
	v_mfma_f32_16x16x128_f8f6f4 v[138:141], v[26:33], v[222:229], 0
	v_mfma_f32_16x16x128_f8f6f4 v[134:137], v[18:25], v[230:237], 0
	v_mfma_f32_16x16x128_f8f6f4 v[130:133], v[26:33], v[230:237], 0
	v_mfma_f32_16x16x128_f8f6f4 v[126:129], v[18:25], v[238:245], 0
	v_mfma_f32_16x16x128_f8f6f4 v[122:125], v[26:33], v[238:245], 0
	v_mfma_f32_16x16x128_f8f6f4 v[118:121], v[18:25], v[246:253], 0
	v_mfma_f32_16x16x128_f8f6f4 v[114:117], v[26:33], v[246:253], 0
	s_nop 3
	v_mfma_f32_16x16x128_f8f6f4 v[110:113], v[2:9], v[222:229], 0
	v_mfma_f32_16x16x128_f8f6f4 v[106:109], v[10:17], v[222:229], 0
	v_mfma_f32_16x16x128_f8f6f4 v[102:105], v[2:9], v[230:237], 0
	v_mfma_f32_16x16x128_f8f6f4 v[98:101], v[10:17], v[230:237], 0
	v_mfma_f32_16x16x128_f8f6f4 v[94:97], v[2:9], v[238:245], 0
	v_mfma_f32_16x16x128_f8f6f4 v[90:93], v[10:17], v[238:245], 0
	v_mfma_f32_16x16x128_f8f6f4 v[86:89], v[2:9], v[246:253], 0
	v_mfma_f32_16x16x128_f8f6f4 v[82:85], v[10:17], v[246:253], 0
	s_setprio 0
	s_add_i32 s30, s12, s48
	v_lshl_add_u64 v[204:205], s[40:41], 0, v[162:163]
	s_mov_b32 m0, s30
	ds_read_b128 v[222:225], v213 offset:16384
	ds_read_b128 v[226:229], v213 offset:17408
	ds_read_b128 v[230:233], v213 offset:18432
	ds_read_b128 v[234:237], v213 offset:19456
	ds_read_b128 v[238:241], v213 offset:20480
	ds_read_b128 v[242:245], v213 offset:21504
	ds_read_b128 v[246:249], v213 offset:22528
	ds_read_b128 v[250:253], v213 offset:23552
	global_load_lds_dwordx4 v[204:205], off
	v_lshl_add_u64 v[204:205], s[40:41], 0, v[164:165]
	s_add_i32 m0, s30, 0x2000
	s_add_i32 s30, s62, s48
	global_load_lds_dwordx4 v[204:205], off
	v_lshl_add_u64 v[204:205], s[40:41], 0, v[166:167]
	s_mov_b32 m0, s30
	v_mov_b32_e32 v203, v171
	global_load_lds_dwordx4 v[204:205], off
	v_lshl_add_u64 v[204:205], s[40:41], 0, v[168:169]
	s_add_i32 m0, s30, 0x2000
	s_nop 0
	global_load_lds_dwordx4 v[204:205], off
	s_mov_b32 m0, s52
	v_lshl_add_u64 v[204:205], s[42:43], 0, v[170:171]
	global_load_lds_dwordx4 v170, s[42:43]
	s_mov_b32 m0, s53
	s_nop 0
	global_load_lds_dwordx4 v202, s[42:43]
	s_waitcnt vmcnt(8)
	s_waitcnt lgkmcnt(0)
	v_lshl_add_u64 v[202:203], s[42:43], 0, v[202:203]
	s_barrier
	s_setprio 2
	v_mfma_f32_16x16x128_f8f6f4 v[78:81], v[18:25], v[222:229], 0
	v_mfma_f32_16x16x128_f8f6f4 v[74:77], v[26:33], v[222:229], 0
	v_mfma_f32_16x16x128_f8f6f4 v[70:73], v[18:25], v[230:237], 0
	v_mfma_f32_16x16x128_f8f6f4 v[66:69], v[26:33], v[230:237], 0
	v_mfma_f32_16x16x128_f8f6f4 v[62:65], v[18:25], v[238:245], 0
	v_mfma_f32_16x16x128_f8f6f4 v[58:61], v[26:33], v[238:245], 0
	v_mfma_f32_16x16x128_f8f6f4 v[54:57], v[18:25], v[246:253], 0
	v_mfma_f32_16x16x128_f8f6f4 v[50:53], v[26:33], v[246:253], 0
	s_nop 3
	v_mfma_f32_16x16x128_f8f6f4 v[46:49], v[2:9], v[222:229], 0
	v_mfma_f32_16x16x128_f8f6f4 v[42:45], v[10:17], v[222:229], 0
	v_mfma_f32_16x16x128_f8f6f4 v[38:41], v[2:9], v[230:237], 0
	v_mfma_f32_16x16x128_f8f6f4 v[34:37], v[10:17], v[230:237], 0
	v_mfma_f32_16x16x128_f8f6f4 v[146:149], v[2:9], v[238:245], 0
	v_mfma_f32_16x16x128_f8f6f4 v[150:153], v[10:17], v[238:245], 0
	v_mfma_f32_16x16x128_f8f6f4 v[154:157], v[2:9], v[246:253], 0
	v_mfma_f32_16x16x128_f8f6f4 v[158:161], v[10:17], v[246:253], 0
	s_setprio 0
	s_add_i32 s70, 0, 0x18000
	s_add_i32 s71, 0, 0x1c000
	v_add_u32_e32 v14, s70, v210
	v_add_u32_e32 v30, s71, v210
	ds_read_b128 v[2:5], v14
	ds_read_b128 v[6:9], v14 offset:1024
	ds_read_b128 v[10:13], v14 offset:2048
	ds_read_b128 v[14:17], v14 offset:3072
	ds_read_b128 v[18:21], v30
	ds_read_b128 v[22:25], v30 offset:1024
	ds_read_b128 v[26:29], v30 offset:2048
	ds_read_b128 v[30:33], v30 offset:3072
	s_mov_b32 m0, s58
	v_lshl_add_u64 v[200:201], s[42:43], 0, v[200:201]
	ds_read_b128 v[222:225], v213 offset:32768
	ds_read_b128 v[226:229], v213 offset:33792
	ds_read_b128 v[230:233], v213 offset:34816
	ds_read_b128 v[234:237], v213 offset:35840
	ds_read_b128 v[238:241], v213 offset:36864
	ds_read_b128 v[242:245], v213 offset:37888
	ds_read_b128 v[246:249], v213 offset:38912
	ds_read_b128 v[250:253], v213 offset:39936
	global_load_lds_dwordx4 v[200:201], off
	v_lshl_add_u64 v[198:199], s[42:43], 0, v[198:199]
	s_mov_b32 m0, s59
	s_nop 0
	global_load_lds_dwordx4 v[198:199], off
	s_waitcnt vmcnt(8)
	s_waitcnt lgkmcnt(0)
	s_barrier
; #define PG8_WAIT_V(n) asm volatile("s_waitcnt vmcnt(" #n ")" ::: "memory")
; template <class Epi, class Sched, bool ALIGN_EPI = true, bool F8 = false>
; __device__ __forceinline__ void gemm_phase(PG8_LAS unsigned char* lds, const Sched& S, const Epi& E) {
;     ...
;         for (int t = 0; t < nt; t += 2) {
;             const bool last = (t == nt - 2);
;             if constexpr (Sched::GATHER) { if (last && has_next) S.a_off(nxt, Rs, Cs, voffAn); }
;             const char* a1 = cA + (size_t)(t + 1) * kstep;
;             const char* a2 = last ? nA : cA + (size_t)(t + 2) * kstep; const char* b2 = last ? nB : cB + (size_t)(t + 2) * kstepB;
;             const char* a3 = a2 + kstep; const char* b3 = b2 + kstepB;
;             unsigned vA2[2][2];
; #pragma unroll
;             for (int h = 0; h < 2; ++h)
; #pragma unroll
;                 for (int i = 0; i < 2; ++i) { if constexpr (Sched::GATHER) vA2[h][i] = (last && has_next) ? voffAn[h][i] : voffA[h][i]; else vA2[h][i] = voffA[h][i]; }
;             PG8_LDB(B0, 0, 0); PG8_LDB(B1, 0, 1); PG8_SCHED; PG8_LDA(At, 0, 0); PG8_STAGE(PG8_SA(1, 1), a1, voffA[1]);
;             PG8_WAIT_V(8); PG8_WAIT_L(0); PG8_BAR; PG8_MMA(0, 0, At, B0); PG8_MMA(0, 1, At, B1); PG8_BAR; PG8_SCHED;
;             PG8_LDA(At, 0, 1); PG8_STAGE(PG8_SB(0, 0), b2, voffB[0]); PG8_STAGE(PG8_SB(0, 1), b2, voffB[1]); PG8_STAGE(PG8_SA(0, 0), a2, vA2[0]);
;             PG8_WAIT_V(8); PG8_WAIT_L(0); PG8_BAR; PG8_MMA(1, 0, At, B0); PG8_MMA(1, 1, At, B1); PG8_BAR; PG8_SCHED;
;             PG8_LDB(B0, 1, 0); PG8_LDB(B1, 1, 1); PG8_SCHED; PG8_LDA(At, 1, 0); PG8_STAGE(PG8_SA(0, 1), a2, vA2[1]);
;             PG8_WAIT_V(8); PG8_WAIT_L(0); PG8_BAR; PG8_MMA(0, 0, At, B0); PG8_MMA(0, 1, At, B1); PG8_BAR; PG8_SCHED;
;             PG8_LDA(At, 1, 1); PG8_STAGE(PG8_SB(1, 0), b3, voffB[0]); PG8_STAGE(PG8_SB(1, 1), b3, voffB[1]); PG8_STAGE(PG8_SA(1, 0), a3, vA2[0]);
;             PG8_WAIT_V(8); PG8_WAIT_L(0); PG8_BAR; PG8_MMA(1, 0, At, B0); PG8_MMA(1, 1, At, B1); PG8_BAR; PG8_SCHED;
;     __device__ __forceinline__ bool next(int i, GUnit& u) const { const int L = i * G + c; const int ti = L >> 3, ct = L & 7; if (ti >= __builtin_amdgcn_readfirstlane(pre[NE])) return false;
;         int e = 0;
; #pragma unroll 1
;         for (int s = 16; s >= 1; s >>= 1) if (pre[e + s] <= ti) e += s;
;         e = __builtin_amdgcn_readfirstlane(e);
	s_setprio 2
	v_mfma_f32_16x16x128_f8f6f4 v[142:145], v[2:9], v[222:229], v[142:145]
	v_mfma_f32_16x16x128_f8f6f4 v[138:141], v[10:17], v[222:229], v[138:141]
	v_mfma_f32_16x16x128_f8f6f4 v[134:137], v[2:9], v[230:237], v[134:137]
	v_mfma_f32_16x16x128_f8f6f4 v[130:133], v[10:17], v[230:237], v[130:133]
	v_mfma_f32_16x16x128_f8f6f4 v[126:129], v[2:9], v[238:245], v[126:129]
	v_mfma_f32_16x16x128_f8f6f4 v[122:125], v[10:17], v[238:245], v[122:125]
	v_mfma_f32_16x16x128_f8f6f4 v[118:121], v[2:9], v[246:253], v[118:121]
	v_mfma_f32_16x16x128_f8f6f4 v[114:117], v[10:17], v[246:253], v[114:117]
	s_nop 3
	v_mfma_f32_16x16x128_f8f6f4 v[110:113], v[18:25], v[222:229], v[110:113]
	v_mfma_f32_16x16x128_f8f6f4 v[106:109], v[26:33], v[222:229], v[106:109]
	v_mfma_f32_16x16x128_f8f6f4 v[102:105], v[18:25], v[230:237], v[102:105]
	v_mfma_f32_16x16x128_f8f6f4 v[98:101], v[26:33], v[230:237], v[98:101]
	v_mfma_f32_16x16x128_f8f6f4 v[94:97], v[18:25], v[238:245], v[94:97]
	v_mfma_f32_16x16x128_f8f6f4 v[90:93], v[26:33], v[238:245], v[90:93]
	v_mfma_f32_16x16x128_f8f6f4 v[86:89], v[18:25], v[246:253], v[86:89]
	v_mfma_f32_16x16x128_f8f6f4 v[82:85], v[26:33], v[246:253], v[82:85]
	s_setprio 0
	s_add_u32 s30, s40, 0x8000
	s_addc_u32 s31, s41, 0
	s_add_i32 s40, s70, s48
	v_lshl_add_u64 v[198:199], s[30:31], 0, v[162:163]
	s_mov_b32 m0, s40
	ds_read_b128 v[222:225], v213 offset:49152
	ds_read_b128 v[226:229], v213 offset:50176
	ds_read_b128 v[230:233], v213 offset:51200
	ds_read_b128 v[234:237], v213 offset:52224
	ds_read_b128 v[238:241], v213 offset:53248
	ds_read_b128 v[242:245], v213 offset:54272
	ds_read_b128 v[246:249], v213 offset:55296
	ds_read_b128 v[250:253], v213 offset:56320
	global_load_lds_dwordx4 v[198:199], off
	v_lshl_add_u64 v[198:199], s[30:31], 0, v[164:165]
	s_add_i32 m0, s40, 0x2000
	s_add_i32 s40, s71, s48
	global_load_lds_dwordx4 v[198:199], off
	v_lshl_add_u64 v[198:199], s[30:31], 0, v[166:167]
	s_mov_b32 m0, s40
	s_nop 0
	global_load_lds_dwordx4 v[198:199], off
	v_lshl_add_u64 v[198:199], s[30:31], 0, v[168:169]
	s_add_i32 m0, s40, 0x2000
	s_nop 0
	global_load_lds_dwordx4 v[198:199], off
	v_lshl_add_u64 v[198:199], v[204:205], 0, s[18:19]
	s_mov_b32 m0, s60
	s_nop 0
	global_load_lds_dwordx4 v[198:199], off
	v_lshl_add_u64 v[198:199], v[202:203], 0, s[18:19]
	s_mov_b32 m0, s61
	s_nop 0
	global_load_lds_dwordx4 v[198:199], off
	s_waitcnt vmcnt(8)
	s_waitcnt lgkmcnt(0)
	s_barrier
	s_setprio 2
	v_mfma_f32_16x16x128_f8f6f4 v[78:81], v[2:9], v[222:229], v[78:81]
	v_mfma_f32_16x16x128_f8f6f4 v[74:77], v[10:17], v[222:229], v[74:77]
	v_mfma_f32_16x16x128_f8f6f4 v[70:73], v[2:9], v[230:237], v[70:73]
	v_mfma_f32_16x16x128_f8f6f4 v[66:69], v[10:17], v[230:237], v[66:69]
	v_mfma_f32_16x16x128_f8f6f4 v[62:65], v[2:9], v[238:245], v[62:65]
	v_mfma_f32_16x16x128_f8f6f4 v[58:61], v[10:17], v[238:245], v[58:61]
	v_mfma_f32_16x16x128_f8f6f4 v[54:57], v[2:9], v[246:253], v[54:57]
	v_mfma_f32_16x16x128_f8f6f4 v[50:53], v[10:17], v[246:253], v[50:53]
	s_nop 3
	v_mfma_f32_16x16x128_f8f6f4 v[46:49], v[18:25], v[222:229], v[46:49]
	v_mfma_f32_16x16x128_f8f6f4 v[42:45], v[26:33], v[222:229], v[42:45]
	v_mfma_f32_16x16x128_f8f6f4 v[38:41], v[18:25], v[230:237], v[38:41]
	v_mfma_f32_16x16x128_f8f6f4 v[34:37], v[26:33], v[230:237], v[34:37]
	v_mfma_f32_16x16x128_f8f6f4 v[146:149], v[18:25], v[238:245], v[146:149]
	v_mfma_f32_16x16x128_f8f6f4 v[150:153], v[26:33], v[238:245], v[150:153]
	v_mfma_f32_16x16x128_f8f6f4 v[154:157], v[18:25], v[246:253], v[154:157]
	v_mfma_f32_16x16x128_f8f6f4 v[158:161], v[26:33], v[246:253], v[158:161]
	s_setprio 0
	s_add_i32 s69, s69, 2
	s_add_u32 s21, s21, 0x10000
	s_addc_u32 s68, s68, 0
	s_cmp_gt_u32 s69, 13
	s_cbranch_scc1 .LBB0_1062
	s_mov_b64 s[30:31], s[28:29]
	s_branch .Lh1_1058

; #define PG8_STAGE(bufoff, gbase, voff) do { _Pragma("unroll") for (int _i = 0; _i < 2; ++_i) \
;         __builtin_amdgcn_global_load_lds((const unsigned*)((const char*)(gbase) + (voff)[_i]), (PG8_LAS unsigned*)(lds + (bufoff) + ldsw + _i * 8192), 16, 0, 0); } while (0)
; #define PG8_WAIT_V(n) asm volatile("s_waitcnt vmcnt(" #n ")" ::: "memory")
; #define PG8_WAIT_L(n) asm volatile("s_waitcnt lgkmcnt(" #n ")" ::: "memory")
; #define PG8_BAR __builtin_amdgcn_s_barrier()
; #define PG8_SCHED __builtin_amdgcn_sched_barrier(0)
; template <class Epi, class Sched, bool ALIGN_EPI = true, bool F8 = false>
; __device__ __forceinline__ void gemm_phase(PG8_LAS unsigned char* lds, const Sched& S, const Epi& E) {
;     ...
;             if constexpr (Sched::GATHER) { if (last && has_next) S.a_off(nxt, Rs, Cs, voffAn); }
;             const char* a1 = cA + (size_t)(t + 1) * kstep;
;             const char* a2 = last ? nA : cA + (size_t)(t + 2) * kstep; const char* b2 = last ? nB : cB + (size_t)(t + 2) * kstepB;
;             const char* a3 = a2 + kstep; const char* b3 = b2 + kstepB;
;             unsigned vA2[2][2];
; #pragma unroll
;             for (int h = 0; h < 2; ++h)
; #pragma unroll
;                 for (int i = 0; i < 2; ++i) { if constexpr (Sched::GATHER) vA2[h][i] = (last && has_next) ? voffAn[h][i] : voffA[h][i]; else vA2[h][i] = voffA[h][i]; }
;             PG8_LDB(B0, 0, 0); PG8_LDB(B1, 0, 1); PG8_SCHED; PG8_LDA(At, 0, 0); PG8_STAGE(PG8_SA(1, 1), a1, voffA[1]);
;             PG8_WAIT_V(8); PG8_WAIT_L(0); PG8_BAR; PG8_MMA(0, 0, At, B0); PG8_MMA(0, 1, At, B1); PG8_BAR; PG8_SCHED;
;             PG8_LDA(At, 0, 1); PG8_STAGE(PG8_SB(0, 0), b2, voffB[0]); PG8_STAGE(PG8_SB(0, 1), b2, voffB[1]); PG8_STAGE(PG8_SA(0, 0), a2, vA2[0]);
;             PG8_WAIT_V(8); PG8_WAIT_L(0); PG8_BAR; PG8_MMA(1, 0, At, B0); PG8_MMA(1, 1, At, B1); PG8_BAR; PG8_SCHED;
;             PG8_LDB(B0, 1, 0); PG8_LDB(B1, 1, 1); PG8_SCHED; PG8_LDA(At, 1, 0); PG8_STAGE(PG8_SA(0, 1), a2, vA2[1]);
;             PG8_WAIT_V(8); PG8_WAIT_L(0); PG8_BAR; PG8_MMA(0, 0, At, B0); PG8_MMA(0, 1, At, B1); PG8_BAR; PG8_SCHED;
;             PG8_LDA(At, 1, 1); PG8_STAGE(PG8_SB(1, 0), b3, voffB[0]); PG8_STAGE(PG8_SB(1, 1), b3, voffB[1]); PG8_STAGE(PG8_SA(1, 0), a3, vA2[0]);
;             PG8_WAIT_V(8); PG8_WAIT_L(0); PG8_BAR; PG8_MMA(1, 0, At, B0); PG8_MMA(1, 1, At, B1); PG8_BAR; PG8_SCHED;
.Lh1_1060:
	v_add_u32_e32 v2, s12, v210
	v_add_u32_e32 v14, s62, v210
	s_add_u32 s28, s30, 0x100
	ds_read_b128 v[18:21], v2
	ds_read_b128 v[22:25], v2 offset:1024
	ds_read_b128 v[26:29], v2 offset:2048
	ds_read_b128 v[30:33], v2 offset:3072
	ds_read_b128 v[2:5], v14
	ds_read_b128 v[6:9], v14 offset:1024
	ds_read_b128 v[10:13], v14 offset:2048
	ds_read_b128 v[14:17], v14 offset:3072
	s_addc_u32 s29, s31, 0
	s_and_b64 s[42:43], s[40:41], exec
	s_cselect_b32 s42, 0, s28
	s_cselect_b32 s43, 0, s29
	s_add_u32 s42, s6, s42
	s_addc_u32 s43, s7, s43
	s_and_b64 s[40:41], s[40:41], exec
	s_cselect_b32 s41, s25, s68
	s_cselect_b32 s40, s24, s21
	v_lshl_add_u64 v[204:205], v[196:197], 0, s[30:31]
	s_add_i32 m0, s52, 0xc000
	ds_read_b128 v[222:225], v213
	ds_read_b128 v[226:229], v213 offset:1024
	ds_read_b128 v[230:233], v213 offset:2048
	ds_read_b128 v[234:237], v213 offset:3072
	ds_read_b128 v[238:241], v213 offset:4096
	ds_read_b128 v[242:245], v213 offset:5120
	ds_read_b128 v[246:249], v213 offset:6144
	ds_read_b128 v[250:253], v213 offset:7168
	global_load_lds_dwordx4 v[204:205], off
	v_lshl_add_u64 v[204:205], v[194:195], 0, s[30:31]
	s_add_i32 m0, s52, 0xe000
	s_nop 0
	global_load_lds_dwordx4 v[204:205], off
	s_waitcnt vmcnt(8)
	s_waitcnt lgkmcnt(0)
	s_barrier
	s_setprio 2
	v_mfma_f32_16x16x128_f8f6f4 v[142:145], v[18:25], v[222:229], v[142:145]
	v_mfma_f32_16x16x128_f8f6f4 v[138:141], v[26:33], v[222:229], v[138:141]
	v_mfma_f32_16x16x128_f8f6f4 v[134:137], v[18:25], v[230:237], v[134:137]
	v_mfma_f32_16x16x128_f8f6f4 v[130:133], v[26:33], v[230:237], v[130:133]
	v_mfma_f32_16x16x128_f8f6f4 v[126:129], v[18:25], v[238:245], v[126:129]
	v_mfma_f32_16x16x128_f8f6f4 v[122:125], v[26:33], v[238:245], v[122:125]
	v_mfma_f32_16x16x128_f8f6f4 v[118:121], v[18:25], v[246:253], v[118:121]
	v_mfma_f32_16x16x128_f8f6f4 v[114:117], v[26:33], v[246:253], v[114:117]
	s_nop 3
	v_mfma_f32_16x16x128_f8f6f4 v[110:113], v[2:9], v[222:229], v[110:113]
	v_mfma_f32_16x16x128_f8f6f4 v[106:109], v[10:17], v[222:229], v[106:109]
	v_mfma_f32_16x16x128_f8f6f4 v[102:105], v[2:9], v[230:237], v[102:105]
	v_mfma_f32_16x16x128_f8f6f4 v[98:101], v[10:17], v[230:237], v[98:101]
	v_mfma_f32_16x16x128_f8f6f4 v[94:97], v[2:9], v[238:245], v[94:97]
	v_mfma_f32_16x16x128_f8f6f4 v[90:93], v[10:17], v[238:245], v[90:93]
	v_mfma_f32_16x16x128_f8f6f4 v[86:89], v[2:9], v[246:253], v[86:89]
	v_mfma_f32_16x16x128_f8f6f4 v[82:85], v[10:17], v[246:253], v[82:85]
	s_setprio 0
	s_add_i32 s30, s12, s48
	v_lshl_add_u64 v[204:205], s[40:41], 0, v[162:163]
	s_mov_b32 m0, s30
	ds_read_b128 v[222:225], v213 offset:16384
	ds_read_b128 v[226:229], v213 offset:17408
	ds_read_b128 v[230:233], v213 offset:18432
	ds_read_b128 v[234:237], v213 offset:19456
	ds_read_b128 v[238:241], v213 offset:20480
	ds_read_b128 v[242:245], v213 offset:21504
	ds_read_b128 v[246:249], v213 offset:22528
	ds_read_b128 v[250:253], v213 offset:23552
	global_load_lds_dwordx4 v[204:205], off
	v_lshl_add_u64 v[204:205], s[40:41], 0, v[164:165]
	s_add_i32 m0, s30, 0x2000
	s_add_i32 s30, s62, s48
	global_load_lds_dwordx4 v[204:205], off
	v_lshl_add_u64 v[204:205], s[40:41], 0, v[166:167]
	s_mov_b32 m0, s30
	v_mov_b32_e32 v203, v171
	global_load_lds_dwordx4 v[204:205], off
	v_lshl_add_u64 v[204:205], s[40:41], 0, v[168:169]
	s_add_i32 m0, s30, 0x2000
	s_nop 0
	global_load_lds_dwordx4 v[204:205], off
	s_mov_b32 m0, s52
	v_lshl_add_u64 v[204:205], s[42:43], 0, v[170:171]
	global_load_lds_dwordx4 v170, s[42:43]
	s_mov_b32 m0, s53
	s_nop 0
	global_load_lds_dwordx4 v202, s[42:43]
	s_waitcnt vmcnt(8)
	s_waitcnt lgkmcnt(0)
	v_lshl_add_u64 v[202:203], s[42:43], 0, v[202:203]
	s_barrier
	s_setprio 2
	v_mfma_f32_16x16x128_f8f6f4 v[78:81], v[18:25], v[222:229], v[78:81]
	v_mfma_f32_16x16x128_f8f6f4 v[74:77], v[26:33], v[222:229], v[74:77]
	v_mfma_f32_16x16x128_f8f6f4 v[70:73], v[18:25], v[230:237], v[70:73]
	v_mfma_f32_16x16x128_f8f6f4 v[66:69], v[26:33], v[230:237], v[66:69]
	v_mfma_f32_16x16x128_f8f6f4 v[62:65], v[18:25], v[238:245], v[62:65]
	v_mfma_f32_16x16x128_f8f6f4 v[58:61], v[26:33], v[238:245], v[58:61]
	v_mfma_f32_16x16x128_f8f6f4 v[54:57], v[18:25], v[246:253], v[54:57]
	v_mfma_f32_16x16x128_f8f6f4 v[50:53], v[26:33], v[246:253], v[50:53]
	s_nop 3
	v_mfma_f32_16x16x128_f8f6f4 v[46:49], v[2:9], v[222:229], v[46:49]
	v_mfma_f32_16x16x128_f8f6f4 v[42:45], v[10:17], v[222:229], v[42:45]
	v_mfma_f32_16x16x128_f8f6f4 v[38:41], v[2:9], v[230:237], v[38:41]
	v_mfma_f32_16x16x128_f8f6f4 v[34:37], v[10:17], v[230:237], v[34:37]
	v_mfma_f32_16x16x128_f8f6f4 v[146:149], v[2:9], v[238:245], v[146:149]
	v_mfma_f32_16x16x128_f8f6f4 v[150:153], v[10:17], v[238:245], v[150:153]
	v_mfma_f32_16x16x128_f8f6f4 v[154:157], v[2:9], v[246:253], v[154:157]
	v_mfma_f32_16x16x128_f8f6f4 v[158:161], v[10:17], v[246:253], v[158:161]
	s_setprio 0
	s_add_i32 s70, 0, 0x18000
	s_add_i32 s71, 0, 0x1c000
	v_add_u32_e32 v14, s70, v210
	v_add_u32_e32 v30, s71, v210
	ds_read_b128 v[2:5], v14
	ds_read_b128 v[6:9], v14 offset:1024
	ds_read_b128 v[10:13], v14 offset:2048
	ds_read_b128 v[14:17], v14 offset:3072
	ds_read_b128 v[18:21], v30
	ds_read_b128 v[22:25], v30 offset:1024
	ds_read_b128 v[26:29], v30 offset:2048
	ds_read_b128 v[30:33], v30 offset:3072
	s_mov_b32 m0, s58
	v_lshl_add_u64 v[200:201], s[42:43], 0, v[200:201]
	ds_read_b128 v[222:225], v213 offset:32768
	ds_read_b128 v[226:229], v213 offset:33792
	ds_read_b128 v[230:233], v213 offset:34816
	ds_read_b128 v[234:237], v213 offset:35840
	ds_read_b128 v[238:241], v213 offset:36864
	ds_read_b128 v[242:245], v213 offset:37888
	ds_read_b128 v[246:249], v213 offset:38912
	ds_read_b128 v[250:253], v213 offset:39936
	global_load_lds_dwordx4 v[200:201], off
	v_lshl_add_u64 v[198:199], s[42:43], 0, v[198:199]
	s_mov_b32 m0, s59
	s_nop 0
	global_load_lds_dwordx4 v[198:199], off
	s_waitcnt vmcnt(8)
	s_waitcnt lgkmcnt(0)
	s_barrier
; #define PG8_STAGE(bufoff, gbase, voff) do { _Pragma("unroll") for (int _i = 0; _i < 2; ++_i) \
;         __builtin_amdgcn_global_load_lds((const unsigned*)((const char*)(gbase) + (voff)[_i]), (PG8_LAS unsigned*)(lds + (bufoff) + ldsw + _i * 8192), 16, 0, 0); } while (0)
; #define PG8_WAIT_V(n) asm volatile("s_waitcnt vmcnt(" #n ")" ::: "memory")
; #define PG8_WAIT_L(n) asm volatile("s_waitcnt lgkmcnt(" #n ")" ::: "memory")
; #define PG8_BAR __builtin_amdgcn_s_barrier()
; #define PG8_SCHED __builtin_amdgcn_sched_barrier(0)
; template <class Epi, class Sched, bool ALIGN_EPI = true, bool F8 = false>
; __device__ __forceinline__ void gemm_phase(PG8_LAS unsigned char* lds, const Sched& S, const Epi& E) {
;     ...
;             if constexpr (Sched::GATHER) { if (last && has_next) S.a_off(nxt, Rs, Cs, voffAn); }
;             const char* a1 = cA + (size_t)(t + 1) * kstep;
;             const char* a2 = last ? nA : cA + (size_t)(t + 2) * kstep; const char* b2 = last ? nB : cB + (size_t)(t + 2) * kstepB;
;             const char* a3 = a2 + kstep; const char* b3 = b2 + kstepB;
;             unsigned vA2[2][2];
; #pragma unroll
;             for (int h = 0; h < 2; ++h)
; #pragma unroll
;                 for (int i = 0; i < 2; ++i) { if constexpr (Sched::GATHER) vA2[h][i] = (last && has_next) ? voffAn[h][i] : voffA[h][i]; else vA2[h][i] = voffA[h][i]; }
;             PG8_LDB(B0, 0, 0); PG8_LDB(B1, 0, 1); PG8_SCHED; PG8_LDA(At, 0, 0); PG8_STAGE(PG8_SA(1, 1), a1, voffA[1]);
;             PG8_WAIT_V(8); PG8_WAIT_L(0); PG8_BAR; PG8_MMA(0, 0, At, B0); PG8_MMA(0, 1, At, B1); PG8_BAR; PG8_SCHED;
;             PG8_LDA(At, 0, 1); PG8_STAGE(PG8_SB(0, 0), b2, voffB[0]); PG8_STAGE(PG8_SB(0, 1), b2, voffB[1]); PG8_STAGE(PG8_SA(0, 0), a2, vA2[0]);
;             PG8_WAIT_V(8); PG8_WAIT_L(0); PG8_BAR; PG8_MMA(1, 0, At, B0); PG8_MMA(1, 1, At, B1); PG8_BAR; PG8_SCHED;
;             PG8_LDB(B0, 1, 0); PG8_LDB(B1, 1, 1); PG8_SCHED; PG8_LDA(At, 1, 0); PG8_STAGE(PG8_SA(0, 1), a2, vA2[1]);
;             PG8_WAIT_V(8); PG8_WAIT_L(0); PG8_BAR; PG8_MMA(0, 0, At, B0); PG8_MMA(0, 1, At, B1); PG8_BAR; PG8_SCHED;
;             PG8_LDA(At, 1, 1); PG8_STAGE(PG8_SB(1, 0), b3, voffB[0]); PG8_STAGE(PG8_SB(1, 1), b3, voffB[1]); PG8_STAGE(PG8_SA(1, 0), a3, vA2[0]);
;             PG8_WAIT_V(8); PG8_WAIT_L(0); PG8_BAR; PG8_MMA(1, 0, At, B0); PG8_MMA(1, 1, At, B1); PG8_BAR; PG8_SCHED;
	s_setprio 2
	v_mfma_f32_16x16x128_f8f6f4 v[142:145], v[2:9], v[222:229], v[142:145]
	v_mfma_f32_16x16x128_f8f6f4 v[138:141], v[10:17], v[222:229], v[138:141]
	v_mfma_f32_16x16x128_f8f6f4 v[134:137], v[2:9], v[230:237], v[134:137]
	v_mfma_f32_16x16x128_f8f6f4 v[130:133], v[10:17], v[230:237], v[130:133]
	v_mfma_f32_16x16x128_f8f6f4 v[126:129], v[2:9], v[238:245], v[126:129]
	v_mfma_f32_16x16x128_f8f6f4 v[122:125], v[10:17], v[238:245], v[122:125]
	v_mfma_f32_16x16x128_f8f6f4 v[118:121], v[2:9], v[246:253], v[118:121]
	v_mfma_f32_16x16x128_f8f6f4 v[114:117], v[10:17], v[246:253], v[114:117]
	s_nop 3
	v_mfma_f32_16x16x128_f8f6f4 v[110:113], v[18:25], v[222:229], v[110:113]
	v_mfma_f32_16x16x128_f8f6f4 v[106:109], v[26:33], v[222:229], v[106:109]
	v_mfma_f32_16x16x128_f8f6f4 v[102:105], v[18:25], v[230:237], v[102:105]
	v_mfma_f32_16x16x128_f8f6f4 v[98:101], v[26:33], v[230:237], v[98:101]
	v_mfma_f32_16x16x128_f8f6f4 v[94:97], v[18:25], v[238:245], v[94:97]
	v_mfma_f32_16x16x128_f8f6f4 v[90:93], v[26:33], v[238:245], v[90:93]
	v_mfma_f32_16x16x128_f8f6f4 v[86:89], v[18:25], v[246:253], v[86:89]
	v_mfma_f32_16x16x128_f8f6f4 v[82:85], v[26:33], v[246:253], v[82:85]
	s_setprio 0
	s_add_u32 s30, s40, 0x8000
	s_addc_u32 s31, s41, 0
	s_add_i32 s40, s70, s48
	v_lshl_add_u64 v[198:199], s[30:31], 0, v[162:163]
	s_mov_b32 m0, s40
	ds_read_b128 v[222:225], v213 offset:49152
	ds_read_b128 v[226:229], v213 offset:50176
	ds_read_b128 v[230:233], v213 offset:51200
	ds_read_b128 v[234:237], v213 offset:52224
	ds_read_b128 v[238:241], v213 offset:53248
	ds_read_b128 v[242:245], v213 offset:54272
	ds_read_b128 v[246:249], v213 offset:55296
	ds_read_b128 v[250:253], v213 offset:56320
	global_load_lds_dwordx4 v[198:199], off
	v_lshl_add_u64 v[198:199], s[30:31], 0, v[164:165]
	s_add_i32 m0, s40, 0x2000
	s_add_i32 s40, s71, s48
	global_load_lds_dwordx4 v[198:199], off
	v_lshl_add_u64 v[198:199], s[30:31], 0, v[166:167]
	s_mov_b32 m0, s40
	s_nop 0
	global_load_lds_dwordx4 v[198:199], off
	v_lshl_add_u64 v[198:199], s[30:31], 0, v[168:169]
	s_add_i32 m0, s40, 0x2000
	s_nop 0
	global_load_lds_dwordx4 v[198:199], off
	v_lshl_add_u64 v[198:199], v[204:205], 0, s[18:19]
	s_mov_b32 m0, s60
	s_nop 0
	global_load_lds_dwordx4 v[198:199], off
	v_lshl_add_u64 v[198:199], v[202:203], 0, s[18:19]
	s_mov_b32 m0, s61
	s_nop 0
	global_load_lds_dwordx4 v[198:199], off
	s_waitcnt vmcnt(8)
	s_waitcnt lgkmcnt(0)
	s_barrier
	s_setprio 2
	v_mfma_f32_16x16x128_f8f6f4 v[78:81], v[2:9], v[222:229], v[78:81]
	v_mfma_f32_16x16x128_f8f6f4 v[74:77], v[10:17], v[222:229], v[74:77]
	v_mfma_f32_16x16x128_f8f6f4 v[70:73], v[2:9], v[230:237], v[70:73]
	v_mfma_f32_16x16x128_f8f6f4 v[66:69], v[10:17], v[230:237], v[66:69]
	v_mfma_f32_16x16x128_f8f6f4 v[62:65], v[2:9], v[238:245], v[62:65]
	v_mfma_f32_16x16x128_f8f6f4 v[58:61], v[10:17], v[238:245], v[58:61]
	v_mfma_f32_16x16x128_f8f6f4 v[54:57], v[2:9], v[246:253], v[54:57]
	v_mfma_f32_16x16x128_f8f6f4 v[50:53], v[10:17], v[246:253], v[50:53]
	s_nop 3
	v_mfma_f32_16x16x128_f8f6f4 v[46:49], v[18:25], v[222:229], v[46:49]
	v_mfma_f32_16x16x128_f8f6f4 v[42:45], v[26:33], v[222:229], v[42:45]
	v_mfma_f32_16x16x128_f8f6f4 v[38:41], v[18:25], v[230:237], v[38:41]
	v_mfma_f32_16x16x128_f8f6f4 v[34:37], v[26:33], v[230:237], v[34:37]
	v_mfma_f32_16x16x128_f8f6f4 v[146:149], v[18:25], v[238:245], v[146:149]
	v_mfma_f32_16x16x128_f8f6f4 v[150:153], v[26:33], v[238:245], v[150:153]
	v_mfma_f32_16x16x128_f8f6f4 v[154:157], v[18:25], v[246:253], v[154:157]
	v_mfma_f32_16x16x128_f8f6f4 v[158:161], v[26:33], v[246:253], v[158:161]
	s_setprio 0
	s_add_i32 s69, s69, 2
	s_add_u32 s21, s21, 0x10000
	s_addc_u32 s68, s68, 0
	s_cmp_gt_u32 s69, 13
	s_cbranch_scc1 .LBB0_1062
	s_mov_b64 s[30:31], s[28:29]
	s_branch .Lh1_1058

; #define PG8_WAIT_V(n) asm volatile("s_waitcnt vmcnt(" #n ")" ::: "memory")
; #define PG8_WAIT_L(n) asm volatile("s_waitcnt lgkmcnt(" #n ")" ::: "memory")
; template <class Epi, class Sched, bool ALIGN_EPI = true, bool F8 = false>
; __device__ __forceinline__ void gemm_phase(PG8_LAS unsigned char* lds, const Sched& S, const Epi& E) {
;     ...
;         for (int t = 0; t < nt; t += 2) {
;             const bool last = (t == nt - 2);
;             if constexpr (Sched::GATHER) { if (last && has_next) S.a_off(nxt, Rs, Cs, voffAn); }
;             const char* a1 = cA + (size_t)(t + 1) * kstep;
;             const char* a2 = last ? nA : cA + (size_t)(t + 2) * kstep; const char* b2 = last ? nB : cB + (size_t)(t + 2) * kstepB;
;             const char* a3 = a2 + kstep; const char* b3 = b2 + kstepB;
;             unsigned vA2[2][2];
; #pragma unroll
;             for (int h = 0; h < 2; ++h)
; #pragma unroll
;                 for (int i = 0; i < 2; ++i) { if constexpr (Sched::GATHER) vA2[h][i] = (last && has_next) ? voffAn[h][i] : voffA[h][i]; else vA2[h][i] = voffA[h][i]; }
;             PG8_LDB(B0, 0, 0); PG8_LDB(B1, 0, 1); PG8_SCHED; PG8_LDA(At, 0, 0); PG8_STAGE(PG8_SA(1, 1), a1, voffA[1]);
;             PG8_WAIT_V(8); PG8_WAIT_L(0); PG8_BAR; PG8_MMA(0, 0, At, B0); PG8_MMA(0, 1, At, B1); PG8_BAR; PG8_SCHED;
;             PG8_LDA(At, 0, 1); PG8_STAGE(PG8_SB(0, 0), b2, voffB[0]); PG8_STAGE(PG8_SB(0, 1), b2, voffB[1]); PG8_STAGE(PG8_SA(0, 0), a2, vA2[0]);
;             PG8_WAIT_V(8); PG8_WAIT_L(0); PG8_BAR; PG8_MMA(1, 0, At, B0); PG8_MMA(1, 1, At, B1); PG8_BAR; PG8_SCHED;
;             PG8_LDB(B0, 1, 0); PG8_LDB(B1, 1, 1); PG8_SCHED; PG8_LDA(At, 1, 0); PG8_STAGE(PG8_SA(0, 1), a2, vA2[1]);
;             PG8_WAIT_V(8); PG8_WAIT_L(0); PG8_BAR; PG8_MMA(0, 0, At, B0); PG8_MMA(0, 1, At, B1); PG8_BAR; PG8_SCHED;
;             PG8_LDA(At, 1, 1); PG8_STAGE(PG8_SB(1, 0), b3, voffB[0]); PG8_STAGE(PG8_SB(1, 1), b3, voffB[1]); PG8_STAGE(PG8_SA(1, 0), a3, vA2[0]);
;             PG8_WAIT_V(8); PG8_WAIT_L(0); PG8_BAR; PG8_MMA(1, 0, At, B0); PG8_MMA(1, 1, At, B1); PG8_BAR; PG8_SCHED;
;     ...
;         for (int a = 0; a < 2; ++a)
; #pragma unroll
;             for (int b = 0; b < 2; ++b)
; #pragma unroll
;                 for (int m = 0; m < 4; ++m)
; #pragma unroll
;                     for (int n = 0; n < 2; ++n) acc[a][b][m][n] = (f32x4){0.f, 0.f, 0.f, 0.f};
.Lpk0_1138:
	ds_read_b128 v[18:21], v189
	ds_read_b128 v[22:25], v189 offset:1024
	ds_read_b128 v[26:29], v189 offset:2048
	ds_read_b128 v[30:33], v189 offset:3072
	ds_read_b128 v[2:5], v190
	ds_read_b128 v[6:9], v190 offset:1024
	ds_read_b128 v[10:13], v190 offset:2048
	ds_read_b128 v[14:17], v190 offset:3072
	s_add_u32 s26, s24, 0x8000
	s_addc_u32 s27, s25, 0
	s_cmp_eq_u32 s68, 4
	s_cselect_b32 s30, s16, s26
	s_cselect_b32 s31, s17, s27
	s_cselect_b32 s28, s18, s23
	s_cselect_b32 s29, s19, s67
	s_add_u32 s26, s30, 0x8000
	s_addc_u32 s27, s31, 0
	s_add_i32 m0, s44, 0xc000
	ds_read_b128 v[194:197], v191
	ds_read_b128 v[198:201], v191 offset:1024
	ds_read_b128 v[202:205], v191 offset:2048
	ds_read_b128 v[206:209], v191 offset:3072
	ds_read_b128 v[210:213], v191 offset:4096
	ds_read_b128 v[214:217], v191 offset:5120
	ds_read_b128 v[218:221], v191 offset:6144
	ds_read_b128 v[222:225], v191 offset:7168
	global_load_lds_dwordx4 v184, s[24:25]
	s_add_i32 m0, s44, 0xe000
	s_nop 0
	global_load_lds_dwordx4 v182, s[24:25]
	s_waitcnt vmcnt(8)
	s_waitcnt lgkmcnt(0)
	s_setprio 1
	v_mfma_f32_16x16x128_f8f6f4 v[158:161], v[18:25], v[194:201], 0
	v_mfma_f32_16x16x128_f8f6f4 v[154:157], v[26:33], v[194:201], 0
	v_mfma_f32_16x16x128_f8f6f4 v[142:145], v[18:25], v[202:209], 0
	v_mfma_f32_16x16x128_f8f6f4 v[138:141], v[26:33], v[202:209], 0
	v_mfma_f32_16x16x128_f8f6f4 v[126:129], v[18:25], v[210:217], 0
	v_mfma_f32_16x16x128_f8f6f4 v[122:125], v[26:33], v[210:217], 0
	v_mfma_f32_16x16x128_f8f6f4 v[110:113], v[18:25], v[218:225], 0
	v_mfma_f32_16x16x128_f8f6f4 v[106:109], v[26:33], v[218:225], 0
	s_nop 3
	v_mfma_f32_16x16x128_f8f6f4 v[150:153], v[2:9], v[194:201], 0
	v_mfma_f32_16x16x128_f8f6f4 v[146:149], v[10:17], v[194:201], 0
	v_mfma_f32_16x16x128_f8f6f4 v[134:137], v[2:9], v[202:209], 0
	v_mfma_f32_16x16x128_f8f6f4 v[130:133], v[10:17], v[202:209], 0
	v_mfma_f32_16x16x128_f8f6f4 v[118:121], v[2:9], v[210:217], 0
	v_mfma_f32_16x16x128_f8f6f4 v[114:117], v[10:17], v[210:217], 0
	v_mfma_f32_16x16x128_f8f6f4 v[102:105], v[2:9], v[218:225], 0
	v_mfma_f32_16x16x128_f8f6f4 v[98:101], v[10:17], v[218:225], 0
	s_setprio 0
	s_barrier
	s_add_i32 s69, s53, s43
	s_mov_b32 m0, s69
	ds_read_b128 v[194:197], v191 offset:16384
	ds_read_b128 v[198:201], v191 offset:17408
	ds_read_b128 v[202:205], v191 offset:18432
	ds_read_b128 v[206:209], v191 offset:19456
	ds_read_b128 v[210:213], v191 offset:20480
	ds_read_b128 v[214:217], v191 offset:21504
	ds_read_b128 v[218:221], v191 offset:22528
	ds_read_b128 v[222:225], v191 offset:23552
	global_load_lds_dwordx4 v164, s[28:29]
	s_add_i32 m0, s69, 0x2000
	s_add_i32 s69, s58, s43
	global_load_lds_dwordx4 v166, s[28:29]
	s_add_u32 s98, s28, s4
	s_addc_u32 s99, s29, s5
	s_mov_b32 m0, s69
	s_nop 0
	global_load_lds_dwordx4 v164, s[98:99]
	s_add_u32 s100, s28, s4
	s_addc_u32 s101, s29, s5
	s_add_i32 m0, s69, 0x2000
	s_nop 0
	global_load_lds_dwordx4 v166, s[100:101]
	s_mov_b32 m0, s44
	s_nop 0
	global_load_lds_dwordx4 v168, s[30:31]
	s_mov_b32 m0, s45
	s_nop 0
	global_load_lds_dwordx4 v170, s[30:31]
	s_waitcnt vmcnt(8)
	s_waitcnt lgkmcnt(0)
	s_setprio 1
	v_mfma_f32_16x16x128_f8f6f4 v[94:97], v[18:25], v[194:201], 0
	v_mfma_f32_16x16x128_f8f6f4 v[90:93], v[26:33], v[194:201], 0
	v_mfma_f32_16x16x128_f8f6f4 v[78:81], v[18:25], v[202:209], 0
	v_mfma_f32_16x16x128_f8f6f4 v[74:77], v[26:33], v[202:209], 0
	v_mfma_f32_16x16x128_f8f6f4 v[62:65], v[18:25], v[210:217], 0
	v_mfma_f32_16x16x128_f8f6f4 v[58:61], v[26:33], v[210:217], 0
	v_mfma_f32_16x16x128_f8f6f4 v[46:49], v[18:25], v[218:225], 0
	v_mfma_f32_16x16x128_f8f6f4 v[42:45], v[26:33], v[218:225], 0
	s_nop 3
	v_mfma_f32_16x16x128_f8f6f4 v[86:89], v[2:9], v[194:201], 0
	v_mfma_f32_16x16x128_f8f6f4 v[82:85], v[10:17], v[194:201], 0
	v_mfma_f32_16x16x128_f8f6f4 v[70:73], v[2:9], v[202:209], 0
	v_mfma_f32_16x16x128_f8f6f4 v[66:69], v[10:17], v[202:209], 0
	v_mfma_f32_16x16x128_f8f6f4 v[54:57], v[2:9], v[210:217], 0
	v_mfma_f32_16x16x128_f8f6f4 v[50:53], v[10:17], v[210:217], 0
	v_mfma_f32_16x16x128_f8f6f4 v[38:41], v[2:9], v[218:225], 0
	v_mfma_f32_16x16x128_f8f6f4 v[34:37], v[10:17], v[218:225], 0
	s_setprio 0
	s_barrier
	s_add_i32 s69, 0, 0x18000
	s_add_i32 s70, 0, 0x1c000
	v_add_u32_e32 v14, s69, v187
	v_add_u32_e32 v30, s70, v187
	ds_read_b128 v[2:5], v14
	ds_read_b128 v[6:9], v14 offset:1024
	ds_read_b128 v[10:13], v14 offset:2048
	ds_read_b128 v[14:17], v14 offset:3072
	ds_read_b128 v[18:21], v30
	ds_read_b128 v[22:25], v30 offset:1024
	ds_read_b128 v[26:29], v30 offset:2048
	ds_read_b128 v[30:33], v30 offset:3072
	s_mov_b32 m0, s46
	ds_read_b128 v[194:197], v191 offset:32768
	ds_read_b128 v[198:201], v191 offset:33792
	ds_read_b128 v[202:205], v191 offset:34816
	ds_read_b128 v[206:209], v191 offset:35840
	ds_read_b128 v[210:213], v191 offset:36864
	ds_read_b128 v[214:217], v191 offset:37888
	ds_read_b128 v[218:221], v191 offset:38912
	ds_read_b128 v[222:225], v191 offset:39936
	global_load_lds_dwordx4 v172, s[30:31]
	s_mov_b32 m0, s47
	s_nop 0
	global_load_lds_dwordx4 v174, s[30:31]
	s_waitcnt vmcnt(8)
	s_waitcnt lgkmcnt(0)
	s_setprio 1
	v_mfma_f32_16x16x128_f8f6f4 v[158:161], v[2:9], v[194:201], v[158:161]
	v_mfma_f32_16x16x128_f8f6f4 v[154:157], v[10:17], v[194:201], v[154:157]
	v_mfma_f32_16x16x128_f8f6f4 v[142:145], v[2:9], v[202:209], v[142:145]
	v_mfma_f32_16x16x128_f8f6f4 v[138:141], v[10:17], v[202:209], v[138:141]
	v_mfma_f32_16x16x128_f8f6f4 v[126:129], v[2:9], v[210:217], v[126:129]
	v_mfma_f32_16x16x128_f8f6f4 v[122:125], v[10:17], v[210:217], v[122:125]
	v_mfma_f32_16x16x128_f8f6f4 v[110:113], v[2:9], v[218:225], v[110:113]
	v_mfma_f32_16x16x128_f8f6f4 v[106:109], v[10:17], v[218:225], v[106:109]
	s_nop 3
	v_mfma_f32_16x16x128_f8f6f4 v[150:153], v[18:25], v[194:201], v[150:153]
	v_mfma_f32_16x16x128_f8f6f4 v[146:149], v[26:33], v[194:201], v[146:149]
	v_mfma_f32_16x16x128_f8f6f4 v[134:137], v[18:25], v[202:209], v[134:137]
	v_mfma_f32_16x16x128_f8f6f4 v[130:133], v[26:33], v[202:209], v[130:133]
	v_mfma_f32_16x16x128_f8f6f4 v[118:121], v[18:25], v[210:217], v[118:121]
	v_mfma_f32_16x16x128_f8f6f4 v[114:117], v[26:33], v[210:217], v[114:117]
	v_mfma_f32_16x16x128_f8f6f4 v[102:105], v[18:25], v[218:225], v[102:105]
	v_mfma_f32_16x16x128_f8f6f4 v[98:101], v[26:33], v[218:225], v[98:101]
	s_setprio 0
	s_barrier
; #define PG8_STAGE(bufoff, gbase, voff) do { _Pragma("unroll") for (int _i = 0; _i < 2; ++_i) \
;         __builtin_amdgcn_global_load_lds((const unsigned*)((const char*)(gbase) + (voff)[_i]), (PG8_LAS unsigned*)(lds + (bufoff) + ldsw + _i * 8192), 16, 0, 0); } while (0)
; #define PG8_WAIT_V(n) asm volatile("s_waitcnt vmcnt(" #n ")" ::: "memory")
; #define PG8_WAIT_L(n) asm volatile("s_waitcnt lgkmcnt(" #n ")" ::: "memory")
; template <class Epi, class Sched, bool ALIGN_EPI = true, bool F8 = false>
; __device__ __forceinline__ void gemm_phase(PG8_LAS unsigned char* lds, const Sched& S, const Epi& E) {
;     ...
;         for (int t = 0; t < nt; t += 2) {
;             const bool last = (t == nt - 2);
;             if constexpr (Sched::GATHER) { if (last && has_next) S.a_off(nxt, Rs, Cs, voffAn); }
;             const char* a1 = cA + (size_t)(t + 1) * kstep;
;             const char* a2 = last ? nA : cA + (size_t)(t + 2) * kstep; const char* b2 = last ? nB : cB + (size_t)(t + 2) * kstepB;
;             const char* a3 = a2 + kstep; const char* b3 = b2 + kstepB;
;             unsigned vA2[2][2];
; #pragma unroll
;             for (int h = 0; h < 2; ++h)
; #pragma unroll
;                 for (int i = 0; i < 2; ++i) { if constexpr (Sched::GATHER) vA2[h][i] = (last && has_next) ? voffAn[h][i] : voffA[h][i]; else vA2[h][i] = voffA[h][i]; }
;             PG8_LDB(B0, 0, 0); PG8_LDB(B1, 0, 1); PG8_SCHED; PG8_LDA(At, 0, 0); PG8_STAGE(PG8_SA(1, 1), a1, voffA[1]);
;             PG8_WAIT_V(8); PG8_WAIT_L(0); PG8_BAR; PG8_MMA(0, 0, At, B0); PG8_MMA(0, 1, At, B1); PG8_BAR; PG8_SCHED;
;             PG8_LDA(At, 0, 1); PG8_STAGE(PG8_SB(0, 0), b2, voffB[0]); PG8_STAGE(PG8_SB(0, 1), b2, voffB[1]); PG8_STAGE(PG8_SA(0, 0), a2, vA2[0]);
;             PG8_WAIT_V(8); PG8_WAIT_L(0); PG8_BAR; PG8_MMA(1, 0, At, B0); PG8_MMA(1, 1, At, B1); PG8_BAR; PG8_SCHED;
;             PG8_LDB(B0, 1, 0); PG8_LDB(B1, 1, 1); PG8_SCHED; PG8_LDA(At, 1, 0); PG8_STAGE(PG8_SA(0, 1), a2, vA2[1]);
;             PG8_WAIT_V(8); PG8_WAIT_L(0); PG8_BAR; PG8_MMA(0, 0, At, B0); PG8_MMA(0, 1, At, B1); PG8_BAR; PG8_SCHED;
;             PG8_LDA(At, 1, 1); PG8_STAGE(PG8_SB(1, 0), b3, voffB[0]); PG8_STAGE(PG8_SB(1, 1), b3, voffB[1]); PG8_STAGE(PG8_SA(1, 0), a3, vA2[0]);
;             PG8_WAIT_V(8); PG8_WAIT_L(0); PG8_BAR; PG8_MMA(1, 0, At, B0); PG8_MMA(1, 1, At, B1); PG8_BAR; PG8_SCHED;
	s_add_u32 s28, s28, 0x8000
	s_addc_u32 s29, s29, 0
	s_add_i32 s30, s69, s43
	s_mov_b32 m0, s30
	ds_read_b128 v[194:197], v191 offset:49152
	ds_read_b128 v[198:201], v191 offset:50176
	ds_read_b128 v[202:205], v191 offset:51200
	ds_read_b128 v[206:209], v191 offset:52224
	ds_read_b128 v[210:213], v191 offset:53248
	ds_read_b128 v[214:217], v191 offset:54272
	ds_read_b128 v[218:221], v191 offset:55296
	ds_read_b128 v[222:225], v191 offset:56320
	global_load_lds_dwordx4 v164, s[28:29]
	s_add_i32 m0, s30, 0x2000
	s_add_i32 s30, s70, s43
	global_load_lds_dwordx4 v166, s[28:29]
	s_mov_b32 m0, s30
	s_nop 0
	global_load_lds_dwordx4 v178, s[28:29]
	s_add_i32 m0, s30, 0x2000
	s_nop 0
	global_load_lds_dwordx4 v180, s[28:29]
	s_mov_b32 m0, s51
	s_nop 0
	global_load_lds_dwordx4 v168, s[26:27]
	s_mov_b32 m0, s52
	s_nop 0
	global_load_lds_dwordx4 v170, s[26:27]
	s_waitcnt vmcnt(8)
	s_waitcnt lgkmcnt(0)
	s_setprio 1
	v_mfma_f32_16x16x128_f8f6f4 v[94:97], v[2:9], v[194:201], v[94:97]
	v_mfma_f32_16x16x128_f8f6f4 v[90:93], v[10:17], v[194:201], v[90:93]
	v_mfma_f32_16x16x128_f8f6f4 v[78:81], v[2:9], v[202:209], v[78:81]
	v_mfma_f32_16x16x128_f8f6f4 v[74:77], v[10:17], v[202:209], v[74:77]
	v_mfma_f32_16x16x128_f8f6f4 v[62:65], v[2:9], v[210:217], v[62:65]
	v_mfma_f32_16x16x128_f8f6f4 v[58:61], v[10:17], v[210:217], v[58:61]
	v_mfma_f32_16x16x128_f8f6f4 v[46:49], v[2:9], v[218:225], v[46:49]
	v_mfma_f32_16x16x128_f8f6f4 v[42:45], v[10:17], v[218:225], v[42:45]
	s_nop 3
	v_mfma_f32_16x16x128_f8f6f4 v[86:89], v[18:25], v[194:201], v[86:89]
	v_mfma_f32_16x16x128_f8f6f4 v[82:85], v[26:33], v[194:201], v[82:85]
	v_mfma_f32_16x16x128_f8f6f4 v[70:73], v[18:25], v[202:209], v[70:73]
	v_mfma_f32_16x16x128_f8f6f4 v[66:69], v[26:33], v[202:209], v[66:69]
	v_mfma_f32_16x16x128_f8f6f4 v[54:57], v[18:25], v[210:217], v[54:57]
	v_mfma_f32_16x16x128_f8f6f4 v[50:53], v[26:33], v[210:217], v[50:53]
	v_mfma_f32_16x16x128_f8f6f4 v[38:41], v[18:25], v[218:225], v[38:41]
	v_mfma_f32_16x16x128_f8f6f4 v[34:37], v[26:33], v[218:225], v[34:37]
	s_setprio 0
	s_barrier
	s_add_i32 s68, s68, 2
	s_add_u32 s23, s23, 0x10000
	s_addc_u32 s67, s67, 0
	s_add_u32 s24, s24, 0x10000
	s_addc_u32 s25, s25, 0
	s_cmp_gt_u32 s68, 5
	s_cbranch_scc0 .LBB0_1138
	s_branch .Lfx_33571
.LBB0_1138:
	ds_read_b128 v[18:21], v189
	ds_read_b128 v[22:25], v189 offset:1024
	ds_read_b128 v[26:29], v189 offset:2048
	ds_read_b128 v[30:33], v189 offset:3072
	ds_read_b128 v[2:5], v190
	ds_read_b128 v[6:9], v190 offset:1024
	ds_read_b128 v[10:13], v190 offset:2048
	ds_read_b128 v[14:17], v190 offset:3072
	s_add_u32 s26, s24, 0x8000
	s_addc_u32 s27, s25, 0
	s_cmp_eq_u32 s68, 4
	s_cselect_b32 s30, s16, s26
	s_cselect_b32 s31, s17, s27
	s_cselect_b32 s28, s18, s23
	s_cselect_b32 s29, s19, s67
	s_add_u32 s26, s30, 0x8000
	s_addc_u32 s27, s31, 0
	s_add_i32 m0, s44, 0xc000
	ds_read_b128 v[194:197], v191
	ds_read_b128 v[198:201], v191 offset:1024
	ds_read_b128 v[202:205], v191 offset:2048
	ds_read_b128 v[206:209], v191 offset:3072
	ds_read_b128 v[210:213], v191 offset:4096
	ds_read_b128 v[214:217], v191 offset:5120
	ds_read_b128 v[218:221], v191 offset:6144
	ds_read_b128 v[222:225], v191 offset:7168
	global_load_lds_dwordx4 v184, s[24:25]
	s_add_i32 m0, s44, 0xe000
	s_nop 0
	global_load_lds_dwordx4 v182, s[24:25]
	s_waitcnt vmcnt(8)
	s_waitcnt lgkmcnt(0)
	s_setprio 1
	v_mfma_f32_16x16x128_f8f6f4 v[158:161], v[18:25], v[194:201], v[158:161]
	v_mfma_f32_16x16x128_f8f6f4 v[154:157], v[26:33], v[194:201], v[154:157]
	v_mfma_f32_16x16x128_f8f6f4 v[142:145], v[18:25], v[202:209], v[142:145]
	v_mfma_f32_16x16x128_f8f6f4 v[138:141], v[26:33], v[202:209], v[138:141]
	v_mfma_f32_16x16x128_f8f6f4 v[126:129], v[18:25], v[210:217], v[126:129]
	v_mfma_f32_16x16x128_f8f6f4 v[122:125], v[26:33], v[210:217], v[122:125]
	v_mfma_f32_16x16x128_f8f6f4 v[110:113], v[18:25], v[218:225], v[110:113]
	v_mfma_f32_16x16x128_f8f6f4 v[106:109], v[26:33], v[218:225], v[106:109]
	s_nop 3
	v_mfma_f32_16x16x128_f8f6f4 v[150:153], v[2:9], v[194:201], v[150:153]
	v_mfma_f32_16x16x128_f8f6f4 v[146:149], v[10:17], v[194:201], v[146:149]
	v_mfma_f32_16x16x128_f8f6f4 v[134:137], v[2:9], v[202:209], v[134:137]
	v_mfma_f32_16x16x128_f8f6f4 v[130:133], v[10:17], v[202:209], v[130:133]
	v_mfma_f32_16x16x128_f8f6f4 v[118:121], v[2:9], v[210:217], v[118:121]
	v_mfma_f32_16x16x128_f8f6f4 v[114:117], v[10:17], v[210:217], v[114:117]
	v_mfma_f32_16x16x128_f8f6f4 v[102:105], v[2:9], v[218:225], v[102:105]
	v_mfma_f32_16x16x128_f8f6f4 v[98:101], v[10:17], v[218:225], v[98:101]
	s_setprio 0
	s_barrier
	s_add_i32 s69, s53, s43
	s_mov_b32 m0, s69
	ds_read_b128 v[194:197], v191 offset:16384
	ds_read_b128 v[198:201], v191 offset:17408
	ds_read_b128 v[202:205], v191 offset:18432
	ds_read_b128 v[206:209], v191 offset:19456
	ds_read_b128 v[210:213], v191 offset:20480
	ds_read_b128 v[214:217], v191 offset:21504
	ds_read_b128 v[218:221], v191 offset:22528
	ds_read_b128 v[222:225], v191 offset:23552
	global_load_lds_dwordx4 v164, s[28:29]
	s_add_i32 m0, s69, 0x2000
	s_add_i32 s69, s58, s43
	global_load_lds_dwordx4 v166, s[28:29]
	s_add_u32 s98, s28, s4
	s_addc_u32 s99, s29, s5
	s_mov_b32 m0, s69
	s_nop 0
	global_load_lds_dwordx4 v164, s[98:99]
	s_add_u32 s100, s28, s4
	s_addc_u32 s101, s29, s5
	s_add_i32 m0, s69, 0x2000
	s_nop 0
	global_load_lds_dwordx4 v166, s[100:101]
	s_mov_b32 m0, s44
	s_nop 0
	global_load_lds_dwordx4 v168, s[30:31]
	s_mov_b32 m0, s45
	s_nop 0
	global_load_lds_dwordx4 v170, s[30:31]
	s_waitcnt vmcnt(8)
	s_waitcnt lgkmcnt(0)
	s_setprio 1
	v_mfma_f32_16x16x128_f8f6f4 v[94:97], v[18:25], v[194:201], v[94:97]
	v_mfma_f32_16x16x128_f8f6f4 v[90:93], v[26:33], v[194:201], v[90:93]
	v_mfma_f32_16x16x128_f8f6f4 v[78:81], v[18:25], v[202:209], v[78:81]
	v_mfma_f32_16x16x128_f8f6f4 v[74:77], v[26:33], v[202:209], v[74:77]
	v_mfma_f32_16x16x128_f8f6f4 v[62:65], v[18:25], v[210:217], v[62:65]
	v_mfma_f32_16x16x128_f8f6f4 v[58:61], v[26:33], v[210:217], v[58:61]
	v_mfma_f32_16x16x128_f8f6f4 v[46:49], v[18:25], v[218:225], v[46:49]
	v_mfma_f32_16x16x128_f8f6f4 v[42:45], v[26:33], v[218:225], v[42:45]
	s_nop 3
	v_mfma_f32_16x16x128_f8f6f4 v[86:89], v[2:9], v[194:201], v[86:89]
	v_mfma_f32_16x16x128_f8f6f4 v[82:85], v[10:17], v[194:201], v[82:85]
	v_mfma_f32_16x16x128_f8f6f4 v[70:73], v[2:9], v[202:209], v[70:73]
	v_mfma_f32_16x16x128_f8f6f4 v[66:69], v[10:17], v[202:209], v[66:69]
	v_mfma_f32_16x16x128_f8f6f4 v[54:57], v[2:9], v[210:217], v[54:57]
	v_mfma_f32_16x16x128_f8f6f4 v[50:53], v[10:17], v[210:217], v[50:53]
	v_mfma_f32_16x16x128_f8f6f4 v[38:41], v[2:9], v[218:225], v[38:41]
	v_mfma_f32_16x16x128_f8f6f4 v[34:37], v[10:17], v[218:225], v[34:37]
	s_setprio 0
	s_barrier
; #define PG8_STAGE(bufoff, gbase, voff) do { _Pragma("unroll") for (int _i = 0; _i < 2; ++_i) \
;         __builtin_amdgcn_global_load_lds((const unsigned*)((const char*)(gbase) + (voff)[_i]), (PG8_LAS unsigned*)(lds + (bufoff) + ldsw + _i * 8192), 16, 0, 0); } while (0)
; #define PG8_WAIT_V(n) asm volatile("s_waitcnt vmcnt(" #n ")" ::: "memory")
; #define PG8_WAIT_L(n) asm volatile("s_waitcnt lgkmcnt(" #n ")" ::: "memory")
; template <class Epi, class Sched, bool ALIGN_EPI = true, bool F8 = false>
; __device__ __forceinline__ void gemm_phase(PG8_LAS unsigned char* lds, const Sched& S, const Epi& E) {
;     ...
;         for (int t = 0; t < nt; t += 2) {
;             const bool last = (t == nt - 2);
;             if constexpr (Sched::GATHER) { if (last && has_next) S.a_off(nxt, Rs, Cs, voffAn); }
;             const char* a1 = cA + (size_t)(t + 1) * kstep;
;             const char* a2 = last ? nA : cA + (size_t)(t + 2) * kstep; const char* b2 = last ? nB : cB + (size_t)(t + 2) * kstepB;
;             const char* a3 = a2 + kstep; const char* b3 = b2 + kstepB;
;             unsigned vA2[2][2];
; #pragma unroll
;             for (int h = 0; h < 2; ++h)
; #pragma unroll
;                 for (int i = 0; i < 2; ++i) { if constexpr (Sched::GATHER) vA2[h][i] = (last && has_next) ? voffAn[h][i] : voffA[h][i]; else vA2[h][i] = voffA[h][i]; }
;             PG8_LDB(B0, 0, 0); PG8_LDB(B1, 0, 1); PG8_SCHED; PG8_LDA(At, 0, 0); PG8_STAGE(PG8_SA(1, 1), a1, voffA[1]);
;             PG8_WAIT_V(8); PG8_WAIT_L(0); PG8_BAR; PG8_MMA(0, 0, At, B0); PG8_MMA(0, 1, At, B1); PG8_BAR; PG8_SCHED;
;             PG8_LDA(At, 0, 1); PG8_STAGE(PG8_SB(0, 0), b2, voffB[0]); PG8_STAGE(PG8_SB(0, 1), b2, voffB[1]); PG8_STAGE(PG8_SA(0, 0), a2, vA2[0]);
;             PG8_WAIT_V(8); PG8_WAIT_L(0); PG8_BAR; PG8_MMA(1, 0, At, B0); PG8_MMA(1, 1, At, B1); PG8_BAR; PG8_SCHED;
;             PG8_LDB(B0, 1, 0); PG8_LDB(B1, 1, 1); PG8_SCHED; PG8_LDA(At, 1, 0); PG8_STAGE(PG8_SA(0, 1), a2, vA2[1]);
;             PG8_WAIT_V(8); PG8_WAIT_L(0); PG8_BAR; PG8_MMA(0, 0, At, B0); PG8_MMA(0, 1, At, B1); PG8_BAR; PG8_SCHED;
;             PG8_LDA(At, 1, 1); PG8_STAGE(PG8_SB(1, 0), b3, voffB[0]); PG8_STAGE(PG8_SB(1, 1), b3, voffB[1]); PG8_STAGE(PG8_SA(1, 0), a3, vA2[0]);
;             PG8_WAIT_V(8); PG8_WAIT_L(0); PG8_BAR; PG8_MMA(1, 0, At, B0); PG8_MMA(1, 1, At, B1); PG8_BAR; PG8_SCHED;
	s_add_i32 s69, 0, 0x18000
	s_add_i32 s70, 0, 0x1c000
	v_add_u32_e32 v14, s69, v187
	v_add_u32_e32 v30, s70, v187
	ds_read_b128 v[2:5], v14
	ds_read_b128 v[6:9], v14 offset:1024
	ds_read_b128 v[10:13], v14 offset:2048
	ds_read_b128 v[14:17], v14 offset:3072
	ds_read_b128 v[18:21], v30
	ds_read_b128 v[22:25], v30 offset:1024
	ds_read_b128 v[26:29], v30 offset:2048
	ds_read_b128 v[30:33], v30 offset:3072
	s_mov_b32 m0, s46
	ds_read_b128 v[194:197], v191 offset:32768
	ds_read_b128 v[198:201], v191 offset:33792
	ds_read_b128 v[202:205], v191 offset:34816
	ds_read_b128 v[206:209], v191 offset:35840
	ds_read_b128 v[210:213], v191 offset:36864
	ds_read_b128 v[214:217], v191 offset:37888
	ds_read_b128 v[218:221], v191 offset:38912
	ds_read_b128 v[222:225], v191 offset:39936
	global_load_lds_dwordx4 v172, s[30:31]
	s_mov_b32 m0, s47
	s_nop 0
	global_load_lds_dwordx4 v174, s[30:31]
	s_waitcnt vmcnt(8)
	s_waitcnt lgkmcnt(0)
	s_setprio 1
	v_mfma_f32_16x16x128_f8f6f4 v[158:161], v[2:9], v[194:201], v[158:161]
	v_mfma_f32_16x16x128_f8f6f4 v[154:157], v[10:17], v[194:201], v[154:157]
	v_mfma_f32_16x16x128_f8f6f4 v[142:145], v[2:9], v[202:209], v[142:145]
	v_mfma_f32_16x16x128_f8f6f4 v[138:141], v[10:17], v[202:209], v[138:141]
	v_mfma_f32_16x16x128_f8f6f4 v[126:129], v[2:9], v[210:217], v[126:129]
	v_mfma_f32_16x16x128_f8f6f4 v[122:125], v[10:17], v[210:217], v[122:125]
	v_mfma_f32_16x16x128_f8f6f4 v[110:113], v[2:9], v[218:225], v[110:113]
	v_mfma_f32_16x16x128_f8f6f4 v[106:109], v[10:17], v[218:225], v[106:109]
	s_nop 3
	v_mfma_f32_16x16x128_f8f6f4 v[150:153], v[18:25], v[194:201], v[150:153]
	v_mfma_f32_16x16x128_f8f6f4 v[146:149], v[26:33], v[194:201], v[146:149]
	v_mfma_f32_16x16x128_f8f6f4 v[134:137], v[18:25], v[202:209], v[134:137]
	v_mfma_f32_16x16x128_f8f6f4 v[130:133], v[26:33], v[202:209], v[130:133]
	v_mfma_f32_16x16x128_f8f6f4 v[118:121], v[18:25], v[210:217], v[118:121]
	v_mfma_f32_16x16x128_f8f6f4 v[114:117], v[26:33], v[210:217], v[114:117]
	v_mfma_f32_16x16x128_f8f6f4 v[102:105], v[18:25], v[218:225], v[102:105]
	v_mfma_f32_16x16x128_f8f6f4 v[98:101], v[26:33], v[218:225], v[98:101]
	s_setprio 0
	s_barrier
	s_add_u32 s28, s28, 0x8000
	s_addc_u32 s29, s29, 0
	s_add_i32 s30, s69, s43
	s_mov_b32 m0, s30
	ds_read_b128 v[194:197], v191 offset:49152
	ds_read_b128 v[198:201], v191 offset:50176
	ds_read_b128 v[202:205], v191 offset:51200
	ds_read_b128 v[206:209], v191 offset:52224
	ds_read_b128 v[210:213], v191 offset:53248
	ds_read_b128 v[214:217], v191 offset:54272
	ds_read_b128 v[218:221], v191 offset:55296
	ds_read_b128 v[222:225], v191 offset:56320
	global_load_lds_dwordx4 v164, s[28:29]
	s_add_i32 m0, s30, 0x2000
	s_add_i32 s30, s70, s43
	global_load_lds_dwordx4 v166, s[28:29]
	s_mov_b32 m0, s30
	s_nop 0
	global_load_lds_dwordx4 v178, s[28:29]
	s_add_i32 m0, s30, 0x2000
	s_nop 0
	global_load_lds_dwordx4 v180, s[28:29]
	s_mov_b32 m0, s51
	s_nop 0
	global_load_lds_dwordx4 v168, s[26:27]
	s_mov_b32 m0, s52
	s_nop 0
	global_load_lds_dwordx4 v170, s[26:27]
	s_waitcnt vmcnt(8)
	s_waitcnt lgkmcnt(0)
	s_setprio 1
	v_mfma_f32_16x16x128_f8f6f4 v[94:97], v[2:9], v[194:201], v[94:97]
	v_mfma_f32_16x16x128_f8f6f4 v[90:93], v[10:17], v[194:201], v[90:93]
	v_mfma_f32_16x16x128_f8f6f4 v[78:81], v[2:9], v[202:209], v[78:81]
	v_mfma_f32_16x16x128_f8f6f4 v[74:77], v[10:17], v[202:209], v[74:77]
	v_mfma_f32_16x16x128_f8f6f4 v[62:65], v[2:9], v[210:217], v[62:65]
	v_mfma_f32_16x16x128_f8f6f4 v[58:61], v[10:17], v[210:217], v[58:61]
	v_mfma_f32_16x16x128_f8f6f4 v[46:49], v[2:9], v[218:225], v[46:49]
	v_mfma_f32_16x16x128_f8f6f4 v[42:45], v[10:17], v[218:225], v[42:45]
	s_nop 3
	v_mfma_f32_16x16x128_f8f6f4 v[86:89], v[18:25], v[194:201], v[86:89]
	v_mfma_f32_16x16x128_f8f6f4 v[82:85], v[26:33], v[194:201], v[82:85]
	v_mfma_f32_16x16x128_f8f6f4 v[70:73], v[18:25], v[202:209], v[70:73]
	v_mfma_f32_16x16x128_f8f6f4 v[66:69], v[26:33], v[202:209], v[66:69]
	v_mfma_f32_16x16x128_f8f6f4 v[54:57], v[18:25], v[210:217], v[54:57]
	v_mfma_f32_16x16x128_f8f6f4 v[50:53], v[26:33], v[210:217], v[50:53]
	v_mfma_f32_16x16x128_f8f6f4 v[38:41], v[18:25], v[218:225], v[38:41]
	v_mfma_f32_16x16x128_f8f6f4 v[34:37], v[26:33], v[218:225], v[34:37]
	s_setprio 0
	s_barrier
	s_add_i32 s68, s68, 2
	s_add_u32 s23, s23, 0x10000
	s_addc_u32 s67, s67, 0
	s_add_u32 s24, s24, 0x10000
	s_addc_u32 s25, s25, 0
	s_cmp_gt_u32 s68, 5
	s_cbranch_scc0 .LBB0_1138
	s_branch .Lfx_33571
; #define PG8_WAIT_V(n) asm volatile("s_waitcnt vmcnt(" #n ")" ::: "memory")
; #define PG8_WAIT_L(n) asm volatile("s_waitcnt lgkmcnt(" #n ")" ::: "memory")
; template <class Epi, class Sched, bool ALIGN_EPI = true, bool F8 = false>
; __device__ __forceinline__ void gemm_phase(PG8_LAS unsigned char* lds, const Sched& S, const Epi& E) {
;     ...
;         for (int t = 0; t < nt; t += 2) {
;             const bool last = (t == nt - 2);
;             if constexpr (Sched::GATHER) { if (last && has_next) S.a_off(nxt, Rs, Cs, voffAn); }
;             const char* a1 = cA + (size_t)(t + 1) * kstep;
;             const char* a2 = last ? nA : cA + (size_t)(t + 2) * kstep; const char* b2 = last ? nB : cB + (size_t)(t + 2) * kstepB;
;             const char* a3 = a2 + kstep; const char* b3 = b2 + kstepB;
;             unsigned vA2[2][2];
; #pragma unroll
;             for (int h = 0; h < 2; ++h)
; #pragma unroll
;                 for (int i = 0; i < 2; ++i) { if constexpr (Sched::GATHER) vA2[h][i] = (last && has_next) ? voffAn[h][i] : voffA[h][i]; else vA2[h][i] = voffA[h][i]; }
;             PG8_LDB(B0, 0, 0); PG8_LDB(B1, 0, 1); PG8_SCHED; PG8_LDA(At, 0, 0); PG8_STAGE(PG8_SA(1, 1), a1, voffA[1]);
;             PG8_WAIT_V(8); PG8_WAIT_L(0); PG8_BAR; PG8_MMA(0, 0, At, B0); PG8_MMA(0, 1, At, B1); PG8_BAR; PG8_SCHED;
;             PG8_LDA(At, 0, 1); PG8_STAGE(PG8_SB(0, 0), b2, voffB[0]); PG8_STAGE(PG8_SB(0, 1), b2, voffB[1]); PG8_STAGE(PG8_SA(0, 0), a2, vA2[0]);
;             PG8_WAIT_V(8); PG8_WAIT_L(0); PG8_BAR; PG8_MMA(1, 0, At, B0); PG8_MMA(1, 1, At, B1); PG8_BAR; PG8_SCHED;
;             PG8_LDB(B0, 1, 0); PG8_LDB(B1, 1, 1); PG8_SCHED; PG8_LDA(At, 1, 0); PG8_STAGE(PG8_SA(0, 1), a2, vA2[1]);
;             PG8_WAIT_V(8); PG8_WAIT_L(0); PG8_BAR; PG8_MMA(0, 0, At, B0); PG8_MMA(0, 1, At, B1); PG8_BAR; PG8_SCHED;
;             PG8_LDA(At, 1, 1); PG8_STAGE(PG8_SB(1, 0), b3, voffB[0]); PG8_STAGE(PG8_SB(1, 1), b3, voffB[1]); PG8_STAGE(PG8_SA(1, 0), a3, vA2[0]);
;             PG8_WAIT_V(8); PG8_WAIT_L(0); PG8_BAR; PG8_MMA(1, 0, At, B0); PG8_MMA(1, 1, At, B1); PG8_BAR; PG8_SCHED;
;     ...
;         for (int a = 0; a < 2; ++a)
; #pragma unroll
;             for (int b = 0; b < 2; ++b)
; #pragma unroll
;                 for (int m = 0; m < 4; ++m)
; #pragma unroll
;                     for (int n = 0; n < 2; ++n) acc[a][b][m][n] = (f32x4){0.f, 0.f, 0.f, 0.f};
.Lh1e_33571:
.Lpk1_1138:
	ds_read_b128 v[18:21], v189
	ds_read_b128 v[22:25], v189 offset:1024
	ds_read_b128 v[26:29], v189 offset:2048
	ds_read_b128 v[30:33], v189 offset:3072
	ds_read_b128 v[2:5], v190
	ds_read_b128 v[6:9], v190 offset:1024
	ds_read_b128 v[10:13], v190 offset:2048
	ds_read_b128 v[14:17], v190 offset:3072
	s_add_u32 s26, s24, 0x8000
	s_addc_u32 s27, s25, 0
	s_cmp_eq_u32 s68, 4
	s_cselect_b32 s30, s16, s26
	s_cselect_b32 s31, s17, s27
	s_cselect_b32 s28, s18, s23
	s_cselect_b32 s29, s19, s67
	s_add_u32 s26, s30, 0x8000
	s_addc_u32 s27, s31, 0
	s_add_i32 m0, s44, 0xc000
	ds_read_b128 v[194:197], v191
	ds_read_b128 v[198:201], v191 offset:1024
	ds_read_b128 v[202:205], v191 offset:2048
	ds_read_b128 v[206:209], v191 offset:3072
	ds_read_b128 v[210:213], v191 offset:4096
	ds_read_b128 v[214:217], v191 offset:5120
	ds_read_b128 v[218:221], v191 offset:6144
	ds_read_b128 v[222:225], v191 offset:7168
	global_load_lds_dwordx4 v184, s[24:25]
	s_add_i32 m0, s44, 0xe000
	s_nop 0
	global_load_lds_dwordx4 v182, s[24:25]
	s_waitcnt vmcnt(8)
	s_waitcnt lgkmcnt(0)
	s_barrier
	s_setprio 2
	v_mfma_f32_16x16x128_f8f6f4 v[158:161], v[18:25], v[194:201], 0
	v_mfma_f32_16x16x128_f8f6f4 v[154:157], v[26:33], v[194:201], 0
	v_mfma_f32_16x16x128_f8f6f4 v[142:145], v[18:25], v[202:209], 0
	v_mfma_f32_16x16x128_f8f6f4 v[138:141], v[26:33], v[202:209], 0
	v_mfma_f32_16x16x128_f8f6f4 v[126:129], v[18:25], v[210:217], 0
	v_mfma_f32_16x16x128_f8f6f4 v[122:125], v[26:33], v[210:217], 0
	v_mfma_f32_16x16x128_f8f6f4 v[110:113], v[18:25], v[218:225], 0
	v_mfma_f32_16x16x128_f8f6f4 v[106:109], v[26:33], v[218:225], 0
	s_nop 3
	v_mfma_f32_16x16x128_f8f6f4 v[150:153], v[2:9], v[194:201], 0
	v_mfma_f32_16x16x128_f8f6f4 v[146:149], v[10:17], v[194:201], 0
	v_mfma_f32_16x16x128_f8f6f4 v[134:137], v[2:9], v[202:209], 0
	v_mfma_f32_16x16x128_f8f6f4 v[130:133], v[10:17], v[202:209], 0
	v_mfma_f32_16x16x128_f8f6f4 v[118:121], v[2:9], v[210:217], 0
	v_mfma_f32_16x16x128_f8f6f4 v[114:117], v[10:17], v[210:217], 0
	v_mfma_f32_16x16x128_f8f6f4 v[102:105], v[2:9], v[218:225], 0
	v_mfma_f32_16x16x128_f8f6f4 v[98:101], v[10:17], v[218:225], 0
	s_setprio 0
	s_add_i32 s69, s53, s43
	s_mov_b32 m0, s69
	ds_read_b128 v[194:197], v191 offset:16384
	ds_read_b128 v[198:201], v191 offset:17408
	ds_read_b128 v[202:205], v191 offset:18432
	ds_read_b128 v[206:209], v191 offset:19456
	ds_read_b128 v[210:213], v191 offset:20480
	ds_read_b128 v[214:217], v191 offset:21504
	ds_read_b128 v[218:221], v191 offset:22528
	ds_read_b128 v[222:225], v191 offset:23552
	global_load_lds_dwordx4 v164, s[28:29]
	s_add_i32 m0, s69, 0x2000
	s_add_i32 s69, s58, s43
	global_load_lds_dwordx4 v166, s[28:29]
	s_add_u32 s98, s28, s4
	s_addc_u32 s99, s29, s5
	s_mov_b32 m0, s69
	s_nop 0
	global_load_lds_dwordx4 v164, s[98:99]
	s_add_u32 s100, s28, s4
	s_addc_u32 s101, s29, s5
	s_add_i32 m0, s69, 0x2000
	s_nop 0
	global_load_lds_dwordx4 v166, s[100:101]
	s_mov_b32 m0, s44
	s_nop 0
	global_load_lds_dwordx4 v168, s[30:31]
	s_mov_b32 m0, s45
	s_nop 0
	global_load_lds_dwordx4 v170, s[30:31]
	s_waitcnt vmcnt(8)
	s_waitcnt lgkmcnt(0)
	s_barrier
	s_setprio 2
	v_mfma_f32_16x16x128_f8f6f4 v[94:97], v[18:25], v[194:201], 0
	v_mfma_f32_16x16x128_f8f6f4 v[90:93], v[26:33], v[194:201], 0
	v_mfma_f32_16x16x128_f8f6f4 v[78:81], v[18:25], v[202:209], 0
	v_mfma_f32_16x16x128_f8f6f4 v[74:77], v[26:33], v[202:209], 0
	v_mfma_f32_16x16x128_f8f6f4 v[62:65], v[18:25], v[210:217], 0
	v_mfma_f32_16x16x128_f8f6f4 v[58:61], v[26:33], v[210:217], 0
	v_mfma_f32_16x16x128_f8f6f4 v[46:49], v[18:25], v[218:225], 0
	v_mfma_f32_16x16x128_f8f6f4 v[42:45], v[26:33], v[218:225], 0
	s_nop 3
	v_mfma_f32_16x16x128_f8f6f4 v[86:89], v[2:9], v[194:201], 0
	v_mfma_f32_16x16x128_f8f6f4 v[82:85], v[10:17], v[194:201], 0
	v_mfma_f32_16x16x128_f8f6f4 v[70:73], v[2:9], v[202:209], 0
	v_mfma_f32_16x16x128_f8f6f4 v[66:69], v[10:17], v[202:209], 0
	v_mfma_f32_16x16x128_f8f6f4 v[54:57], v[2:9], v[210:217], 0
	v_mfma_f32_16x16x128_f8f6f4 v[50:53], v[10:17], v[210:217], 0
	v_mfma_f32_16x16x128_f8f6f4 v[38:41], v[2:9], v[218:225], 0
	v_mfma_f32_16x16x128_f8f6f4 v[34:37], v[10:17], v[218:225], 0
	s_setprio 0
	s_add_i32 s69, 0, 0x18000
	s_add_i32 s70, 0, 0x1c000
	v_add_u32_e32 v14, s69, v187
	v_add_u32_e32 v30, s70, v187
	ds_read_b128 v[2:5], v14
	ds_read_b128 v[6:9], v14 offset:1024
	ds_read_b128 v[10:13], v14 offset:2048
	ds_read_b128 v[14:17], v14 offset:3072
	ds_read_b128 v[18:21], v30
	ds_read_b128 v[22:25], v30 offset:1024
	ds_read_b128 v[26:29], v30 offset:2048
	ds_read_b128 v[30:33], v30 offset:3072
	s_mov_b32 m0, s46
	ds_read_b128 v[194:197], v191 offset:32768
	ds_read_b128 v[198:201], v191 offset:33792
	ds_read_b128 v[202:205], v191 offset:34816
	ds_read_b128 v[206:209], v191 offset:35840
	ds_read_b128 v[210:213], v191 offset:36864
	ds_read_b128 v[214:217], v191 offset:37888
	ds_read_b128 v[218:221], v191 offset:38912
	ds_read_b128 v[222:225], v191 offset:39936
	global_load_lds_dwordx4 v172, s[30:31]
	s_mov_b32 m0, s47
	s_nop 0
	global_load_lds_dwordx4 v174, s[30:31]
	s_waitcnt vmcnt(8)
	s_waitcnt lgkmcnt(0)
	s_barrier
; #define PG8_STAGE(bufoff, gbase, voff) do { _Pragma("unroll") for (int _i = 0; _i < 2; ++_i) \
;         __builtin_amdgcn_global_load_lds((const unsigned*)((const char*)(gbase) + (voff)[_i]), (PG8_LAS unsigned*)(lds + (bufoff) + ldsw + _i * 8192), 16, 0, 0); } while (0)
; #define PG8_WAIT_V(n) asm volatile("s_waitcnt vmcnt(" #n ")" ::: "memory")
; #define PG8_WAIT_L(n) asm volatile("s_waitcnt lgkmcnt(" #n ")" ::: "memory")
; template <class Epi, class Sched, bool ALIGN_EPI = true, bool F8 = false>
; __device__ __forceinline__ void gemm_phase(PG8_LAS unsigned char* lds, const Sched& S, const Epi& E) {
;     ...
;         for (int t = 0; t < nt; t += 2) {
;             const bool last = (t == nt - 2);
;             if constexpr (Sched::GATHER) { if (last && has_next) S.a_off(nxt, Rs, Cs, voffAn); }
;             const char* a1 = cA + (size_t)(t + 1) * kstep;
;             const char* a2 = last ? nA : cA + (size_t)(t + 2) * kstep; const char* b2 = last ? nB : cB + (size_t)(t + 2) * kstepB;
;             const char* a3 = a2 + kstep; const char* b3 = b2 + kstepB;
;             unsigned vA2[2][2];
; #pragma unroll
;             for (int h = 0; h < 2; ++h)
; #pragma unroll
;                 for (int i = 0; i < 2; ++i) { if constexpr (Sched::GATHER) vA2[h][i] = (last && has_next) ? voffAn[h][i] : voffA[h][i]; else vA2[h][i] = voffA[h][i]; }
;             PG8_LDB(B0, 0, 0); PG8_LDB(B1, 0, 1); PG8_SCHED; PG8_LDA(At, 0, 0); PG8_STAGE(PG8_SA(1, 1), a1, voffA[1]);
;             PG8_WAIT_V(8); PG8_WAIT_L(0); PG8_BAR; PG8_MMA(0, 0, At, B0); PG8_MMA(0, 1, At, B1); PG8_BAR; PG8_SCHED;
;             PG8_LDA(At, 0, 1); PG8_STAGE(PG8_SB(0, 0), b2, voffB[0]); PG8_STAGE(PG8_SB(0, 1), b2, voffB[1]); PG8_STAGE(PG8_SA(0, 0), a2, vA2[0]);
;             PG8_WAIT_V(8); PG8_WAIT_L(0); PG8_BAR; PG8_MMA(1, 0, At, B0); PG8_MMA(1, 1, At, B1); PG8_BAR; PG8_SCHED;
;             PG8_LDB(B0, 1, 0); PG8_LDB(B1, 1, 1); PG8_SCHED; PG8_LDA(At, 1, 0); PG8_STAGE(PG8_SA(0, 1), a2, vA2[1]);
;             PG8_WAIT_V(8); PG8_WAIT_L(0); PG8_BAR; PG8_MMA(0, 0, At, B0); PG8_MMA(0, 1, At, B1); PG8_BAR; PG8_SCHED;
;             PG8_LDA(At, 1, 1); PG8_STAGE(PG8_SB(1, 0), b3, voffB[0]); PG8_STAGE(PG8_SB(1, 1), b3, voffB[1]); PG8_STAGE(PG8_SA(1, 0), a3, vA2[0]);
;             PG8_WAIT_V(8); PG8_WAIT_L(0); PG8_BAR; PG8_MMA(1, 0, At, B0); PG8_MMA(1, 1, At, B1); PG8_BAR; PG8_SCHED;
	s_setprio 2
	v_mfma_f32_16x16x128_f8f6f4 v[158:161], v[2:9], v[194:201], v[158:161]
	v_mfma_f32_16x16x128_f8f6f4 v[154:157], v[10:17], v[194:201], v[154:157]
	v_mfma_f32_16x16x128_f8f6f4 v[142:145], v[2:9], v[202:209], v[142:145]
	v_mfma_f32_16x16x128_f8f6f4 v[138:141], v[10:17], v[202:209], v[138:141]
	v_mfma_f32_16x16x128_f8f6f4 v[126:129], v[2:9], v[210:217], v[126:129]
	v_mfma_f32_16x16x128_f8f6f4 v[122:125], v[10:17], v[210:217], v[122:125]
	v_mfma_f32_16x16x128_f8f6f4 v[110:113], v[2:9], v[218:225], v[110:113]
	v_mfma_f32_16x16x128_f8f6f4 v[106:109], v[10:17], v[218:225], v[106:109]
	s_nop 3
	v_mfma_f32_16x16x128_f8f6f4 v[150:153], v[18:25], v[194:201], v[150:153]
	v_mfma_f32_16x16x128_f8f6f4 v[146:149], v[26:33], v[194:201], v[146:149]
	v_mfma_f32_16x16x128_f8f6f4 v[134:137], v[18:25], v[202:209], v[134:137]
	v_mfma_f32_16x16x128_f8f6f4 v[130:133], v[26:33], v[202:209], v[130:133]
	v_mfma_f32_16x16x128_f8f6f4 v[118:121], v[18:25], v[210:217], v[118:121]
	v_mfma_f32_16x16x128_f8f6f4 v[114:117], v[26:33], v[210:217], v[114:117]
	v_mfma_f32_16x16x128_f8f6f4 v[102:105], v[18:25], v[218:225], v[102:105]
	v_mfma_f32_16x16x128_f8f6f4 v[98:101], v[26:33], v[218:225], v[98:101]
	s_setprio 0
	s_add_u32 s28, s28, 0x8000
	s_addc_u32 s29, s29, 0
	s_add_i32 s30, s69, s43
	s_mov_b32 m0, s30
	ds_read_b128 v[194:197], v191 offset:49152
	ds_read_b128 v[198:201], v191 offset:50176
	ds_read_b128 v[202:205], v191 offset:51200
	ds_read_b128 v[206:209], v191 offset:52224
	ds_read_b128 v[210:213], v191 offset:53248
	ds_read_b128 v[214:217], v191 offset:54272
	ds_read_b128 v[218:221], v191 offset:55296
	ds_read_b128 v[222:225], v191 offset:56320
	global_load_lds_dwordx4 v164, s[28:29]
	s_add_i32 m0, s30, 0x2000
	s_add_i32 s30, s70, s43
	global_load_lds_dwordx4 v166, s[28:29]
	s_mov_b32 m0, s30
	s_nop 0
	global_load_lds_dwordx4 v178, s[28:29]
	s_add_i32 m0, s30, 0x2000
	s_nop 0
	global_load_lds_dwordx4 v180, s[28:29]
	s_mov_b32 m0, s51
	s_nop 0
	global_load_lds_dwordx4 v168, s[26:27]
	s_mov_b32 m0, s52
	s_nop 0
	global_load_lds_dwordx4 v170, s[26:27]
	s_waitcnt vmcnt(8)
	s_waitcnt lgkmcnt(0)
	s_barrier
	s_setprio 2
	v_mfma_f32_16x16x128_f8f6f4 v[94:97], v[2:9], v[194:201], v[94:97]
	v_mfma_f32_16x16x128_f8f6f4 v[90:93], v[10:17], v[194:201], v[90:93]
	v_mfma_f32_16x16x128_f8f6f4 v[78:81], v[2:9], v[202:209], v[78:81]
	v_mfma_f32_16x16x128_f8f6f4 v[74:77], v[10:17], v[202:209], v[74:77]
	v_mfma_f32_16x16x128_f8f6f4 v[62:65], v[2:9], v[210:217], v[62:65]
	v_mfma_f32_16x16x128_f8f6f4 v[58:61], v[10:17], v[210:217], v[58:61]
	v_mfma_f32_16x16x128_f8f6f4 v[46:49], v[2:9], v[218:225], v[46:49]
	v_mfma_f32_16x16x128_f8f6f4 v[42:45], v[10:17], v[218:225], v[42:45]
	s_nop 3
	v_mfma_f32_16x16x128_f8f6f4 v[86:89], v[18:25], v[194:201], v[86:89]
	v_mfma_f32_16x16x128_f8f6f4 v[82:85], v[26:33], v[194:201], v[82:85]
	v_mfma_f32_16x16x128_f8f6f4 v[70:73], v[18:25], v[202:209], v[70:73]
	v_mfma_f32_16x16x128_f8f6f4 v[66:69], v[26:33], v[202:209], v[66:69]
	v_mfma_f32_16x16x128_f8f6f4 v[54:57], v[18:25], v[210:217], v[54:57]
	v_mfma_f32_16x16x128_f8f6f4 v[50:53], v[26:33], v[210:217], v[50:53]
	v_mfma_f32_16x16x128_f8f6f4 v[38:41], v[18:25], v[218:225], v[38:41]
	v_mfma_f32_16x16x128_f8f6f4 v[34:37], v[26:33], v[218:225], v[34:37]
	s_setprio 0
	s_add_i32 s68, s68, 2
	s_add_u32 s23, s23, 0x10000
	s_addc_u32 s67, s67, 0
	s_add_u32 s24, s24, 0x10000
	s_addc_u32 s25, s25, 0
	s_cmp_gt_u32 s68, 5
	s_cbranch_scc0 .Lh1_1138
	s_branch .Lfx_33571
.Lh1_1138:
	ds_read_b128 v[18:21], v189
	ds_read_b128 v[22:25], v189 offset:1024
	ds_read_b128 v[26:29], v189 offset:2048
	ds_read_b128 v[30:33], v189 offset:3072
	ds_read_b128 v[2:5], v190
	ds_read_b128 v[6:9], v190 offset:1024
	ds_read_b128 v[10:13], v190 offset:2048
	ds_read_b128 v[14:17], v190 offset:3072
	s_add_u32 s26, s24, 0x8000
	s_addc_u32 s27, s25, 0
	s_cmp_eq_u32 s68, 4
	s_cselect_b32 s30, s16, s26
	s_cselect_b32 s31, s17, s27
	s_cselect_b32 s28, s18, s23
	s_cselect_b32 s29, s19, s67
	s_add_u32 s26, s30, 0x8000
	s_addc_u32 s27, s31, 0
	s_add_i32 m0, s44, 0xc000
	ds_read_b128 v[194:197], v191
	ds_read_b128 v[198:201], v191 offset:1024
	ds_read_b128 v[202:205], v191 offset:2048
	ds_read_b128 v[206:209], v191 offset:3072
	ds_read_b128 v[210:213], v191 offset:4096
	ds_read_b128 v[214:217], v191 offset:5120
	ds_read_b128 v[218:221], v191 offset:6144
	ds_read_b128 v[222:225], v191 offset:7168
	global_load_lds_dwordx4 v184, s[24:25]
	s_add_i32 m0, s44, 0xe000
	s_nop 0
	global_load_lds_dwordx4 v182, s[24:25]
	s_waitcnt vmcnt(8)
	s_waitcnt lgkmcnt(0)
	s_barrier
	s_setprio 2
	v_mfma_f32_16x16x128_f8f6f4 v[158:161], v[18:25], v[194:201], v[158:161]
	v_mfma_f32_16x16x128_f8f6f4 v[154:157], v[26:33], v[194:201], v[154:157]
	v_mfma_f32_16x16x128_f8f6f4 v[142:145], v[18:25], v[202:209], v[142:145]
	v_mfma_f32_16x16x128_f8f6f4 v[138:141], v[26:33], v[202:209], v[138:141]
	v_mfma_f32_16x16x128_f8f6f4 v[126:129], v[18:25], v[210:217], v[126:129]
	v_mfma_f32_16x16x128_f8f6f4 v[122:125], v[26:33], v[210:217], v[122:125]
	v_mfma_f32_16x16x128_f8f6f4 v[110:113], v[18:25], v[218:225], v[110:113]
	v_mfma_f32_16x16x128_f8f6f4 v[106:109], v[26:33], v[218:225], v[106:109]
	s_nop 3
	v_mfma_f32_16x16x128_f8f6f4 v[150:153], v[2:9], v[194:201], v[150:153]
	v_mfma_f32_16x16x128_f8f6f4 v[146:149], v[10:17], v[194:201], v[146:149]
	v_mfma_f32_16x16x128_f8f6f4 v[134:137], v[2:9], v[202:209], v[134:137]
	v_mfma_f32_16x16x128_f8f6f4 v[130:133], v[10:17], v[202:209], v[130:133]
	v_mfma_f32_16x16x128_f8f6f4 v[118:121], v[2:9], v[210:217], v[118:121]
	v_mfma_f32_16x16x128_f8f6f4 v[114:117], v[10:17], v[210:217], v[114:117]
	v_mfma_f32_16x16x128_f8f6f4 v[102:105], v[2:9], v[218:225], v[102:105]
	v_mfma_f32_16x16x128_f8f6f4 v[98:101], v[10:17], v[218:225], v[98:101]
	s_setprio 0
	s_add_i32 s69, s53, s43
	s_mov_b32 m0, s69
	ds_read_b128 v[194:197], v191 offset:16384
	ds_read_b128 v[198:201], v191 offset:17408
	ds_read_b128 v[202:205], v191 offset:18432
	ds_read_b128 v[206:209], v191 offset:19456
	ds_read_b128 v[210:213], v191 offset:20480
	ds_read_b128 v[214:217], v191 offset:21504
	ds_read_b128 v[218:221], v191 offset:22528
	ds_read_b128 v[222:225], v191 offset:23552
	global_load_lds_dwordx4 v164, s[28:29]
	s_add_i32 m0, s69, 0x2000
	s_add_i32 s69, s58, s43
	global_load_lds_dwordx4 v166, s[28:29]
	s_add_u32 s98, s28, s4
	s_addc_u32 s99, s29, s5
	s_mov_b32 m0, s69
	s_nop 0
	global_load_lds_dwordx4 v164, s[98:99]
	s_add_u32 s100, s28, s4
	s_addc_u32 s101, s29, s5
	s_add_i32 m0, s69, 0x2000
	s_nop 0
	global_load_lds_dwordx4 v166, s[100:101]
	s_mov_b32 m0, s44
	s_nop 0
	global_load_lds_dwordx4 v168, s[30:31]
	s_mov_b32 m0, s45
	s_nop 0
	global_load_lds_dwordx4 v170, s[30:31]
	s_waitcnt vmcnt(8)
	s_waitcnt lgkmcnt(0)
	s_barrier
; #define PG8_STAGE(bufoff, gbase, voff) do { _Pragma("unroll") for (int _i = 0; _i < 2; ++_i) \
;         __builtin_amdgcn_global_load_lds((const unsigned*)((const char*)(gbase) + (voff)[_i]), (PG8_LAS unsigned*)(lds + (bufoff) + ldsw + _i * 8192), 16, 0, 0); } while (0)
; #define PG8_WAIT_V(n) asm volatile("s_waitcnt vmcnt(" #n ")" ::: "memory")
; #define PG8_WAIT_L(n) asm volatile("s_waitcnt lgkmcnt(" #n ")" ::: "memory")
; template <class Epi, class Sched, bool ALIGN_EPI = true, bool F8 = false>
; __device__ __forceinline__ void gemm_phase(PG8_LAS unsigned char* lds, const Sched& S, const Epi& E) {
;     ...
;         for (int t = 0; t < nt; t += 2) {
;             const bool last = (t == nt - 2);
;             if constexpr (Sched::GATHER) { if (last && has_next) S.a_off(nxt, Rs, Cs, voffAn); }
;             const char* a1 = cA + (size_t)(t + 1) * kstep;
;             const char* a2 = last ? nA : cA + (size_t)(t + 2) * kstep; const char* b2 = last ? nB : cB + (size_t)(t + 2) * kstepB;
;             const char* a3 = a2 + kstep; const char* b3 = b2 + kstepB;
;             unsigned vA2[2][2];
; #pragma unroll
;             for (int h = 0; h < 2; ++h)
; #pragma unroll
;                 for (int i = 0; i < 2; ++i) { if constexpr (Sched::GATHER) vA2[h][i] = (last && has_next) ? voffAn[h][i] : voffA[h][i]; else vA2[h][i] = voffA[h][i]; }
;             PG8_LDB(B0, 0, 0); PG8_LDB(B1, 0, 1); PG8_SCHED; PG8_LDA(At, 0, 0); PG8_STAGE(PG8_SA(1, 1), a1, voffA[1]);
;             PG8_WAIT_V(8); PG8_WAIT_L(0); PG8_BAR; PG8_MMA(0, 0, At, B0); PG8_MMA(0, 1, At, B1); PG8_BAR; PG8_SCHED;
;             PG8_LDA(At, 0, 1); PG8_STAGE(PG8_SB(0, 0), b2, voffB[0]); PG8_STAGE(PG8_SB(0, 1), b2, voffB[1]); PG8_STAGE(PG8_SA(0, 0), a2, vA2[0]);
;             PG8_WAIT_V(8); PG8_WAIT_L(0); PG8_BAR; PG8_MMA(1, 0, At, B0); PG8_MMA(1, 1, At, B1); PG8_BAR; PG8_SCHED;
;             PG8_LDB(B0, 1, 0); PG8_LDB(B1, 1, 1); PG8_SCHED; PG8_LDA(At, 1, 0); PG8_STAGE(PG8_SA(0, 1), a2, vA2[1]);
;             PG8_WAIT_V(8); PG8_WAIT_L(0); PG8_BAR; PG8_MMA(0, 0, At, B0); PG8_MMA(0, 1, At, B1); PG8_BAR; PG8_SCHED;
;             PG8_LDA(At, 1, 1); PG8_STAGE(PG8_SB(1, 0), b3, voffB[0]); PG8_STAGE(PG8_SB(1, 1), b3, voffB[1]); PG8_STAGE(PG8_SA(1, 0), a3, vA2[0]);
;             PG8_WAIT_V(8); PG8_WAIT_L(0); PG8_BAR; PG8_MMA(1, 0, At, B0); PG8_MMA(1, 1, At, B1); PG8_BAR; PG8_SCHED;
	s_setprio 2
	v_mfma_f32_16x16x128_f8f6f4 v[94:97], v[18:25], v[194:201], v[94:97]
	v_mfma_f32_16x16x128_f8f6f4 v[90:93], v[26:33], v[194:201], v[90:93]
	v_mfma_f32_16x16x128_f8f6f4 v[78:81], v[18:25], v[202:209], v[78:81]
	v_mfma_f32_16x16x128_f8f6f4 v[74:77], v[26:33], v[202:209], v[74:77]
	v_mfma_f32_16x16x128_f8f6f4 v[62:65], v[18:25], v[210:217], v[62:65]
	v_mfma_f32_16x16x128_f8f6f4 v[58:61], v[26:33], v[210:217], v[58:61]
	v_mfma_f32_16x16x128_f8f6f4 v[46:49], v[18:25], v[218:225], v[46:49]
	v_mfma_f32_16x16x128_f8f6f4 v[42:45], v[26:33], v[218:225], v[42:45]
	s_nop 3
	v_mfma_f32_16x16x128_f8f6f4 v[86:89], v[2:9], v[194:201], v[86:89]
	v_mfma_f32_16x16x128_f8f6f4 v[82:85], v[10:17], v[194:201], v[82:85]
	v_mfma_f32_16x16x128_f8f6f4 v[70:73], v[2:9], v[202:209], v[70:73]
	v_mfma_f32_16x16x128_f8f6f4 v[66:69], v[10:17], v[202:209], v[66:69]
	v_mfma_f32_16x16x128_f8f6f4 v[54:57], v[2:9], v[210:217], v[54:57]
	v_mfma_f32_16x16x128_f8f6f4 v[50:53], v[10:17], v[210:217], v[50:53]
	v_mfma_f32_16x16x128_f8f6f4 v[38:41], v[2:9], v[218:225], v[38:41]
	v_mfma_f32_16x16x128_f8f6f4 v[34:37], v[10:17], v[218:225], v[34:37]
	s_setprio 0
	s_add_i32 s69, 0, 0x18000
	s_add_i32 s70, 0, 0x1c000
	v_add_u32_e32 v14, s69, v187
	v_add_u32_e32 v30, s70, v187
	ds_read_b128 v[2:5], v14
	ds_read_b128 v[6:9], v14 offset:1024
	ds_read_b128 v[10:13], v14 offset:2048
	ds_read_b128 v[14:17], v14 offset:3072
	ds_read_b128 v[18:21], v30
	ds_read_b128 v[22:25], v30 offset:1024
	ds_read_b128 v[26:29], v30 offset:2048
	ds_read_b128 v[30:33], v30 offset:3072
	s_mov_b32 m0, s46
	ds_read_b128 v[194:197], v191 offset:32768
	ds_read_b128 v[198:201], v191 offset:33792
	ds_read_b128 v[202:205], v191 offset:34816
	ds_read_b128 v[206:209], v191 offset:35840
	ds_read_b128 v[210:213], v191 offset:36864
	ds_read_b128 v[214:217], v191 offset:37888
	ds_read_b128 v[218:221], v191 offset:38912
	ds_read_b128 v[222:225], v191 offset:39936
	global_load_lds_dwordx4 v172, s[30:31]
	s_mov_b32 m0, s47
	s_nop 0
	global_load_lds_dwordx4 v174, s[30:31]
	s_waitcnt vmcnt(8)
	s_waitcnt lgkmcnt(0)
	s_barrier
	s_setprio 2
	v_mfma_f32_16x16x128_f8f6f4 v[158:161], v[2:9], v[194:201], v[158:161]
	v_mfma_f32_16x16x128_f8f6f4 v[154:157], v[10:17], v[194:201], v[154:157]
	v_mfma_f32_16x16x128_f8f6f4 v[142:145], v[2:9], v[202:209], v[142:145]
	v_mfma_f32_16x16x128_f8f6f4 v[138:141], v[10:17], v[202:209], v[138:141]
	v_mfma_f32_16x16x128_f8f6f4 v[126:129], v[2:9], v[210:217], v[126:129]
	v_mfma_f32_16x16x128_f8f6f4 v[122:125], v[10:17], v[210:217], v[122:125]
	v_mfma_f32_16x16x128_f8f6f4 v[110:113], v[2:9], v[218:225], v[110:113]
	v_mfma_f32_16x16x128_f8f6f4 v[106:109], v[10:17], v[218:225], v[106:109]
	s_nop 3
	v_mfma_f32_16x16x128_f8f6f4 v[150:153], v[18:25], v[194:201], v[150:153]
	v_mfma_f32_16x16x128_f8f6f4 v[146:149], v[26:33], v[194:201], v[146:149]
	v_mfma_f32_16x16x128_f8f6f4 v[134:137], v[18:25], v[202:209], v[134:137]
	v_mfma_f32_16x16x128_f8f6f4 v[130:133], v[26:33], v[202:209], v[130:133]
	v_mfma_f32_16x16x128_f8f6f4 v[118:121], v[18:25], v[210:217], v[118:121]
	v_mfma_f32_16x16x128_f8f6f4 v[114:117], v[26:33], v[210:217], v[114:117]
	v_mfma_f32_16x16x128_f8f6f4 v[102:105], v[18:25], v[218:225], v[102:105]
	v_mfma_f32_16x16x128_f8f6f4 v[98:101], v[26:33], v[218:225], v[98:101]
	s_setprio 0
	s_add_u32 s28, s28, 0x8000
	s_addc_u32 s29, s29, 0
	s_add_i32 s30, s69, s43
	s_mov_b32 m0, s30
	ds_read_b128 v[194:197], v191 offset:49152
	ds_read_b128 v[198:201], v191 offset:50176
	ds_read_b128 v[202:205], v191 offset:51200
	ds_read_b128 v[206:209], v191 offset:52224
	ds_read_b128 v[210:213], v191 offset:53248
	ds_read_b128 v[214:217], v191 offset:54272
	ds_read_b128 v[218:221], v191 offset:55296
	ds_read_b128 v[222:225], v191 offset:56320
	global_load_lds_dwordx4 v164, s[28:29]
	s_add_i32 m0, s30, 0x2000
	s_add_i32 s30, s70, s43
	global_load_lds_dwordx4 v166, s[28:29]
	s_mov_b32 m0, s30
	s_nop 0
	global_load_lds_dwordx4 v178, s[28:29]
	s_add_i32 m0, s30, 0x2000
	s_nop 0
	global_load_lds_dwordx4 v180, s[28:29]
	s_mov_b32 m0, s51
	s_nop 0
	global_load_lds_dwordx4 v168, s[26:27]
	s_mov_b32 m0, s52
	s_nop 0
	global_load_lds_dwordx4 v170, s[26:27]
	s_waitcnt vmcnt(8)
	s_waitcnt lgkmcnt(0)
	s_barrier
	s_setprio 2
	v_mfma_f32_16x16x128_f8f6f4 v[94:97], v[2:9], v[194:201], v[94:97]
	v_mfma_f32_16x16x128_f8f6f4 v[90:93], v[10:17], v[194:201], v[90:93]
	v_mfma_f32_16x16x128_f8f6f4 v[78:81], v[2:9], v[202:209], v[78:81]
	v_mfma_f32_16x16x128_f8f6f4 v[74:77], v[10:17], v[202:209], v[74:77]
	v_mfma_f32_16x16x128_f8f6f4 v[62:65], v[2:9], v[210:217], v[62:65]
	v_mfma_f32_16x16x128_f8f6f4 v[58:61], v[10:17], v[210:217], v[58:61]
	v_mfma_f32_16x16x128_f8f6f4 v[46:49], v[2:9], v[218:225], v[46:49]
	v_mfma_f32_16x16x128_f8f6f4 v[42:45], v[10:17], v[218:225], v[42:45]
	s_nop 3
	v_mfma_f32_16x16x128_f8f6f4 v[86:89], v[18:25], v[194:201], v[86:89]
	v_mfma_f32_16x16x128_f8f6f4 v[82:85], v[26:33], v[194:201], v[82:85]
	v_mfma_f32_16x16x128_f8f6f4 v[70:73], v[18:25], v[202:209], v[70:73]
	v_mfma_f32_16x16x128_f8f6f4 v[66:69], v[26:33], v[202:209], v[66:69]
	v_mfma_f32_16x16x128_f8f6f4 v[54:57], v[18:25], v[210:217], v[54:57]
	v_mfma_f32_16x16x128_f8f6f4 v[50:53], v[26:33], v[210:217], v[50:53]
	v_mfma_f32_16x16x128_f8f6f4 v[38:41], v[18:25], v[218:225], v[38:41]
	v_mfma_f32_16x16x128_f8f6f4 v[34:37], v[26:33], v[218:225], v[34:37]
	s_setprio 0
	s_add_i32 s68, s68, 2
	s_add_u32 s23, s23, 0x10000
	s_addc_u32 s67, s67, 0
	s_add_u32 s24, s24, 0x10000
	s_addc_u32 s25, s25, 0
	s_cmp_gt_u32 s68, 5
	s_cbranch_scc0 .Lh1_1138
